# speedup vs baseline: 1.0074x; 1.0028x over previous
.LBB3_5:
	s_waitcnt lgkmcnt(0)
	v_cvt_f16_f32_e32 v180, s7
	v_cvt_f16_f32_e32 v182, s6
	v_cvt_f16_f32_e32 v181, s28
	s_cmp_lt_u32 s94, 4
	s_cbranch_scc1 .Lmylp3_1
	s_setprio 1
.Lmylp3_1:
	s_waitcnt vmcnt(3)
	v_pk_mul_f16 v183, v182, v184 op_sel_hi:[0,1]
	v_pk_mul_f16 v190, v182, v187 op_sel_hi:[0,1]
	v_pk_mul_f16 v194, v180, v187 op_sel_hi:[0,1]
	v_pk_mul_f16 v198, v181, v187 op_sel_hi:[0,1]
	v_pk_mul_f16 v188, v182, v185 op_sel_hi:[0,1]
	v_pk_mul_f16 v189, v182, v186 op_sel_hi:[0,1]
	v_pk_mul_f16 v191, v180, v184 op_sel_hi:[0,1]
	s_mov_b64 exec, s[64:65]
	buffer_load_dwordx4 v[18:21], v249, s[16:19], 0 offen
	buffer_load_dwordx4 v[6:9], v249, s[16:19], 0 offen offset:512
	s_mov_b64 exec, -1
	v_pk_mul_f16 v192, v180, v185 op_sel_hi:[0,1]
	v_pk_mul_f16 v193, v180, v186 op_sel_hi:[0,1]
	v_pk_mul_f16 v195, v181, v184 op_sel_hi:[0,1]
	v_pk_mul_f16 v196, v181, v185 op_sel_hi:[0,1]
	v_pk_mul_f16 v197, v181, v186 op_sel_hi:[0,1]
	v_pk_fma_f16 v113, v113, v187, v190
	v_pk_fma_f16 v110, v110, v184, v183
	v_pk_fma_f16 v129, v129, v187, v190
	v_pk_fma_f16 v126, v126, v184, v183
	v_pk_fma_f16 v141, v141, v187, v190
	v_pk_fma_f16 v138, v138, v184, v183
	v_pk_fma_f16 v183, v89, v187, v194
	v_pk_fma_f16 v199, v109, v187, v194
	buffer_load_dwordx4 v[30:33], v250, s[16:19], 0 offen offset:512
	buffer_load_dwordx4 v[10:13], v250, s[16:19], 0 offen offset:1024
	v_pk_fma_f16 v194, v125, v187, v194
	v_pk_fma_f16 v203, v53, v187, v198
	v_pk_fma_f16 v207, v69, v187, v198
	v_pk_fma_f16 v187, v97, v187, v198
	v_pk_maximum3_f16 v198, v113, v129, v141
	v_pk_fma_f16 v112, v112, v186, v189
	v_pk_fma_f16 v111, v111, v185, v188
	v_pk_fma_f16 v128, v128, v186, v189
	v_pk_fma_f16 v127, v127, v185, v188
	v_pk_fma_f16 v140, v140, v186, v189
	v_pk_fma_f16 v139, v139, v185, v188
	v_pk_fma_f16 v188, v88, v186, v193
	v_pk_fma_f16 v189, v87, v185, v192
	v_pk_fma_f16 v190, v86, v184, v191
	v_pk_fma_f16 v200, v108, v186, v193
	v_pk_fma_f16 v201, v107, v185, v192
	s_mov_b64 exec, s[66:67]
	buffer_load_dwordx4 v[54:57], v250, s[16:19], 0 offen offset:2048
	buffer_load_dwordx4 v[14:17], v250, s[16:19], 0 offen offset:2560
	s_mov_b64 exec, -1
	v_pk_fma_f16 v202, v106, v184, v191
	v_pk_fma_f16 v193, v124, v186, v193
	v_pk_fma_f16 v192, v123, v185, v192
	v_pk_fma_f16 v191, v122, v184, v191
	v_pk_fma_f16 v204, v52, v186, v197
	v_pk_fma_f16 v205, v51, v185, v196
	v_pk_fma_f16 v206, v50, v184, v195
	v_pk_fma_f16 v208, v68, v186, v197
	v_pk_fma_f16 v209, v67, v185, v196
	v_pk_fma_f16 v210, v66, v184, v195
	v_pk_fma_f16 v186, v96, v186, v197
	v_pk_fma_f16 v185, v95, v185, v196
	v_pk_fma_f16 v184, v94, v184, v195
	v_pk_maximum3_f16 v195, v110, v126, v138
	v_pk_maximum3_f16 v196, v111, v127, v139
	v_pk_maximum3_f16 v197, v112, v128, v140
	v_pk_maximum3_f16 v214, v183, v199, v194
	v_pk_maximum3_f16 v218, v203, v207, v187
	v_pk_maximum3_f16 v211, v190, v202, v191
	v_pk_maximum3_f16 v212, v189, v201, v192
	v_pk_maximum3_f16 v213, v188, v200, v193
	v_pk_maximum3_f16 v215, v206, v210, v184
	v_pk_maximum3_f16 v216, v205, v209, v185
	v_pk_maximum3_f16 v198, v198, v214, v218
	v_pk_maximum3_f16 v217, v204, v208, v186
	v_pk_maximum3_f16 v195, v195, v211, v215
	v_pk_maximum3_f16 v196, v196, v212, v216
	v_pk_maximum3_f16 v197, v197, v213, v217
	v_pk_add_f16 v113, v113, v198 neg_lo:[0,1] neg_hi:[0,1]
	s_mov_b64 exec, s[64:65]
	buffer_load_dwordx4 v[74:77], v251, s[16:19], 0 offen
	buffer_load_dwordx4 v[26:29], v251, s[16:19], 0 offen offset:512
	s_mov_b64 exec, -1
	v_pk_add_f16 v110, v110, v195 neg_lo:[0,1] neg_hi:[0,1]
	v_pk_add_f16 v111, v111, v196 neg_lo:[0,1] neg_hi:[0,1]
	v_pk_add_f16 v112, v112, v197 neg_lo:[0,1] neg_hi:[0,1]
	v_pk_add_f16 v126, v126, v195 neg_lo:[0,1] neg_hi:[0,1]
	v_exp_f16_sdwa v211, v110 dst_sel:WORD_0 dst_unused:UNUSED_PAD src0_sel:WORD_0
	v_exp_f16_sdwa v212, v111 dst_sel:WORD_0 dst_unused:UNUSED_PAD src0_sel:WORD_0
	v_exp_f16_sdwa v213, v112 dst_sel:WORD_0 dst_unused:UNUSED_PAD src0_sel:WORD_0
	v_exp_f16_sdwa v214, v113 dst_sel:WORD_0 dst_unused:UNUSED_PAD src0_sel:WORD_0
	v_exp_f16_sdwa v211, v110 dst_sel:WORD_1 dst_unused:UNUSED_PRESERVE src0_sel:WORD_1
	v_exp_f16_sdwa v212, v111 dst_sel:WORD_1 dst_unused:UNUSED_PRESERVE src0_sel:WORD_1
	v_exp_f16_sdwa v213, v112 dst_sel:WORD_1 dst_unused:UNUSED_PRESERVE src0_sel:WORD_1
	v_exp_f16_sdwa v214, v113 dst_sel:WORD_1 dst_unused:UNUSED_PRESERVE src0_sel:WORD_1
	v_pk_add_f16 v127, v127, v196 neg_lo:[0,1] neg_hi:[0,1]
	v_pk_add_f16 v113, v211, 0
	v_pk_fma_f16 v81, v81, v214, 0
	v_pk_add_f16 v110, v214, 0
	v_pk_add_f16 v111, v213, 0
	v_pk_add_f16 v112, v212, 0
	v_pk_fma_f16 v80, v80, v213, 0
	v_pk_fma_f16 v79, v79, v212, 0
	v_pk_fma_f16 v78, v78, v211, 0
	v_pk_add_f16 v128, v128, v197 neg_lo:[0,1] neg_hi:[0,1]
	buffer_load_dwordx4 v[98:101], v252, s[16:19], 0 offen offset:512
	buffer_load_dwordx4 v[38:41], v252, s[16:19], 0 offen offset:1024
	v_pk_add_f16 v129, v129, v198 neg_lo:[0,1] neg_hi:[0,1]
	v_exp_f16_sdwa v211, v126 dst_sel:WORD_0 dst_unused:UNUSED_PAD src0_sel:WORD_0
	v_exp_f16_sdwa v212, v127 dst_sel:WORD_0 dst_unused:UNUSED_PAD src0_sel:WORD_0
	v_exp_f16_sdwa v213, v128 dst_sel:WORD_0 dst_unused:UNUSED_PAD src0_sel:WORD_0
	v_exp_f16_sdwa v214, v129 dst_sel:WORD_0 dst_unused:UNUSED_PAD src0_sel:WORD_0
	v_exp_f16_sdwa v211, v126 dst_sel:WORD_1 dst_unused:UNUSED_PRESERVE src0_sel:WORD_1
	v_exp_f16_sdwa v212, v127 dst_sel:WORD_1 dst_unused:UNUSED_PRESERVE src0_sel:WORD_1
	v_exp_f16_sdwa v213, v128 dst_sel:WORD_1 dst_unused:UNUSED_PRESERVE src0_sel:WORD_1
	v_exp_f16_sdwa v214, v129 dst_sel:WORD_1 dst_unused:UNUSED_PRESERVE src0_sel:WORD_1
	v_pk_add_f16 v113, v113, v211
	v_pk_fma_f16 v81, v105, v214, v81
	v_pk_add_f16 v105, v141, v198 neg_lo:[0,1] neg_hi:[0,1]
	v_pk_add_f16 v112, v112, v212
	v_pk_add_f16 v111, v111, v213
	v_pk_add_f16 v110, v110, v214
	v_pk_fma_f16 v78, v102, v211, v78
	v_pk_fma_f16 v79, v103, v212, v79
	v_pk_fma_f16 v80, v104, v213, v80
	v_pk_add_f16 v102, v138, v195 neg_lo:[0,1] neg_hi:[0,1]
	v_pk_add_f16 v103, v139, v196 neg_lo:[0,1] neg_hi:[0,1]
	v_pk_add_f16 v104, v140, v197 neg_lo:[0,1] neg_hi:[0,1]
	v_exp_f16_sdwa v126, v102 dst_sel:WORD_0 dst_unused:UNUSED_PAD src0_sel:WORD_0
	v_exp_f16_sdwa v127, v103 dst_sel:WORD_0 dst_unused:UNUSED_PAD src0_sel:WORD_0
	v_exp_f16_sdwa v128, v104 dst_sel:WORD_0 dst_unused:UNUSED_PAD src0_sel:WORD_0
	v_exp_f16_sdwa v129, v105 dst_sel:WORD_0 dst_unused:UNUSED_PAD src0_sel:WORD_0
	v_exp_f16_sdwa v126, v102 dst_sel:WORD_1 dst_unused:UNUSED_PRESERVE src0_sel:WORD_1
	v_exp_f16_sdwa v127, v103 dst_sel:WORD_1 dst_unused:UNUSED_PRESERVE src0_sel:WORD_1
	v_exp_f16_sdwa v128, v104 dst_sel:WORD_1 dst_unused:UNUSED_PRESERVE src0_sel:WORD_1
	v_exp_f16_sdwa v129, v105 dst_sel:WORD_1 dst_unused:UNUSED_PRESERVE src0_sel:WORD_1
	v_pk_add_f16 v105, v113, v126
	v_pk_add_f16 v102, v110, v129
	s_mov_b64 exec, s[66:67]
	buffer_load_dwordx4 v[114:117], v252, s[16:19], 0 offen offset:2048
	buffer_load_dwordx4 v[58:61], v252, s[16:19], 0 offen offset:2560
	s_mov_b64 exec, -1
	v_pk_add_f16 v103, v111, v128
	v_pk_add_f16 v104, v112, v127
	v_pk_fma_f16 v81, v121, v129, v81
	v_pk_fma_f16 v80, v120, v128, v80
	v_pk_fma_f16 v79, v119, v127, v79
	v_pk_fma_f16 v78, v118, v126, v78
	v_pk_add_f16 v110, v190, v195 neg_lo:[0,1] neg_hi:[0,1]
	v_pk_add_f16 v111, v189, v196 neg_lo:[0,1] neg_hi:[0,1]
	v_pk_add_f16 v112, v188, v197 neg_lo:[0,1] neg_hi:[0,1]
	v_pk_add_f16 v113, v183, v198 neg_lo:[0,1] neg_hi:[0,1]
	v_exp_f16_sdwa v118, v110 dst_sel:WORD_0 dst_unused:UNUSED_PAD src0_sel:WORD_0
	v_exp_f16_sdwa v119, v111 dst_sel:WORD_0 dst_unused:UNUSED_PAD src0_sel:WORD_0
	v_exp_f16_sdwa v120, v112 dst_sel:WORD_0 dst_unused:UNUSED_PAD src0_sel:WORD_0
	v_exp_f16_sdwa v121, v113 dst_sel:WORD_0 dst_unused:UNUSED_PAD src0_sel:WORD_0
	v_exp_f16_sdwa v118, v110 dst_sel:WORD_1 dst_unused:UNUSED_PRESERVE src0_sel:WORD_1
	v_exp_f16_sdwa v119, v111 dst_sel:WORD_1 dst_unused:UNUSED_PRESERVE src0_sel:WORD_1
	v_exp_f16_sdwa v120, v112 dst_sel:WORD_1 dst_unused:UNUSED_PRESERVE src0_sel:WORD_1
	v_exp_f16_sdwa v121, v113 dst_sel:WORD_1 dst_unused:UNUSED_PRESERVE src0_sel:WORD_1
	v_pk_add_f16 v110, v202, v195 neg_lo:[0,1] neg_hi:[0,1]
	v_pk_add_f16 v105, v105, v118
	v_pk_add_f16 v104, v104, v119
	v_pk_add_f16 v103, v103, v120
	s_mov_b64 exec, s[76:77]
	buffer_load_dwordx4 v[130:133], v253, s[16:19], 0 offen
	buffer_load_dwordx4 v[70:73], v253, s[16:19], 0 offen offset:512
	s_mov_b64 exec, -1
	v_pk_add_f16 v102, v102, v121
	v_pk_fma_f16 v78, v46, v118, v78
	v_pk_fma_f16 v79, v47, v119, v79
	v_pk_fma_f16 v80, v48, v120, v80
	v_pk_fma_f16 v81, v49, v121, v81
	v_pk_add_f16 v111, v201, v196 neg_lo:[0,1] neg_hi:[0,1]
	v_pk_add_f16 v112, v200, v197 neg_lo:[0,1] neg_hi:[0,1]
	v_pk_add_f16 v113, v199, v198 neg_lo:[0,1] neg_hi:[0,1]
	v_exp_f16_sdwa v118, v110 dst_sel:WORD_0 dst_unused:UNUSED_PAD src0_sel:WORD_0
	v_exp_f16_sdwa v119, v111 dst_sel:WORD_0 dst_unused:UNUSED_PAD src0_sel:WORD_0
	v_exp_f16_sdwa v120, v112 dst_sel:WORD_0 dst_unused:UNUSED_PAD src0_sel:WORD_0
	v_exp_f16_sdwa v121, v113 dst_sel:WORD_0 dst_unused:UNUSED_PAD src0_sel:WORD_0
	v_exp_f16_sdwa v118, v110 dst_sel:WORD_1 dst_unused:UNUSED_PRESERVE src0_sel:WORD_1
	v_exp_f16_sdwa v119, v111 dst_sel:WORD_1 dst_unused:UNUSED_PRESERVE src0_sel:WORD_1
	v_exp_f16_sdwa v120, v112 dst_sel:WORD_1 dst_unused:UNUSED_PRESERVE src0_sel:WORD_1
	v_exp_f16_sdwa v121, v113 dst_sel:WORD_1 dst_unused:UNUSED_PRESERVE src0_sel:WORD_1
	v_pk_add_f16 v110, v191, v195 neg_lo:[0,1] neg_hi:[0,1]
	v_pk_add_f16 v105, v105, v118
	v_pk_add_f16 v102, v102, v121
	v_pk_add_f16 v103, v103, v120
	v_pk_add_f16 v104, v104, v119
	v_pk_fma_f16 v81, v65, v121, v81
	v_pk_fma_f16 v80, v64, v120, v80
	s_mov_b64 exec, s[70:71]
	buffer_load_dwordx4 v[134:137], v254, s[16:19], 0 offen offset:512
	buffer_load_dwordx4 v[90:93], v254, s[16:19], 0 offen offset:1024
	s_mov_b64 exec, -1
	v_pk_fma_f16 v79, v63, v119, v79
	v_pk_fma_f16 v78, v62, v118, v78
	v_pk_add_f16 v111, v192, v196 neg_lo:[0,1] neg_hi:[0,1]
	v_pk_add_f16 v112, v193, v197 neg_lo:[0,1] neg_hi:[0,1]
	v_pk_add_f16 v113, v194, v198 neg_lo:[0,1] neg_hi:[0,1]
	v_exp_f16_sdwa v118, v110 dst_sel:WORD_0 dst_unused:UNUSED_PAD src0_sel:WORD_0
	v_exp_f16_sdwa v119, v111 dst_sel:WORD_0 dst_unused:UNUSED_PAD src0_sel:WORD_0
	v_exp_f16_sdwa v120, v112 dst_sel:WORD_0 dst_unused:UNUSED_PAD src0_sel:WORD_0
	v_exp_f16_sdwa v121, v113 dst_sel:WORD_0 dst_unused:UNUSED_PAD src0_sel:WORD_0
	v_exp_f16_sdwa v118, v110 dst_sel:WORD_1 dst_unused:UNUSED_PRESERVE src0_sel:WORD_1
	v_exp_f16_sdwa v119, v111 dst_sel:WORD_1 dst_unused:UNUSED_PRESERVE src0_sel:WORD_1
	v_exp_f16_sdwa v120, v112 dst_sel:WORD_1 dst_unused:UNUSED_PRESERVE src0_sel:WORD_1
	v_exp_f16_sdwa v121, v113 dst_sel:WORD_1 dst_unused:UNUSED_PRESERVE src0_sel:WORD_1
	v_pk_add_f16 v110, v206, v195 neg_lo:[0,1] neg_hi:[0,1]
	v_pk_add_f16 v105, v105, v118
	v_pk_add_f16 v104, v104, v119
	v_pk_add_f16 v103, v103, v120
	v_pk_add_f16 v102, v102, v121
	v_pk_fma_f16 v78, v82, v118, v78
	v_pk_fma_f16 v79, v83, v119, v79
	v_pk_fma_f16 v80, v84, v120, v80
	v_pk_fma_f16 v81, v85, v121, v81
	s_mov_b64 exec, s[78:79]
	buffer_load_dwordx4 v[142:145], v254, s[16:19], 0 offen offset:2048
	buffer_load_dwordx4 v[2:5], v254, s[16:19], 0 offen offset:2560
	s_mov_b64 exec, -1
	v_pk_add_f16 v111, v205, v196 neg_lo:[0,1] neg_hi:[0,1]
	v_pk_add_f16 v112, v204, v197 neg_lo:[0,1] neg_hi:[0,1]
	v_pk_add_f16 v113, v203, v198 neg_lo:[0,1] neg_hi:[0,1]
	v_exp_f16_sdwa v118, v110 dst_sel:WORD_0 dst_unused:UNUSED_PAD src0_sel:WORD_0
	v_exp_f16_sdwa v119, v111 dst_sel:WORD_0 dst_unused:UNUSED_PAD src0_sel:WORD_0
	v_exp_f16_sdwa v120, v112 dst_sel:WORD_0 dst_unused:UNUSED_PAD src0_sel:WORD_0
	v_exp_f16_sdwa v121, v113 dst_sel:WORD_0 dst_unused:UNUSED_PAD src0_sel:WORD_0
	v_exp_f16_sdwa v118, v110 dst_sel:WORD_1 dst_unused:UNUSED_PRESERVE src0_sel:WORD_1
	v_exp_f16_sdwa v119, v111 dst_sel:WORD_1 dst_unused:UNUSED_PRESERVE src0_sel:WORD_1
	v_exp_f16_sdwa v120, v112 dst_sel:WORD_1 dst_unused:UNUSED_PRESERVE src0_sel:WORD_1
	v_exp_f16_sdwa v121, v113 dst_sel:WORD_1 dst_unused:UNUSED_PRESERVE src0_sel:WORD_1
	v_pk_add_f16 v110, v210, v195 neg_lo:[0,1] neg_hi:[0,1]
	v_pk_add_f16 v105, v105, v118
	v_pk_add_f16 v102, v102, v121
	v_pk_add_f16 v103, v103, v120
	v_pk_add_f16 v104, v104, v119
	v_pk_fma_f16 v81, v25, v121, v81
	v_pk_fma_f16 v80, v24, v120, v80
	v_pk_fma_f16 v79, v23, v119, v79
	v_pk_fma_f16 v78, v22, v118, v78
	v_pk_add_f16 v111, v209, v196 neg_lo:[0,1] neg_hi:[0,1]
	v_pk_add_f16 v112, v208, v197 neg_lo:[0,1] neg_hi:[0,1]
	v_pk_add_f16 v113, v207, v198 neg_lo:[0,1] neg_hi:[0,1]
	v_exp_f16_sdwa v118, v110 dst_sel:WORD_0 dst_unused:UNUSED_PAD src0_sel:WORD_0
	v_exp_f16_sdwa v119, v111 dst_sel:WORD_0 dst_unused:UNUSED_PAD src0_sel:WORD_0
	v_exp_f16_sdwa v120, v112 dst_sel:WORD_0 dst_unused:UNUSED_PAD src0_sel:WORD_0
	v_exp_f16_sdwa v121, v113 dst_sel:WORD_0 dst_unused:UNUSED_PAD src0_sel:WORD_0
	v_exp_f16_sdwa v118, v110 dst_sel:WORD_1 dst_unused:UNUSED_PRESERVE src0_sel:WORD_1
	v_exp_f16_sdwa v119, v111 dst_sel:WORD_1 dst_unused:UNUSED_PRESERVE src0_sel:WORD_1
	v_exp_f16_sdwa v120, v112 dst_sel:WORD_1 dst_unused:UNUSED_PRESERVE src0_sel:WORD_1
	v_exp_f16_sdwa v121, v113 dst_sel:WORD_1 dst_unused:UNUSED_PRESERVE src0_sel:WORD_1
	v_pk_add_f16 v110, v184, v195 neg_lo:[0,1] neg_hi:[0,1]
	v_pk_add_f16 v105, v105, v118
	v_pk_add_f16 v104, v104, v119
	v_pk_add_f16 v103, v103, v120
	v_pk_add_f16 v102, v102, v121
	v_pk_fma_f16 v78, v34, v118, v78
	v_pk_fma_f16 v79, v35, v119, v79
	v_pk_fma_f16 v80, v36, v120, v80
	v_pk_fma_f16 v81, v37, v121, v81
	v_pk_add_f16 v111, v185, v196 neg_lo:[0,1] neg_hi:[0,1]
	v_pk_add_f16 v112, v186, v197 neg_lo:[0,1] neg_hi:[0,1]
	v_pk_add_f16 v113, v187, v198 neg_lo:[0,1] neg_hi:[0,1]
	v_exp_f16_sdwa v118, v110 dst_sel:WORD_0 dst_unused:UNUSED_PAD src0_sel:WORD_0
	v_exp_f16_sdwa v119, v111 dst_sel:WORD_0 dst_unused:UNUSED_PAD src0_sel:WORD_0
	v_exp_f16_sdwa v120, v112 dst_sel:WORD_0 dst_unused:UNUSED_PAD src0_sel:WORD_0
	v_exp_f16_sdwa v121, v113 dst_sel:WORD_0 dst_unused:UNUSED_PAD src0_sel:WORD_0
	v_exp_f16_sdwa v118, v110 dst_sel:WORD_1 dst_unused:UNUSED_PRESERVE src0_sel:WORD_1
	v_exp_f16_sdwa v119, v111 dst_sel:WORD_1 dst_unused:UNUSED_PRESERVE src0_sel:WORD_1
	v_exp_f16_sdwa v120, v112 dst_sel:WORD_1 dst_unused:UNUSED_PRESERVE src0_sel:WORD_1
	v_exp_f16_sdwa v121, v113 dst_sel:WORD_1 dst_unused:UNUSED_PRESERVE src0_sel:WORD_1
	v_pk_add_f16 v105, v105, v118
	v_pk_add_f16 v104, v104, v119
	v_rcp_f16_e32 v110, v105
	v_rcp_f16_sdwa v105, v105 dst_sel:DWORD dst_unused:UNUSED_PAD src0_sel:WORD_1
	v_pk_add_f16 v103, v103, v120
	v_rcp_f16_e32 v111, v104
	v_rcp_f16_sdwa v104, v104 dst_sel:DWORD dst_unused:UNUSED_PAD src0_sel:WORD_1
	v_pk_add_f16 v102, v102, v121
	v_rcp_f16_e32 v112, v103
	v_rcp_f16_sdwa v103, v103 dst_sel:DWORD dst_unused:UNUSED_PAD src0_sel:WORD_1
	v_rcp_f16_e32 v113, v102
	v_rcp_f16_sdwa v102, v102 dst_sel:DWORD dst_unused:UNUSED_PAD src0_sel:WORD_1
	v_pk_fma_f16 v78, v42, v118, v78
	v_pack_b32_f16 v105, v110, v105
	v_pk_fma_f16 v79, v43, v119, v79
	v_pk_mul_f16 v110, v78, v105
	v_pack_b32_f16 v78, v111, v104
	v_pk_fma_f16 v80, v44, v120, v80
	v_pk_mul_f16 v111, v79, v78
	v_pack_b32_f16 v78, v112, v103
	v_pk_fma_f16 v81, v45, v121, v81
	v_pk_mul_f16 v112, v80, v78
	v_pack_b32_f16 v78, v113, v102
	v_pk_mul_f16 v113, v81, v78
	s_waitcnt vmcnt(12)
	v_pk_mul_f16 v78, v182, v154 op_sel_hi:[0,1]
	v_pk_mul_f16 v81, v182, v157 op_sel_hi:[0,1]
	v_pk_mul_f16 v105, v180, v157 op_sel_hi:[0,1]
	v_pk_mul_f16 v121, v181, v157 op_sel_hi:[0,1]
	v_pk_mul_f16 v79, v182, v155 op_sel_hi:[0,1]
	v_pk_mul_f16 v80, v182, v156 op_sel_hi:[0,1]
	v_pk_mul_f16 v102, v180, v154 op_sel_hi:[0,1]
	v_pk_mul_f16 v103, v180, v155 op_sel_hi:[0,1]
	v_pk_mul_f16 v104, v180, v156 op_sel_hi:[0,1]
	v_pk_mul_f16 v118, v181, v154 op_sel_hi:[0,1]
	v_pk_mul_f16 v119, v181, v155 op_sel_hi:[0,1]
	v_pk_mul_f16 v120, v181, v156 op_sel_hi:[0,1]
	v_pk_fma_f16 v89, v89, v157, v81
	v_pk_fma_f16 v86, v86, v154, v78
	v_pk_fma_f16 v109, v109, v157, v81
	v_pk_fma_f16 v106, v106, v154, v78
	v_pk_fma_f16 v81, v125, v157, v81
	v_pk_fma_f16 v78, v122, v154, v78
	v_pk_fma_f16 v122, v53, v157, v105
	v_pk_fma_f16 v126, v69, v157, v105
	v_pk_fma_f16 v105, v97, v157, v105
	v_pk_fma_f16 v138, v21, v157, v121
	v_pk_fma_f16 v183, v33, v157, v121
	v_pk_fma_f16 v121, v57, v157, v121
	v_pk_maximum3_f16 v157, v89, v109, v81
	v_pk_fma_f16 v88, v88, v156, v80
	v_pk_fma_f16 v87, v87, v155, v79
	v_pk_fma_f16 v108, v108, v156, v80
	v_pk_fma_f16 v107, v107, v155, v79
	v_pk_fma_f16 v80, v124, v156, v80
	v_pk_fma_f16 v79, v123, v155, v79
	v_pk_fma_f16 v123, v52, v156, v104
	v_pk_fma_f16 v124, v51, v155, v103
	v_pk_fma_f16 v125, v50, v154, v102
	v_pk_fma_f16 v127, v68, v156, v104
	v_pk_fma_f16 v128, v67, v155, v103
	v_pk_fma_f16 v129, v66, v154, v102
	v_pk_fma_f16 v104, v96, v156, v104
	v_pk_fma_f16 v103, v95, v155, v103
	v_pk_fma_f16 v102, v94, v154, v102
	v_pk_fma_f16 v139, v20, v156, v120
	v_pk_fma_f16 v140, v19, v155, v119
	v_pk_fma_f16 v141, v18, v154, v118
	v_pk_fma_f16 v184, v32, v156, v120
	v_pk_fma_f16 v185, v31, v155, v119
	v_pk_fma_f16 v186, v30, v154, v118
	v_pk_fma_f16 v120, v56, v156, v120
	v_pk_fma_f16 v119, v55, v155, v119
	v_pk_fma_f16 v118, v54, v154, v118
	v_pk_maximum3_f16 v154, v86, v106, v78
	v_pk_maximum3_f16 v155, v87, v107, v79
	v_pk_maximum3_f16 v156, v88, v108, v80
	v_pk_maximum3_f16 v190, v122, v126, v105
	v_pk_maximum3_f16 v194, v138, v183, v121
	v_pk_maximum3_f16 v187, v125, v129, v102
	v_pk_maximum3_f16 v188, v124, v128, v103
	v_pk_maximum3_f16 v189, v123, v127, v104
	v_pk_maximum3_f16 v191, v141, v186, v118
	v_pk_maximum3_f16 v192, v140, v185, v119
	v_pk_maximum3_f16 v157, v157, v190, v194
	v_pk_maximum3_f16 v193, v139, v184, v120
	v_pk_maximum3_f16 v154, v154, v187, v191
	v_pk_maximum3_f16 v155, v155, v188, v192
	v_pk_maximum3_f16 v156, v156, v189, v193
	v_pk_add_f16 v89, v89, v157 neg_lo:[0,1] neg_hi:[0,1]
	v_pk_add_f16 v86, v86, v154 neg_lo:[0,1] neg_hi:[0,1]
	v_pk_add_f16 v87, v87, v155 neg_lo:[0,1] neg_hi:[0,1]
	v_pk_add_f16 v88, v88, v156 neg_lo:[0,1] neg_hi:[0,1]
	v_pk_add_f16 v106, v106, v154 neg_lo:[0,1] neg_hi:[0,1]
	v_exp_f16_sdwa v187, v86 dst_sel:WORD_0 dst_unused:UNUSED_PAD src0_sel:WORD_0
	v_exp_f16_sdwa v188, v87 dst_sel:WORD_0 dst_unused:UNUSED_PAD src0_sel:WORD_0
	v_exp_f16_sdwa v189, v88 dst_sel:WORD_0 dst_unused:UNUSED_PAD src0_sel:WORD_0
	v_exp_f16_sdwa v190, v89 dst_sel:WORD_0 dst_unused:UNUSED_PAD src0_sel:WORD_0
	v_exp_f16_sdwa v187, v86 dst_sel:WORD_1 dst_unused:UNUSED_PRESERVE src0_sel:WORD_1
	v_exp_f16_sdwa v188, v87 dst_sel:WORD_1 dst_unused:UNUSED_PRESERVE src0_sel:WORD_1
	v_exp_f16_sdwa v189, v88 dst_sel:WORD_1 dst_unused:UNUSED_PRESERVE src0_sel:WORD_1
	v_exp_f16_sdwa v190, v89 dst_sel:WORD_1 dst_unused:UNUSED_PRESERVE src0_sel:WORD_1
	v_pk_add_f16 v107, v107, v155 neg_lo:[0,1] neg_hi:[0,1]
	v_pk_add_f16 v89, v187, 0
	v_pk_fma_f16 v49, v49, v190, 0
	v_pk_add_f16 v86, v190, 0
	v_pk_add_f16 v87, v189, 0
	v_pk_add_f16 v88, v188, 0
	v_pk_fma_f16 v48, v48, v189, 0
	v_pk_fma_f16 v47, v47, v188, 0
	v_pk_fma_f16 v46, v46, v187, 0
	v_pk_add_f16 v108, v108, v156 neg_lo:[0,1] neg_hi:[0,1]
	v_pk_add_f16 v109, v109, v157 neg_lo:[0,1] neg_hi:[0,1]
	v_exp_f16_sdwa v187, v106 dst_sel:WORD_0 dst_unused:UNUSED_PAD src0_sel:WORD_0
	v_exp_f16_sdwa v188, v107 dst_sel:WORD_0 dst_unused:UNUSED_PAD src0_sel:WORD_0
	v_exp_f16_sdwa v189, v108 dst_sel:WORD_0 dst_unused:UNUSED_PAD src0_sel:WORD_0
	v_exp_f16_sdwa v190, v109 dst_sel:WORD_0 dst_unused:UNUSED_PAD src0_sel:WORD_0
	v_exp_f16_sdwa v187, v106 dst_sel:WORD_1 dst_unused:UNUSED_PRESERVE src0_sel:WORD_1
	v_exp_f16_sdwa v188, v107 dst_sel:WORD_1 dst_unused:UNUSED_PRESERVE src0_sel:WORD_1
	v_exp_f16_sdwa v189, v108 dst_sel:WORD_1 dst_unused:UNUSED_PRESERVE src0_sel:WORD_1
	v_exp_f16_sdwa v190, v109 dst_sel:WORD_1 dst_unused:UNUSED_PRESERVE src0_sel:WORD_1
	v_pk_add_f16 v89, v89, v187
	v_pk_fma_f16 v49, v65, v190, v49
	v_pk_add_f16 v65, v81, v157 neg_lo:[0,1] neg_hi:[0,1]
	v_pk_add_f16 v88, v88, v188
	v_pk_add_f16 v87, v87, v189
	v_pk_add_f16 v86, v86, v190
	v_pk_fma_f16 v46, v62, v187, v46
	v_pk_fma_f16 v47, v63, v188, v47
	v_pk_fma_f16 v48, v64, v189, v48
	v_pk_add_f16 v62, v78, v154 neg_lo:[0,1] neg_hi:[0,1]
	v_pk_add_f16 v63, v79, v155 neg_lo:[0,1] neg_hi:[0,1]
	v_pk_add_f16 v64, v80, v156 neg_lo:[0,1] neg_hi:[0,1]
	v_exp_f16_sdwa v78, v62 dst_sel:WORD_0 dst_unused:UNUSED_PAD src0_sel:WORD_0
	v_exp_f16_sdwa v79, v63 dst_sel:WORD_0 dst_unused:UNUSED_PAD src0_sel:WORD_0
	v_exp_f16_sdwa v80, v64 dst_sel:WORD_0 dst_unused:UNUSED_PAD src0_sel:WORD_0
	v_exp_f16_sdwa v81, v65 dst_sel:WORD_0 dst_unused:UNUSED_PAD src0_sel:WORD_0
	v_exp_f16_sdwa v78, v62 dst_sel:WORD_1 dst_unused:UNUSED_PRESERVE src0_sel:WORD_1
	v_exp_f16_sdwa v79, v63 dst_sel:WORD_1 dst_unused:UNUSED_PRESERVE src0_sel:WORD_1
	v_exp_f16_sdwa v80, v64 dst_sel:WORD_1 dst_unused:UNUSED_PRESERVE src0_sel:WORD_1
	v_exp_f16_sdwa v81, v65 dst_sel:WORD_1 dst_unused:UNUSED_PRESERVE src0_sel:WORD_1
	v_pk_add_f16 v65, v89, v78
	v_pk_add_f16 v62, v86, v81
	v_pk_add_f16 v63, v87, v80
	v_pk_add_f16 v64, v88, v79
	v_pk_fma_f16 v49, v85, v81, v49
	v_pk_fma_f16 v48, v84, v80, v48
	v_pk_fma_f16 v47, v83, v79, v47
	v_pk_fma_f16 v46, v82, v78, v46
	v_pk_add_f16 v78, v125, v154 neg_lo:[0,1] neg_hi:[0,1]
	v_pk_add_f16 v79, v124, v155 neg_lo:[0,1] neg_hi:[0,1]
	v_pk_add_f16 v80, v123, v156 neg_lo:[0,1] neg_hi:[0,1]
	v_pk_add_f16 v81, v122, v157 neg_lo:[0,1] neg_hi:[0,1]
	v_exp_f16_sdwa v82, v78 dst_sel:WORD_0 dst_unused:UNUSED_PAD src0_sel:WORD_0
	v_exp_f16_sdwa v83, v79 dst_sel:WORD_0 dst_unused:UNUSED_PAD src0_sel:WORD_0
	v_exp_f16_sdwa v84, v80 dst_sel:WORD_0 dst_unused:UNUSED_PAD src0_sel:WORD_0
	v_exp_f16_sdwa v85, v81 dst_sel:WORD_0 dst_unused:UNUSED_PAD src0_sel:WORD_0
	v_exp_f16_sdwa v82, v78 dst_sel:WORD_1 dst_unused:UNUSED_PRESERVE src0_sel:WORD_1
	v_exp_f16_sdwa v83, v79 dst_sel:WORD_1 dst_unused:UNUSED_PRESERVE src0_sel:WORD_1
	v_exp_f16_sdwa v84, v80 dst_sel:WORD_1 dst_unused:UNUSED_PRESERVE src0_sel:WORD_1
	v_exp_f16_sdwa v85, v81 dst_sel:WORD_1 dst_unused:UNUSED_PRESERVE src0_sel:WORD_1
	v_pk_add_f16 v78, v129, v154 neg_lo:[0,1] neg_hi:[0,1]
	v_pk_add_f16 v65, v65, v82
	v_pk_add_f16 v64, v64, v83
	v_pk_add_f16 v63, v63, v84
	v_pk_add_f16 v62, v62, v85
	v_pk_fma_f16 v46, v22, v82, v46
	v_pk_fma_f16 v47, v23, v83, v47
	v_pk_fma_f16 v48, v24, v84, v48
	v_pk_fma_f16 v49, v25, v85, v49
	v_pk_add_f16 v79, v128, v155 neg_lo:[0,1] neg_hi:[0,1]
	v_pk_add_f16 v80, v127, v156 neg_lo:[0,1] neg_hi:[0,1]
	v_pk_add_f16 v81, v126, v157 neg_lo:[0,1] neg_hi:[0,1]
	v_exp_f16_sdwa v82, v78 dst_sel:WORD_0 dst_unused:UNUSED_PAD src0_sel:WORD_0
	v_exp_f16_sdwa v83, v79 dst_sel:WORD_0 dst_unused:UNUSED_PAD src0_sel:WORD_0
	v_exp_f16_sdwa v84, v80 dst_sel:WORD_0 dst_unused:UNUSED_PAD src0_sel:WORD_0
	v_exp_f16_sdwa v85, v81 dst_sel:WORD_0 dst_unused:UNUSED_PAD src0_sel:WORD_0
	v_exp_f16_sdwa v82, v78 dst_sel:WORD_1 dst_unused:UNUSED_PRESERVE src0_sel:WORD_1
	v_exp_f16_sdwa v83, v79 dst_sel:WORD_1 dst_unused:UNUSED_PRESERVE src0_sel:WORD_1
	v_exp_f16_sdwa v84, v80 dst_sel:WORD_1 dst_unused:UNUSED_PRESERVE src0_sel:WORD_1
	v_exp_f16_sdwa v85, v81 dst_sel:WORD_1 dst_unused:UNUSED_PRESERVE src0_sel:WORD_1
	v_pk_add_f16 v78, v102, v154 neg_lo:[0,1] neg_hi:[0,1]
	v_pk_add_f16 v65, v65, v82
	v_pk_add_f16 v62, v62, v85
	v_pk_add_f16 v63, v63, v84
	v_pk_add_f16 v64, v64, v83
	v_pk_fma_f16 v49, v37, v85, v49
	v_pk_fma_f16 v48, v36, v84, v48
	v_pk_fma_f16 v47, v35, v83, v47
	v_pk_fma_f16 v46, v34, v82, v46
	v_pk_add_f16 v79, v103, v155 neg_lo:[0,1] neg_hi:[0,1]
	v_pk_add_f16 v80, v104, v156 neg_lo:[0,1] neg_hi:[0,1]
	v_pk_add_f16 v81, v105, v157 neg_lo:[0,1] neg_hi:[0,1]
	v_exp_f16_sdwa v82, v78 dst_sel:WORD_0 dst_unused:UNUSED_PAD src0_sel:WORD_0
	v_exp_f16_sdwa v83, v79 dst_sel:WORD_0 dst_unused:UNUSED_PAD src0_sel:WORD_0
	v_exp_f16_sdwa v84, v80 dst_sel:WORD_0 dst_unused:UNUSED_PAD src0_sel:WORD_0
	v_exp_f16_sdwa v85, v81 dst_sel:WORD_0 dst_unused:UNUSED_PAD src0_sel:WORD_0
	v_exp_f16_sdwa v82, v78 dst_sel:WORD_1 dst_unused:UNUSED_PRESERVE src0_sel:WORD_1
	v_exp_f16_sdwa v83, v79 dst_sel:WORD_1 dst_unused:UNUSED_PRESERVE src0_sel:WORD_1
	v_exp_f16_sdwa v84, v80 dst_sel:WORD_1 dst_unused:UNUSED_PRESERVE src0_sel:WORD_1
	v_exp_f16_sdwa v85, v81 dst_sel:WORD_1 dst_unused:UNUSED_PRESERVE src0_sel:WORD_1
	v_pk_add_f16 v78, v141, v154 neg_lo:[0,1] neg_hi:[0,1]
	v_pk_add_f16 v65, v65, v82
	v_pk_add_f16 v64, v64, v83
	v_pk_add_f16 v63, v63, v84
	v_pk_add_f16 v62, v62, v85
	v_pk_fma_f16 v46, v42, v82, v46
	v_pk_fma_f16 v47, v43, v83, v47
	v_pk_fma_f16 v48, v44, v84, v48
	v_pk_fma_f16 v49, v45, v85, v49
	v_pk_add_f16 v79, v140, v155 neg_lo:[0,1] neg_hi:[0,1]
	v_pk_add_f16 v80, v139, v156 neg_lo:[0,1] neg_hi:[0,1]
	v_pk_add_f16 v81, v138, v157 neg_lo:[0,1] neg_hi:[0,1]
	v_exp_f16_sdwa v82, v78 dst_sel:WORD_0 dst_unused:UNUSED_PAD src0_sel:WORD_0
	v_exp_f16_sdwa v83, v79 dst_sel:WORD_0 dst_unused:UNUSED_PAD src0_sel:WORD_0
	v_exp_f16_sdwa v84, v80 dst_sel:WORD_0 dst_unused:UNUSED_PAD src0_sel:WORD_0
	v_exp_f16_sdwa v85, v81 dst_sel:WORD_0 dst_unused:UNUSED_PAD src0_sel:WORD_0
	v_exp_f16_sdwa v82, v78 dst_sel:WORD_1 dst_unused:UNUSED_PRESERVE src0_sel:WORD_1
	v_exp_f16_sdwa v83, v79 dst_sel:WORD_1 dst_unused:UNUSED_PRESERVE src0_sel:WORD_1
	v_exp_f16_sdwa v84, v80 dst_sel:WORD_1 dst_unused:UNUSED_PRESERVE src0_sel:WORD_1
	v_exp_f16_sdwa v85, v81 dst_sel:WORD_1 dst_unused:UNUSED_PRESERVE src0_sel:WORD_1
	v_pk_add_f16 v78, v186, v154 neg_lo:[0,1] neg_hi:[0,1]
	v_pk_add_f16 v65, v65, v82
	v_pk_add_f16 v62, v62, v85
	v_pk_add_f16 v63, v63, v84
	v_pk_add_f16 v64, v64, v83
	v_pk_fma_f16 v49, v9, v85, v49
	v_pk_fma_f16 v48, v8, v84, v48
	v_pk_fma_f16 v47, v7, v83, v47
	v_pk_fma_f16 v46, v6, v82, v46
	v_pk_add_f16 v79, v185, v155 neg_lo:[0,1] neg_hi:[0,1]
	v_pk_add_f16 v80, v184, v156 neg_lo:[0,1] neg_hi:[0,1]
	v_pk_add_f16 v81, v183, v157 neg_lo:[0,1] neg_hi:[0,1]
	v_exp_f16_sdwa v82, v78 dst_sel:WORD_0 dst_unused:UNUSED_PAD src0_sel:WORD_0
	v_exp_f16_sdwa v83, v79 dst_sel:WORD_0 dst_unused:UNUSED_PAD src0_sel:WORD_0
	v_exp_f16_sdwa v84, v80 dst_sel:WORD_0 dst_unused:UNUSED_PAD src0_sel:WORD_0
	v_exp_f16_sdwa v85, v81 dst_sel:WORD_0 dst_unused:UNUSED_PAD src0_sel:WORD_0
	v_exp_f16_sdwa v82, v78 dst_sel:WORD_1 dst_unused:UNUSED_PRESERVE src0_sel:WORD_1
	v_exp_f16_sdwa v83, v79 dst_sel:WORD_1 dst_unused:UNUSED_PRESERVE src0_sel:WORD_1
	v_exp_f16_sdwa v84, v80 dst_sel:WORD_1 dst_unused:UNUSED_PRESERVE src0_sel:WORD_1
	v_exp_f16_sdwa v85, v81 dst_sel:WORD_1 dst_unused:UNUSED_PRESERVE src0_sel:WORD_1
	v_pk_add_f16 v78, v118, v154 neg_lo:[0,1] neg_hi:[0,1]
	v_pk_add_f16 v65, v65, v82
	v_pk_add_f16 v64, v64, v83
	v_pk_add_f16 v63, v63, v84
	v_pk_add_f16 v62, v62, v85
	v_pk_fma_f16 v46, v10, v82, v46
	v_pk_fma_f16 v47, v11, v83, v47
	v_pk_fma_f16 v48, v12, v84, v48
	v_pk_fma_f16 v49, v13, v85, v49
	v_pk_add_f16 v79, v119, v155 neg_lo:[0,1] neg_hi:[0,1]
	v_pk_add_f16 v80, v120, v156 neg_lo:[0,1] neg_hi:[0,1]
	v_pk_add_f16 v81, v121, v157 neg_lo:[0,1] neg_hi:[0,1]
	v_exp_f16_sdwa v82, v78 dst_sel:WORD_0 dst_unused:UNUSED_PAD src0_sel:WORD_0
	v_exp_f16_sdwa v83, v79 dst_sel:WORD_0 dst_unused:UNUSED_PAD src0_sel:WORD_0
	v_exp_f16_sdwa v84, v80 dst_sel:WORD_0 dst_unused:UNUSED_PAD src0_sel:WORD_0
	v_exp_f16_sdwa v85, v81 dst_sel:WORD_0 dst_unused:UNUSED_PAD src0_sel:WORD_0
	v_exp_f16_sdwa v82, v78 dst_sel:WORD_1 dst_unused:UNUSED_PRESERVE src0_sel:WORD_1
	v_exp_f16_sdwa v83, v79 dst_sel:WORD_1 dst_unused:UNUSED_PRESERVE src0_sel:WORD_1
	v_exp_f16_sdwa v84, v80 dst_sel:WORD_1 dst_unused:UNUSED_PRESERVE src0_sel:WORD_1
	v_exp_f16_sdwa v85, v81 dst_sel:WORD_1 dst_unused:UNUSED_PRESERVE src0_sel:WORD_1
	v_pk_add_f16 v65, v65, v82
	v_pk_add_f16 v64, v64, v83
	v_rcp_f16_e32 v78, v65
	v_rcp_f16_sdwa v65, v65 dst_sel:DWORD dst_unused:UNUSED_PAD src0_sel:WORD_1
	v_pk_add_f16 v63, v63, v84
	v_rcp_f16_e32 v79, v64
	v_rcp_f16_sdwa v64, v64 dst_sel:DWORD dst_unused:UNUSED_PAD src0_sel:WORD_1
	v_pk_add_f16 v62, v62, v85
	v_rcp_f16_e32 v80, v63
	v_rcp_f16_sdwa v81, v63 dst_sel:DWORD dst_unused:UNUSED_PAD src0_sel:WORD_1
	v_pk_fma_f16 v47, v15, v83, v47
	v_pk_fma_f16 v46, v14, v82, v46
	v_rcp_f16_e32 v82, v62
	v_rcp_f16_sdwa v83, v62 dst_sel:DWORD dst_unused:UNUSED_PAD src0_sel:WORD_1
	v_pack_b32_f16 v62, v78, v65
	v_pk_mul_f16 v62, v46, v62
	v_pack_b32_f16 v46, v79, v64
	v_pk_fma_f16 v48, v16, v84, v48
	v_pk_mul_f16 v63, v47, v46
	v_pack_b32_f16 v46, v80, v81
	v_pk_fma_f16 v49, v17, v85, v49
	v_pk_mul_f16 v64, v48, v46
	v_pack_b32_f16 v46, v82, v83
	v_pk_mul_f16 v65, v49, v46
	s_waitcnt vmcnt(6)
	v_pk_mul_f16 v46, v182, v150 op_sel_hi:[0,1]
	v_pk_mul_f16 v47, v182, v151 op_sel_hi:[0,1]
	v_pk_mul_f16 v48, v182, v152 op_sel_hi:[0,1]
	v_pk_mul_f16 v49, v182, v153 op_sel_hi:[0,1]
	v_pk_mul_f16 v78, v180, v150 op_sel_hi:[0,1]
	v_pk_mul_f16 v82, v181, v150 op_sel_hi:[0,1]
	v_pk_fma_f16 v50, v50, v150, v46
	v_pk_fma_f16 v66, v66, v150, v46
	v_pk_fma_f16 v46, v94, v150, v46
	v_pk_mul_f16 v79, v180, v151 op_sel_hi:[0,1]
	v_pk_maximum3_f16 v118, v50, v66, v46
	v_pk_mul_f16 v80, v180, v152 op_sel_hi:[0,1]
	v_pk_mul_f16 v81, v180, v153 op_sel_hi:[0,1]
	v_pk_mul_f16 v83, v181, v151 op_sel_hi:[0,1]
	v_pk_mul_f16 v84, v181, v152 op_sel_hi:[0,1]
	v_pk_mul_f16 v85, v181, v153 op_sel_hi:[0,1]
	v_pk_fma_f16 v53, v53, v153, v49
	v_pk_fma_f16 v52, v52, v152, v48
	v_pk_fma_f16 v51, v51, v151, v47
	v_pk_fma_f16 v69, v69, v153, v49
	v_pk_fma_f16 v68, v68, v152, v48
	v_pk_fma_f16 v67, v67, v151, v47
	v_pk_fma_f16 v49, v97, v153, v49
	v_pk_fma_f16 v48, v96, v152, v48
	v_pk_fma_f16 v47, v95, v151, v47
	v_pk_fma_f16 v89, v18, v150, v78
	v_pk_fma_f16 v97, v30, v150, v78
	v_pk_fma_f16 v78, v54, v150, v78
	v_pk_fma_f16 v105, v74, v150, v82
	v_pk_fma_f16 v109, v98, v150, v82
	v_pk_fma_f16 v82, v114, v150, v82
	v_pk_maximum3_f16 v119, v51, v67, v47
	v_pk_maximum3_f16 v120, v52, v68, v48
	v_pk_maximum3_f16 v121, v53, v69, v49
	v_pk_maximum3_f16 v122, v89, v97, v78
	v_pk_fma_f16 v86, v21, v153, v81
	v_pk_maximum3_f16 v126, v105, v109, v82
	v_pk_fma_f16 v87, v20, v152, v80
	v_pk_maximum3_f16 v118, v118, v122, v126
	v_pk_fma_f16 v88, v19, v151, v79
	v_pk_fma_f16 v94, v33, v153, v81
	v_pk_fma_f16 v95, v32, v152, v80
	v_pk_fma_f16 v96, v31, v151, v79
	v_pk_fma_f16 v81, v57, v153, v81
	v_pk_fma_f16 v80, v56, v152, v80
	v_pk_fma_f16 v79, v55, v151, v79
	v_pk_fma_f16 v102, v77, v153, v85
	v_pk_fma_f16 v103, v76, v152, v84
	v_pk_fma_f16 v104, v75, v151, v83
	v_pk_fma_f16 v106, v101, v153, v85
	v_pk_fma_f16 v107, v100, v152, v84
	v_pk_fma_f16 v108, v99, v151, v83
	v_pk_fma_f16 v85, v117, v153, v85
	v_pk_fma_f16 v84, v116, v152, v84
	v_pk_fma_f16 v83, v115, v151, v83
	v_pk_maximum3_f16 v123, v88, v96, v79
	v_pk_maximum3_f16 v124, v87, v95, v80
	v_pk_maximum3_f16 v125, v86, v94, v81
	v_pk_maximum3_f16 v128, v103, v107, v84
	v_pk_maximum3_f16 v129, v102, v106, v85
	v_pk_maximum3_f16 v127, v104, v108, v83
	v_pk_maximum3_f16 v119, v119, v123, v127
	v_pk_maximum3_f16 v120, v120, v124, v128
	v_pk_maximum3_f16 v121, v121, v125, v129
	v_pk_add_f16 v50, v50, v118 neg_lo:[0,1] neg_hi:[0,1]
	v_pk_add_f16 v51, v51, v119 neg_lo:[0,1] neg_hi:[0,1]
	v_pk_add_f16 v52, v52, v120 neg_lo:[0,1] neg_hi:[0,1]
	v_pk_add_f16 v53, v53, v121 neg_lo:[0,1] neg_hi:[0,1]
	v_pk_add_f16 v66, v66, v118 neg_lo:[0,1] neg_hi:[0,1]
	v_exp_f16_sdwa v122, v50 dst_sel:WORD_0 dst_unused:UNUSED_PAD src0_sel:WORD_0
	v_exp_f16_sdwa v123, v51 dst_sel:WORD_0 dst_unused:UNUSED_PAD src0_sel:WORD_0
	v_exp_f16_sdwa v124, v52 dst_sel:WORD_0 dst_unused:UNUSED_PAD src0_sel:WORD_0
	v_exp_f16_sdwa v125, v53 dst_sel:WORD_0 dst_unused:UNUSED_PAD src0_sel:WORD_0
	v_exp_f16_sdwa v122, v50 dst_sel:WORD_1 dst_unused:UNUSED_PRESERVE src0_sel:WORD_1
	v_exp_f16_sdwa v123, v51 dst_sel:WORD_1 dst_unused:UNUSED_PRESERVE src0_sel:WORD_1
	v_exp_f16_sdwa v124, v52 dst_sel:WORD_1 dst_unused:UNUSED_PRESERVE src0_sel:WORD_1
	v_exp_f16_sdwa v125, v53 dst_sel:WORD_1 dst_unused:UNUSED_PRESERVE src0_sel:WORD_1
	v_pk_add_f16 v67, v67, v119 neg_lo:[0,1] neg_hi:[0,1]
	v_pk_add_f16 v50, v125, 0
	v_pk_fma_f16 v22, v22, v122, 0
	v_pk_add_f16 v51, v124, 0
	v_pk_add_f16 v52, v123, 0
	v_pk_add_f16 v53, v122, 0
	v_pk_fma_f16 v23, v23, v123, 0
	v_pk_fma_f16 v24, v24, v124, 0
	v_pk_fma_f16 v25, v25, v125, 0
	v_pk_add_f16 v68, v68, v120 neg_lo:[0,1] neg_hi:[0,1]
	v_pk_add_f16 v69, v69, v121 neg_lo:[0,1] neg_hi:[0,1]
	v_exp_f16_sdwa v122, v66 dst_sel:WORD_0 dst_unused:UNUSED_PAD src0_sel:WORD_0
	v_exp_f16_sdwa v123, v67 dst_sel:WORD_0 dst_unused:UNUSED_PAD src0_sel:WORD_0
	v_exp_f16_sdwa v124, v68 dst_sel:WORD_0 dst_unused:UNUSED_PAD src0_sel:WORD_0
	v_exp_f16_sdwa v125, v69 dst_sel:WORD_0 dst_unused:UNUSED_PAD src0_sel:WORD_0
	v_exp_f16_sdwa v122, v66 dst_sel:WORD_1 dst_unused:UNUSED_PRESERVE src0_sel:WORD_1
	v_exp_f16_sdwa v123, v67 dst_sel:WORD_1 dst_unused:UNUSED_PRESERVE src0_sel:WORD_1
	v_exp_f16_sdwa v124, v68 dst_sel:WORD_1 dst_unused:UNUSED_PRESERVE src0_sel:WORD_1
	v_exp_f16_sdwa v125, v69 dst_sel:WORD_1 dst_unused:UNUSED_PRESERVE src0_sel:WORD_1
	s_nop 0
	v_pk_add_f16 v50, v50, v125
	v_pk_fma_f16 v22, v34, v122, v22
	v_pk_add_f16 v34, v46, v118 neg_lo:[0,1] neg_hi:[0,1]
	v_pk_add_f16 v53, v53, v122
	v_pk_add_f16 v52, v52, v123
	v_pk_add_f16 v51, v51, v124
	v_pk_fma_f16 v25, v37, v125, v25
	v_pk_fma_f16 v24, v36, v124, v24
	v_pk_fma_f16 v23, v35, v123, v23
	v_pk_add_f16 v35, v47, v119 neg_lo:[0,1] neg_hi:[0,1]
	v_pk_add_f16 v36, v48, v120 neg_lo:[0,1] neg_hi:[0,1]
	v_pk_add_f16 v37, v49, v121 neg_lo:[0,1] neg_hi:[0,1]
	v_exp_f16_sdwa v46, v34 dst_sel:WORD_0 dst_unused:UNUSED_PAD src0_sel:WORD_0
	v_exp_f16_sdwa v47, v35 dst_sel:WORD_0 dst_unused:UNUSED_PAD src0_sel:WORD_0
	v_exp_f16_sdwa v48, v36 dst_sel:WORD_0 dst_unused:UNUSED_PAD src0_sel:WORD_0
	v_exp_f16_sdwa v49, v37 dst_sel:WORD_0 dst_unused:UNUSED_PAD src0_sel:WORD_0
	v_exp_f16_sdwa v46, v34 dst_sel:WORD_1 dst_unused:UNUSED_PRESERVE src0_sel:WORD_1
	v_exp_f16_sdwa v47, v35 dst_sel:WORD_1 dst_unused:UNUSED_PRESERVE src0_sel:WORD_1
	v_exp_f16_sdwa v48, v36 dst_sel:WORD_1 dst_unused:UNUSED_PRESERVE src0_sel:WORD_1
	v_exp_f16_sdwa v49, v37 dst_sel:WORD_1 dst_unused:UNUSED_PRESERVE src0_sel:WORD_1
	s_nop 0
	v_pk_add_f16 v34, v50, v49
	v_pk_add_f16 v35, v51, v48
	v_pk_add_f16 v36, v52, v47
	v_pk_add_f16 v37, v53, v46
	v_pk_fma_f16 v22, v42, v46, v22
	v_pk_fma_f16 v23, v43, v47, v23
	v_pk_fma_f16 v24, v44, v48, v24
	v_pk_fma_f16 v25, v45, v49, v25
	v_pk_add_f16 v42, v89, v118 neg_lo:[0,1] neg_hi:[0,1]
	v_pk_add_f16 v43, v88, v119 neg_lo:[0,1] neg_hi:[0,1]
	v_pk_add_f16 v44, v87, v120 neg_lo:[0,1] neg_hi:[0,1]
	v_pk_add_f16 v45, v86, v121 neg_lo:[0,1] neg_hi:[0,1]
	v_exp_f16_sdwa v46, v42 dst_sel:WORD_0 dst_unused:UNUSED_PAD src0_sel:WORD_0
	v_exp_f16_sdwa v47, v43 dst_sel:WORD_0 dst_unused:UNUSED_PAD src0_sel:WORD_0
	v_exp_f16_sdwa v48, v44 dst_sel:WORD_0 dst_unused:UNUSED_PAD src0_sel:WORD_0
	v_exp_f16_sdwa v49, v45 dst_sel:WORD_0 dst_unused:UNUSED_PAD src0_sel:WORD_0
	v_exp_f16_sdwa v46, v42 dst_sel:WORD_1 dst_unused:UNUSED_PRESERVE src0_sel:WORD_1
	v_exp_f16_sdwa v47, v43 dst_sel:WORD_1 dst_unused:UNUSED_PRESERVE src0_sel:WORD_1
	v_exp_f16_sdwa v48, v44 dst_sel:WORD_1 dst_unused:UNUSED_PRESERVE src0_sel:WORD_1
	v_exp_f16_sdwa v49, v45 dst_sel:WORD_1 dst_unused:UNUSED_PRESERVE src0_sel:WORD_1
	v_pk_add_f16 v42, v97, v118 neg_lo:[0,1] neg_hi:[0,1]
	v_pk_add_f16 v34, v34, v49
	v_pk_add_f16 v37, v37, v46
	v_pk_add_f16 v36, v36, v47
	v_pk_add_f16 v35, v35, v48
	v_pk_fma_f16 v25, v9, v49, v25
	v_pk_fma_f16 v24, v8, v48, v24
	v_pk_fma_f16 v23, v7, v47, v23
	v_pk_fma_f16 v22, v6, v46, v22
	v_pk_add_f16 v43, v96, v119 neg_lo:[0,1] neg_hi:[0,1]
	v_pk_add_f16 v44, v95, v120 neg_lo:[0,1] neg_hi:[0,1]
	v_pk_add_f16 v45, v94, v121 neg_lo:[0,1] neg_hi:[0,1]
	v_exp_f16_sdwa v46, v42 dst_sel:WORD_0 dst_unused:UNUSED_PAD src0_sel:WORD_0
	v_exp_f16_sdwa v47, v43 dst_sel:WORD_0 dst_unused:UNUSED_PAD src0_sel:WORD_0
	v_exp_f16_sdwa v48, v44 dst_sel:WORD_0 dst_unused:UNUSED_PAD src0_sel:WORD_0
	v_exp_f16_sdwa v49, v45 dst_sel:WORD_0 dst_unused:UNUSED_PAD src0_sel:WORD_0
	v_exp_f16_sdwa v46, v42 dst_sel:WORD_1 dst_unused:UNUSED_PRESERVE src0_sel:WORD_1
	v_exp_f16_sdwa v47, v43 dst_sel:WORD_1 dst_unused:UNUSED_PRESERVE src0_sel:WORD_1
	v_exp_f16_sdwa v48, v44 dst_sel:WORD_1 dst_unused:UNUSED_PRESERVE src0_sel:WORD_1
	v_exp_f16_sdwa v49, v45 dst_sel:WORD_1 dst_unused:UNUSED_PRESERVE src0_sel:WORD_1
	v_pk_add_f16 v42, v78, v118 neg_lo:[0,1] neg_hi:[0,1]
	v_pk_add_f16 v34, v34, v49
	v_pk_add_f16 v35, v35, v48
	v_pk_add_f16 v36, v36, v47
	v_pk_add_f16 v37, v37, v46
	v_pk_fma_f16 v22, v10, v46, v22
	v_pk_fma_f16 v23, v11, v47, v23
	v_pk_fma_f16 v24, v12, v48, v24
	v_pk_fma_f16 v25, v13, v49, v25
	v_pk_add_f16 v43, v79, v119 neg_lo:[0,1] neg_hi:[0,1]
	v_pk_add_f16 v44, v80, v120 neg_lo:[0,1] neg_hi:[0,1]
	v_pk_add_f16 v45, v81, v121 neg_lo:[0,1] neg_hi:[0,1]
	v_exp_f16_sdwa v46, v42 dst_sel:WORD_0 dst_unused:UNUSED_PAD src0_sel:WORD_0
	v_exp_f16_sdwa v47, v43 dst_sel:WORD_0 dst_unused:UNUSED_PAD src0_sel:WORD_0
	v_exp_f16_sdwa v48, v44 dst_sel:WORD_0 dst_unused:UNUSED_PAD src0_sel:WORD_0
	v_exp_f16_sdwa v49, v45 dst_sel:WORD_0 dst_unused:UNUSED_PAD src0_sel:WORD_0
	v_exp_f16_sdwa v46, v42 dst_sel:WORD_1 dst_unused:UNUSED_PRESERVE src0_sel:WORD_1
	v_exp_f16_sdwa v47, v43 dst_sel:WORD_1 dst_unused:UNUSED_PRESERVE src0_sel:WORD_1
	v_exp_f16_sdwa v48, v44 dst_sel:WORD_1 dst_unused:UNUSED_PRESERVE src0_sel:WORD_1
	v_exp_f16_sdwa v49, v45 dst_sel:WORD_1 dst_unused:UNUSED_PRESERVE src0_sel:WORD_1
	v_pk_add_f16 v42, v105, v118 neg_lo:[0,1] neg_hi:[0,1]
	v_pk_add_f16 v34, v34, v49
	v_pk_add_f16 v37, v37, v46
	v_pk_add_f16 v36, v36, v47
	v_pk_add_f16 v35, v35, v48
	v_pk_fma_f16 v25, v17, v49, v25
	v_pk_fma_f16 v24, v16, v48, v24
	v_pk_fma_f16 v23, v15, v47, v23
	v_pk_fma_f16 v22, v14, v46, v22
	v_pk_add_f16 v43, v104, v119 neg_lo:[0,1] neg_hi:[0,1]
	v_pk_add_f16 v44, v103, v120 neg_lo:[0,1] neg_hi:[0,1]
	v_pk_add_f16 v45, v102, v121 neg_lo:[0,1] neg_hi:[0,1]
	v_exp_f16_sdwa v46, v42 dst_sel:WORD_0 dst_unused:UNUSED_PAD src0_sel:WORD_0
	v_exp_f16_sdwa v47, v43 dst_sel:WORD_0 dst_unused:UNUSED_PAD src0_sel:WORD_0
	v_exp_f16_sdwa v48, v44 dst_sel:WORD_0 dst_unused:UNUSED_PAD src0_sel:WORD_0
	v_exp_f16_sdwa v49, v45 dst_sel:WORD_0 dst_unused:UNUSED_PAD src0_sel:WORD_0
	v_exp_f16_sdwa v46, v42 dst_sel:WORD_1 dst_unused:UNUSED_PRESERVE src0_sel:WORD_1
	v_exp_f16_sdwa v47, v43 dst_sel:WORD_1 dst_unused:UNUSED_PRESERVE src0_sel:WORD_1
	v_exp_f16_sdwa v48, v44 dst_sel:WORD_1 dst_unused:UNUSED_PRESERVE src0_sel:WORD_1
	v_exp_f16_sdwa v49, v45 dst_sel:WORD_1 dst_unused:UNUSED_PRESERVE src0_sel:WORD_1
	v_pk_add_f16 v42, v109, v118 neg_lo:[0,1] neg_hi:[0,1]
	v_pk_add_f16 v34, v34, v49
	v_pk_add_f16 v35, v35, v48
	v_pk_add_f16 v36, v36, v47
	v_pk_add_f16 v37, v37, v46
	v_pk_fma_f16 v22, v26, v46, v22
	v_pk_fma_f16 v23, v27, v47, v23
	v_pk_fma_f16 v24, v28, v48, v24
	v_pk_fma_f16 v25, v29, v49, v25
	v_pk_add_f16 v43, v108, v119 neg_lo:[0,1] neg_hi:[0,1]
	v_pk_add_f16 v44, v107, v120 neg_lo:[0,1] neg_hi:[0,1]
	v_pk_add_f16 v45, v106, v121 neg_lo:[0,1] neg_hi:[0,1]
	v_exp_f16_sdwa v46, v42 dst_sel:WORD_0 dst_unused:UNUSED_PAD src0_sel:WORD_0
	v_exp_f16_sdwa v47, v43 dst_sel:WORD_0 dst_unused:UNUSED_PAD src0_sel:WORD_0
	v_exp_f16_sdwa v48, v44 dst_sel:WORD_0 dst_unused:UNUSED_PAD src0_sel:WORD_0
	v_exp_f16_sdwa v49, v45 dst_sel:WORD_0 dst_unused:UNUSED_PAD src0_sel:WORD_0
	v_exp_f16_sdwa v46, v42 dst_sel:WORD_1 dst_unused:UNUSED_PRESERVE src0_sel:WORD_1
	v_exp_f16_sdwa v47, v43 dst_sel:WORD_1 dst_unused:UNUSED_PRESERVE src0_sel:WORD_1
	v_exp_f16_sdwa v48, v44 dst_sel:WORD_1 dst_unused:UNUSED_PRESERVE src0_sel:WORD_1
	v_exp_f16_sdwa v49, v45 dst_sel:WORD_1 dst_unused:UNUSED_PRESERVE src0_sel:WORD_1
	v_pk_add_f16 v42, v82, v118 neg_lo:[0,1] neg_hi:[0,1]
	v_pk_add_f16 v34, v34, v49
	v_pk_add_f16 v37, v37, v46
	v_pk_add_f16 v36, v36, v47
	v_pk_add_f16 v35, v35, v48
	v_pk_fma_f16 v25, v41, v49, v25
	v_pk_fma_f16 v24, v40, v48, v24
	v_pk_fma_f16 v23, v39, v47, v23
	v_pk_fma_f16 v22, v38, v46, v22
	v_pk_add_f16 v43, v83, v119 neg_lo:[0,1] neg_hi:[0,1]
	v_pk_add_f16 v44, v84, v120 neg_lo:[0,1] neg_hi:[0,1]
	v_pk_add_f16 v45, v85, v121 neg_lo:[0,1] neg_hi:[0,1]
	v_exp_f16_sdwa v46, v42 dst_sel:WORD_0 dst_unused:UNUSED_PAD src0_sel:WORD_0
	v_exp_f16_sdwa v47, v43 dst_sel:WORD_0 dst_unused:UNUSED_PAD src0_sel:WORD_0
	v_exp_f16_sdwa v48, v44 dst_sel:WORD_0 dst_unused:UNUSED_PAD src0_sel:WORD_0
	v_exp_f16_sdwa v49, v45 dst_sel:WORD_0 dst_unused:UNUSED_PAD src0_sel:WORD_0
	v_exp_f16_sdwa v46, v42 dst_sel:WORD_1 dst_unused:UNUSED_PRESERVE src0_sel:WORD_1
	v_exp_f16_sdwa v47, v43 dst_sel:WORD_1 dst_unused:UNUSED_PRESERVE src0_sel:WORD_1
	v_exp_f16_sdwa v48, v44 dst_sel:WORD_1 dst_unused:UNUSED_PRESERVE src0_sel:WORD_1
	v_exp_f16_sdwa v49, v45 dst_sel:WORD_1 dst_unused:UNUSED_PRESERVE src0_sel:WORD_1
	s_nop 0
	v_pk_add_f16 v34, v34, v49
	v_pk_add_f16 v35, v35, v48
	v_rcp_f16_e32 v44, v34
	v_rcp_f16_sdwa v34, v34 dst_sel:DWORD dst_unused:UNUSED_PAD src0_sel:WORD_1
	v_pk_add_f16 v36, v36, v47
	v_rcp_f16_e32 v45, v35
	v_rcp_f16_sdwa v35, v35 dst_sel:DWORD dst_unused:UNUSED_PAD src0_sel:WORD_1
	v_pk_add_f16 v37, v37, v46
	v_rcp_f16_e32 v43, v36
	v_rcp_f16_sdwa v36, v36 dst_sel:DWORD dst_unused:UNUSED_PAD src0_sel:WORD_1
	v_rcp_f16_e32 v42, v37
	v_rcp_f16_sdwa v37, v37 dst_sel:DWORD dst_unused:UNUSED_PAD src0_sel:WORD_1
	v_pk_fma_f16 v25, v61, v49, v25
	v_pack_b32_f16 v34, v44, v34
	v_pk_fma_f16 v24, v60, v48, v24
	v_pk_mul_f16 v25, v25, v34
	v_pack_b32_f16 v34, v45, v35
	v_pk_fma_f16 v23, v59, v47, v23
	v_pk_mul_f16 v24, v24, v34
	v_pack_b32_f16 v34, v43, v36
	v_pk_fma_f16 v22, v58, v46, v22
	v_pk_mul_f16 v23, v23, v34
	v_pack_b32_f16 v34, v42, v37
	v_pk_mul_f16 v22, v22, v34
	s_waitcnt vmcnt(0)
	v_pk_mul_f16 v34, v182, v146 op_sel_hi:[0,1]
	v_pk_mul_f16 v35, v182, v147 op_sel_hi:[0,1]
	v_pk_mul_f16 v36, v182, v148 op_sel_hi:[0,1]
	v_pk_mul_f16 v37, v182, v149 op_sel_hi:[0,1]
	v_pk_mul_f16 v42, v180, v146 op_sel_hi:[0,1]
	v_pk_mul_f16 v43, v180, v147 op_sel_hi:[0,1]
	v_pk_mul_f16 v44, v180, v148 op_sel_hi:[0,1]
	v_pk_mul_f16 v45, v180, v149 op_sel_hi:[0,1]
	v_pk_mul_f16 v46, v181, v146 op_sel_hi:[0,1]
	v_pk_mul_f16 v47, v181, v147 op_sel_hi:[0,1]
	v_pk_mul_f16 v48, v181, v148 op_sel_hi:[0,1]
	v_pk_mul_f16 v49, v181, v149 op_sel_hi:[0,1]
	v_pk_fma_f16 v21, v21, v149, v37
	v_pk_fma_f16 v20, v20, v148, v36
	v_pk_fma_f16 v19, v19, v147, v35
	v_pk_fma_f16 v18, v18, v146, v34
	v_pk_fma_f16 v33, v33, v149, v37
	v_pk_fma_f16 v32, v32, v148, v36
	v_pk_fma_f16 v31, v31, v147, v35
	v_pk_fma_f16 v30, v30, v146, v34
	v_pk_fma_f16 v37, v57, v149, v37
	v_pk_fma_f16 v36, v56, v148, v36
	v_pk_fma_f16 v35, v55, v147, v35
	v_pk_fma_f16 v34, v54, v146, v34
	v_pk_maximum3_f16 v79, v19, v31, v35
	v_pk_maximum3_f16 v80, v20, v32, v36
	v_pk_maximum3_f16 v81, v21, v33, v37
	v_pk_fma_f16 v50, v77, v149, v45
	v_pk_maximum3_f16 v78, v18, v30, v34
	v_pk_fma_f16 v51, v76, v148, v44
	v_pk_fma_f16 v52, v75, v147, v43
	v_pk_fma_f16 v53, v74, v146, v42
	v_pk_fma_f16 v54, v101, v149, v45
	v_pk_fma_f16 v55, v100, v148, v44
	v_pk_fma_f16 v56, v99, v147, v43
	v_pk_fma_f16 v57, v98, v146, v42
	v_pk_fma_f16 v45, v117, v149, v45
	v_pk_fma_f16 v44, v116, v148, v44
	v_pk_fma_f16 v43, v115, v147, v43
	v_pk_fma_f16 v42, v114, v146, v42
	v_pk_fma_f16 v66, v133, v149, v49
	v_pk_fma_f16 v67, v132, v148, v48
	v_pk_fma_f16 v68, v131, v147, v47
	v_pk_fma_f16 v69, v130, v146, v46
	v_pk_fma_f16 v74, v137, v149, v49
	v_pk_fma_f16 v75, v136, v148, v48
	v_pk_fma_f16 v76, v135, v147, v47
	v_pk_fma_f16 v77, v134, v146, v46
	v_pk_fma_f16 v49, v145, v149, v49
	v_pk_fma_f16 v48, v144, v148, v48
	v_pk_fma_f16 v47, v143, v147, v47
	v_pk_fma_f16 v46, v142, v146, v46
	v_pk_maximum3_f16 v82, v53, v57, v42
	v_pk_maximum3_f16 v83, v52, v56, v43
	v_pk_maximum3_f16 v84, v51, v55, v44
	v_pk_maximum3_f16 v85, v50, v54, v45
	v_pk_maximum3_f16 v87, v68, v76, v47
	v_pk_maximum3_f16 v86, v69, v77, v46
	v_pk_maximum3_f16 v88, v67, v75, v48
	v_pk_maximum3_f16 v89, v66, v74, v49
	v_pk_maximum3_f16 v78, v78, v82, v86
	v_pk_maximum3_f16 v79, v79, v83, v87
	v_pk_maximum3_f16 v80, v80, v84, v88
	v_pk_maximum3_f16 v81, v81, v85, v89
	s_nop 0
	v_pk_add_f16 v18, v18, v78 neg_lo:[0,1] neg_hi:[0,1]
	v_pk_add_f16 v19, v19, v79 neg_lo:[0,1] neg_hi:[0,1]
	v_pk_add_f16 v20, v20, v80 neg_lo:[0,1] neg_hi:[0,1]
	v_pk_add_f16 v21, v21, v81 neg_lo:[0,1] neg_hi:[0,1]
	v_pk_add_f16 v30, v30, v78 neg_lo:[0,1] neg_hi:[0,1]
	v_exp_f16_sdwa v82, v18 dst_sel:WORD_0 dst_unused:UNUSED_PAD src0_sel:WORD_0
	v_exp_f16_sdwa v83, v19 dst_sel:WORD_0 dst_unused:UNUSED_PAD src0_sel:WORD_0
	v_exp_f16_sdwa v84, v20 dst_sel:WORD_0 dst_unused:UNUSED_PAD src0_sel:WORD_0
	v_exp_f16_sdwa v85, v21 dst_sel:WORD_0 dst_unused:UNUSED_PAD src0_sel:WORD_0
	v_exp_f16_sdwa v82, v18 dst_sel:WORD_1 dst_unused:UNUSED_PRESERVE src0_sel:WORD_1
	v_exp_f16_sdwa v83, v19 dst_sel:WORD_1 dst_unused:UNUSED_PRESERVE src0_sel:WORD_1
	v_exp_f16_sdwa v84, v20 dst_sel:WORD_1 dst_unused:UNUSED_PRESERVE src0_sel:WORD_1
	v_exp_f16_sdwa v85, v21 dst_sel:WORD_1 dst_unused:UNUSED_PRESERVE src0_sel:WORD_1
	v_pk_add_f16 v31, v31, v79 neg_lo:[0,1] neg_hi:[0,1]
	v_pk_add_f16 v18, v82, 0
	v_pk_add_f16 v19, v83, 0
	v_pk_add_f16 v20, v84, 0
	v_pk_add_f16 v21, v85, 0
	v_pk_fma_f16 v6, v6, v82, 0
	v_pk_fma_f16 v7, v7, v83, 0
	v_pk_fma_f16 v8, v8, v84, 0
	v_pk_fma_f16 v9, v9, v85, 0
	v_pk_add_f16 v32, v32, v80 neg_lo:[0,1] neg_hi:[0,1]
	v_pk_add_f16 v33, v33, v81 neg_lo:[0,1] neg_hi:[0,1]
	v_exp_f16_sdwa v82, v30 dst_sel:WORD_0 dst_unused:UNUSED_PAD src0_sel:WORD_0
	v_exp_f16_sdwa v83, v31 dst_sel:WORD_0 dst_unused:UNUSED_PAD src0_sel:WORD_0
	v_exp_f16_sdwa v84, v32 dst_sel:WORD_0 dst_unused:UNUSED_PAD src0_sel:WORD_0
	v_exp_f16_sdwa v85, v33 dst_sel:WORD_0 dst_unused:UNUSED_PAD src0_sel:WORD_0
	v_exp_f16_sdwa v82, v30 dst_sel:WORD_1 dst_unused:UNUSED_PRESERVE src0_sel:WORD_1
	v_exp_f16_sdwa v83, v31 dst_sel:WORD_1 dst_unused:UNUSED_PRESERVE src0_sel:WORD_1
	v_exp_f16_sdwa v84, v32 dst_sel:WORD_1 dst_unused:UNUSED_PRESERVE src0_sel:WORD_1
	v_exp_f16_sdwa v85, v33 dst_sel:WORD_1 dst_unused:UNUSED_PRESERVE src0_sel:WORD_1
	s_nop 0
	v_pk_add_f16 v21, v21, v85
	v_pk_add_f16 v20, v20, v84
	v_pk_add_f16 v19, v19, v83
	v_pk_add_f16 v18, v18, v82
	v_pk_fma_f16 v9, v13, v85, v9
	v_pk_fma_f16 v8, v12, v84, v8
	v_pk_fma_f16 v7, v11, v83, v7
	v_pk_fma_f16 v6, v10, v82, v6
	v_pk_add_f16 v10, v34, v78 neg_lo:[0,1] neg_hi:[0,1]
	v_pk_add_f16 v11, v35, v79 neg_lo:[0,1] neg_hi:[0,1]
	v_pk_add_f16 v12, v36, v80 neg_lo:[0,1] neg_hi:[0,1]
	v_pk_add_f16 v13, v37, v81 neg_lo:[0,1] neg_hi:[0,1]
	v_exp_f16_sdwa v30, v10 dst_sel:WORD_0 dst_unused:UNUSED_PAD src0_sel:WORD_0
	v_exp_f16_sdwa v31, v11 dst_sel:WORD_0 dst_unused:UNUSED_PAD src0_sel:WORD_0
	v_exp_f16_sdwa v32, v12 dst_sel:WORD_0 dst_unused:UNUSED_PAD src0_sel:WORD_0
	v_exp_f16_sdwa v33, v13 dst_sel:WORD_0 dst_unused:UNUSED_PAD src0_sel:WORD_0
	v_exp_f16_sdwa v30, v10 dst_sel:WORD_1 dst_unused:UNUSED_PRESERVE src0_sel:WORD_1
	v_exp_f16_sdwa v31, v11 dst_sel:WORD_1 dst_unused:UNUSED_PRESERVE src0_sel:WORD_1
	v_exp_f16_sdwa v32, v12 dst_sel:WORD_1 dst_unused:UNUSED_PRESERVE src0_sel:WORD_1
	v_exp_f16_sdwa v33, v13 dst_sel:WORD_1 dst_unused:UNUSED_PRESERVE src0_sel:WORD_1
	v_pk_add_f16 v10, v18, v30
	v_pk_add_f16 v11, v19, v31
	v_pk_add_f16 v12, v20, v32
	v_pk_add_f16 v13, v21, v33
	v_pk_fma_f16 v6, v14, v30, v6
	v_pk_fma_f16 v7, v15, v31, v7
	v_pk_fma_f16 v8, v16, v32, v8
	v_pk_fma_f16 v9, v17, v33, v9
	v_pk_add_f16 v14, v53, v78 neg_lo:[0,1] neg_hi:[0,1]
	v_pk_add_f16 v15, v52, v79 neg_lo:[0,1] neg_hi:[0,1]
	v_pk_add_f16 v16, v51, v80 neg_lo:[0,1] neg_hi:[0,1]
	v_pk_add_f16 v17, v50, v81 neg_lo:[0,1] neg_hi:[0,1]
	v_exp_f16_sdwa v18, v14 dst_sel:WORD_0 dst_unused:UNUSED_PAD src0_sel:WORD_0
	v_exp_f16_sdwa v19, v15 dst_sel:WORD_0 dst_unused:UNUSED_PAD src0_sel:WORD_0
	v_exp_f16_sdwa v20, v16 dst_sel:WORD_0 dst_unused:UNUSED_PAD src0_sel:WORD_0
	v_exp_f16_sdwa v21, v17 dst_sel:WORD_0 dst_unused:UNUSED_PAD src0_sel:WORD_0
	v_exp_f16_sdwa v18, v14 dst_sel:WORD_1 dst_unused:UNUSED_PRESERVE src0_sel:WORD_1
	v_exp_f16_sdwa v19, v15 dst_sel:WORD_1 dst_unused:UNUSED_PRESERVE src0_sel:WORD_1
	v_exp_f16_sdwa v20, v16 dst_sel:WORD_1 dst_unused:UNUSED_PRESERVE src0_sel:WORD_1
	v_exp_f16_sdwa v21, v17 dst_sel:WORD_1 dst_unused:UNUSED_PRESERVE src0_sel:WORD_1
	v_pk_add_f16 v14, v57, v78 neg_lo:[0,1] neg_hi:[0,1]
	v_pk_add_f16 v13, v13, v21
	v_pk_add_f16 v12, v12, v20
	v_pk_add_f16 v11, v11, v19
	v_pk_add_f16 v10, v10, v18
	v_pk_fma_f16 v9, v29, v21, v9
	v_pk_fma_f16 v8, v28, v20, v8
	v_pk_fma_f16 v7, v27, v19, v7
	v_pk_fma_f16 v6, v26, v18, v6
	v_pk_add_f16 v15, v56, v79 neg_lo:[0,1] neg_hi:[0,1]
	v_pk_add_f16 v16, v55, v80 neg_lo:[0,1] neg_hi:[0,1]
	v_pk_add_f16 v17, v54, v81 neg_lo:[0,1] neg_hi:[0,1]
	v_exp_f16_sdwa v18, v14 dst_sel:WORD_0 dst_unused:UNUSED_PAD src0_sel:WORD_0
	v_exp_f16_sdwa v19, v15 dst_sel:WORD_0 dst_unused:UNUSED_PAD src0_sel:WORD_0
	v_exp_f16_sdwa v20, v16 dst_sel:WORD_0 dst_unused:UNUSED_PAD src0_sel:WORD_0
	v_exp_f16_sdwa v21, v17 dst_sel:WORD_0 dst_unused:UNUSED_PAD src0_sel:WORD_0
	v_exp_f16_sdwa v18, v14 dst_sel:WORD_1 dst_unused:UNUSED_PRESERVE src0_sel:WORD_1
	v_exp_f16_sdwa v19, v15 dst_sel:WORD_1 dst_unused:UNUSED_PRESERVE src0_sel:WORD_1
	v_exp_f16_sdwa v20, v16 dst_sel:WORD_1 dst_unused:UNUSED_PRESERVE src0_sel:WORD_1
	v_exp_f16_sdwa v21, v17 dst_sel:WORD_1 dst_unused:UNUSED_PRESERVE src0_sel:WORD_1
	v_pk_add_f16 v14, v42, v78 neg_lo:[0,1] neg_hi:[0,1]
	v_pk_add_f16 v10, v10, v18
	v_pk_add_f16 v11, v11, v19
	v_pk_add_f16 v12, v12, v20
	v_pk_add_f16 v13, v13, v21
	v_pk_fma_f16 v6, v38, v18, v6
	v_pk_fma_f16 v7, v39, v19, v7
	v_pk_fma_f16 v8, v40, v20, v8
	v_pk_fma_f16 v9, v41, v21, v9
	v_pk_add_f16 v15, v43, v79 neg_lo:[0,1] neg_hi:[0,1]
	v_pk_add_f16 v16, v44, v80 neg_lo:[0,1] neg_hi:[0,1]
	v_pk_add_f16 v17, v45, v81 neg_lo:[0,1] neg_hi:[0,1]
	v_exp_f16_sdwa v18, v14 dst_sel:WORD_0 dst_unused:UNUSED_PAD src0_sel:WORD_0
	v_exp_f16_sdwa v19, v15 dst_sel:WORD_0 dst_unused:UNUSED_PAD src0_sel:WORD_0
	v_exp_f16_sdwa v20, v16 dst_sel:WORD_0 dst_unused:UNUSED_PAD src0_sel:WORD_0
	v_exp_f16_sdwa v21, v17 dst_sel:WORD_0 dst_unused:UNUSED_PAD src0_sel:WORD_0
	v_exp_f16_sdwa v18, v14 dst_sel:WORD_1 dst_unused:UNUSED_PRESERVE src0_sel:WORD_1
	v_exp_f16_sdwa v19, v15 dst_sel:WORD_1 dst_unused:UNUSED_PRESERVE src0_sel:WORD_1
	v_exp_f16_sdwa v20, v16 dst_sel:WORD_1 dst_unused:UNUSED_PRESERVE src0_sel:WORD_1
	v_exp_f16_sdwa v21, v17 dst_sel:WORD_1 dst_unused:UNUSED_PRESERVE src0_sel:WORD_1
	v_pk_add_f16 v14, v69, v78 neg_lo:[0,1] neg_hi:[0,1]
	v_pk_add_f16 v13, v13, v21
	v_pk_add_f16 v12, v12, v20
	v_pk_add_f16 v11, v11, v19
	v_pk_add_f16 v10, v10, v18
	v_pk_fma_f16 v9, v61, v21, v9
	v_pk_fma_f16 v8, v60, v20, v8
	v_pk_fma_f16 v7, v59, v19, v7
	v_pk_fma_f16 v6, v58, v18, v6
	v_pk_add_f16 v15, v68, v79 neg_lo:[0,1] neg_hi:[0,1]
	v_pk_add_f16 v16, v67, v80 neg_lo:[0,1] neg_hi:[0,1]
	v_pk_add_f16 v17, v66, v81 neg_lo:[0,1] neg_hi:[0,1]
	v_exp_f16_sdwa v18, v14 dst_sel:WORD_0 dst_unused:UNUSED_PAD src0_sel:WORD_0
	v_exp_f16_sdwa v19, v15 dst_sel:WORD_0 dst_unused:UNUSED_PAD src0_sel:WORD_0
	v_exp_f16_sdwa v20, v16 dst_sel:WORD_0 dst_unused:UNUSED_PAD src0_sel:WORD_0
	v_exp_f16_sdwa v21, v17 dst_sel:WORD_0 dst_unused:UNUSED_PAD src0_sel:WORD_0
	v_exp_f16_sdwa v18, v14 dst_sel:WORD_1 dst_unused:UNUSED_PRESERVE src0_sel:WORD_1
	v_exp_f16_sdwa v19, v15 dst_sel:WORD_1 dst_unused:UNUSED_PRESERVE src0_sel:WORD_1
	v_exp_f16_sdwa v20, v16 dst_sel:WORD_1 dst_unused:UNUSED_PRESERVE src0_sel:WORD_1
	v_exp_f16_sdwa v21, v17 dst_sel:WORD_1 dst_unused:UNUSED_PRESERVE src0_sel:WORD_1
	v_pk_add_f16 v10, v10, v18
	v_pk_add_f16 v11, v11, v19
	v_pk_add_f16 v12, v12, v20
	v_pk_add_f16 v13, v13, v21
	v_pk_fma_f16 v14, v70, v18, v6
	v_pk_fma_f16 v15, v71, v19, v7
	v_pk_fma_f16 v16, v72, v20, v8
	v_pk_fma_f16 v17, v73, v21, v9
	v_pk_add_f16 v6, v77, v78 neg_lo:[0,1] neg_hi:[0,1]
	v_pk_add_f16 v7, v76, v79 neg_lo:[0,1] neg_hi:[0,1]
	v_pk_add_f16 v8, v75, v80 neg_lo:[0,1] neg_hi:[0,1]
	v_pk_add_f16 v9, v74, v81 neg_lo:[0,1] neg_hi:[0,1]
	v_exp_f16_sdwa v18, v6 dst_sel:WORD_0 dst_unused:UNUSED_PAD src0_sel:WORD_0
	v_exp_f16_sdwa v19, v7 dst_sel:WORD_0 dst_unused:UNUSED_PAD src0_sel:WORD_0
	v_exp_f16_sdwa v20, v8 dst_sel:WORD_0 dst_unused:UNUSED_PAD src0_sel:WORD_0
	v_exp_f16_sdwa v21, v9 dst_sel:WORD_0 dst_unused:UNUSED_PAD src0_sel:WORD_0
	v_exp_f16_sdwa v18, v6 dst_sel:WORD_1 dst_unused:UNUSED_PRESERVE src0_sel:WORD_1
	v_exp_f16_sdwa v19, v7 dst_sel:WORD_1 dst_unused:UNUSED_PRESERVE src0_sel:WORD_1
	v_exp_f16_sdwa v20, v8 dst_sel:WORD_1 dst_unused:UNUSED_PRESERVE src0_sel:WORD_1
	v_exp_f16_sdwa v21, v9 dst_sel:WORD_1 dst_unused:UNUSED_PRESERVE src0_sel:WORD_1
	s_nop 0
	v_pk_add_f16 v9, v13, v21
	v_pk_add_f16 v8, v12, v20
	v_pk_add_f16 v7, v11, v19
	v_pk_add_f16 v6, v10, v18
	v_pk_fma_f16 v13, v93, v21, v17
	v_pk_fma_f16 v12, v92, v20, v16
	v_pk_fma_f16 v11, v91, v19, v15
	v_pk_fma_f16 v10, v90, v18, v14
	v_pk_add_f16 v18, v46, v78 neg_lo:[0,1] neg_hi:[0,1]
	v_pk_add_f16 v19, v47, v79 neg_lo:[0,1] neg_hi:[0,1]
	v_pk_add_f16 v20, v48, v80 neg_lo:[0,1] neg_hi:[0,1]
	v_pk_add_f16 v21, v49, v81 neg_lo:[0,1] neg_hi:[0,1]
	v_exp_f16_sdwa v14, v18 dst_sel:WORD_0 dst_unused:UNUSED_PAD src0_sel:WORD_0
	v_exp_f16_sdwa v17, v19 dst_sel:WORD_0 dst_unused:UNUSED_PAD src0_sel:WORD_0
	v_exp_f16_sdwa v15, v20 dst_sel:WORD_0 dst_unused:UNUSED_PAD src0_sel:WORD_0
	v_exp_f16_sdwa v16, v21 dst_sel:WORD_0 dst_unused:UNUSED_PAD src0_sel:WORD_0
	v_exp_f16_sdwa v14, v18 dst_sel:WORD_1 dst_unused:UNUSED_PRESERVE src0_sel:WORD_1
	v_exp_f16_sdwa v17, v19 dst_sel:WORD_1 dst_unused:UNUSED_PRESERVE src0_sel:WORD_1
	v_exp_f16_sdwa v15, v20 dst_sel:WORD_1 dst_unused:UNUSED_PRESERVE src0_sel:WORD_1
	v_exp_f16_sdwa v16, v21 dst_sel:WORD_1 dst_unused:UNUSED_PRESERVE src0_sel:WORD_1
	s_nop 0

.Lmyf_B1_7:
	s_mov_b64 exec, -1
	s_waitcnt lgkmcnt(0)
	v_cvt_f16_f32_e32 v183, s27
	v_cvt_f16_f32_e32 v185, s26
	v_cvt_f16_f32_e32 v184, s34
	s_mov_b64 s[4:5], 0
	s_cmp_lt_u32 s94, 4
	s_cbranch_scc1 .Lmylp3_0
	s_setprio 1
.Lmylp3_0:
	s_waitcnt vmcnt(3)
	v_pk_mul_f16 v193, v185, v189 op_sel_hi:[0,1]
	v_pk_mul_f16 v197, v183, v189 op_sel_hi:[0,1]
	v_pk_mul_f16 v201, v184, v189 op_sel_hi:[0,1]
	v_pk_mul_f16 v190, v185, v186 op_sel_hi:[0,1]
	v_pk_mul_f16 v191, v185, v187 op_sel_hi:[0,1]
	v_pk_mul_f16 v192, v185, v188 op_sel_hi:[0,1]
	v_pk_mul_f16 v194, v183, v186 op_sel_hi:[0,1]
	s_mov_b64 exec, s[64:65]
	buffer_load_dwordx4 v[18:21], v249, s[16:19], 0 offen
	buffer_load_dwordx4 v[6:9], v249, s[16:19], 0 offen offset:512
	s_mov_b64 exec, -1
	v_pk_mul_f16 v195, v183, v187 op_sel_hi:[0,1]
	v_pk_mul_f16 v196, v183, v188 op_sel_hi:[0,1]
	v_pk_mul_f16 v198, v184, v186 op_sel_hi:[0,1]
	v_pk_mul_f16 v199, v184, v187 op_sel_hi:[0,1]
	v_pk_mul_f16 v200, v184, v188 op_sel_hi:[0,1]
	v_pk_fma_f16 v113, v113, v189, v193
	v_pk_fma_f16 v129, v129, v189, v197
	v_pk_fma_f16 v137, v137, v189, v201
	v_pk_fma_f16 v202, v85, v189, v193
	v_pk_fma_f16 v206, v109, v189, v197
	v_pk_fma_f16 v210, v125, v189, v201
	v_pk_fma_f16 v193, v53, v189, v193
	v_pk_fma_f16 v197, v69, v189, v197
	buffer_load_dwordx4 v[34:37], v250, s[16:19], 0 offen offset:512
	buffer_load_dwordx4 v[10:13], v250, s[16:19], 0 offen offset:1024
	v_pk_fma_f16 v189, v97, v189, v201
	v_pk_maximum3_f16 v201, v113, v129, v137
	v_pk_fma_f16 v112, v112, v188, v192
	v_pk_fma_f16 v111, v111, v187, v191
	v_pk_fma_f16 v110, v110, v186, v190
	v_pk_fma_f16 v128, v128, v188, v196
	v_pk_fma_f16 v127, v127, v187, v195
	v_pk_fma_f16 v126, v126, v186, v194
	v_pk_fma_f16 v136, v136, v188, v200
	v_pk_fma_f16 v135, v135, v187, v199
	v_pk_fma_f16 v134, v134, v186, v198
	v_pk_fma_f16 v203, v84, v188, v192
	v_pk_fma_f16 v204, v83, v187, v191
	v_pk_fma_f16 v205, v82, v186, v190
	v_pk_fma_f16 v207, v108, v188, v196
	v_pk_fma_f16 v208, v107, v187, v195
	s_mov_b64 exec, s[66:67]
	buffer_load_dwordx4 v[54:57], v250, s[16:19], 0 offen offset:2048
	buffer_load_dwordx4 v[14:17], v250, s[16:19], 0 offen offset:2560
	s_mov_b64 exec, -1
	v_pk_fma_f16 v209, v106, v186, v194
	v_pk_fma_f16 v211, v124, v188, v200
	v_pk_fma_f16 v212, v123, v187, v199
	v_pk_fma_f16 v213, v122, v186, v198
	v_pk_fma_f16 v192, v52, v188, v192
	v_pk_fma_f16 v191, v51, v187, v191
	v_pk_fma_f16 v190, v50, v186, v190
	v_pk_fma_f16 v196, v68, v188, v196
	v_pk_fma_f16 v195, v67, v187, v195
	v_pk_fma_f16 v194, v66, v186, v194
	v_pk_fma_f16 v188, v96, v188, v200
	v_pk_fma_f16 v187, v95, v187, v199
	v_pk_fma_f16 v186, v94, v186, v198
	v_pk_maximum3_f16 v198, v110, v126, v134
	v_pk_maximum3_f16 v199, v111, v127, v135
	v_pk_maximum3_f16 v200, v112, v128, v136
	v_pk_maximum3_f16 v217, v202, v206, v210
	v_pk_maximum3_f16 v221, v193, v197, v189
	v_pk_maximum3_f16 v214, v205, v209, v213
	v_pk_maximum3_f16 v215, v204, v208, v212
	v_pk_maximum3_f16 v216, v203, v207, v211
	v_pk_maximum3_f16 v218, v190, v194, v186
	v_pk_maximum3_f16 v219, v191, v195, v187
	v_pk_maximum3_f16 v201, v201, v217, v221
	v_pk_maximum3_f16 v220, v192, v196, v188
	v_pk_maximum3_f16 v198, v198, v214, v218
	v_pk_maximum3_f16 v199, v199, v215, v219
	v_pk_maximum3_f16 v200, v200, v216, v220
	v_pk_add_f16 v113, v113, v201 neg_lo:[0,1] neg_hi:[0,1]
	s_mov_b64 exec, s[64:65]
	buffer_load_dwordx4 v[74:77], v251, s[16:19], 0 offen
	buffer_load_dwordx4 v[26:29], v251, s[16:19], 0 offen offset:512
	s_mov_b64 exec, -1
	v_pk_add_f16 v110, v110, v198 neg_lo:[0,1] neg_hi:[0,1]
	v_pk_add_f16 v111, v111, v199 neg_lo:[0,1] neg_hi:[0,1]
	v_pk_add_f16 v112, v112, v200 neg_lo:[0,1] neg_hi:[0,1]
	v_pk_add_f16 v126, v126, v198 neg_lo:[0,1] neg_hi:[0,1]
	v_exp_f16_sdwa v214, v110 dst_sel:WORD_0 dst_unused:UNUSED_PAD src0_sel:WORD_0
	v_exp_f16_sdwa v215, v111 dst_sel:WORD_0 dst_unused:UNUSED_PAD src0_sel:WORD_0
	v_exp_f16_sdwa v216, v112 dst_sel:WORD_0 dst_unused:UNUSED_PAD src0_sel:WORD_0
	v_exp_f16_sdwa v217, v113 dst_sel:WORD_0 dst_unused:UNUSED_PAD src0_sel:WORD_0
	v_exp_f16_sdwa v214, v110 dst_sel:WORD_1 dst_unused:UNUSED_PRESERVE src0_sel:WORD_1
	v_exp_f16_sdwa v215, v111 dst_sel:WORD_1 dst_unused:UNUSED_PRESERVE src0_sel:WORD_1
	v_exp_f16_sdwa v216, v112 dst_sel:WORD_1 dst_unused:UNUSED_PRESERVE src0_sel:WORD_1
	v_exp_f16_sdwa v217, v113 dst_sel:WORD_1 dst_unused:UNUSED_PRESERVE src0_sel:WORD_1
	v_pk_add_f16 v127, v127, v199 neg_lo:[0,1] neg_hi:[0,1]
	v_pk_add_f16 v113, v214, 0
	v_pk_fma_f16 v73, v73, v217, 0
	v_pk_add_f16 v110, v217, 0
	v_pk_add_f16 v111, v216, 0
	v_pk_add_f16 v112, v215, 0
	v_pk_fma_f16 v72, v72, v216, 0
	v_pk_fma_f16 v71, v71, v215, 0
	v_pk_fma_f16 v70, v70, v214, 0
	v_pk_add_f16 v128, v128, v200 neg_lo:[0,1] neg_hi:[0,1]
	buffer_load_dwordx4 v[102:105], v252, s[16:19], 0 offen offset:512
	buffer_load_dwordx4 v[38:41], v252, s[16:19], 0 offen offset:1024
	v_pk_add_f16 v129, v129, v201 neg_lo:[0,1] neg_hi:[0,1]
	v_exp_f16_sdwa v214, v126 dst_sel:WORD_0 dst_unused:UNUSED_PAD src0_sel:WORD_0
	v_exp_f16_sdwa v215, v127 dst_sel:WORD_0 dst_unused:UNUSED_PAD src0_sel:WORD_0
	v_exp_f16_sdwa v216, v128 dst_sel:WORD_0 dst_unused:UNUSED_PAD src0_sel:WORD_0
	v_exp_f16_sdwa v217, v129 dst_sel:WORD_0 dst_unused:UNUSED_PAD src0_sel:WORD_0
	v_exp_f16_sdwa v214, v126 dst_sel:WORD_1 dst_unused:UNUSED_PRESERVE src0_sel:WORD_1
	v_exp_f16_sdwa v215, v127 dst_sel:WORD_1 dst_unused:UNUSED_PRESERVE src0_sel:WORD_1
	v_exp_f16_sdwa v216, v128 dst_sel:WORD_1 dst_unused:UNUSED_PRESERVE src0_sel:WORD_1
	v_exp_f16_sdwa v217, v129 dst_sel:WORD_1 dst_unused:UNUSED_PRESERVE src0_sel:WORD_1
	v_pk_add_f16 v113, v113, v214
	v_pk_fma_f16 v73, v101, v217, v73
	v_pk_add_f16 v101, v137, v201 neg_lo:[0,1] neg_hi:[0,1]
	v_pk_add_f16 v112, v112, v215
	v_pk_add_f16 v111, v111, v216
	v_pk_add_f16 v110, v110, v217
	v_pk_fma_f16 v70, v98, v214, v70
	v_pk_fma_f16 v71, v99, v215, v71
	v_pk_fma_f16 v72, v100, v216, v72
	v_pk_add_f16 v98, v134, v198 neg_lo:[0,1] neg_hi:[0,1]
	v_pk_add_f16 v99, v135, v199 neg_lo:[0,1] neg_hi:[0,1]
	v_pk_add_f16 v100, v136, v200 neg_lo:[0,1] neg_hi:[0,1]
	v_exp_f16_sdwa v126, v98 dst_sel:WORD_0 dst_unused:UNUSED_PAD src0_sel:WORD_0
	v_exp_f16_sdwa v127, v99 dst_sel:WORD_0 dst_unused:UNUSED_PAD src0_sel:WORD_0
	v_exp_f16_sdwa v128, v100 dst_sel:WORD_0 dst_unused:UNUSED_PAD src0_sel:WORD_0
	v_exp_f16_sdwa v129, v101 dst_sel:WORD_0 dst_unused:UNUSED_PAD src0_sel:WORD_0
	v_exp_f16_sdwa v126, v98 dst_sel:WORD_1 dst_unused:UNUSED_PRESERVE src0_sel:WORD_1
	v_exp_f16_sdwa v127, v99 dst_sel:WORD_1 dst_unused:UNUSED_PRESERVE src0_sel:WORD_1
	v_exp_f16_sdwa v128, v100 dst_sel:WORD_1 dst_unused:UNUSED_PRESERVE src0_sel:WORD_1
	v_exp_f16_sdwa v129, v101 dst_sel:WORD_1 dst_unused:UNUSED_PRESERVE src0_sel:WORD_1
	v_pk_add_f16 v101, v113, v126
	v_pk_add_f16 v98, v110, v129
	s_mov_b64 exec, s[66:67]
	buffer_load_dwordx4 v[118:121], v252, s[16:19], 0 offen offset:2048
	buffer_load_dwordx4 v[58:61], v252, s[16:19], 0 offen offset:2560
	s_mov_b64 exec, -1
	v_pk_add_f16 v99, v111, v128
	v_pk_add_f16 v100, v112, v127
	v_pk_fma_f16 v73, v117, v129, v73
	v_pk_fma_f16 v72, v116, v128, v72
	v_pk_fma_f16 v71, v115, v127, v71
	v_pk_fma_f16 v70, v114, v126, v70
	v_pk_add_f16 v110, v205, v198 neg_lo:[0,1] neg_hi:[0,1]
	v_pk_add_f16 v111, v204, v199 neg_lo:[0,1] neg_hi:[0,1]
	v_pk_add_f16 v112, v203, v200 neg_lo:[0,1] neg_hi:[0,1]
	v_pk_add_f16 v113, v202, v201 neg_lo:[0,1] neg_hi:[0,1]
	v_exp_f16_sdwa v114, v110 dst_sel:WORD_0 dst_unused:UNUSED_PAD src0_sel:WORD_0
	v_exp_f16_sdwa v115, v111 dst_sel:WORD_0 dst_unused:UNUSED_PAD src0_sel:WORD_0
	v_exp_f16_sdwa v116, v112 dst_sel:WORD_0 dst_unused:UNUSED_PAD src0_sel:WORD_0
	v_exp_f16_sdwa v117, v113 dst_sel:WORD_0 dst_unused:UNUSED_PAD src0_sel:WORD_0
	v_exp_f16_sdwa v114, v110 dst_sel:WORD_1 dst_unused:UNUSED_PRESERVE src0_sel:WORD_1
	v_exp_f16_sdwa v115, v111 dst_sel:WORD_1 dst_unused:UNUSED_PRESERVE src0_sel:WORD_1
	v_exp_f16_sdwa v116, v112 dst_sel:WORD_1 dst_unused:UNUSED_PRESERVE src0_sel:WORD_1
	v_exp_f16_sdwa v117, v113 dst_sel:WORD_1 dst_unused:UNUSED_PRESERVE src0_sel:WORD_1
	v_pk_add_f16 v110, v209, v198 neg_lo:[0,1] neg_hi:[0,1]
	v_pk_add_f16 v101, v101, v114
	v_pk_add_f16 v100, v100, v115
	v_pk_add_f16 v99, v99, v116
	s_mov_b64 exec, s[76:77]
	buffer_load_dwordx4 v[130:133], v253, s[16:19], 0 offen
	buffer_load_dwordx4 v[78:81], v253, s[16:19], 0 offen offset:512
	s_mov_b64 exec, -1
	v_pk_add_f16 v98, v98, v117
	v_pk_fma_f16 v70, v42, v114, v70
	v_pk_fma_f16 v71, v43, v115, v71
	v_pk_fma_f16 v72, v44, v116, v72
	v_pk_fma_f16 v73, v45, v117, v73
	v_pk_add_f16 v111, v208, v199 neg_lo:[0,1] neg_hi:[0,1]
	v_pk_add_f16 v112, v207, v200 neg_lo:[0,1] neg_hi:[0,1]
	v_pk_add_f16 v113, v206, v201 neg_lo:[0,1] neg_hi:[0,1]
	v_exp_f16_sdwa v114, v110 dst_sel:WORD_0 dst_unused:UNUSED_PAD src0_sel:WORD_0
	v_exp_f16_sdwa v115, v111 dst_sel:WORD_0 dst_unused:UNUSED_PAD src0_sel:WORD_0
	v_exp_f16_sdwa v116, v112 dst_sel:WORD_0 dst_unused:UNUSED_PAD src0_sel:WORD_0
	v_exp_f16_sdwa v117, v113 dst_sel:WORD_0 dst_unused:UNUSED_PAD src0_sel:WORD_0
	v_exp_f16_sdwa v114, v110 dst_sel:WORD_1 dst_unused:UNUSED_PRESERVE src0_sel:WORD_1
	v_exp_f16_sdwa v115, v111 dst_sel:WORD_1 dst_unused:UNUSED_PRESERVE src0_sel:WORD_1
	v_exp_f16_sdwa v116, v112 dst_sel:WORD_1 dst_unused:UNUSED_PRESERVE src0_sel:WORD_1
	v_exp_f16_sdwa v117, v113 dst_sel:WORD_1 dst_unused:UNUSED_PRESERVE src0_sel:WORD_1
	v_pk_add_f16 v110, v213, v198 neg_lo:[0,1] neg_hi:[0,1]
	v_pk_add_f16 v101, v101, v114
	v_pk_add_f16 v98, v98, v117
	v_pk_add_f16 v99, v99, v116
	v_pk_add_f16 v100, v100, v115
	v_pk_fma_f16 v73, v65, v117, v73
	v_pk_fma_f16 v72, v64, v116, v72
	s_mov_b64 exec, s[70:71]
	buffer_load_dwordx4 v[138:141], v254, s[16:19], 0 offen offset:512
	buffer_load_dwordx4 v[90:93], v254, s[16:19], 0 offen offset:1024
	s_mov_b64 exec, -1
	v_pk_fma_f16 v71, v63, v115, v71
	v_pk_fma_f16 v70, v62, v114, v70
	v_pk_add_f16 v111, v212, v199 neg_lo:[0,1] neg_hi:[0,1]
	v_pk_add_f16 v112, v211, v200 neg_lo:[0,1] neg_hi:[0,1]
	v_pk_add_f16 v113, v210, v201 neg_lo:[0,1] neg_hi:[0,1]
	v_exp_f16_sdwa v114, v110 dst_sel:WORD_0 dst_unused:UNUSED_PAD src0_sel:WORD_0
	v_exp_f16_sdwa v115, v111 dst_sel:WORD_0 dst_unused:UNUSED_PAD src0_sel:WORD_0
	v_exp_f16_sdwa v116, v112 dst_sel:WORD_0 dst_unused:UNUSED_PAD src0_sel:WORD_0
	v_exp_f16_sdwa v117, v113 dst_sel:WORD_0 dst_unused:UNUSED_PAD src0_sel:WORD_0
	v_exp_f16_sdwa v114, v110 dst_sel:WORD_1 dst_unused:UNUSED_PRESERVE src0_sel:WORD_1
	v_exp_f16_sdwa v115, v111 dst_sel:WORD_1 dst_unused:UNUSED_PRESERVE src0_sel:WORD_1
	v_exp_f16_sdwa v116, v112 dst_sel:WORD_1 dst_unused:UNUSED_PRESERVE src0_sel:WORD_1
	v_exp_f16_sdwa v117, v113 dst_sel:WORD_1 dst_unused:UNUSED_PRESERVE src0_sel:WORD_1
	v_pk_add_f16 v110, v190, v198 neg_lo:[0,1] neg_hi:[0,1]
	v_pk_add_f16 v101, v101, v114
	v_pk_add_f16 v100, v100, v115
	v_pk_add_f16 v99, v99, v116
	v_pk_add_f16 v98, v98, v117
	v_pk_fma_f16 v70, v86, v114, v70
	v_pk_fma_f16 v71, v87, v115, v71
	v_pk_fma_f16 v72, v88, v116, v72
	v_pk_fma_f16 v73, v89, v117, v73
	s_mov_b64 exec, s[78:79]
	buffer_load_dwordx4 v[142:145], v254, s[16:19], 0 offen offset:2048
	buffer_load_dwordx4 v[2:5], v254, s[16:19], 0 offen offset:2560
	s_mov_b64 exec, -1
	v_pk_add_f16 v111, v191, v199 neg_lo:[0,1] neg_hi:[0,1]
	v_pk_add_f16 v112, v192, v200 neg_lo:[0,1] neg_hi:[0,1]
	v_pk_add_f16 v113, v193, v201 neg_lo:[0,1] neg_hi:[0,1]
	v_exp_f16_sdwa v114, v110 dst_sel:WORD_0 dst_unused:UNUSED_PAD src0_sel:WORD_0
	v_exp_f16_sdwa v115, v111 dst_sel:WORD_0 dst_unused:UNUSED_PAD src0_sel:WORD_0
	v_exp_f16_sdwa v116, v112 dst_sel:WORD_0 dst_unused:UNUSED_PAD src0_sel:WORD_0
	v_exp_f16_sdwa v117, v113 dst_sel:WORD_0 dst_unused:UNUSED_PAD src0_sel:WORD_0
	v_exp_f16_sdwa v114, v110 dst_sel:WORD_1 dst_unused:UNUSED_PRESERVE src0_sel:WORD_1
	v_exp_f16_sdwa v115, v111 dst_sel:WORD_1 dst_unused:UNUSED_PRESERVE src0_sel:WORD_1
	v_exp_f16_sdwa v116, v112 dst_sel:WORD_1 dst_unused:UNUSED_PRESERVE src0_sel:WORD_1
	v_exp_f16_sdwa v117, v113 dst_sel:WORD_1 dst_unused:UNUSED_PRESERVE src0_sel:WORD_1
	v_pk_add_f16 v110, v194, v198 neg_lo:[0,1] neg_hi:[0,1]
	v_pk_add_f16 v101, v101, v114
	v_pk_add_f16 v98, v98, v117
	v_pk_add_f16 v99, v99, v116
	v_pk_add_f16 v100, v100, v115
	v_pk_fma_f16 v73, v25, v117, v73
	v_pk_fma_f16 v72, v24, v116, v72
	v_pk_fma_f16 v71, v23, v115, v71
	v_pk_fma_f16 v70, v22, v114, v70
	v_pk_add_f16 v111, v195, v199 neg_lo:[0,1] neg_hi:[0,1]
	v_pk_add_f16 v112, v196, v200 neg_lo:[0,1] neg_hi:[0,1]
	v_pk_add_f16 v113, v197, v201 neg_lo:[0,1] neg_hi:[0,1]
	v_exp_f16_sdwa v114, v110 dst_sel:WORD_0 dst_unused:UNUSED_PAD src0_sel:WORD_0
	v_exp_f16_sdwa v115, v111 dst_sel:WORD_0 dst_unused:UNUSED_PAD src0_sel:WORD_0
	v_exp_f16_sdwa v116, v112 dst_sel:WORD_0 dst_unused:UNUSED_PAD src0_sel:WORD_0
	v_exp_f16_sdwa v117, v113 dst_sel:WORD_0 dst_unused:UNUSED_PAD src0_sel:WORD_0
	v_exp_f16_sdwa v114, v110 dst_sel:WORD_1 dst_unused:UNUSED_PRESERVE src0_sel:WORD_1
	v_exp_f16_sdwa v115, v111 dst_sel:WORD_1 dst_unused:UNUSED_PRESERVE src0_sel:WORD_1
	v_exp_f16_sdwa v116, v112 dst_sel:WORD_1 dst_unused:UNUSED_PRESERVE src0_sel:WORD_1
	v_exp_f16_sdwa v117, v113 dst_sel:WORD_1 dst_unused:UNUSED_PRESERVE src0_sel:WORD_1
	v_pk_add_f16 v110, v186, v198 neg_lo:[0,1] neg_hi:[0,1]
	v_pk_add_f16 v101, v101, v114
	v_pk_add_f16 v100, v100, v115
	v_pk_add_f16 v99, v99, v116
	v_pk_add_f16 v98, v98, v117
	v_pk_fma_f16 v70, v30, v114, v70
	v_pk_fma_f16 v71, v31, v115, v71
	v_pk_fma_f16 v72, v32, v116, v72
	v_pk_fma_f16 v73, v33, v117, v73
	v_pk_add_f16 v111, v187, v199 neg_lo:[0,1] neg_hi:[0,1]
	v_pk_add_f16 v112, v188, v200 neg_lo:[0,1] neg_hi:[0,1]
	v_pk_add_f16 v113, v189, v201 neg_lo:[0,1] neg_hi:[0,1]
	v_exp_f16_sdwa v114, v110 dst_sel:WORD_0 dst_unused:UNUSED_PAD src0_sel:WORD_0
	v_exp_f16_sdwa v115, v111 dst_sel:WORD_0 dst_unused:UNUSED_PAD src0_sel:WORD_0
	v_exp_f16_sdwa v116, v112 dst_sel:WORD_0 dst_unused:UNUSED_PAD src0_sel:WORD_0
	v_exp_f16_sdwa v117, v113 dst_sel:WORD_0 dst_unused:UNUSED_PAD src0_sel:WORD_0
	v_exp_f16_sdwa v114, v110 dst_sel:WORD_1 dst_unused:UNUSED_PRESERVE src0_sel:WORD_1
	v_exp_f16_sdwa v115, v111 dst_sel:WORD_1 dst_unused:UNUSED_PRESERVE src0_sel:WORD_1
	v_exp_f16_sdwa v116, v112 dst_sel:WORD_1 dst_unused:UNUSED_PRESERVE src0_sel:WORD_1
	v_exp_f16_sdwa v117, v113 dst_sel:WORD_1 dst_unused:UNUSED_PRESERVE src0_sel:WORD_1
	v_pk_add_f16 v101, v101, v114
	v_pk_add_f16 v100, v100, v115
	v_rcp_f16_e32 v110, v101
	v_rcp_f16_sdwa v101, v101 dst_sel:DWORD dst_unused:UNUSED_PAD src0_sel:WORD_1
	v_pk_add_f16 v99, v99, v116
	v_rcp_f16_e32 v111, v100
	v_rcp_f16_sdwa v100, v100 dst_sel:DWORD dst_unused:UNUSED_PAD src0_sel:WORD_1
	v_pk_add_f16 v98, v98, v117
	v_rcp_f16_e32 v112, v99
	v_rcp_f16_sdwa v99, v99 dst_sel:DWORD dst_unused:UNUSED_PAD src0_sel:WORD_1
	v_rcp_f16_e32 v113, v98
	v_rcp_f16_sdwa v98, v98 dst_sel:DWORD dst_unused:UNUSED_PAD src0_sel:WORD_1
	v_pk_fma_f16 v70, v46, v114, v70
	v_pack_b32_f16 v101, v110, v101
	v_pk_fma_f16 v71, v47, v115, v71
	v_pk_mul_f16 v110, v70, v101
	v_pack_b32_f16 v70, v111, v100
	v_pk_fma_f16 v72, v48, v116, v72
	v_pk_mul_f16 v111, v71, v70
	v_pack_b32_f16 v70, v112, v99
	v_pk_fma_f16 v73, v49, v117, v73
	v_pk_mul_f16 v112, v72, v70
	v_pack_b32_f16 v70, v113, v98
	v_pk_mul_f16 v113, v73, v70
	s_waitcnt vmcnt(12)
	v_pk_mul_f16 v73, v185, v157 op_sel_hi:[0,1]
	v_pk_mul_f16 v101, v183, v157 op_sel_hi:[0,1]
	v_pk_mul_f16 v117, v184, v157 op_sel_hi:[0,1]
	v_pk_mul_f16 v70, v185, v154 op_sel_hi:[0,1]
	v_pk_mul_f16 v71, v185, v155 op_sel_hi:[0,1]
	v_pk_mul_f16 v72, v185, v156 op_sel_hi:[0,1]
	v_pk_mul_f16 v98, v183, v154 op_sel_hi:[0,1]
	v_pk_mul_f16 v99, v183, v155 op_sel_hi:[0,1]
	v_pk_mul_f16 v100, v183, v156 op_sel_hi:[0,1]
	v_pk_mul_f16 v114, v184, v154 op_sel_hi:[0,1]
	v_pk_mul_f16 v115, v184, v155 op_sel_hi:[0,1]
	v_pk_mul_f16 v116, v184, v156 op_sel_hi:[0,1]
	v_pk_fma_f16 v85, v85, v157, v73
	v_pk_fma_f16 v109, v109, v157, v101
	v_pk_fma_f16 v125, v125, v157, v117
	v_pk_fma_f16 v126, v53, v157, v73
	v_pk_fma_f16 v134, v69, v157, v101
	v_pk_fma_f16 v186, v97, v157, v117
	v_pk_fma_f16 v73, v21, v157, v73
	v_pk_fma_f16 v101, v37, v157, v101
	v_pk_fma_f16 v117, v57, v157, v117
	v_pk_maximum3_f16 v157, v85, v109, v125
	v_pk_fma_f16 v84, v84, v156, v72
	v_pk_fma_f16 v83, v83, v155, v71
	v_pk_fma_f16 v82, v82, v154, v70
	v_pk_fma_f16 v108, v108, v156, v100
	v_pk_fma_f16 v107, v107, v155, v99
	v_pk_fma_f16 v106, v106, v154, v98
	v_pk_fma_f16 v124, v124, v156, v116
	v_pk_fma_f16 v123, v123, v155, v115
	v_pk_fma_f16 v122, v122, v154, v114
	v_pk_fma_f16 v127, v52, v156, v72
	v_pk_fma_f16 v128, v51, v155, v71
	v_pk_fma_f16 v129, v50, v154, v70
	v_pk_fma_f16 v135, v68, v156, v100
	v_pk_fma_f16 v136, v67, v155, v99
	v_pk_fma_f16 v137, v66, v154, v98
	v_pk_fma_f16 v187, v96, v156, v116
	v_pk_fma_f16 v188, v95, v155, v115
	v_pk_fma_f16 v189, v94, v154, v114
	v_pk_fma_f16 v72, v20, v156, v72
	v_pk_fma_f16 v71, v19, v155, v71
	v_pk_fma_f16 v70, v18, v154, v70
	v_pk_fma_f16 v100, v36, v156, v100
	v_pk_fma_f16 v99, v35, v155, v99
	v_pk_fma_f16 v98, v34, v154, v98
	v_pk_fma_f16 v116, v56, v156, v116
	v_pk_fma_f16 v115, v55, v155, v115
	v_pk_fma_f16 v114, v54, v154, v114
	v_pk_maximum3_f16 v154, v82, v106, v122
	v_pk_maximum3_f16 v155, v83, v107, v123
	v_pk_maximum3_f16 v156, v84, v108, v124
	v_pk_maximum3_f16 v193, v126, v134, v186
	v_pk_maximum3_f16 v197, v73, v101, v117
	v_pk_maximum3_f16 v190, v129, v137, v189
	v_pk_maximum3_f16 v191, v128, v136, v188
	v_pk_maximum3_f16 v192, v127, v135, v187
	v_pk_maximum3_f16 v194, v70, v98, v114
	v_pk_maximum3_f16 v195, v71, v99, v115
	v_pk_maximum3_f16 v157, v157, v193, v197
	v_pk_maximum3_f16 v196, v72, v100, v116
	v_pk_maximum3_f16 v154, v154, v190, v194
	v_pk_maximum3_f16 v155, v155, v191, v195
	v_pk_maximum3_f16 v156, v156, v192, v196
	v_pk_add_f16 v85, v85, v157 neg_lo:[0,1] neg_hi:[0,1]
	v_pk_add_f16 v82, v82, v154 neg_lo:[0,1] neg_hi:[0,1]
	v_pk_add_f16 v83, v83, v155 neg_lo:[0,1] neg_hi:[0,1]
	v_pk_add_f16 v84, v84, v156 neg_lo:[0,1] neg_hi:[0,1]
	v_pk_add_f16 v106, v106, v154 neg_lo:[0,1] neg_hi:[0,1]
	v_exp_f16_sdwa v190, v82 dst_sel:WORD_0 dst_unused:UNUSED_PAD src0_sel:WORD_0
	v_exp_f16_sdwa v191, v83 dst_sel:WORD_0 dst_unused:UNUSED_PAD src0_sel:WORD_0
	v_exp_f16_sdwa v192, v84 dst_sel:WORD_0 dst_unused:UNUSED_PAD src0_sel:WORD_0
	v_exp_f16_sdwa v193, v85 dst_sel:WORD_0 dst_unused:UNUSED_PAD src0_sel:WORD_0
	v_exp_f16_sdwa v190, v82 dst_sel:WORD_1 dst_unused:UNUSED_PRESERVE src0_sel:WORD_1
	v_exp_f16_sdwa v191, v83 dst_sel:WORD_1 dst_unused:UNUSED_PRESERVE src0_sel:WORD_1
	v_exp_f16_sdwa v192, v84 dst_sel:WORD_1 dst_unused:UNUSED_PRESERVE src0_sel:WORD_1
	v_exp_f16_sdwa v193, v85 dst_sel:WORD_1 dst_unused:UNUSED_PRESERVE src0_sel:WORD_1
	v_pk_add_f16 v107, v107, v155 neg_lo:[0,1] neg_hi:[0,1]
	v_pk_add_f16 v85, v190, 0
	v_pk_fma_f16 v45, v45, v193, 0
	v_pk_add_f16 v82, v193, 0
	v_pk_add_f16 v83, v192, 0
	v_pk_add_f16 v84, v191, 0
	v_pk_fma_f16 v44, v44, v192, 0
	v_pk_fma_f16 v43, v43, v191, 0
	v_pk_fma_f16 v42, v42, v190, 0
	v_pk_add_f16 v108, v108, v156 neg_lo:[0,1] neg_hi:[0,1]
	v_pk_add_f16 v109, v109, v157 neg_lo:[0,1] neg_hi:[0,1]
	v_pk_add_f16 v70, v70, v154 neg_lo:[0,1] neg_hi:[0,1]
	v_exp_f16_sdwa v190, v106 dst_sel:WORD_0 dst_unused:UNUSED_PAD src0_sel:WORD_0
	v_exp_f16_sdwa v191, v107 dst_sel:WORD_0 dst_unused:UNUSED_PAD src0_sel:WORD_0
	v_exp_f16_sdwa v192, v108 dst_sel:WORD_0 dst_unused:UNUSED_PAD src0_sel:WORD_0
	v_exp_f16_sdwa v193, v109 dst_sel:WORD_0 dst_unused:UNUSED_PAD src0_sel:WORD_0
	v_exp_f16_sdwa v190, v106 dst_sel:WORD_1 dst_unused:UNUSED_PRESERVE src0_sel:WORD_1
	v_exp_f16_sdwa v191, v107 dst_sel:WORD_1 dst_unused:UNUSED_PRESERVE src0_sel:WORD_1
	v_exp_f16_sdwa v192, v108 dst_sel:WORD_1 dst_unused:UNUSED_PRESERVE src0_sel:WORD_1
	v_exp_f16_sdwa v193, v109 dst_sel:WORD_1 dst_unused:UNUSED_PRESERVE src0_sel:WORD_1
	v_pk_add_f16 v71, v71, v155 neg_lo:[0,1] neg_hi:[0,1]
	v_pk_add_f16 v85, v85, v190
	v_pk_fma_f16 v45, v65, v193, v45
	v_pk_add_f16 v65, v125, v157 neg_lo:[0,1] neg_hi:[0,1]
	v_pk_add_f16 v84, v84, v191
	v_pk_add_f16 v83, v83, v192
	v_pk_add_f16 v82, v82, v193
	v_pk_fma_f16 v42, v62, v190, v42
	v_pk_fma_f16 v43, v63, v191, v43
	v_pk_fma_f16 v44, v64, v192, v44
	v_pk_add_f16 v62, v122, v154 neg_lo:[0,1] neg_hi:[0,1]
	v_pk_add_f16 v63, v123, v155 neg_lo:[0,1] neg_hi:[0,1]
	v_pk_add_f16 v64, v124, v156 neg_lo:[0,1] neg_hi:[0,1]
	v_pk_add_f16 v72, v72, v156 neg_lo:[0,1] neg_hi:[0,1]
	v_exp_f16_sdwa v106, v62 dst_sel:WORD_0 dst_unused:UNUSED_PAD src0_sel:WORD_0
	v_exp_f16_sdwa v107, v63 dst_sel:WORD_0 dst_unused:UNUSED_PAD src0_sel:WORD_0
	v_exp_f16_sdwa v108, v64 dst_sel:WORD_0 dst_unused:UNUSED_PAD src0_sel:WORD_0
	v_exp_f16_sdwa v109, v65 dst_sel:WORD_0 dst_unused:UNUSED_PAD src0_sel:WORD_0
	v_exp_f16_sdwa v106, v62 dst_sel:WORD_1 dst_unused:UNUSED_PRESERVE src0_sel:WORD_1
	v_exp_f16_sdwa v107, v63 dst_sel:WORD_1 dst_unused:UNUSED_PRESERVE src0_sel:WORD_1
	v_exp_f16_sdwa v108, v64 dst_sel:WORD_1 dst_unused:UNUSED_PRESERVE src0_sel:WORD_1
	v_exp_f16_sdwa v109, v65 dst_sel:WORD_1 dst_unused:UNUSED_PRESERVE src0_sel:WORD_1
	v_pk_add_f16 v73, v73, v157 neg_lo:[0,1] neg_hi:[0,1]
	v_pk_add_f16 v65, v85, v106
	v_pk_add_f16 v62, v82, v109
	v_pk_add_f16 v63, v83, v108
	v_pk_add_f16 v64, v84, v107
	v_pk_fma_f16 v45, v89, v109, v45
	v_pk_fma_f16 v44, v88, v108, v44
	v_pk_fma_f16 v43, v87, v107, v43
	v_pk_fma_f16 v42, v86, v106, v42
	v_pk_add_f16 v82, v129, v154 neg_lo:[0,1] neg_hi:[0,1]
	v_pk_add_f16 v83, v128, v155 neg_lo:[0,1] neg_hi:[0,1]
	v_pk_add_f16 v84, v127, v156 neg_lo:[0,1] neg_hi:[0,1]
	v_pk_add_f16 v85, v126, v157 neg_lo:[0,1] neg_hi:[0,1]
	v_exp_f16_sdwa v86, v82 dst_sel:WORD_0 dst_unused:UNUSED_PAD src0_sel:WORD_0
	v_exp_f16_sdwa v87, v83 dst_sel:WORD_0 dst_unused:UNUSED_PAD src0_sel:WORD_0
	v_exp_f16_sdwa v88, v84 dst_sel:WORD_0 dst_unused:UNUSED_PAD src0_sel:WORD_0
	v_exp_f16_sdwa v89, v85 dst_sel:WORD_0 dst_unused:UNUSED_PAD src0_sel:WORD_0
	v_exp_f16_sdwa v86, v82 dst_sel:WORD_1 dst_unused:UNUSED_PRESERVE src0_sel:WORD_1
	v_exp_f16_sdwa v87, v83 dst_sel:WORD_1 dst_unused:UNUSED_PRESERVE src0_sel:WORD_1
	v_exp_f16_sdwa v88, v84 dst_sel:WORD_1 dst_unused:UNUSED_PRESERVE src0_sel:WORD_1
	v_exp_f16_sdwa v89, v85 dst_sel:WORD_1 dst_unused:UNUSED_PRESERVE src0_sel:WORD_1
	v_pk_add_f16 v82, v137, v154 neg_lo:[0,1] neg_hi:[0,1]
	v_pk_add_f16 v65, v65, v86
	v_pk_add_f16 v64, v64, v87
	v_pk_add_f16 v63, v63, v88
	v_pk_add_f16 v62, v62, v89
	v_pk_fma_f16 v42, v22, v86, v42
	v_pk_fma_f16 v43, v23, v87, v43
	v_pk_fma_f16 v44, v24, v88, v44
	v_pk_fma_f16 v45, v25, v89, v45
	v_pk_add_f16 v83, v136, v155 neg_lo:[0,1] neg_hi:[0,1]
	v_pk_add_f16 v84, v135, v156 neg_lo:[0,1] neg_hi:[0,1]
	v_pk_add_f16 v85, v134, v157 neg_lo:[0,1] neg_hi:[0,1]
	v_exp_f16_sdwa v86, v82 dst_sel:WORD_0 dst_unused:UNUSED_PAD src0_sel:WORD_0
	v_exp_f16_sdwa v87, v83 dst_sel:WORD_0 dst_unused:UNUSED_PAD src0_sel:WORD_0
	v_exp_f16_sdwa v88, v84 dst_sel:WORD_0 dst_unused:UNUSED_PAD src0_sel:WORD_0
	v_exp_f16_sdwa v89, v85 dst_sel:WORD_0 dst_unused:UNUSED_PAD src0_sel:WORD_0
	v_exp_f16_sdwa v86, v82 dst_sel:WORD_1 dst_unused:UNUSED_PRESERVE src0_sel:WORD_1
	v_exp_f16_sdwa v87, v83 dst_sel:WORD_1 dst_unused:UNUSED_PRESERVE src0_sel:WORD_1
	v_exp_f16_sdwa v88, v84 dst_sel:WORD_1 dst_unused:UNUSED_PRESERVE src0_sel:WORD_1
	v_exp_f16_sdwa v89, v85 dst_sel:WORD_1 dst_unused:UNUSED_PRESERVE src0_sel:WORD_1
	v_pk_add_f16 v82, v189, v154 neg_lo:[0,1] neg_hi:[0,1]
	v_pk_add_f16 v65, v65, v86
	v_pk_add_f16 v62, v62, v89
	v_pk_add_f16 v63, v63, v88
	v_pk_add_f16 v64, v64, v87
	v_pk_fma_f16 v45, v33, v89, v45
	v_pk_fma_f16 v44, v32, v88, v44
	v_pk_fma_f16 v43, v31, v87, v43
	v_pk_fma_f16 v42, v30, v86, v42
	v_pk_add_f16 v83, v188, v155 neg_lo:[0,1] neg_hi:[0,1]
	v_pk_add_f16 v84, v187, v156 neg_lo:[0,1] neg_hi:[0,1]
	v_pk_add_f16 v85, v186, v157 neg_lo:[0,1] neg_hi:[0,1]
	v_exp_f16_sdwa v86, v82 dst_sel:WORD_0 dst_unused:UNUSED_PAD src0_sel:WORD_0
	v_exp_f16_sdwa v87, v83 dst_sel:WORD_0 dst_unused:UNUSED_PAD src0_sel:WORD_0
	v_exp_f16_sdwa v88, v84 dst_sel:WORD_0 dst_unused:UNUSED_PAD src0_sel:WORD_0
	v_exp_f16_sdwa v89, v85 dst_sel:WORD_0 dst_unused:UNUSED_PAD src0_sel:WORD_0
	v_exp_f16_sdwa v86, v82 dst_sel:WORD_1 dst_unused:UNUSED_PRESERVE src0_sel:WORD_1
	v_exp_f16_sdwa v87, v83 dst_sel:WORD_1 dst_unused:UNUSED_PRESERVE src0_sel:WORD_1
	v_exp_f16_sdwa v88, v84 dst_sel:WORD_1 dst_unused:UNUSED_PRESERVE src0_sel:WORD_1
	v_exp_f16_sdwa v89, v85 dst_sel:WORD_1 dst_unused:UNUSED_PRESERVE src0_sel:WORD_1
	v_exp_f16_sdwa v82, v70 dst_sel:WORD_0 dst_unused:UNUSED_PAD src0_sel:WORD_0
	v_exp_f16_sdwa v83, v71 dst_sel:WORD_0 dst_unused:UNUSED_PAD src0_sel:WORD_0
	v_exp_f16_sdwa v84, v72 dst_sel:WORD_0 dst_unused:UNUSED_PAD src0_sel:WORD_0
	v_exp_f16_sdwa v85, v73 dst_sel:WORD_0 dst_unused:UNUSED_PAD src0_sel:WORD_0
	v_exp_f16_sdwa v82, v70 dst_sel:WORD_1 dst_unused:UNUSED_PRESERVE src0_sel:WORD_1
	v_exp_f16_sdwa v83, v71 dst_sel:WORD_1 dst_unused:UNUSED_PRESERVE src0_sel:WORD_1
	v_exp_f16_sdwa v84, v72 dst_sel:WORD_1 dst_unused:UNUSED_PRESERVE src0_sel:WORD_1
	v_exp_f16_sdwa v85, v73 dst_sel:WORD_1 dst_unused:UNUSED_PRESERVE src0_sel:WORD_1
	v_pk_add_f16 v70, v98, v154 neg_lo:[0,1] neg_hi:[0,1]
	v_pk_add_f16 v65, v65, v86
	v_pk_add_f16 v64, v64, v87
	v_pk_add_f16 v63, v63, v88
	v_pk_add_f16 v62, v62, v89
	v_pk_fma_f16 v42, v46, v86, v42
	v_pk_fma_f16 v43, v47, v87, v43
	v_pk_fma_f16 v44, v48, v88, v44
	v_pk_fma_f16 v45, v49, v89, v45
	v_pk_add_f16 v65, v65, v82
	v_pk_add_f16 v62, v62, v85
	v_pk_add_f16 v63, v63, v84
	v_pk_add_f16 v64, v64, v83
	v_pk_fma_f16 v45, v9, v85, v45
	v_pk_fma_f16 v44, v8, v84, v44
	v_pk_fma_f16 v43, v7, v83, v43
	v_pk_fma_f16 v42, v6, v82, v42
	v_pk_add_f16 v71, v99, v155 neg_lo:[0,1] neg_hi:[0,1]
	v_pk_add_f16 v72, v100, v156 neg_lo:[0,1] neg_hi:[0,1]
	v_pk_add_f16 v73, v101, v157 neg_lo:[0,1] neg_hi:[0,1]
	v_exp_f16_sdwa v82, v70 dst_sel:WORD_0 dst_unused:UNUSED_PAD src0_sel:WORD_0
	v_exp_f16_sdwa v83, v71 dst_sel:WORD_0 dst_unused:UNUSED_PAD src0_sel:WORD_0
	v_exp_f16_sdwa v84, v72 dst_sel:WORD_0 dst_unused:UNUSED_PAD src0_sel:WORD_0
	v_exp_f16_sdwa v85, v73 dst_sel:WORD_0 dst_unused:UNUSED_PAD src0_sel:WORD_0
	v_exp_f16_sdwa v82, v70 dst_sel:WORD_1 dst_unused:UNUSED_PRESERVE src0_sel:WORD_1
	v_exp_f16_sdwa v83, v71 dst_sel:WORD_1 dst_unused:UNUSED_PRESERVE src0_sel:WORD_1
	v_exp_f16_sdwa v84, v72 dst_sel:WORD_1 dst_unused:UNUSED_PRESERVE src0_sel:WORD_1
	v_exp_f16_sdwa v85, v73 dst_sel:WORD_1 dst_unused:UNUSED_PRESERVE src0_sel:WORD_1
	v_pk_add_f16 v70, v114, v154 neg_lo:[0,1] neg_hi:[0,1]
	v_pk_add_f16 v65, v65, v82
	v_pk_add_f16 v64, v64, v83
	v_pk_add_f16 v63, v63, v84
	v_pk_add_f16 v62, v62, v85
	v_pk_fma_f16 v42, v10, v82, v42
	v_pk_fma_f16 v43, v11, v83, v43
	v_pk_fma_f16 v44, v12, v84, v44
	v_pk_fma_f16 v45, v13, v85, v45
	v_pk_add_f16 v71, v115, v155 neg_lo:[0,1] neg_hi:[0,1]
	v_pk_add_f16 v72, v116, v156 neg_lo:[0,1] neg_hi:[0,1]
	v_pk_add_f16 v73, v117, v157 neg_lo:[0,1] neg_hi:[0,1]
	v_exp_f16_sdwa v82, v70 dst_sel:WORD_0 dst_unused:UNUSED_PAD src0_sel:WORD_0
	v_exp_f16_sdwa v83, v71 dst_sel:WORD_0 dst_unused:UNUSED_PAD src0_sel:WORD_0
	v_exp_f16_sdwa v84, v72 dst_sel:WORD_0 dst_unused:UNUSED_PAD src0_sel:WORD_0
	v_exp_f16_sdwa v85, v73 dst_sel:WORD_0 dst_unused:UNUSED_PAD src0_sel:WORD_0
	v_exp_f16_sdwa v82, v70 dst_sel:WORD_1 dst_unused:UNUSED_PRESERVE src0_sel:WORD_1
	v_exp_f16_sdwa v83, v71 dst_sel:WORD_1 dst_unused:UNUSED_PRESERVE src0_sel:WORD_1
	v_exp_f16_sdwa v84, v72 dst_sel:WORD_1 dst_unused:UNUSED_PRESERVE src0_sel:WORD_1
	v_exp_f16_sdwa v85, v73 dst_sel:WORD_1 dst_unused:UNUSED_PRESERVE src0_sel:WORD_1
	v_pk_add_f16 v65, v65, v82
	v_pk_add_f16 v64, v64, v83
	v_rcp_f16_e32 v70, v65
	v_rcp_f16_sdwa v65, v65 dst_sel:DWORD dst_unused:UNUSED_PAD src0_sel:WORD_1
	v_pk_add_f16 v63, v63, v84
	v_rcp_f16_e32 v71, v64
	v_rcp_f16_sdwa v64, v64 dst_sel:DWORD dst_unused:UNUSED_PAD src0_sel:WORD_1
	v_pk_add_f16 v62, v62, v85
	v_rcp_f16_e32 v72, v63
	v_rcp_f16_sdwa v73, v63 dst_sel:DWORD dst_unused:UNUSED_PAD src0_sel:WORD_1
	v_pk_fma_f16 v43, v15, v83, v43
	v_pk_fma_f16 v42, v14, v82, v42
	v_rcp_f16_e32 v82, v62
	v_rcp_f16_sdwa v83, v62 dst_sel:DWORD dst_unused:UNUSED_PAD src0_sel:WORD_1
	v_pack_b32_f16 v62, v70, v65
	v_pk_mul_f16 v62, v42, v62
	v_pack_b32_f16 v42, v71, v64
	v_pk_fma_f16 v44, v16, v84, v44
	v_pk_mul_f16 v63, v43, v42
	v_pack_b32_f16 v42, v72, v73
	v_pk_fma_f16 v45, v17, v85, v45
	v_pk_mul_f16 v64, v44, v42
	v_pack_b32_f16 v42, v82, v83
	v_pk_mul_f16 v65, v45, v42
	s_waitcnt vmcnt(6)
	v_pk_mul_f16 v42, v185, v150 op_sel_hi:[0,1]
	v_pk_mul_f16 v70, v183, v150 op_sel_hi:[0,1]
	v_pk_mul_f16 v82, v184, v150 op_sel_hi:[0,1]
	v_pk_mul_f16 v43, v185, v151 op_sel_hi:[0,1]
	v_pk_mul_f16 v44, v185, v152 op_sel_hi:[0,1]
	v_pk_mul_f16 v45, v185, v153 op_sel_hi:[0,1]
	v_pk_mul_f16 v71, v183, v151 op_sel_hi:[0,1]
	v_pk_mul_f16 v72, v183, v152 op_sel_hi:[0,1]
	v_pk_mul_f16 v73, v183, v153 op_sel_hi:[0,1]
	v_pk_mul_f16 v83, v184, v151 op_sel_hi:[0,1]
	v_pk_mul_f16 v84, v184, v152 op_sel_hi:[0,1]
	v_pk_mul_f16 v85, v184, v153 op_sel_hi:[0,1]
	v_pk_fma_f16 v50, v50, v150, v42
	v_pk_fma_f16 v66, v66, v150, v70
	v_pk_fma_f16 v89, v94, v150, v82
	v_pk_fma_f16 v53, v53, v153, v45
	v_pk_maximum3_f16 v114, v50, v66, v89
	v_pk_fma_f16 v52, v52, v152, v44
	v_pk_fma_f16 v51, v51, v151, v43
	v_pk_fma_f16 v69, v69, v153, v73
	v_pk_fma_f16 v68, v68, v152, v72
	v_pk_fma_f16 v67, v67, v151, v71
	v_pk_fma_f16 v86, v97, v153, v85
	v_pk_fma_f16 v87, v96, v152, v84
	v_pk_fma_f16 v88, v95, v151, v83
	v_pk_fma_f16 v97, v18, v150, v42
	v_pk_fma_f16 v101, v34, v150, v70
	v_pk_fma_f16 v109, v54, v150, v82
	v_pk_fma_f16 v42, v74, v150, v42
	v_pk_fma_f16 v70, v102, v150, v70
	v_pk_fma_f16 v82, v118, v150, v82
	v_pk_maximum3_f16 v115, v51, v67, v88
	v_pk_maximum3_f16 v116, v52, v68, v87
	v_pk_maximum3_f16 v117, v53, v69, v86
	v_pk_maximum3_f16 v122, v97, v101, v109
	v_pk_fma_f16 v94, v21, v153, v45
	v_pk_maximum3_f16 v126, v42, v70, v82
	v_pk_fma_f16 v95, v20, v152, v44
	v_pk_maximum3_f16 v114, v114, v122, v126
	v_pk_fma_f16 v96, v19, v151, v43
	v_pk_fma_f16 v98, v37, v153, v73
	v_pk_fma_f16 v99, v36, v152, v72
	v_pk_fma_f16 v100, v35, v151, v71
	v_pk_fma_f16 v106, v57, v153, v85
	v_pk_fma_f16 v107, v56, v152, v84
	v_pk_fma_f16 v108, v55, v151, v83
	v_pk_fma_f16 v45, v77, v153, v45
	v_pk_fma_f16 v44, v76, v152, v44
	v_pk_fma_f16 v43, v75, v151, v43
	v_pk_fma_f16 v73, v105, v153, v73
	v_pk_fma_f16 v72, v104, v152, v72
	v_pk_fma_f16 v71, v103, v151, v71
	v_pk_fma_f16 v85, v121, v153, v85
	v_pk_fma_f16 v84, v120, v152, v84
	v_pk_fma_f16 v83, v119, v151, v83
	v_pk_maximum3_f16 v123, v96, v100, v108
	v_pk_maximum3_f16 v124, v95, v99, v107
	v_pk_maximum3_f16 v125, v94, v98, v106
	v_pk_maximum3_f16 v128, v44, v72, v84
	v_pk_maximum3_f16 v129, v45, v73, v85
	v_pk_maximum3_f16 v127, v43, v71, v83
	v_pk_maximum3_f16 v115, v115, v123, v127
	v_pk_maximum3_f16 v116, v116, v124, v128
	v_pk_maximum3_f16 v117, v117, v125, v129
	v_pk_add_f16 v50, v50, v114 neg_lo:[0,1] neg_hi:[0,1]
	v_pk_add_f16 v51, v51, v115 neg_lo:[0,1] neg_hi:[0,1]
	v_pk_add_f16 v52, v52, v116 neg_lo:[0,1] neg_hi:[0,1]
	v_pk_add_f16 v53, v53, v117 neg_lo:[0,1] neg_hi:[0,1]
	v_pk_add_f16 v66, v66, v114 neg_lo:[0,1] neg_hi:[0,1]
	v_exp_f16_sdwa v122, v50 dst_sel:WORD_0 dst_unused:UNUSED_PAD src0_sel:WORD_0
	v_exp_f16_sdwa v123, v51 dst_sel:WORD_0 dst_unused:UNUSED_PAD src0_sel:WORD_0
	v_exp_f16_sdwa v124, v52 dst_sel:WORD_0 dst_unused:UNUSED_PAD src0_sel:WORD_0
	v_exp_f16_sdwa v125, v53 dst_sel:WORD_0 dst_unused:UNUSED_PAD src0_sel:WORD_0
	v_exp_f16_sdwa v122, v50 dst_sel:WORD_1 dst_unused:UNUSED_PRESERVE src0_sel:WORD_1
	v_exp_f16_sdwa v123, v51 dst_sel:WORD_1 dst_unused:UNUSED_PRESERVE src0_sel:WORD_1
	v_exp_f16_sdwa v124, v52 dst_sel:WORD_1 dst_unused:UNUSED_PRESERVE src0_sel:WORD_1
	v_exp_f16_sdwa v125, v53 dst_sel:WORD_1 dst_unused:UNUSED_PRESERVE src0_sel:WORD_1
	v_pk_add_f16 v67, v67, v115 neg_lo:[0,1] neg_hi:[0,1]
	v_pk_add_f16 v50, v125, 0
	v_pk_fma_f16 v22, v22, v122, 0
	v_pk_add_f16 v51, v124, 0
	v_pk_add_f16 v52, v123, 0
	v_pk_add_f16 v53, v122, 0
	v_pk_fma_f16 v23, v23, v123, 0
	v_pk_fma_f16 v24, v24, v124, 0
	v_pk_fma_f16 v25, v25, v125, 0
	v_pk_add_f16 v68, v68, v116 neg_lo:[0,1] neg_hi:[0,1]
	v_pk_add_f16 v69, v69, v117 neg_lo:[0,1] neg_hi:[0,1]
	v_pk_add_f16 v42, v42, v114 neg_lo:[0,1] neg_hi:[0,1]
	v_exp_f16_sdwa v122, v66 dst_sel:WORD_0 dst_unused:UNUSED_PAD src0_sel:WORD_0
	v_exp_f16_sdwa v123, v67 dst_sel:WORD_0 dst_unused:UNUSED_PAD src0_sel:WORD_0
	v_exp_f16_sdwa v124, v68 dst_sel:WORD_0 dst_unused:UNUSED_PAD src0_sel:WORD_0
	v_exp_f16_sdwa v125, v69 dst_sel:WORD_0 dst_unused:UNUSED_PAD src0_sel:WORD_0
	v_exp_f16_sdwa v122, v66 dst_sel:WORD_1 dst_unused:UNUSED_PRESERVE src0_sel:WORD_1
	v_exp_f16_sdwa v123, v67 dst_sel:WORD_1 dst_unused:UNUSED_PRESERVE src0_sel:WORD_1
	v_exp_f16_sdwa v124, v68 dst_sel:WORD_1 dst_unused:UNUSED_PRESERVE src0_sel:WORD_1
	v_exp_f16_sdwa v125, v69 dst_sel:WORD_1 dst_unused:UNUSED_PRESERVE src0_sel:WORD_1
	v_pk_add_f16 v43, v43, v115 neg_lo:[0,1] neg_hi:[0,1]
	v_pk_add_f16 v50, v50, v125
	v_pk_fma_f16 v22, v30, v122, v22
	v_pk_add_f16 v30, v89, v114 neg_lo:[0,1] neg_hi:[0,1]
	v_pk_add_f16 v53, v53, v122
	v_pk_add_f16 v52, v52, v123
	v_pk_add_f16 v51, v51, v124
	v_pk_fma_f16 v25, v33, v125, v25
	v_pk_fma_f16 v24, v32, v124, v24
	v_pk_fma_f16 v23, v31, v123, v23
	v_pk_add_f16 v31, v88, v115 neg_lo:[0,1] neg_hi:[0,1]
	v_pk_add_f16 v32, v87, v116 neg_lo:[0,1] neg_hi:[0,1]
	v_pk_add_f16 v33, v86, v117 neg_lo:[0,1] neg_hi:[0,1]
	v_pk_add_f16 v44, v44, v116 neg_lo:[0,1] neg_hi:[0,1]
	v_exp_f16_sdwa v66, v30 dst_sel:WORD_0 dst_unused:UNUSED_PAD src0_sel:WORD_0
	v_exp_f16_sdwa v67, v31 dst_sel:WORD_0 dst_unused:UNUSED_PAD src0_sel:WORD_0
	v_exp_f16_sdwa v68, v32 dst_sel:WORD_0 dst_unused:UNUSED_PAD src0_sel:WORD_0
	v_exp_f16_sdwa v69, v33 dst_sel:WORD_0 dst_unused:UNUSED_PAD src0_sel:WORD_0
	v_exp_f16_sdwa v66, v30 dst_sel:WORD_1 dst_unused:UNUSED_PRESERVE src0_sel:WORD_1
	v_exp_f16_sdwa v67, v31 dst_sel:WORD_1 dst_unused:UNUSED_PRESERVE src0_sel:WORD_1
	v_exp_f16_sdwa v68, v32 dst_sel:WORD_1 dst_unused:UNUSED_PRESERVE src0_sel:WORD_1
	v_exp_f16_sdwa v69, v33 dst_sel:WORD_1 dst_unused:UNUSED_PRESERVE src0_sel:WORD_1
	v_pk_add_f16 v45, v45, v117 neg_lo:[0,1] neg_hi:[0,1]
	v_pk_add_f16 v30, v50, v69
	v_pk_add_f16 v31, v51, v68
	v_pk_add_f16 v32, v52, v67
	v_pk_add_f16 v33, v53, v66
	v_pk_fma_f16 v22, v46, v66, v22
	v_pk_fma_f16 v23, v47, v67, v23
	v_pk_fma_f16 v24, v48, v68, v24
	v_pk_fma_f16 v25, v49, v69, v25
	v_pk_add_f16 v46, v97, v114 neg_lo:[0,1] neg_hi:[0,1]
	v_pk_add_f16 v47, v96, v115 neg_lo:[0,1] neg_hi:[0,1]
	v_pk_add_f16 v48, v95, v116 neg_lo:[0,1] neg_hi:[0,1]
	v_pk_add_f16 v49, v94, v117 neg_lo:[0,1] neg_hi:[0,1]
	v_exp_f16_sdwa v50, v46 dst_sel:WORD_0 dst_unused:UNUSED_PAD src0_sel:WORD_0
	v_exp_f16_sdwa v51, v47 dst_sel:WORD_0 dst_unused:UNUSED_PAD src0_sel:WORD_0
	v_exp_f16_sdwa v52, v48 dst_sel:WORD_0 dst_unused:UNUSED_PAD src0_sel:WORD_0
	v_exp_f16_sdwa v53, v49 dst_sel:WORD_0 dst_unused:UNUSED_PAD src0_sel:WORD_0
	v_exp_f16_sdwa v50, v46 dst_sel:WORD_1 dst_unused:UNUSED_PRESERVE src0_sel:WORD_1
	v_exp_f16_sdwa v51, v47 dst_sel:WORD_1 dst_unused:UNUSED_PRESERVE src0_sel:WORD_1
	v_exp_f16_sdwa v52, v48 dst_sel:WORD_1 dst_unused:UNUSED_PRESERVE src0_sel:WORD_1
	v_exp_f16_sdwa v53, v49 dst_sel:WORD_1 dst_unused:UNUSED_PRESERVE src0_sel:WORD_1
	v_pk_add_f16 v46, v101, v114 neg_lo:[0,1] neg_hi:[0,1]
	v_pk_add_f16 v30, v30, v53
	v_pk_add_f16 v33, v33, v50
	v_pk_add_f16 v32, v32, v51
	v_pk_add_f16 v31, v31, v52
	v_pk_fma_f16 v25, v9, v53, v25
	v_pk_fma_f16 v24, v8, v52, v24
	v_pk_fma_f16 v23, v7, v51, v23
	v_pk_fma_f16 v22, v6, v50, v22
	v_pk_add_f16 v47, v100, v115 neg_lo:[0,1] neg_hi:[0,1]
	v_pk_add_f16 v48, v99, v116 neg_lo:[0,1] neg_hi:[0,1]
	v_pk_add_f16 v49, v98, v117 neg_lo:[0,1] neg_hi:[0,1]
	v_exp_f16_sdwa v50, v46 dst_sel:WORD_0 dst_unused:UNUSED_PAD src0_sel:WORD_0
	v_exp_f16_sdwa v51, v47 dst_sel:WORD_0 dst_unused:UNUSED_PAD src0_sel:WORD_0
	v_exp_f16_sdwa v52, v48 dst_sel:WORD_0 dst_unused:UNUSED_PAD src0_sel:WORD_0
	v_exp_f16_sdwa v53, v49 dst_sel:WORD_0 dst_unused:UNUSED_PAD src0_sel:WORD_0
	v_exp_f16_sdwa v50, v46 dst_sel:WORD_1 dst_unused:UNUSED_PRESERVE src0_sel:WORD_1
	v_exp_f16_sdwa v51, v47 dst_sel:WORD_1 dst_unused:UNUSED_PRESERVE src0_sel:WORD_1
	v_exp_f16_sdwa v52, v48 dst_sel:WORD_1 dst_unused:UNUSED_PRESERVE src0_sel:WORD_1
	v_exp_f16_sdwa v53, v49 dst_sel:WORD_1 dst_unused:UNUSED_PRESERVE src0_sel:WORD_1
	v_pk_add_f16 v46, v109, v114 neg_lo:[0,1] neg_hi:[0,1]
	v_pk_add_f16 v30, v30, v53
	v_pk_add_f16 v31, v31, v52
	v_pk_add_f16 v32, v32, v51
	v_pk_add_f16 v33, v33, v50
	v_pk_fma_f16 v22, v10, v50, v22
	v_pk_fma_f16 v23, v11, v51, v23
	v_pk_fma_f16 v24, v12, v52, v24
	v_pk_fma_f16 v25, v13, v53, v25
	v_pk_add_f16 v47, v108, v115 neg_lo:[0,1] neg_hi:[0,1]
	v_pk_add_f16 v48, v107, v116 neg_lo:[0,1] neg_hi:[0,1]
	v_pk_add_f16 v49, v106, v117 neg_lo:[0,1] neg_hi:[0,1]
	v_exp_f16_sdwa v50, v46 dst_sel:WORD_0 dst_unused:UNUSED_PAD src0_sel:WORD_0
	v_exp_f16_sdwa v51, v47 dst_sel:WORD_0 dst_unused:UNUSED_PAD src0_sel:WORD_0
	v_exp_f16_sdwa v52, v48 dst_sel:WORD_0 dst_unused:UNUSED_PAD src0_sel:WORD_0
	v_exp_f16_sdwa v53, v49 dst_sel:WORD_0 dst_unused:UNUSED_PAD src0_sel:WORD_0
	v_exp_f16_sdwa v50, v46 dst_sel:WORD_1 dst_unused:UNUSED_PRESERVE src0_sel:WORD_1
	v_exp_f16_sdwa v51, v47 dst_sel:WORD_1 dst_unused:UNUSED_PRESERVE src0_sel:WORD_1
	v_exp_f16_sdwa v52, v48 dst_sel:WORD_1 dst_unused:UNUSED_PRESERVE src0_sel:WORD_1
	v_exp_f16_sdwa v53, v49 dst_sel:WORD_1 dst_unused:UNUSED_PRESERVE src0_sel:WORD_1
	v_exp_f16_sdwa v46, v42 dst_sel:WORD_0 dst_unused:UNUSED_PAD src0_sel:WORD_0
	v_exp_f16_sdwa v47, v43 dst_sel:WORD_0 dst_unused:UNUSED_PAD src0_sel:WORD_0
	v_exp_f16_sdwa v48, v44 dst_sel:WORD_0 dst_unused:UNUSED_PAD src0_sel:WORD_0
	v_exp_f16_sdwa v49, v45 dst_sel:WORD_0 dst_unused:UNUSED_PAD src0_sel:WORD_0
	v_exp_f16_sdwa v46, v42 dst_sel:WORD_1 dst_unused:UNUSED_PRESERVE src0_sel:WORD_1
	v_exp_f16_sdwa v47, v43 dst_sel:WORD_1 dst_unused:UNUSED_PRESERVE src0_sel:WORD_1
	v_exp_f16_sdwa v48, v44 dst_sel:WORD_1 dst_unused:UNUSED_PRESERVE src0_sel:WORD_1
	v_exp_f16_sdwa v49, v45 dst_sel:WORD_1 dst_unused:UNUSED_PRESERVE src0_sel:WORD_1
	v_pk_add_f16 v42, v70, v114 neg_lo:[0,1] neg_hi:[0,1]
	v_pk_add_f16 v30, v30, v53
	v_pk_add_f16 v33, v33, v50
	v_pk_add_f16 v32, v32, v51
	v_pk_add_f16 v31, v31, v52
	v_pk_fma_f16 v25, v17, v53, v25
	v_pk_fma_f16 v24, v16, v52, v24
	v_pk_fma_f16 v23, v15, v51, v23
	v_pk_fma_f16 v22, v14, v50, v22
	v_pk_add_f16 v30, v30, v49
	v_pk_add_f16 v31, v31, v48
	v_pk_add_f16 v32, v32, v47
	v_pk_add_f16 v33, v33, v46
	v_pk_fma_f16 v22, v26, v46, v22
	v_pk_fma_f16 v23, v27, v47, v23
	v_pk_fma_f16 v24, v28, v48, v24
	v_pk_fma_f16 v25, v29, v49, v25
	v_pk_add_f16 v43, v71, v115 neg_lo:[0,1] neg_hi:[0,1]
	v_pk_add_f16 v44, v72, v116 neg_lo:[0,1] neg_hi:[0,1]
	v_pk_add_f16 v45, v73, v117 neg_lo:[0,1] neg_hi:[0,1]
	v_exp_f16_sdwa v46, v42 dst_sel:WORD_0 dst_unused:UNUSED_PAD src0_sel:WORD_0
	v_exp_f16_sdwa v47, v43 dst_sel:WORD_0 dst_unused:UNUSED_PAD src0_sel:WORD_0
	v_exp_f16_sdwa v48, v44 dst_sel:WORD_0 dst_unused:UNUSED_PAD src0_sel:WORD_0
	v_exp_f16_sdwa v49, v45 dst_sel:WORD_0 dst_unused:UNUSED_PAD src0_sel:WORD_0
	v_exp_f16_sdwa v46, v42 dst_sel:WORD_1 dst_unused:UNUSED_PRESERVE src0_sel:WORD_1
	v_exp_f16_sdwa v47, v43 dst_sel:WORD_1 dst_unused:UNUSED_PRESERVE src0_sel:WORD_1
	v_exp_f16_sdwa v48, v44 dst_sel:WORD_1 dst_unused:UNUSED_PRESERVE src0_sel:WORD_1
	v_exp_f16_sdwa v49, v45 dst_sel:WORD_1 dst_unused:UNUSED_PRESERVE src0_sel:WORD_1
	v_pk_add_f16 v42, v82, v114 neg_lo:[0,1] neg_hi:[0,1]
	v_pk_add_f16 v30, v30, v49
	v_pk_add_f16 v33, v33, v46
	v_pk_add_f16 v32, v32, v47
	v_pk_add_f16 v31, v31, v48
	v_pk_fma_f16 v25, v41, v49, v25
	v_pk_fma_f16 v24, v40, v48, v24
	v_pk_fma_f16 v23, v39, v47, v23
	v_pk_fma_f16 v22, v38, v46, v22
	v_pk_add_f16 v43, v83, v115 neg_lo:[0,1] neg_hi:[0,1]
	v_pk_add_f16 v44, v84, v116 neg_lo:[0,1] neg_hi:[0,1]
	v_pk_add_f16 v45, v85, v117 neg_lo:[0,1] neg_hi:[0,1]
	v_exp_f16_sdwa v46, v42 dst_sel:WORD_0 dst_unused:UNUSED_PAD src0_sel:WORD_0
	v_exp_f16_sdwa v47, v43 dst_sel:WORD_0 dst_unused:UNUSED_PAD src0_sel:WORD_0
	v_exp_f16_sdwa v48, v44 dst_sel:WORD_0 dst_unused:UNUSED_PAD src0_sel:WORD_0
	v_exp_f16_sdwa v49, v45 dst_sel:WORD_0 dst_unused:UNUSED_PAD src0_sel:WORD_0
	v_exp_f16_sdwa v46, v42 dst_sel:WORD_1 dst_unused:UNUSED_PRESERVE src0_sel:WORD_1
	v_exp_f16_sdwa v47, v43 dst_sel:WORD_1 dst_unused:UNUSED_PRESERVE src0_sel:WORD_1
	v_exp_f16_sdwa v48, v44 dst_sel:WORD_1 dst_unused:UNUSED_PRESERVE src0_sel:WORD_1
	v_exp_f16_sdwa v49, v45 dst_sel:WORD_1 dst_unused:UNUSED_PRESERVE src0_sel:WORD_1
	s_nop 0
	v_pk_add_f16 v30, v30, v49
	v_pk_add_f16 v31, v31, v48
	v_rcp_f16_e32 v44, v30
	v_rcp_f16_sdwa v30, v30 dst_sel:DWORD dst_unused:UNUSED_PAD src0_sel:WORD_1
	v_pk_add_f16 v32, v32, v47
	v_rcp_f16_e32 v45, v31
	v_rcp_f16_sdwa v31, v31 dst_sel:DWORD dst_unused:UNUSED_PAD src0_sel:WORD_1
	v_pk_add_f16 v33, v33, v46
	v_rcp_f16_e32 v43, v32
	v_rcp_f16_sdwa v32, v32 dst_sel:DWORD dst_unused:UNUSED_PAD src0_sel:WORD_1
	v_rcp_f16_e32 v42, v33
	v_rcp_f16_sdwa v33, v33 dst_sel:DWORD dst_unused:UNUSED_PAD src0_sel:WORD_1
	v_pk_fma_f16 v25, v61, v49, v25
	v_pack_b32_f16 v30, v44, v30
	v_pk_fma_f16 v24, v60, v48, v24
	v_pk_mul_f16 v25, v25, v30
	v_pack_b32_f16 v30, v45, v31
	v_pk_fma_f16 v23, v59, v47, v23
	v_pk_mul_f16 v24, v24, v30
	v_pack_b32_f16 v30, v43, v32
	v_pk_fma_f16 v22, v58, v46, v22
	v_pk_mul_f16 v23, v23, v30
	v_pack_b32_f16 v30, v42, v33
	v_pk_mul_f16 v22, v22, v30
	s_waitcnt vmcnt(0)
	v_pk_mul_f16 v30, v185, v146 op_sel_hi:[0,1]
	v_pk_mul_f16 v31, v185, v147 op_sel_hi:[0,1]
	v_pk_mul_f16 v32, v185, v148 op_sel_hi:[0,1]
	v_pk_mul_f16 v33, v185, v149 op_sel_hi:[0,1]
	v_pk_mul_f16 v42, v183, v146 op_sel_hi:[0,1]
	v_pk_mul_f16 v43, v183, v147 op_sel_hi:[0,1]
	v_pk_mul_f16 v44, v183, v148 op_sel_hi:[0,1]
	v_pk_mul_f16 v45, v183, v149 op_sel_hi:[0,1]
	v_pk_mul_f16 v46, v184, v146 op_sel_hi:[0,1]
	v_pk_mul_f16 v47, v184, v147 op_sel_hi:[0,1]
	v_pk_mul_f16 v48, v184, v148 op_sel_hi:[0,1]
	v_pk_mul_f16 v49, v184, v149 op_sel_hi:[0,1]
	v_pk_fma_f16 v21, v21, v149, v33
	v_pk_fma_f16 v20, v20, v148, v32
	v_pk_fma_f16 v19, v19, v147, v31
	v_pk_fma_f16 v18, v18, v146, v30
	v_pk_fma_f16 v37, v37, v149, v45
	v_pk_fma_f16 v36, v36, v148, v44
	v_pk_fma_f16 v35, v35, v147, v43
	v_pk_fma_f16 v34, v34, v146, v42
	v_pk_fma_f16 v50, v57, v149, v49
	v_pk_fma_f16 v51, v56, v148, v48
	v_pk_fma_f16 v52, v55, v147, v47
	v_pk_fma_f16 v53, v54, v146, v46
	v_pk_fma_f16 v54, v77, v149, v33
	v_pk_fma_f16 v55, v76, v148, v32
	v_pk_fma_f16 v56, v75, v147, v31
	v_pk_fma_f16 v57, v74, v146, v30
	v_pk_maximum3_f16 v74, v18, v34, v53
	v_pk_maximum3_f16 v75, v19, v35, v52
	v_pk_maximum3_f16 v76, v20, v36, v51
	v_pk_maximum3_f16 v77, v21, v37, v50
	v_pk_fma_f16 v66, v105, v149, v45
	v_pk_fma_f16 v67, v104, v148, v44
	v_pk_fma_f16 v68, v103, v147, v43
	v_pk_fma_f16 v69, v102, v146, v42
	v_pk_fma_f16 v70, v121, v149, v49
	v_pk_fma_f16 v71, v120, v148, v48
	v_pk_fma_f16 v72, v119, v147, v47
	v_pk_fma_f16 v73, v118, v146, v46
	v_pk_fma_f16 v33, v133, v149, v33
	v_pk_fma_f16 v32, v132, v148, v32
	v_pk_fma_f16 v31, v131, v147, v31
	v_pk_fma_f16 v30, v130, v146, v30
	v_pk_fma_f16 v45, v141, v149, v45
	v_pk_fma_f16 v44, v140, v148, v44
	v_pk_fma_f16 v43, v139, v147, v43
	v_pk_fma_f16 v42, v138, v146, v42
	v_pk_fma_f16 v49, v145, v149, v49
	v_pk_fma_f16 v48, v144, v148, v48
	v_pk_fma_f16 v47, v143, v147, v47
	v_pk_fma_f16 v46, v142, v146, v46
	v_pk_maximum3_f16 v82, v57, v69, v73
	v_pk_maximum3_f16 v83, v56, v68, v72
	v_pk_maximum3_f16 v84, v55, v67, v71
	v_pk_maximum3_f16 v85, v54, v66, v70
	v_pk_maximum3_f16 v87, v31, v43, v47
	v_pk_maximum3_f16 v86, v30, v42, v46
	v_pk_maximum3_f16 v88, v32, v44, v48
	v_pk_maximum3_f16 v89, v33, v45, v49
	v_pk_maximum3_f16 v74, v74, v82, v86
	v_pk_maximum3_f16 v75, v75, v83, v87
	v_pk_maximum3_f16 v76, v76, v84, v88
	v_pk_maximum3_f16 v77, v77, v85, v89
	s_nop 0
	v_pk_add_f16 v18, v18, v74 neg_lo:[0,1] neg_hi:[0,1]
	v_pk_add_f16 v19, v19, v75 neg_lo:[0,1] neg_hi:[0,1]
	v_pk_add_f16 v20, v20, v76 neg_lo:[0,1] neg_hi:[0,1]
	v_pk_add_f16 v21, v21, v77 neg_lo:[0,1] neg_hi:[0,1]
	v_pk_add_f16 v34, v34, v74 neg_lo:[0,1] neg_hi:[0,1]
	v_exp_f16_sdwa v82, v18 dst_sel:WORD_0 dst_unused:UNUSED_PAD src0_sel:WORD_0
	v_exp_f16_sdwa v83, v19 dst_sel:WORD_0 dst_unused:UNUSED_PAD src0_sel:WORD_0
	v_exp_f16_sdwa v84, v20 dst_sel:WORD_0 dst_unused:UNUSED_PAD src0_sel:WORD_0
	v_exp_f16_sdwa v85, v21 dst_sel:WORD_0 dst_unused:UNUSED_PAD src0_sel:WORD_0
	v_exp_f16_sdwa v82, v18 dst_sel:WORD_1 dst_unused:UNUSED_PRESERVE src0_sel:WORD_1
	v_exp_f16_sdwa v83, v19 dst_sel:WORD_1 dst_unused:UNUSED_PRESERVE src0_sel:WORD_1
	v_exp_f16_sdwa v84, v20 dst_sel:WORD_1 dst_unused:UNUSED_PRESERVE src0_sel:WORD_1
	v_exp_f16_sdwa v85, v21 dst_sel:WORD_1 dst_unused:UNUSED_PRESERVE src0_sel:WORD_1
	v_pk_add_f16 v35, v35, v75 neg_lo:[0,1] neg_hi:[0,1]
	v_pk_add_f16 v18, v82, 0
	v_pk_add_f16 v19, v83, 0
	v_pk_add_f16 v20, v84, 0
	v_pk_add_f16 v21, v85, 0
	v_pk_fma_f16 v6, v6, v82, 0
	v_pk_fma_f16 v7, v7, v83, 0
	v_pk_fma_f16 v8, v8, v84, 0
	v_pk_fma_f16 v9, v9, v85, 0
	v_pk_add_f16 v36, v36, v76 neg_lo:[0,1] neg_hi:[0,1]
	v_pk_add_f16 v37, v37, v77 neg_lo:[0,1] neg_hi:[0,1]
	v_exp_f16_sdwa v82, v34 dst_sel:WORD_0 dst_unused:UNUSED_PAD src0_sel:WORD_0
	v_exp_f16_sdwa v83, v35 dst_sel:WORD_0 dst_unused:UNUSED_PAD src0_sel:WORD_0
	v_exp_f16_sdwa v84, v36 dst_sel:WORD_0 dst_unused:UNUSED_PAD src0_sel:WORD_0
	v_exp_f16_sdwa v85, v37 dst_sel:WORD_0 dst_unused:UNUSED_PAD src0_sel:WORD_0
	v_exp_f16_sdwa v82, v34 dst_sel:WORD_1 dst_unused:UNUSED_PRESERVE src0_sel:WORD_1
	v_exp_f16_sdwa v83, v35 dst_sel:WORD_1 dst_unused:UNUSED_PRESERVE src0_sel:WORD_1
	v_exp_f16_sdwa v84, v36 dst_sel:WORD_1 dst_unused:UNUSED_PRESERVE src0_sel:WORD_1
	v_exp_f16_sdwa v85, v37 dst_sel:WORD_1 dst_unused:UNUSED_PRESERVE src0_sel:WORD_1
	s_nop 0
	v_pk_add_f16 v21, v21, v85
	v_pk_add_f16 v20, v20, v84
	v_pk_add_f16 v19, v19, v83
	v_pk_add_f16 v18, v18, v82
	v_pk_fma_f16 v9, v13, v85, v9
	v_pk_fma_f16 v8, v12, v84, v8
	v_pk_fma_f16 v7, v11, v83, v7
	v_pk_fma_f16 v6, v10, v82, v6
	v_pk_add_f16 v10, v53, v74 neg_lo:[0,1] neg_hi:[0,1]
	v_pk_add_f16 v11, v52, v75 neg_lo:[0,1] neg_hi:[0,1]
	v_pk_add_f16 v12, v51, v76 neg_lo:[0,1] neg_hi:[0,1]
	v_pk_add_f16 v13, v50, v77 neg_lo:[0,1] neg_hi:[0,1]
	v_exp_f16_sdwa v34, v10 dst_sel:WORD_0 dst_unused:UNUSED_PAD src0_sel:WORD_0
	v_exp_f16_sdwa v35, v11 dst_sel:WORD_0 dst_unused:UNUSED_PAD src0_sel:WORD_0
	v_exp_f16_sdwa v36, v12 dst_sel:WORD_0 dst_unused:UNUSED_PAD src0_sel:WORD_0
	v_exp_f16_sdwa v37, v13 dst_sel:WORD_0 dst_unused:UNUSED_PAD src0_sel:WORD_0
	v_exp_f16_sdwa v34, v10 dst_sel:WORD_1 dst_unused:UNUSED_PRESERVE src0_sel:WORD_1
	v_exp_f16_sdwa v35, v11 dst_sel:WORD_1 dst_unused:UNUSED_PRESERVE src0_sel:WORD_1
	v_exp_f16_sdwa v36, v12 dst_sel:WORD_1 dst_unused:UNUSED_PRESERVE src0_sel:WORD_1
	v_exp_f16_sdwa v37, v13 dst_sel:WORD_1 dst_unused:UNUSED_PRESERVE src0_sel:WORD_1
	v_pk_add_f16 v10, v18, v34
	v_pk_add_f16 v11, v19, v35
	v_pk_add_f16 v12, v20, v36
	v_pk_add_f16 v13, v21, v37
	v_pk_fma_f16 v6, v14, v34, v6
	v_pk_fma_f16 v7, v15, v35, v7
	v_pk_fma_f16 v8, v16, v36, v8
	v_pk_fma_f16 v9, v17, v37, v9
	v_pk_add_f16 v14, v57, v74 neg_lo:[0,1] neg_hi:[0,1]
	v_pk_add_f16 v15, v56, v75 neg_lo:[0,1] neg_hi:[0,1]
	v_pk_add_f16 v16, v55, v76 neg_lo:[0,1] neg_hi:[0,1]
	v_pk_add_f16 v17, v54, v77 neg_lo:[0,1] neg_hi:[0,1]
	v_exp_f16_sdwa v18, v14 dst_sel:WORD_0 dst_unused:UNUSED_PAD src0_sel:WORD_0
	v_exp_f16_sdwa v19, v15 dst_sel:WORD_0 dst_unused:UNUSED_PAD src0_sel:WORD_0
	v_exp_f16_sdwa v20, v16 dst_sel:WORD_0 dst_unused:UNUSED_PAD src0_sel:WORD_0
	v_exp_f16_sdwa v21, v17 dst_sel:WORD_0 dst_unused:UNUSED_PAD src0_sel:WORD_0
	v_exp_f16_sdwa v18, v14 dst_sel:WORD_1 dst_unused:UNUSED_PRESERVE src0_sel:WORD_1
	v_exp_f16_sdwa v19, v15 dst_sel:WORD_1 dst_unused:UNUSED_PRESERVE src0_sel:WORD_1
	v_exp_f16_sdwa v20, v16 dst_sel:WORD_1 dst_unused:UNUSED_PRESERVE src0_sel:WORD_1
	v_exp_f16_sdwa v21, v17 dst_sel:WORD_1 dst_unused:UNUSED_PRESERVE src0_sel:WORD_1
	v_pk_add_f16 v14, v69, v74 neg_lo:[0,1] neg_hi:[0,1]
	v_pk_add_f16 v13, v13, v21
	v_pk_add_f16 v12, v12, v20
	v_pk_add_f16 v11, v11, v19
	v_pk_add_f16 v10, v10, v18
	v_pk_fma_f16 v9, v29, v21, v9
	v_pk_fma_f16 v8, v28, v20, v8
	v_pk_fma_f16 v7, v27, v19, v7
	v_pk_fma_f16 v6, v26, v18, v6
	v_pk_add_f16 v15, v68, v75 neg_lo:[0,1] neg_hi:[0,1]
	v_pk_add_f16 v16, v67, v76 neg_lo:[0,1] neg_hi:[0,1]
	v_pk_add_f16 v17, v66, v77 neg_lo:[0,1] neg_hi:[0,1]
	v_exp_f16_sdwa v18, v14 dst_sel:WORD_0 dst_unused:UNUSED_PAD src0_sel:WORD_0
	v_exp_f16_sdwa v19, v15 dst_sel:WORD_0 dst_unused:UNUSED_PAD src0_sel:WORD_0
	v_exp_f16_sdwa v20, v16 dst_sel:WORD_0 dst_unused:UNUSED_PAD src0_sel:WORD_0
	v_exp_f16_sdwa v21, v17 dst_sel:WORD_0 dst_unused:UNUSED_PAD src0_sel:WORD_0
	v_exp_f16_sdwa v18, v14 dst_sel:WORD_1 dst_unused:UNUSED_PRESERVE src0_sel:WORD_1
	v_exp_f16_sdwa v19, v15 dst_sel:WORD_1 dst_unused:UNUSED_PRESERVE src0_sel:WORD_1
	v_exp_f16_sdwa v20, v16 dst_sel:WORD_1 dst_unused:UNUSED_PRESERVE src0_sel:WORD_1
	v_exp_f16_sdwa v21, v17 dst_sel:WORD_1 dst_unused:UNUSED_PRESERVE src0_sel:WORD_1
	v_pk_add_f16 v14, v73, v74 neg_lo:[0,1] neg_hi:[0,1]
	v_pk_add_f16 v10, v10, v18
	v_pk_add_f16 v11, v11, v19
	v_pk_add_f16 v12, v12, v20
	v_pk_add_f16 v13, v13, v21
	v_pk_fma_f16 v6, v38, v18, v6
	v_pk_fma_f16 v7, v39, v19, v7
	v_pk_fma_f16 v8, v40, v20, v8
	v_pk_fma_f16 v9, v41, v21, v9
	v_pk_add_f16 v15, v72, v75 neg_lo:[0,1] neg_hi:[0,1]
	v_pk_add_f16 v16, v71, v76 neg_lo:[0,1] neg_hi:[0,1]
	v_pk_add_f16 v17, v70, v77 neg_lo:[0,1] neg_hi:[0,1]
	v_exp_f16_sdwa v18, v14 dst_sel:WORD_0 dst_unused:UNUSED_PAD src0_sel:WORD_0
	v_exp_f16_sdwa v19, v15 dst_sel:WORD_0 dst_unused:UNUSED_PAD src0_sel:WORD_0
	v_exp_f16_sdwa v20, v16 dst_sel:WORD_0 dst_unused:UNUSED_PAD src0_sel:WORD_0
	v_exp_f16_sdwa v21, v17 dst_sel:WORD_0 dst_unused:UNUSED_PAD src0_sel:WORD_0
	v_exp_f16_sdwa v18, v14 dst_sel:WORD_1 dst_unused:UNUSED_PRESERVE src0_sel:WORD_1
	v_exp_f16_sdwa v19, v15 dst_sel:WORD_1 dst_unused:UNUSED_PRESERVE src0_sel:WORD_1
	v_exp_f16_sdwa v20, v16 dst_sel:WORD_1 dst_unused:UNUSED_PRESERVE src0_sel:WORD_1
	v_exp_f16_sdwa v21, v17 dst_sel:WORD_1 dst_unused:UNUSED_PRESERVE src0_sel:WORD_1
	v_pk_add_f16 v14, v30, v74 neg_lo:[0,1] neg_hi:[0,1]
	v_pk_add_f16 v13, v13, v21
	v_pk_add_f16 v12, v12, v20
	v_pk_add_f16 v11, v11, v19
	v_pk_add_f16 v10, v10, v18
	v_pk_fma_f16 v9, v61, v21, v9
	v_pk_fma_f16 v8, v60, v20, v8
	v_pk_fma_f16 v7, v59, v19, v7
	v_pk_fma_f16 v6, v58, v18, v6
	v_pk_add_f16 v15, v31, v75 neg_lo:[0,1] neg_hi:[0,1]
	v_pk_add_f16 v16, v32, v76 neg_lo:[0,1] neg_hi:[0,1]
	v_pk_add_f16 v17, v33, v77 neg_lo:[0,1] neg_hi:[0,1]
	v_exp_f16_sdwa v18, v14 dst_sel:WORD_0 dst_unused:UNUSED_PAD src0_sel:WORD_0
	v_exp_f16_sdwa v19, v15 dst_sel:WORD_0 dst_unused:UNUSED_PAD src0_sel:WORD_0
	v_exp_f16_sdwa v20, v16 dst_sel:WORD_0 dst_unused:UNUSED_PAD src0_sel:WORD_0
	v_exp_f16_sdwa v21, v17 dst_sel:WORD_0 dst_unused:UNUSED_PAD src0_sel:WORD_0
	v_exp_f16_sdwa v18, v14 dst_sel:WORD_1 dst_unused:UNUSED_PRESERVE src0_sel:WORD_1
	v_exp_f16_sdwa v19, v15 dst_sel:WORD_1 dst_unused:UNUSED_PRESERVE src0_sel:WORD_1
	v_exp_f16_sdwa v20, v16 dst_sel:WORD_1 dst_unused:UNUSED_PRESERVE src0_sel:WORD_1
	v_exp_f16_sdwa v21, v17 dst_sel:WORD_1 dst_unused:UNUSED_PRESERVE src0_sel:WORD_1
	v_pk_add_f16 v10, v10, v18
	v_pk_add_f16 v11, v11, v19
	v_pk_add_f16 v12, v12, v20
	v_pk_add_f16 v13, v13, v21
	v_pk_fma_f16 v14, v78, v18, v6
	v_pk_fma_f16 v15, v79, v19, v7
	v_pk_fma_f16 v16, v80, v20, v8
	v_pk_fma_f16 v17, v81, v21, v9
	v_pk_add_f16 v6, v42, v74 neg_lo:[0,1] neg_hi:[0,1]
	v_pk_add_f16 v7, v43, v75 neg_lo:[0,1] neg_hi:[0,1]
	v_pk_add_f16 v8, v44, v76 neg_lo:[0,1] neg_hi:[0,1]
	v_pk_add_f16 v9, v45, v77 neg_lo:[0,1] neg_hi:[0,1]
	v_exp_f16_sdwa v18, v6 dst_sel:WORD_0 dst_unused:UNUSED_PAD src0_sel:WORD_0
	v_exp_f16_sdwa v19, v7 dst_sel:WORD_0 dst_unused:UNUSED_PAD src0_sel:WORD_0
	v_exp_f16_sdwa v20, v8 dst_sel:WORD_0 dst_unused:UNUSED_PAD src0_sel:WORD_0
	v_exp_f16_sdwa v21, v9 dst_sel:WORD_0 dst_unused:UNUSED_PAD src0_sel:WORD_0
	v_exp_f16_sdwa v18, v6 dst_sel:WORD_1 dst_unused:UNUSED_PRESERVE src0_sel:WORD_1
	v_exp_f16_sdwa v19, v7 dst_sel:WORD_1 dst_unused:UNUSED_PRESERVE src0_sel:WORD_1
	v_exp_f16_sdwa v20, v8 dst_sel:WORD_1 dst_unused:UNUSED_PRESERVE src0_sel:WORD_1
	v_exp_f16_sdwa v21, v9 dst_sel:WORD_1 dst_unused:UNUSED_PRESERVE src0_sel:WORD_1
	s_nop 0
	v_pk_add_f16 v9, v13, v21
	v_pk_add_f16 v8, v12, v20
	v_pk_add_f16 v7, v11, v19
	v_pk_add_f16 v6, v10, v18
	v_pk_fma_f16 v13, v93, v21, v17
	v_pk_fma_f16 v12, v92, v20, v16
	v_pk_fma_f16 v11, v91, v19, v15
	v_pk_fma_f16 v10, v90, v18, v14
	v_pk_add_f16 v18, v46, v74 neg_lo:[0,1] neg_hi:[0,1]
	v_pk_add_f16 v19, v47, v75 neg_lo:[0,1] neg_hi:[0,1]
	v_pk_add_f16 v20, v48, v76 neg_lo:[0,1] neg_hi:[0,1]
	v_pk_add_f16 v21, v49, v77 neg_lo:[0,1] neg_hi:[0,1]
	v_exp_f16_sdwa v14, v18 dst_sel:WORD_0 dst_unused:UNUSED_PAD src0_sel:WORD_0
	v_exp_f16_sdwa v17, v19 dst_sel:WORD_0 dst_unused:UNUSED_PAD src0_sel:WORD_0
	v_exp_f16_sdwa v15, v20 dst_sel:WORD_0 dst_unused:UNUSED_PAD src0_sel:WORD_0
	v_exp_f16_sdwa v16, v21 dst_sel:WORD_0 dst_unused:UNUSED_PAD src0_sel:WORD_0
	v_exp_f16_sdwa v14, v18 dst_sel:WORD_1 dst_unused:UNUSED_PRESERVE src0_sel:WORD_1
	v_exp_f16_sdwa v17, v19 dst_sel:WORD_1 dst_unused:UNUSED_PRESERVE src0_sel:WORD_1
	v_exp_f16_sdwa v15, v20 dst_sel:WORD_1 dst_unused:UNUSED_PRESERVE src0_sel:WORD_1
	v_exp_f16_sdwa v16, v21 dst_sel:WORD_1 dst_unused:UNUSED_PRESERVE src0_sel:WORD_1
	s_nop 0

.LBB4_2:
	s_cmp_lt_u32 s94, 4
	s_cbranch_scc1 .Lmylp4_3
	s_setprio 1

.Lmyf_C1_7:
	s_mov_b64 exec, -1
	s_waitcnt vmcnt(21)
	v_cvt_f16_f32_e32 v202, v155
	v_cvt_f16_f32_e32 v204, v154
	v_cvt_f16_f32_e32 v203, v156
	v_add_u32_e32 v251, 0x48000, v200
	buffer_load_dwordx4 v[154:157], v251, s[36:39], 0 offen
	s_mov_b64 s[4:5], 0
	s_cmp_lt_u32 s94, 4
	s_cbranch_scc1 .Lmylp4_2
	s_setprio 1
.Lmylp4_2:
	s_waitcnt vmcnt(3)
	v_pk_mul_f16 v212, v204, v209 op_sel_hi:[0,1]
	v_pk_mul_f16 v216, v202, v209 op_sel_hi:[0,1]
	v_pk_mul_f16 v220, v203, v209 op_sel_hi:[0,1]
	v_pk_mul_f16 v205, v204, v206 op_sel_hi:[0,1]
	v_pk_mul_f16 v210, v204, v207 op_sel_hi:[0,1]
	v_pk_mul_f16 v211, v204, v208 op_sel_hi:[0,1]
	v_pk_mul_f16 v213, v202, v206 op_sel_hi:[0,1]
	s_mov_b64 exec, s[64:65]
	buffer_load_dwordx4 v[34:37], v245, s[36:39], 0 offen
	buffer_load_dwordx4 v[18:21], v245, s[36:39], 0 offen offset:512
	s_mov_b64 exec, -1
	v_pk_mul_f16 v214, v202, v207 op_sel_hi:[0,1]
	v_pk_mul_f16 v215, v202, v208 op_sel_hi:[0,1]
	v_pk_mul_f16 v217, v203, v206 op_sel_hi:[0,1]
	v_pk_mul_f16 v218, v203, v207 op_sel_hi:[0,1]
	v_pk_mul_f16 v219, v203, v208 op_sel_hi:[0,1]
	v_pk_fma_f16 v125, v125, v209, v212
	v_pk_fma_f16 v141, v141, v209, v216
	v_pk_fma_f16 v149, v149, v209, v220
	v_pk_fma_f16 v221, v97, v209, v212
	v_pk_fma_f16 v225, v121, v209, v216
	v_pk_fma_f16 v229, v137, v209, v220
	v_pk_fma_f16 v212, v65, v209, v212
	v_pk_fma_f16 v216, v81, v209, v216
	buffer_load_dwordx4 v[46:49], v246, s[36:39], 0 offen offset:512
	buffer_load_dwordx4 v[22:25], v246, s[36:39], 0 offen offset:1024
	v_pk_fma_f16 v209, v105, v209, v220
	v_pk_maximum3_f16 v220, v125, v141, v149
	v_pk_fma_f16 v124, v124, v208, v211
	v_pk_fma_f16 v123, v123, v207, v210
	v_pk_fma_f16 v122, v122, v206, v205
	v_pk_fma_f16 v140, v140, v208, v215
	v_pk_fma_f16 v139, v139, v207, v214
	v_pk_fma_f16 v138, v138, v206, v213
	v_pk_fma_f16 v148, v148, v208, v219
	v_pk_fma_f16 v147, v147, v207, v218
	v_pk_fma_f16 v146, v146, v206, v217
	v_pk_fma_f16 v222, v96, v208, v211
	v_pk_fma_f16 v223, v95, v207, v210
	v_pk_fma_f16 v224, v94, v206, v205
	v_pk_fma_f16 v226, v120, v208, v215
	v_pk_fma_f16 v227, v119, v207, v214
	s_mov_b64 exec, s[66:67]
	buffer_load_dwordx4 v[66:69], v246, s[36:39], 0 offen offset:2048
	buffer_load_dwordx4 v[26:29], v246, s[36:39], 0 offen offset:2560
	s_mov_b64 exec, -1
	v_pk_fma_f16 v228, v118, v206, v213
	v_pk_fma_f16 v230, v136, v208, v219
	v_pk_fma_f16 v231, v135, v207, v218
	v_pk_fma_f16 v232, v134, v206, v217
	v_pk_fma_f16 v211, v64, v208, v211
	v_pk_fma_f16 v210, v63, v207, v210
	v_pk_fma_f16 v205, v62, v206, v205
	v_pk_fma_f16 v215, v80, v208, v215
	v_pk_fma_f16 v214, v79, v207, v214
	v_pk_fma_f16 v213, v78, v206, v213
	v_pk_fma_f16 v208, v104, v208, v219
	v_pk_fma_f16 v207, v103, v207, v218
	v_pk_fma_f16 v206, v102, v206, v217
	v_pk_maximum3_f16 v217, v122, v138, v146
	v_pk_maximum3_f16 v218, v123, v139, v147
	v_pk_maximum3_f16 v219, v124, v140, v148
	v_pk_maximum3_f16 v236, v221, v225, v229
	v_pk_maximum3_f16 v240, v212, v216, v209
	v_pk_maximum3_f16 v233, v224, v228, v232
	v_pk_maximum3_f16 v234, v223, v227, v231
	v_pk_maximum3_f16 v235, v222, v226, v230
	v_pk_maximum3_f16 v237, v205, v213, v206
	v_pk_maximum3_f16 v238, v210, v214, v207
	v_pk_maximum3_f16 v220, v220, v236, v240
	v_pk_maximum3_f16 v239, v211, v215, v208
	v_pk_maximum3_f16 v217, v217, v233, v237
	v_pk_maximum3_f16 v218, v218, v234, v238
	v_pk_maximum3_f16 v219, v219, v235, v239
	v_pk_add_f16 v125, v125, v220 neg_lo:[0,1] neg_hi:[0,1]
	s_mov_b64 exec, s[64:65]
	buffer_load_dwordx4 v[86:89], v247, s[36:39], 0 offen
	buffer_load_dwordx4 v[38:41], v247, s[36:39], 0 offen offset:512
	s_mov_b64 exec, -1
	v_pk_add_f16 v122, v122, v217 neg_lo:[0,1] neg_hi:[0,1]
	v_pk_add_f16 v123, v123, v218 neg_lo:[0,1] neg_hi:[0,1]
	v_pk_add_f16 v124, v124, v219 neg_lo:[0,1] neg_hi:[0,1]
	v_pk_add_f16 v138, v138, v217 neg_lo:[0,1] neg_hi:[0,1]
	v_exp_f16_sdwa v233, v122 dst_sel:WORD_0 dst_unused:UNUSED_PAD src0_sel:WORD_0
	v_exp_f16_sdwa v234, v123 dst_sel:WORD_0 dst_unused:UNUSED_PAD src0_sel:WORD_0
	v_exp_f16_sdwa v235, v124 dst_sel:WORD_0 dst_unused:UNUSED_PAD src0_sel:WORD_0
	v_exp_f16_sdwa v236, v125 dst_sel:WORD_0 dst_unused:UNUSED_PAD src0_sel:WORD_0
	v_exp_f16_sdwa v233, v122 dst_sel:WORD_1 dst_unused:UNUSED_PRESERVE src0_sel:WORD_1
	v_exp_f16_sdwa v234, v123 dst_sel:WORD_1 dst_unused:UNUSED_PRESERVE src0_sel:WORD_1
	v_exp_f16_sdwa v235, v124 dst_sel:WORD_1 dst_unused:UNUSED_PRESERVE src0_sel:WORD_1
	v_exp_f16_sdwa v236, v125 dst_sel:WORD_1 dst_unused:UNUSED_PRESERVE src0_sel:WORD_1
	v_pk_add_f16 v139, v139, v218 neg_lo:[0,1] neg_hi:[0,1]
	v_pk_add_f16 v125, v233, 0
	v_pk_fma_f16 v85, v85, v236, 0
	v_pk_add_f16 v122, v236, 0
	v_pk_add_f16 v123, v235, 0
	v_pk_add_f16 v124, v234, 0
	v_pk_fma_f16 v84, v84, v235, 0
	v_pk_fma_f16 v83, v83, v234, 0
	v_pk_fma_f16 v82, v82, v233, 0
	v_pk_add_f16 v140, v140, v219 neg_lo:[0,1] neg_hi:[0,1]
	buffer_load_dwordx4 v[114:117], v248, s[36:39], 0 offen offset:512
	buffer_load_dwordx4 v[50:53], v248, s[36:39], 0 offen offset:1024
	v_pk_add_f16 v141, v141, v220 neg_lo:[0,1] neg_hi:[0,1]
	v_exp_f16_sdwa v233, v138 dst_sel:WORD_0 dst_unused:UNUSED_PAD src0_sel:WORD_0
	v_exp_f16_sdwa v234, v139 dst_sel:WORD_0 dst_unused:UNUSED_PAD src0_sel:WORD_0
	v_exp_f16_sdwa v235, v140 dst_sel:WORD_0 dst_unused:UNUSED_PAD src0_sel:WORD_0
	v_exp_f16_sdwa v236, v141 dst_sel:WORD_0 dst_unused:UNUSED_PAD src0_sel:WORD_0
	v_exp_f16_sdwa v233, v138 dst_sel:WORD_1 dst_unused:UNUSED_PRESERVE src0_sel:WORD_1
	v_exp_f16_sdwa v234, v139 dst_sel:WORD_1 dst_unused:UNUSED_PRESERVE src0_sel:WORD_1
	v_exp_f16_sdwa v235, v140 dst_sel:WORD_1 dst_unused:UNUSED_PRESERVE src0_sel:WORD_1
	v_exp_f16_sdwa v236, v141 dst_sel:WORD_1 dst_unused:UNUSED_PRESERVE src0_sel:WORD_1
	v_pk_add_f16 v125, v125, v233
	v_pk_fma_f16 v85, v109, v236, v85
	v_pk_add_f16 v109, v149, v220 neg_lo:[0,1] neg_hi:[0,1]
	v_pk_add_f16 v124, v124, v234
	v_pk_add_f16 v123, v123, v235
	v_pk_add_f16 v122, v122, v236
	v_pk_fma_f16 v82, v106, v233, v82
	v_pk_fma_f16 v83, v107, v234, v83
	v_pk_fma_f16 v84, v108, v235, v84
	v_pk_add_f16 v106, v146, v217 neg_lo:[0,1] neg_hi:[0,1]
	v_pk_add_f16 v107, v147, v218 neg_lo:[0,1] neg_hi:[0,1]
	v_pk_add_f16 v108, v148, v219 neg_lo:[0,1] neg_hi:[0,1]
	v_exp_f16_sdwa v138, v106 dst_sel:WORD_0 dst_unused:UNUSED_PAD src0_sel:WORD_0
	v_exp_f16_sdwa v139, v107 dst_sel:WORD_0 dst_unused:UNUSED_PAD src0_sel:WORD_0
	v_exp_f16_sdwa v140, v108 dst_sel:WORD_0 dst_unused:UNUSED_PAD src0_sel:WORD_0
	v_exp_f16_sdwa v141, v109 dst_sel:WORD_0 dst_unused:UNUSED_PAD src0_sel:WORD_0
	v_exp_f16_sdwa v138, v106 dst_sel:WORD_1 dst_unused:UNUSED_PRESERVE src0_sel:WORD_1
	v_exp_f16_sdwa v139, v107 dst_sel:WORD_1 dst_unused:UNUSED_PRESERVE src0_sel:WORD_1
	v_exp_f16_sdwa v140, v108 dst_sel:WORD_1 dst_unused:UNUSED_PRESERVE src0_sel:WORD_1
	v_exp_f16_sdwa v141, v109 dst_sel:WORD_1 dst_unused:UNUSED_PRESERVE src0_sel:WORD_1
	v_pk_add_f16 v109, v125, v138
	v_pk_add_f16 v106, v122, v141
	s_mov_b64 exec, s[66:67]
	buffer_load_dwordx4 v[130:133], v248, s[36:39], 0 offen offset:2048
	buffer_load_dwordx4 v[70:73], v248, s[36:39], 0 offen offset:2560
	s_mov_b64 exec, -1
	v_pk_add_f16 v107, v123, v140
	v_pk_add_f16 v108, v124, v139
	v_pk_fma_f16 v85, v129, v141, v85
	v_pk_fma_f16 v84, v128, v140, v84
	v_pk_fma_f16 v83, v127, v139, v83
	v_pk_fma_f16 v82, v126, v138, v82
	v_pk_add_f16 v122, v224, v217 neg_lo:[0,1] neg_hi:[0,1]
	v_pk_add_f16 v123, v223, v218 neg_lo:[0,1] neg_hi:[0,1]
	v_pk_add_f16 v124, v222, v219 neg_lo:[0,1] neg_hi:[0,1]
	v_pk_add_f16 v125, v221, v220 neg_lo:[0,1] neg_hi:[0,1]
	v_exp_f16_sdwa v126, v122 dst_sel:WORD_0 dst_unused:UNUSED_PAD src0_sel:WORD_0
	v_exp_f16_sdwa v127, v123 dst_sel:WORD_0 dst_unused:UNUSED_PAD src0_sel:WORD_0
	v_exp_f16_sdwa v128, v124 dst_sel:WORD_0 dst_unused:UNUSED_PAD src0_sel:WORD_0
	v_exp_f16_sdwa v129, v125 dst_sel:WORD_0 dst_unused:UNUSED_PAD src0_sel:WORD_0
	v_exp_f16_sdwa v126, v122 dst_sel:WORD_1 dst_unused:UNUSED_PRESERVE src0_sel:WORD_1
	v_exp_f16_sdwa v127, v123 dst_sel:WORD_1 dst_unused:UNUSED_PRESERVE src0_sel:WORD_1
	v_exp_f16_sdwa v128, v124 dst_sel:WORD_1 dst_unused:UNUSED_PRESERVE src0_sel:WORD_1
	v_exp_f16_sdwa v129, v125 dst_sel:WORD_1 dst_unused:UNUSED_PRESERVE src0_sel:WORD_1
	v_pk_add_f16 v122, v228, v217 neg_lo:[0,1] neg_hi:[0,1]
	v_pk_add_f16 v109, v109, v126
	v_pk_add_f16 v108, v108, v127
	v_pk_add_f16 v107, v107, v128
	s_mov_b64 exec, s[76:77]
	buffer_load_dwordx4 v[142:145], v249, s[36:39], 0 offen
	buffer_load_dwordx4 v[90:93], v249, s[36:39], 0 offen offset:512
	s_mov_b64 exec, -1
	v_pk_add_f16 v106, v106, v129
	v_pk_fma_f16 v82, v54, v126, v82
	v_pk_fma_f16 v83, v55, v127, v83
	v_pk_fma_f16 v84, v56, v128, v84
	v_pk_fma_f16 v85, v57, v129, v85
	v_pk_add_f16 v123, v227, v218 neg_lo:[0,1] neg_hi:[0,1]
	v_pk_add_f16 v124, v226, v219 neg_lo:[0,1] neg_hi:[0,1]
	v_pk_add_f16 v125, v225, v220 neg_lo:[0,1] neg_hi:[0,1]
	v_exp_f16_sdwa v126, v122 dst_sel:WORD_0 dst_unused:UNUSED_PAD src0_sel:WORD_0
	v_exp_f16_sdwa v127, v123 dst_sel:WORD_0 dst_unused:UNUSED_PAD src0_sel:WORD_0
	v_exp_f16_sdwa v128, v124 dst_sel:WORD_0 dst_unused:UNUSED_PAD src0_sel:WORD_0
	v_exp_f16_sdwa v129, v125 dst_sel:WORD_0 dst_unused:UNUSED_PAD src0_sel:WORD_0
	v_exp_f16_sdwa v126, v122 dst_sel:WORD_1 dst_unused:UNUSED_PRESERVE src0_sel:WORD_1
	v_exp_f16_sdwa v127, v123 dst_sel:WORD_1 dst_unused:UNUSED_PRESERVE src0_sel:WORD_1
	v_exp_f16_sdwa v128, v124 dst_sel:WORD_1 dst_unused:UNUSED_PRESERVE src0_sel:WORD_1
	v_exp_f16_sdwa v129, v125 dst_sel:WORD_1 dst_unused:UNUSED_PRESERVE src0_sel:WORD_1
	v_pk_add_f16 v122, v232, v217 neg_lo:[0,1] neg_hi:[0,1]
	v_pk_add_f16 v109, v109, v126
	v_pk_add_f16 v106, v106, v129
	v_pk_add_f16 v107, v107, v128
	v_pk_add_f16 v108, v108, v127
	v_pk_fma_f16 v85, v77, v129, v85
	v_pk_fma_f16 v84, v76, v128, v84
	s_mov_b64 exec, s[70:71]
	buffer_load_dwordx4 v[150:153], v250, s[36:39], 0 offen offset:512
	buffer_load_dwordx4 v[110:113], v250, s[36:39], 0 offen offset:1024
	s_mov_b64 exec, -1
	v_pk_fma_f16 v83, v75, v127, v83
	v_pk_fma_f16 v82, v74, v126, v82
	v_pk_add_f16 v123, v231, v218 neg_lo:[0,1] neg_hi:[0,1]
	v_pk_add_f16 v124, v230, v219 neg_lo:[0,1] neg_hi:[0,1]
	v_pk_add_f16 v125, v229, v220 neg_lo:[0,1] neg_hi:[0,1]
	v_exp_f16_sdwa v126, v122 dst_sel:WORD_0 dst_unused:UNUSED_PAD src0_sel:WORD_0
	v_exp_f16_sdwa v127, v123 dst_sel:WORD_0 dst_unused:UNUSED_PAD src0_sel:WORD_0
	v_exp_f16_sdwa v128, v124 dst_sel:WORD_0 dst_unused:UNUSED_PAD src0_sel:WORD_0
	v_exp_f16_sdwa v129, v125 dst_sel:WORD_0 dst_unused:UNUSED_PAD src0_sel:WORD_0
	v_exp_f16_sdwa v126, v122 dst_sel:WORD_1 dst_unused:UNUSED_PRESERVE src0_sel:WORD_1
	v_exp_f16_sdwa v127, v123 dst_sel:WORD_1 dst_unused:UNUSED_PRESERVE src0_sel:WORD_1
	v_exp_f16_sdwa v128, v124 dst_sel:WORD_1 dst_unused:UNUSED_PRESERVE src0_sel:WORD_1
	v_exp_f16_sdwa v129, v125 dst_sel:WORD_1 dst_unused:UNUSED_PRESERVE src0_sel:WORD_1
	v_pk_add_f16 v122, v205, v217 neg_lo:[0,1] neg_hi:[0,1]
	v_pk_add_f16 v109, v109, v126
	v_pk_add_f16 v108, v108, v127
	v_pk_add_f16 v107, v107, v128
	v_pk_add_f16 v106, v106, v129
	v_pk_fma_f16 v82, v98, v126, v82
	v_pk_fma_f16 v83, v99, v127, v83
	v_pk_fma_f16 v84, v100, v128, v84
	v_pk_fma_f16 v85, v101, v129, v85
	s_mov_b64 exec, s[78:79]
	buffer_load_dwordx4 v[14:17], v250, s[36:39], 0 offen offset:2048
	buffer_load_dwordx4 v[10:13], v250, s[36:39], 0 offen offset:2560
	s_mov_b64 exec, -1
	v_pk_add_f16 v123, v210, v218 neg_lo:[0,1] neg_hi:[0,1]
	v_pk_add_f16 v124, v211, v219 neg_lo:[0,1] neg_hi:[0,1]
	v_pk_add_f16 v125, v212, v220 neg_lo:[0,1] neg_hi:[0,1]
	v_exp_f16_sdwa v126, v122 dst_sel:WORD_0 dst_unused:UNUSED_PAD src0_sel:WORD_0
	v_exp_f16_sdwa v127, v123 dst_sel:WORD_0 dst_unused:UNUSED_PAD src0_sel:WORD_0
	v_exp_f16_sdwa v128, v124 dst_sel:WORD_0 dst_unused:UNUSED_PAD src0_sel:WORD_0
	v_exp_f16_sdwa v129, v125 dst_sel:WORD_0 dst_unused:UNUSED_PAD src0_sel:WORD_0
	v_exp_f16_sdwa v126, v122 dst_sel:WORD_1 dst_unused:UNUSED_PRESERVE src0_sel:WORD_1
	v_exp_f16_sdwa v127, v123 dst_sel:WORD_1 dst_unused:UNUSED_PRESERVE src0_sel:WORD_1
	v_exp_f16_sdwa v128, v124 dst_sel:WORD_1 dst_unused:UNUSED_PRESERVE src0_sel:WORD_1
	v_exp_f16_sdwa v129, v125 dst_sel:WORD_1 dst_unused:UNUSED_PRESERVE src0_sel:WORD_1
	v_pk_add_f16 v122, v213, v217 neg_lo:[0,1] neg_hi:[0,1]
	v_pk_add_f16 v109, v109, v126
	v_pk_add_f16 v106, v106, v129
	v_pk_add_f16 v107, v107, v128
	v_pk_add_f16 v108, v108, v127
	v_pk_fma_f16 v85, v33, v129, v85
	v_pk_fma_f16 v84, v32, v128, v84
	v_pk_fma_f16 v83, v31, v127, v83
	v_pk_fma_f16 v82, v30, v126, v82
	v_pk_add_f16 v123, v214, v218 neg_lo:[0,1] neg_hi:[0,1]
	v_pk_add_f16 v124, v215, v219 neg_lo:[0,1] neg_hi:[0,1]
	v_pk_add_f16 v125, v216, v220 neg_lo:[0,1] neg_hi:[0,1]
	v_exp_f16_sdwa v126, v122 dst_sel:WORD_0 dst_unused:UNUSED_PAD src0_sel:WORD_0
	v_exp_f16_sdwa v127, v123 dst_sel:WORD_0 dst_unused:UNUSED_PAD src0_sel:WORD_0
	v_exp_f16_sdwa v128, v124 dst_sel:WORD_0 dst_unused:UNUSED_PAD src0_sel:WORD_0
	v_exp_f16_sdwa v129, v125 dst_sel:WORD_0 dst_unused:UNUSED_PAD src0_sel:WORD_0
	v_exp_f16_sdwa v126, v122 dst_sel:WORD_1 dst_unused:UNUSED_PRESERVE src0_sel:WORD_1
	v_exp_f16_sdwa v127, v123 dst_sel:WORD_1 dst_unused:UNUSED_PRESERVE src0_sel:WORD_1
	v_exp_f16_sdwa v128, v124 dst_sel:WORD_1 dst_unused:UNUSED_PRESERVE src0_sel:WORD_1
	v_exp_f16_sdwa v129, v125 dst_sel:WORD_1 dst_unused:UNUSED_PRESERVE src0_sel:WORD_1
	v_pk_add_f16 v122, v206, v217 neg_lo:[0,1] neg_hi:[0,1]
	v_pk_add_f16 v109, v109, v126
	v_pk_add_f16 v108, v108, v127
	v_pk_add_f16 v107, v107, v128
	v_pk_add_f16 v106, v106, v129
	v_pk_fma_f16 v82, v42, v126, v82
	v_pk_fma_f16 v83, v43, v127, v83
	v_pk_fma_f16 v84, v44, v128, v84
	v_pk_fma_f16 v85, v45, v129, v85
	v_pk_add_f16 v123, v207, v218 neg_lo:[0,1] neg_hi:[0,1]
	v_pk_add_f16 v124, v208, v219 neg_lo:[0,1] neg_hi:[0,1]
	v_pk_add_f16 v125, v209, v220 neg_lo:[0,1] neg_hi:[0,1]
	v_exp_f16_sdwa v126, v122 dst_sel:WORD_0 dst_unused:UNUSED_PAD src0_sel:WORD_0
	v_exp_f16_sdwa v127, v123 dst_sel:WORD_0 dst_unused:UNUSED_PAD src0_sel:WORD_0
	v_exp_f16_sdwa v128, v124 dst_sel:WORD_0 dst_unused:UNUSED_PAD src0_sel:WORD_0
	v_exp_f16_sdwa v129, v125 dst_sel:WORD_0 dst_unused:UNUSED_PAD src0_sel:WORD_0
	v_exp_f16_sdwa v126, v122 dst_sel:WORD_1 dst_unused:UNUSED_PRESERVE src0_sel:WORD_1
	v_exp_f16_sdwa v127, v123 dst_sel:WORD_1 dst_unused:UNUSED_PRESERVE src0_sel:WORD_1
	v_exp_f16_sdwa v128, v124 dst_sel:WORD_1 dst_unused:UNUSED_PRESERVE src0_sel:WORD_1
	v_exp_f16_sdwa v129, v125 dst_sel:WORD_1 dst_unused:UNUSED_PRESERVE src0_sel:WORD_1
	v_pk_add_f16 v109, v109, v126
	v_pk_add_f16 v108, v108, v127
	v_rcp_f16_e32 v122, v109
	v_rcp_f16_sdwa v109, v109 dst_sel:DWORD dst_unused:UNUSED_PAD src0_sel:WORD_1
	v_pk_add_f16 v107, v107, v128
	v_rcp_f16_e32 v123, v108
	v_rcp_f16_sdwa v108, v108 dst_sel:DWORD dst_unused:UNUSED_PAD src0_sel:WORD_1
	v_pk_add_f16 v106, v106, v129
	v_rcp_f16_e32 v124, v107
	v_rcp_f16_sdwa v107, v107 dst_sel:DWORD dst_unused:UNUSED_PAD src0_sel:WORD_1
	v_rcp_f16_e32 v125, v106
	v_rcp_f16_sdwa v106, v106 dst_sel:DWORD dst_unused:UNUSED_PAD src0_sel:WORD_1
	v_pk_fma_f16 v82, v58, v126, v82
	v_pack_b32_f16 v109, v122, v109
	v_pk_fma_f16 v83, v59, v127, v83
	v_pk_mul_f16 v138, v82, v109
	v_pack_b32_f16 v82, v123, v108
	v_pk_fma_f16 v84, v60, v128, v84
	v_pk_mul_f16 v139, v83, v82
	v_pack_b32_f16 v82, v124, v107
	v_pk_fma_f16 v85, v61, v129, v85
	v_pk_mul_f16 v140, v84, v82
	v_pack_b32_f16 v82, v125, v106
	v_pk_mul_f16 v141, v85, v82
	s_waitcnt vmcnt(12)
	v_pk_mul_f16 v85, v204, v165 op_sel_hi:[0,1]
	v_pk_mul_f16 v109, v202, v165 op_sel_hi:[0,1]
	v_pk_mul_f16 v122, v203, v162 op_sel_hi:[0,1]
	v_pk_mul_f16 v125, v203, v165 op_sel_hi:[0,1]
	v_pk_mul_f16 v82, v204, v162 op_sel_hi:[0,1]
	v_pk_mul_f16 v83, v204, v163 op_sel_hi:[0,1]
	v_pk_mul_f16 v84, v204, v164 op_sel_hi:[0,1]
	v_pk_mul_f16 v106, v202, v162 op_sel_hi:[0,1]
	v_pk_mul_f16 v107, v202, v163 op_sel_hi:[0,1]
	v_pk_mul_f16 v108, v202, v164 op_sel_hi:[0,1]
	v_pk_mul_f16 v123, v203, v163 op_sel_hi:[0,1]
	v_pk_mul_f16 v124, v203, v164 op_sel_hi:[0,1]
	v_pk_fma_f16 v97, v97, v165, v85
	v_pk_fma_f16 v121, v121, v165, v109
	v_pk_fma_f16 v126, v137, v165, v125
	v_pk_fma_f16 v129, v134, v162, v122
	v_pk_fma_f16 v134, v65, v165, v85
	v_pk_fma_f16 v146, v81, v165, v109
	v_pk_fma_f16 v205, v105, v165, v125
	v_pk_fma_f16 v85, v37, v165, v85
	v_pk_fma_f16 v109, v49, v165, v109
	v_pk_fma_f16 v125, v69, v165, v125
	v_pk_maximum3_f16 v165, v97, v121, v126
	v_pk_fma_f16 v96, v96, v164, v84
	v_pk_fma_f16 v95, v95, v163, v83
	v_pk_fma_f16 v94, v94, v162, v82
	v_pk_fma_f16 v120, v120, v164, v108
	v_pk_fma_f16 v119, v119, v163, v107
	v_pk_fma_f16 v118, v118, v162, v106
	v_pk_fma_f16 v127, v136, v164, v124
	v_pk_fma_f16 v128, v135, v163, v123
	v_pk_fma_f16 v135, v64, v164, v84
	v_pk_fma_f16 v136, v63, v163, v83
	v_pk_fma_f16 v137, v62, v162, v82
	v_pk_fma_f16 v147, v80, v164, v108
	v_pk_fma_f16 v148, v79, v163, v107
	v_pk_fma_f16 v149, v78, v162, v106
	v_pk_fma_f16 v206, v104, v164, v124
	v_pk_fma_f16 v207, v103, v163, v123
	v_pk_fma_f16 v208, v102, v162, v122
	v_pk_fma_f16 v84, v36, v164, v84
	v_pk_fma_f16 v83, v35, v163, v83
	v_pk_fma_f16 v82, v34, v162, v82
	v_pk_fma_f16 v108, v48, v164, v108
	v_pk_fma_f16 v107, v47, v163, v107
	v_pk_fma_f16 v106, v46, v162, v106
	v_pk_fma_f16 v124, v68, v164, v124
	v_pk_fma_f16 v123, v67, v163, v123
	v_pk_fma_f16 v122, v66, v162, v122
	v_pk_maximum3_f16 v162, v94, v118, v129
	v_pk_maximum3_f16 v163, v95, v119, v128
	v_pk_maximum3_f16 v164, v96, v120, v127
	v_pk_maximum3_f16 v212, v134, v146, v205
	v_pk_maximum3_f16 v216, v85, v109, v125
	v_pk_maximum3_f16 v209, v137, v149, v208
	v_pk_maximum3_f16 v210, v136, v148, v207
	v_pk_maximum3_f16 v211, v135, v147, v206
	v_pk_maximum3_f16 v213, v82, v106, v122
	v_pk_maximum3_f16 v214, v83, v107, v123
	v_pk_maximum3_f16 v165, v165, v212, v216
	v_pk_maximum3_f16 v215, v84, v108, v124
	v_pk_maximum3_f16 v162, v162, v209, v213
	v_pk_maximum3_f16 v163, v163, v210, v214
	v_pk_maximum3_f16 v164, v164, v211, v215
	v_pk_add_f16 v97, v97, v165 neg_lo:[0,1] neg_hi:[0,1]
	v_pk_add_f16 v94, v94, v162 neg_lo:[0,1] neg_hi:[0,1]
	v_pk_add_f16 v95, v95, v163 neg_lo:[0,1] neg_hi:[0,1]
	v_pk_add_f16 v96, v96, v164 neg_lo:[0,1] neg_hi:[0,1]
	v_pk_add_f16 v118, v118, v162 neg_lo:[0,1] neg_hi:[0,1]
	v_exp_f16_sdwa v209, v94 dst_sel:WORD_0 dst_unused:UNUSED_PAD src0_sel:WORD_0
	v_exp_f16_sdwa v210, v95 dst_sel:WORD_0 dst_unused:UNUSED_PAD src0_sel:WORD_0
	v_exp_f16_sdwa v211, v96 dst_sel:WORD_0 dst_unused:UNUSED_PAD src0_sel:WORD_0
	v_exp_f16_sdwa v212, v97 dst_sel:WORD_0 dst_unused:UNUSED_PAD src0_sel:WORD_0
	v_exp_f16_sdwa v209, v94 dst_sel:WORD_1 dst_unused:UNUSED_PRESERVE src0_sel:WORD_1
	v_exp_f16_sdwa v210, v95 dst_sel:WORD_1 dst_unused:UNUSED_PRESERVE src0_sel:WORD_1
	v_exp_f16_sdwa v211, v96 dst_sel:WORD_1 dst_unused:UNUSED_PRESERVE src0_sel:WORD_1
	v_exp_f16_sdwa v212, v97 dst_sel:WORD_1 dst_unused:UNUSED_PRESERVE src0_sel:WORD_1
	v_pk_add_f16 v119, v119, v163 neg_lo:[0,1] neg_hi:[0,1]
	v_pk_add_f16 v97, v209, 0
	v_pk_fma_f16 v57, v57, v212, 0
	v_pk_add_f16 v94, v212, 0
	v_pk_add_f16 v95, v211, 0
	v_pk_add_f16 v96, v210, 0
	v_pk_fma_f16 v56, v56, v211, 0
	v_pk_fma_f16 v55, v55, v210, 0
	v_pk_fma_f16 v54, v54, v209, 0
	v_pk_add_f16 v120, v120, v164 neg_lo:[0,1] neg_hi:[0,1]
	v_pk_add_f16 v121, v121, v165 neg_lo:[0,1] neg_hi:[0,1]
	v_pk_add_f16 v82, v82, v162 neg_lo:[0,1] neg_hi:[0,1]
	v_exp_f16_sdwa v209, v118 dst_sel:WORD_0 dst_unused:UNUSED_PAD src0_sel:WORD_0
	v_exp_f16_sdwa v210, v119 dst_sel:WORD_0 dst_unused:UNUSED_PAD src0_sel:WORD_0
	v_exp_f16_sdwa v211, v120 dst_sel:WORD_0 dst_unused:UNUSED_PAD src0_sel:WORD_0
	v_exp_f16_sdwa v212, v121 dst_sel:WORD_0 dst_unused:UNUSED_PAD src0_sel:WORD_0
	v_exp_f16_sdwa v209, v118 dst_sel:WORD_1 dst_unused:UNUSED_PRESERVE src0_sel:WORD_1
	v_exp_f16_sdwa v210, v119 dst_sel:WORD_1 dst_unused:UNUSED_PRESERVE src0_sel:WORD_1
	v_exp_f16_sdwa v211, v120 dst_sel:WORD_1 dst_unused:UNUSED_PRESERVE src0_sel:WORD_1
	v_exp_f16_sdwa v212, v121 dst_sel:WORD_1 dst_unused:UNUSED_PRESERVE src0_sel:WORD_1
	v_pk_add_f16 v83, v83, v163 neg_lo:[0,1] neg_hi:[0,1]
	v_pk_add_f16 v97, v97, v209
	v_pk_fma_f16 v57, v77, v212, v57
	v_pk_add_f16 v77, v126, v165 neg_lo:[0,1] neg_hi:[0,1]
	v_pk_add_f16 v96, v96, v210
	v_pk_add_f16 v95, v95, v211
	v_pk_add_f16 v94, v94, v212
	v_pk_fma_f16 v54, v74, v209, v54
	v_pk_fma_f16 v55, v75, v210, v55
	v_pk_fma_f16 v56, v76, v211, v56
	v_pk_add_f16 v74, v129, v162 neg_lo:[0,1] neg_hi:[0,1]
	v_pk_add_f16 v75, v128, v163 neg_lo:[0,1] neg_hi:[0,1]
	v_pk_add_f16 v76, v127, v164 neg_lo:[0,1] neg_hi:[0,1]
	v_pk_add_f16 v84, v84, v164 neg_lo:[0,1] neg_hi:[0,1]
	v_exp_f16_sdwa v118, v74 dst_sel:WORD_0 dst_unused:UNUSED_PAD src0_sel:WORD_0
	v_exp_f16_sdwa v119, v75 dst_sel:WORD_0 dst_unused:UNUSED_PAD src0_sel:WORD_0
	v_exp_f16_sdwa v120, v76 dst_sel:WORD_0 dst_unused:UNUSED_PAD src0_sel:WORD_0
	v_exp_f16_sdwa v121, v77 dst_sel:WORD_0 dst_unused:UNUSED_PAD src0_sel:WORD_0
	v_exp_f16_sdwa v118, v74 dst_sel:WORD_1 dst_unused:UNUSED_PRESERVE src0_sel:WORD_1
	v_exp_f16_sdwa v119, v75 dst_sel:WORD_1 dst_unused:UNUSED_PRESERVE src0_sel:WORD_1
	v_exp_f16_sdwa v120, v76 dst_sel:WORD_1 dst_unused:UNUSED_PRESERVE src0_sel:WORD_1
	v_exp_f16_sdwa v121, v77 dst_sel:WORD_1 dst_unused:UNUSED_PRESERVE src0_sel:WORD_1
	v_pk_add_f16 v85, v85, v165 neg_lo:[0,1] neg_hi:[0,1]
	v_pk_add_f16 v77, v97, v118
	v_pk_add_f16 v74, v94, v121
	v_pk_add_f16 v75, v95, v120
	v_pk_add_f16 v76, v96, v119
	v_pk_fma_f16 v57, v101, v121, v57
	v_pk_fma_f16 v56, v100, v120, v56
	v_pk_fma_f16 v55, v99, v119, v55
	v_pk_fma_f16 v54, v98, v118, v54
	v_pk_add_f16 v94, v137, v162 neg_lo:[0,1] neg_hi:[0,1]
	v_pk_add_f16 v95, v136, v163 neg_lo:[0,1] neg_hi:[0,1]
	v_pk_add_f16 v96, v135, v164 neg_lo:[0,1] neg_hi:[0,1]
	v_pk_add_f16 v97, v134, v165 neg_lo:[0,1] neg_hi:[0,1]
	v_exp_f16_sdwa v98, v94 dst_sel:WORD_0 dst_unused:UNUSED_PAD src0_sel:WORD_0
	v_exp_f16_sdwa v99, v95 dst_sel:WORD_0 dst_unused:UNUSED_PAD src0_sel:WORD_0
	v_exp_f16_sdwa v100, v96 dst_sel:WORD_0 dst_unused:UNUSED_PAD src0_sel:WORD_0
	v_exp_f16_sdwa v101, v97 dst_sel:WORD_0 dst_unused:UNUSED_PAD src0_sel:WORD_0
	v_exp_f16_sdwa v98, v94 dst_sel:WORD_1 dst_unused:UNUSED_PRESERVE src0_sel:WORD_1
	v_exp_f16_sdwa v99, v95 dst_sel:WORD_1 dst_unused:UNUSED_PRESERVE src0_sel:WORD_1
	v_exp_f16_sdwa v100, v96 dst_sel:WORD_1 dst_unused:UNUSED_PRESERVE src0_sel:WORD_1
	v_exp_f16_sdwa v101, v97 dst_sel:WORD_1 dst_unused:UNUSED_PRESERVE src0_sel:WORD_1
	v_pk_add_f16 v94, v149, v162 neg_lo:[0,1] neg_hi:[0,1]
	v_pk_add_f16 v77, v77, v98
	v_pk_add_f16 v76, v76, v99
	v_pk_add_f16 v75, v75, v100
	v_pk_add_f16 v74, v74, v101
	v_pk_fma_f16 v54, v30, v98, v54
	v_pk_fma_f16 v55, v31, v99, v55
	v_pk_fma_f16 v56, v32, v100, v56
	v_pk_fma_f16 v57, v33, v101, v57
	v_pk_add_f16 v95, v148, v163 neg_lo:[0,1] neg_hi:[0,1]
	v_pk_add_f16 v96, v147, v164 neg_lo:[0,1] neg_hi:[0,1]
	v_pk_add_f16 v97, v146, v165 neg_lo:[0,1] neg_hi:[0,1]
	v_exp_f16_sdwa v98, v94 dst_sel:WORD_0 dst_unused:UNUSED_PAD src0_sel:WORD_0
	v_exp_f16_sdwa v99, v95 dst_sel:WORD_0 dst_unused:UNUSED_PAD src0_sel:WORD_0
	v_exp_f16_sdwa v100, v96 dst_sel:WORD_0 dst_unused:UNUSED_PAD src0_sel:WORD_0
	v_exp_f16_sdwa v101, v97 dst_sel:WORD_0 dst_unused:UNUSED_PAD src0_sel:WORD_0
	v_exp_f16_sdwa v98, v94 dst_sel:WORD_1 dst_unused:UNUSED_PRESERVE src0_sel:WORD_1
	v_exp_f16_sdwa v99, v95 dst_sel:WORD_1 dst_unused:UNUSED_PRESERVE src0_sel:WORD_1
	v_exp_f16_sdwa v100, v96 dst_sel:WORD_1 dst_unused:UNUSED_PRESERVE src0_sel:WORD_1
	v_exp_f16_sdwa v101, v97 dst_sel:WORD_1 dst_unused:UNUSED_PRESERVE src0_sel:WORD_1
	v_pk_add_f16 v94, v208, v162 neg_lo:[0,1] neg_hi:[0,1]
	v_pk_add_f16 v77, v77, v98
	v_pk_add_f16 v74, v74, v101
	v_pk_add_f16 v75, v75, v100
	v_pk_add_f16 v76, v76, v99
	v_pk_fma_f16 v57, v45, v101, v57
	v_pk_fma_f16 v56, v44, v100, v56
	v_pk_fma_f16 v55, v43, v99, v55
	v_pk_fma_f16 v54, v42, v98, v54
	v_pk_add_f16 v95, v207, v163 neg_lo:[0,1] neg_hi:[0,1]
	v_pk_add_f16 v96, v206, v164 neg_lo:[0,1] neg_hi:[0,1]
	v_pk_add_f16 v97, v205, v165 neg_lo:[0,1] neg_hi:[0,1]
	v_exp_f16_sdwa v98, v94 dst_sel:WORD_0 dst_unused:UNUSED_PAD src0_sel:WORD_0
	v_exp_f16_sdwa v99, v95 dst_sel:WORD_0 dst_unused:UNUSED_PAD src0_sel:WORD_0
	v_exp_f16_sdwa v100, v96 dst_sel:WORD_0 dst_unused:UNUSED_PAD src0_sel:WORD_0
	v_exp_f16_sdwa v101, v97 dst_sel:WORD_0 dst_unused:UNUSED_PAD src0_sel:WORD_0
	v_exp_f16_sdwa v98, v94 dst_sel:WORD_1 dst_unused:UNUSED_PRESERVE src0_sel:WORD_1
	v_exp_f16_sdwa v99, v95 dst_sel:WORD_1 dst_unused:UNUSED_PRESERVE src0_sel:WORD_1
	v_exp_f16_sdwa v100, v96 dst_sel:WORD_1 dst_unused:UNUSED_PRESERVE src0_sel:WORD_1
	v_exp_f16_sdwa v101, v97 dst_sel:WORD_1 dst_unused:UNUSED_PRESERVE src0_sel:WORD_1
	v_exp_f16_sdwa v94, v82 dst_sel:WORD_0 dst_unused:UNUSED_PAD src0_sel:WORD_0
	v_exp_f16_sdwa v95, v83 dst_sel:WORD_0 dst_unused:UNUSED_PAD src0_sel:WORD_0
	v_exp_f16_sdwa v96, v84 dst_sel:WORD_0 dst_unused:UNUSED_PAD src0_sel:WORD_0
	v_exp_f16_sdwa v97, v85 dst_sel:WORD_0 dst_unused:UNUSED_PAD src0_sel:WORD_0
	v_exp_f16_sdwa v94, v82 dst_sel:WORD_1 dst_unused:UNUSED_PRESERVE src0_sel:WORD_1
	v_exp_f16_sdwa v95, v83 dst_sel:WORD_1 dst_unused:UNUSED_PRESERVE src0_sel:WORD_1
	v_exp_f16_sdwa v96, v84 dst_sel:WORD_1 dst_unused:UNUSED_PRESERVE src0_sel:WORD_1
	v_exp_f16_sdwa v97, v85 dst_sel:WORD_1 dst_unused:UNUSED_PRESERVE src0_sel:WORD_1
	v_pk_add_f16 v82, v106, v162 neg_lo:[0,1] neg_hi:[0,1]
	v_pk_add_f16 v77, v77, v98
	v_pk_add_f16 v76, v76, v99
	v_pk_add_f16 v75, v75, v100
	v_pk_add_f16 v74, v74, v101
	v_pk_fma_f16 v54, v58, v98, v54
	v_pk_fma_f16 v55, v59, v99, v55
	v_pk_fma_f16 v56, v60, v100, v56
	v_pk_fma_f16 v57, v61, v101, v57
	v_pk_add_f16 v77, v77, v94
	v_pk_add_f16 v74, v74, v97
	v_pk_add_f16 v75, v75, v96
	v_pk_add_f16 v76, v76, v95
	v_pk_fma_f16 v57, v21, v97, v57
	v_pk_fma_f16 v56, v20, v96, v56
	v_pk_fma_f16 v55, v19, v95, v55
	v_pk_fma_f16 v54, v18, v94, v54
	v_pk_add_f16 v83, v107, v163 neg_lo:[0,1] neg_hi:[0,1]
	v_pk_add_f16 v84, v108, v164 neg_lo:[0,1] neg_hi:[0,1]
	v_pk_add_f16 v85, v109, v165 neg_lo:[0,1] neg_hi:[0,1]
	v_exp_f16_sdwa v94, v82 dst_sel:WORD_0 dst_unused:UNUSED_PAD src0_sel:WORD_0
	v_exp_f16_sdwa v95, v83 dst_sel:WORD_0 dst_unused:UNUSED_PAD src0_sel:WORD_0
	v_exp_f16_sdwa v96, v84 dst_sel:WORD_0 dst_unused:UNUSED_PAD src0_sel:WORD_0
	v_exp_f16_sdwa v97, v85 dst_sel:WORD_0 dst_unused:UNUSED_PAD src0_sel:WORD_0
	v_exp_f16_sdwa v94, v82 dst_sel:WORD_1 dst_unused:UNUSED_PRESERVE src0_sel:WORD_1
	v_exp_f16_sdwa v95, v83 dst_sel:WORD_1 dst_unused:UNUSED_PRESERVE src0_sel:WORD_1
	v_exp_f16_sdwa v96, v84 dst_sel:WORD_1 dst_unused:UNUSED_PRESERVE src0_sel:WORD_1
	v_exp_f16_sdwa v97, v85 dst_sel:WORD_1 dst_unused:UNUSED_PRESERVE src0_sel:WORD_1
	v_pk_add_f16 v82, v122, v162 neg_lo:[0,1] neg_hi:[0,1]
	v_pk_add_f16 v77, v77, v94
	v_pk_add_f16 v76, v76, v95
	v_pk_add_f16 v75, v75, v96
	v_pk_add_f16 v74, v74, v97
	v_pk_fma_f16 v54, v22, v94, v54
	v_pk_fma_f16 v55, v23, v95, v55
	v_pk_fma_f16 v56, v24, v96, v56
	v_pk_fma_f16 v57, v25, v97, v57
	v_pk_add_f16 v83, v123, v163 neg_lo:[0,1] neg_hi:[0,1]
	v_pk_add_f16 v84, v124, v164 neg_lo:[0,1] neg_hi:[0,1]
	v_pk_add_f16 v85, v125, v165 neg_lo:[0,1] neg_hi:[0,1]
	v_exp_f16_sdwa v94, v82 dst_sel:WORD_0 dst_unused:UNUSED_PAD src0_sel:WORD_0
	v_exp_f16_sdwa v95, v83 dst_sel:WORD_0 dst_unused:UNUSED_PAD src0_sel:WORD_0
	v_exp_f16_sdwa v96, v84 dst_sel:WORD_0 dst_unused:UNUSED_PAD src0_sel:WORD_0
	v_exp_f16_sdwa v97, v85 dst_sel:WORD_0 dst_unused:UNUSED_PAD src0_sel:WORD_0
	v_exp_f16_sdwa v94, v82 dst_sel:WORD_1 dst_unused:UNUSED_PRESERVE src0_sel:WORD_1
	v_exp_f16_sdwa v95, v83 dst_sel:WORD_1 dst_unused:UNUSED_PRESERVE src0_sel:WORD_1
	v_exp_f16_sdwa v96, v84 dst_sel:WORD_1 dst_unused:UNUSED_PRESERVE src0_sel:WORD_1
	v_exp_f16_sdwa v97, v85 dst_sel:WORD_1 dst_unused:UNUSED_PRESERVE src0_sel:WORD_1
	v_pk_add_f16 v77, v77, v94
	v_pk_add_f16 v76, v76, v95
	v_rcp_f16_e32 v82, v77
	v_rcp_f16_sdwa v77, v77 dst_sel:DWORD dst_unused:UNUSED_PAD src0_sel:WORD_1
	v_pk_add_f16 v75, v75, v96
	v_rcp_f16_e32 v83, v76
	v_rcp_f16_sdwa v76, v76 dst_sel:DWORD dst_unused:UNUSED_PAD src0_sel:WORD_1
	v_pk_add_f16 v74, v74, v97
	v_rcp_f16_e32 v84, v75
	v_rcp_f16_sdwa v75, v75 dst_sel:DWORD dst_unused:UNUSED_PAD src0_sel:WORD_1
	v_rcp_f16_e32 v85, v74
	v_rcp_f16_sdwa v74, v74 dst_sel:DWORD dst_unused:UNUSED_PAD src0_sel:WORD_1
	v_pk_fma_f16 v54, v26, v94, v54
	v_pack_b32_f16 v77, v82, v77
	v_pk_fma_f16 v55, v27, v95, v55
	v_pk_mul_f16 v77, v54, v77
	v_pack_b32_f16 v54, v83, v76
	v_pk_fma_f16 v56, v28, v96, v56
	v_pk_mul_f16 v76, v55, v54
	v_pack_b32_f16 v54, v84, v75
	v_pk_fma_f16 v57, v29, v97, v57
	v_pk_mul_f16 v75, v56, v54
	v_pack_b32_f16 v54, v85, v74
	v_pk_mul_f16 v74, v57, v54
	s_waitcnt vmcnt(6)
	v_pk_mul_f16 v57, v204, v161 op_sel_hi:[0,1]
	v_pk_mul_f16 v85, v202, v161 op_sel_hi:[0,1]
	v_pk_mul_f16 v97, v203, v161 op_sel_hi:[0,1]
	v_pk_mul_f16 v54, v204, v158 op_sel_hi:[0,1]
	v_pk_mul_f16 v55, v204, v159 op_sel_hi:[0,1]
	v_pk_mul_f16 v56, v204, v160 op_sel_hi:[0,1]
	v_pk_mul_f16 v82, v202, v158 op_sel_hi:[0,1]
	v_pk_mul_f16 v83, v202, v159 op_sel_hi:[0,1]
	v_pk_mul_f16 v84, v202, v160 op_sel_hi:[0,1]
	v_pk_mul_f16 v94, v203, v158 op_sel_hi:[0,1]
	v_pk_mul_f16 v95, v203, v159 op_sel_hi:[0,1]
	v_pk_mul_f16 v96, v203, v160 op_sel_hi:[0,1]
	v_pk_fma_f16 v65, v65, v161, v57
	v_pk_fma_f16 v81, v81, v161, v85
	v_pk_fma_f16 v98, v105, v161, v97
	v_pk_fma_f16 v64, v64, v160, v56
	v_pk_maximum3_f16 v125, v65, v81, v98
	v_pk_fma_f16 v63, v63, v159, v55
	v_pk_fma_f16 v62, v62, v158, v54
	v_pk_fma_f16 v80, v80, v160, v84
	v_pk_fma_f16 v79, v79, v159, v83
	v_pk_fma_f16 v78, v78, v158, v82
	v_pk_fma_f16 v99, v104, v160, v96
	v_pk_fma_f16 v100, v103, v159, v95
	v_pk_fma_f16 v101, v102, v158, v94
	v_pk_fma_f16 v102, v37, v161, v57
	v_pk_fma_f16 v106, v49, v161, v85
	v_pk_fma_f16 v118, v69, v161, v97
	v_pk_fma_f16 v57, v89, v161, v57
	v_pk_fma_f16 v85, v117, v161, v85
	v_pk_fma_f16 v97, v133, v161, v97
	v_pk_maximum3_f16 v122, v62, v78, v101
	v_pk_maximum3_f16 v123, v63, v79, v100
	v_pk_maximum3_f16 v124, v64, v80, v99
	v_pk_maximum3_f16 v129, v102, v106, v118
	v_pk_fma_f16 v103, v36, v160, v56
	v_pk_maximum3_f16 v137, v57, v85, v97
	v_pk_fma_f16 v104, v35, v159, v55
	v_pk_maximum3_f16 v125, v125, v129, v137
	v_pk_fma_f16 v105, v34, v158, v54
	v_pk_fma_f16 v107, v48, v160, v84
	v_pk_fma_f16 v108, v47, v159, v83
	v_pk_fma_f16 v109, v46, v158, v82
	v_pk_fma_f16 v119, v68, v160, v96
	v_pk_fma_f16 v120, v67, v159, v95
	v_pk_fma_f16 v121, v66, v158, v94
	v_pk_fma_f16 v56, v88, v160, v56
	v_pk_fma_f16 v55, v87, v159, v55
	v_pk_fma_f16 v54, v86, v158, v54
	v_pk_fma_f16 v84, v116, v160, v84
	v_pk_fma_f16 v83, v115, v159, v83
	v_pk_fma_f16 v82, v114, v158, v82
	v_pk_fma_f16 v96, v132, v160, v96
	v_pk_fma_f16 v95, v131, v159, v95
	v_pk_fma_f16 v94, v130, v158, v94
	v_pk_maximum3_f16 v126, v105, v109, v121
	v_pk_maximum3_f16 v127, v104, v108, v120
	v_pk_maximum3_f16 v128, v103, v107, v119
	v_pk_maximum3_f16 v135, v55, v83, v95
	v_pk_maximum3_f16 v136, v56, v84, v96
	v_pk_maximum3_f16 v134, v54, v82, v94
	v_pk_maximum3_f16 v122, v122, v126, v134
	v_pk_maximum3_f16 v123, v123, v127, v135
	v_pk_maximum3_f16 v124, v124, v128, v136
	v_pk_add_f16 v65, v65, v125 neg_lo:[0,1] neg_hi:[0,1]
	v_pk_add_f16 v62, v62, v122 neg_lo:[0,1] neg_hi:[0,1]
	v_pk_add_f16 v63, v63, v123 neg_lo:[0,1] neg_hi:[0,1]
	v_pk_add_f16 v64, v64, v124 neg_lo:[0,1] neg_hi:[0,1]
	v_pk_add_f16 v78, v78, v122 neg_lo:[0,1] neg_hi:[0,1]
	v_exp_f16_sdwa v126, v62 dst_sel:WORD_0 dst_unused:UNUSED_PAD src0_sel:WORD_0
	v_exp_f16_sdwa v127, v63 dst_sel:WORD_0 dst_unused:UNUSED_PAD src0_sel:WORD_0
	v_exp_f16_sdwa v128, v64 dst_sel:WORD_0 dst_unused:UNUSED_PAD src0_sel:WORD_0
	v_exp_f16_sdwa v129, v65 dst_sel:WORD_0 dst_unused:UNUSED_PAD src0_sel:WORD_0
	v_exp_f16_sdwa v126, v62 dst_sel:WORD_1 dst_unused:UNUSED_PRESERVE src0_sel:WORD_1
	v_exp_f16_sdwa v127, v63 dst_sel:WORD_1 dst_unused:UNUSED_PRESERVE src0_sel:WORD_1
	v_exp_f16_sdwa v128, v64 dst_sel:WORD_1 dst_unused:UNUSED_PRESERVE src0_sel:WORD_1
	v_exp_f16_sdwa v129, v65 dst_sel:WORD_1 dst_unused:UNUSED_PRESERVE src0_sel:WORD_1
	v_pk_add_f16 v79, v79, v123 neg_lo:[0,1] neg_hi:[0,1]
	v_pk_add_f16 v65, v126, 0
	v_pk_fma_f16 v33, v33, v129, 0
	v_pk_add_f16 v62, v129, 0
	v_pk_add_f16 v63, v128, 0
	v_pk_add_f16 v64, v127, 0
	v_pk_fma_f16 v32, v32, v128, 0
	v_pk_fma_f16 v31, v31, v127, 0
	v_pk_fma_f16 v30, v30, v126, 0
	v_pk_add_f16 v80, v80, v124 neg_lo:[0,1] neg_hi:[0,1]
	v_pk_add_f16 v81, v81, v125 neg_lo:[0,1] neg_hi:[0,1]
	v_pk_add_f16 v54, v54, v122 neg_lo:[0,1] neg_hi:[0,1]
	v_exp_f16_sdwa v126, v78 dst_sel:WORD_0 dst_unused:UNUSED_PAD src0_sel:WORD_0
	v_exp_f16_sdwa v127, v79 dst_sel:WORD_0 dst_unused:UNUSED_PAD src0_sel:WORD_0
	v_exp_f16_sdwa v128, v80 dst_sel:WORD_0 dst_unused:UNUSED_PAD src0_sel:WORD_0
	v_exp_f16_sdwa v129, v81 dst_sel:WORD_0 dst_unused:UNUSED_PAD src0_sel:WORD_0
	v_exp_f16_sdwa v126, v78 dst_sel:WORD_1 dst_unused:UNUSED_PRESERVE src0_sel:WORD_1
	v_exp_f16_sdwa v127, v79 dst_sel:WORD_1 dst_unused:UNUSED_PRESERVE src0_sel:WORD_1
	v_exp_f16_sdwa v128, v80 dst_sel:WORD_1 dst_unused:UNUSED_PRESERVE src0_sel:WORD_1
	v_exp_f16_sdwa v129, v81 dst_sel:WORD_1 dst_unused:UNUSED_PRESERVE src0_sel:WORD_1
	v_pk_add_f16 v55, v55, v123 neg_lo:[0,1] neg_hi:[0,1]
	v_pk_add_f16 v65, v65, v126
	v_pk_fma_f16 v33, v45, v129, v33
	v_pk_add_f16 v45, v98, v125 neg_lo:[0,1] neg_hi:[0,1]
	v_pk_add_f16 v64, v64, v127
	v_pk_add_f16 v63, v63, v128
	v_pk_add_f16 v62, v62, v129
	v_pk_fma_f16 v30, v42, v126, v30
	v_pk_fma_f16 v31, v43, v127, v31
	v_pk_fma_f16 v32, v44, v128, v32
	v_pk_add_f16 v42, v101, v122 neg_lo:[0,1] neg_hi:[0,1]
	v_pk_add_f16 v43, v100, v123 neg_lo:[0,1] neg_hi:[0,1]
	v_pk_add_f16 v44, v99, v124 neg_lo:[0,1] neg_hi:[0,1]
	v_pk_add_f16 v56, v56, v124 neg_lo:[0,1] neg_hi:[0,1]
	v_exp_f16_sdwa v78, v42 dst_sel:WORD_0 dst_unused:UNUSED_PAD src0_sel:WORD_0
	v_exp_f16_sdwa v79, v43 dst_sel:WORD_0 dst_unused:UNUSED_PAD src0_sel:WORD_0
	v_exp_f16_sdwa v80, v44 dst_sel:WORD_0 dst_unused:UNUSED_PAD src0_sel:WORD_0
	v_exp_f16_sdwa v81, v45 dst_sel:WORD_0 dst_unused:UNUSED_PAD src0_sel:WORD_0
	v_exp_f16_sdwa v78, v42 dst_sel:WORD_1 dst_unused:UNUSED_PRESERVE src0_sel:WORD_1
	v_exp_f16_sdwa v79, v43 dst_sel:WORD_1 dst_unused:UNUSED_PRESERVE src0_sel:WORD_1
	v_exp_f16_sdwa v80, v44 dst_sel:WORD_1 dst_unused:UNUSED_PRESERVE src0_sel:WORD_1
	v_exp_f16_sdwa v81, v45 dst_sel:WORD_1 dst_unused:UNUSED_PRESERVE src0_sel:WORD_1
	v_pk_add_f16 v57, v57, v125 neg_lo:[0,1] neg_hi:[0,1]
	v_pk_add_f16 v45, v65, v78
	v_pk_add_f16 v42, v62, v81
	v_pk_add_f16 v43, v63, v80
	v_pk_add_f16 v44, v64, v79
	v_pk_fma_f16 v33, v61, v81, v33
	v_pk_fma_f16 v32, v60, v80, v32
	v_pk_fma_f16 v31, v59, v79, v31
	v_pk_fma_f16 v30, v58, v78, v30
	v_pk_add_f16 v58, v105, v122 neg_lo:[0,1] neg_hi:[0,1]
	v_pk_add_f16 v59, v104, v123 neg_lo:[0,1] neg_hi:[0,1]
	v_pk_add_f16 v60, v103, v124 neg_lo:[0,1] neg_hi:[0,1]
	v_pk_add_f16 v61, v102, v125 neg_lo:[0,1] neg_hi:[0,1]
	v_exp_f16_sdwa v62, v58 dst_sel:WORD_0 dst_unused:UNUSED_PAD src0_sel:WORD_0
	v_exp_f16_sdwa v63, v59 dst_sel:WORD_0 dst_unused:UNUSED_PAD src0_sel:WORD_0
	v_exp_f16_sdwa v64, v60 dst_sel:WORD_0 dst_unused:UNUSED_PAD src0_sel:WORD_0
	v_exp_f16_sdwa v65, v61 dst_sel:WORD_0 dst_unused:UNUSED_PAD src0_sel:WORD_0
	v_exp_f16_sdwa v62, v58 dst_sel:WORD_1 dst_unused:UNUSED_PRESERVE src0_sel:WORD_1
	v_exp_f16_sdwa v63, v59 dst_sel:WORD_1 dst_unused:UNUSED_PRESERVE src0_sel:WORD_1
	v_exp_f16_sdwa v64, v60 dst_sel:WORD_1 dst_unused:UNUSED_PRESERVE src0_sel:WORD_1
	v_exp_f16_sdwa v65, v61 dst_sel:WORD_1 dst_unused:UNUSED_PRESERVE src0_sel:WORD_1
	v_pk_add_f16 v58, v109, v122 neg_lo:[0,1] neg_hi:[0,1]
	v_pk_add_f16 v45, v45, v62
	v_pk_add_f16 v44, v44, v63
	v_pk_add_f16 v43, v43, v64
	v_pk_add_f16 v42, v42, v65
	v_pk_fma_f16 v30, v18, v62, v30
	v_pk_fma_f16 v31, v19, v63, v31
	v_pk_fma_f16 v32, v20, v64, v32
	v_pk_fma_f16 v33, v21, v65, v33
	v_pk_add_f16 v59, v108, v123 neg_lo:[0,1] neg_hi:[0,1]
	v_pk_add_f16 v60, v107, v124 neg_lo:[0,1] neg_hi:[0,1]
	v_pk_add_f16 v61, v106, v125 neg_lo:[0,1] neg_hi:[0,1]
	v_exp_f16_sdwa v62, v58 dst_sel:WORD_0 dst_unused:UNUSED_PAD src0_sel:WORD_0
	v_exp_f16_sdwa v63, v59 dst_sel:WORD_0 dst_unused:UNUSED_PAD src0_sel:WORD_0
	v_exp_f16_sdwa v64, v60 dst_sel:WORD_0 dst_unused:UNUSED_PAD src0_sel:WORD_0
	v_exp_f16_sdwa v65, v61 dst_sel:WORD_0 dst_unused:UNUSED_PAD src0_sel:WORD_0
	v_exp_f16_sdwa v62, v58 dst_sel:WORD_1 dst_unused:UNUSED_PRESERVE src0_sel:WORD_1
	v_exp_f16_sdwa v63, v59 dst_sel:WORD_1 dst_unused:UNUSED_PRESERVE src0_sel:WORD_1
	v_exp_f16_sdwa v64, v60 dst_sel:WORD_1 dst_unused:UNUSED_PRESERVE src0_sel:WORD_1
	v_exp_f16_sdwa v65, v61 dst_sel:WORD_1 dst_unused:UNUSED_PRESERVE src0_sel:WORD_1
	v_pk_add_f16 v58, v121, v122 neg_lo:[0,1] neg_hi:[0,1]
	v_pk_add_f16 v45, v45, v62
	v_pk_add_f16 v42, v42, v65
	v_pk_add_f16 v43, v43, v64
	v_pk_add_f16 v44, v44, v63
	v_pk_fma_f16 v33, v25, v65, v33
	v_pk_fma_f16 v32, v24, v64, v32
	v_pk_fma_f16 v31, v23, v63, v31
	v_pk_fma_f16 v30, v22, v62, v30
	v_pk_add_f16 v59, v120, v123 neg_lo:[0,1] neg_hi:[0,1]
	v_pk_add_f16 v60, v119, v124 neg_lo:[0,1] neg_hi:[0,1]
	v_pk_add_f16 v61, v118, v125 neg_lo:[0,1] neg_hi:[0,1]
	v_exp_f16_sdwa v62, v58 dst_sel:WORD_0 dst_unused:UNUSED_PAD src0_sel:WORD_0
	v_exp_f16_sdwa v63, v59 dst_sel:WORD_0 dst_unused:UNUSED_PAD src0_sel:WORD_0
	v_exp_f16_sdwa v64, v60 dst_sel:WORD_0 dst_unused:UNUSED_PAD src0_sel:WORD_0
	v_exp_f16_sdwa v65, v61 dst_sel:WORD_0 dst_unused:UNUSED_PAD src0_sel:WORD_0
	v_exp_f16_sdwa v62, v58 dst_sel:WORD_1 dst_unused:UNUSED_PRESERVE src0_sel:WORD_1
	v_exp_f16_sdwa v63, v59 dst_sel:WORD_1 dst_unused:UNUSED_PRESERVE src0_sel:WORD_1
	v_exp_f16_sdwa v64, v60 dst_sel:WORD_1 dst_unused:UNUSED_PRESERVE src0_sel:WORD_1
	v_exp_f16_sdwa v65, v61 dst_sel:WORD_1 dst_unused:UNUSED_PRESERVE src0_sel:WORD_1
	v_exp_f16_sdwa v58, v54 dst_sel:WORD_0 dst_unused:UNUSED_PAD src0_sel:WORD_0
	v_exp_f16_sdwa v59, v55 dst_sel:WORD_0 dst_unused:UNUSED_PAD src0_sel:WORD_0
	v_exp_f16_sdwa v60, v56 dst_sel:WORD_0 dst_unused:UNUSED_PAD src0_sel:WORD_0
	v_exp_f16_sdwa v61, v57 dst_sel:WORD_0 dst_unused:UNUSED_PAD src0_sel:WORD_0
	v_exp_f16_sdwa v58, v54 dst_sel:WORD_1 dst_unused:UNUSED_PRESERVE src0_sel:WORD_1
	v_exp_f16_sdwa v59, v55 dst_sel:WORD_1 dst_unused:UNUSED_PRESERVE src0_sel:WORD_1
	v_exp_f16_sdwa v60, v56 dst_sel:WORD_1 dst_unused:UNUSED_PRESERVE src0_sel:WORD_1
	v_exp_f16_sdwa v61, v57 dst_sel:WORD_1 dst_unused:UNUSED_PRESERVE src0_sel:WORD_1
	v_pk_add_f16 v54, v82, v122 neg_lo:[0,1] neg_hi:[0,1]
	v_pk_add_f16 v45, v45, v62
	v_pk_add_f16 v44, v44, v63
	v_pk_add_f16 v43, v43, v64
	v_pk_add_f16 v42, v42, v65
	v_pk_fma_f16 v30, v26, v62, v30
	v_pk_fma_f16 v31, v27, v63, v31
	v_pk_fma_f16 v32, v28, v64, v32
	v_pk_fma_f16 v33, v29, v65, v33
	v_pk_add_f16 v45, v45, v58
	v_pk_add_f16 v42, v42, v61
	v_pk_add_f16 v43, v43, v60
	v_pk_add_f16 v44, v44, v59
	v_pk_fma_f16 v33, v41, v61, v33
	v_pk_fma_f16 v32, v40, v60, v32
	v_pk_fma_f16 v31, v39, v59, v31
	v_pk_fma_f16 v30, v38, v58, v30
	v_pk_add_f16 v55, v83, v123 neg_lo:[0,1] neg_hi:[0,1]
	v_pk_add_f16 v56, v84, v124 neg_lo:[0,1] neg_hi:[0,1]
	v_pk_add_f16 v57, v85, v125 neg_lo:[0,1] neg_hi:[0,1]
	v_exp_f16_sdwa v58, v54 dst_sel:WORD_0 dst_unused:UNUSED_PAD src0_sel:WORD_0
	v_exp_f16_sdwa v59, v55 dst_sel:WORD_0 dst_unused:UNUSED_PAD src0_sel:WORD_0
	v_exp_f16_sdwa v60, v56 dst_sel:WORD_0 dst_unused:UNUSED_PAD src0_sel:WORD_0
	v_exp_f16_sdwa v61, v57 dst_sel:WORD_0 dst_unused:UNUSED_PAD src0_sel:WORD_0
	v_exp_f16_sdwa v58, v54 dst_sel:WORD_1 dst_unused:UNUSED_PRESERVE src0_sel:WORD_1
	v_exp_f16_sdwa v59, v55 dst_sel:WORD_1 dst_unused:UNUSED_PRESERVE src0_sel:WORD_1
	v_exp_f16_sdwa v60, v56 dst_sel:WORD_1 dst_unused:UNUSED_PRESERVE src0_sel:WORD_1
	v_exp_f16_sdwa v61, v57 dst_sel:WORD_1 dst_unused:UNUSED_PRESERVE src0_sel:WORD_1
	v_pk_add_f16 v54, v94, v122 neg_lo:[0,1] neg_hi:[0,1]
	v_pk_add_f16 v45, v45, v58
	v_pk_add_f16 v44, v44, v59
	v_pk_add_f16 v43, v43, v60
	v_pk_add_f16 v42, v42, v61
	v_pk_fma_f16 v30, v50, v58, v30
	v_pk_fma_f16 v31, v51, v59, v31
	v_pk_fma_f16 v32, v52, v60, v32
	v_pk_fma_f16 v33, v53, v61, v33
	v_pk_add_f16 v55, v95, v123 neg_lo:[0,1] neg_hi:[0,1]
	v_pk_add_f16 v56, v96, v124 neg_lo:[0,1] neg_hi:[0,1]
	v_pk_add_f16 v57, v97, v125 neg_lo:[0,1] neg_hi:[0,1]
	v_exp_f16_sdwa v58, v54 dst_sel:WORD_0 dst_unused:UNUSED_PAD src0_sel:WORD_0
	v_exp_f16_sdwa v59, v55 dst_sel:WORD_0 dst_unused:UNUSED_PAD src0_sel:WORD_0
	v_exp_f16_sdwa v60, v56 dst_sel:WORD_0 dst_unused:UNUSED_PAD src0_sel:WORD_0
	v_exp_f16_sdwa v61, v57 dst_sel:WORD_0 dst_unused:UNUSED_PAD src0_sel:WORD_0
	v_exp_f16_sdwa v58, v54 dst_sel:WORD_1 dst_unused:UNUSED_PRESERVE src0_sel:WORD_1
	v_exp_f16_sdwa v59, v55 dst_sel:WORD_1 dst_unused:UNUSED_PRESERVE src0_sel:WORD_1
	v_exp_f16_sdwa v60, v56 dst_sel:WORD_1 dst_unused:UNUSED_PRESERVE src0_sel:WORD_1
	v_exp_f16_sdwa v61, v57 dst_sel:WORD_1 dst_unused:UNUSED_PRESERVE src0_sel:WORD_1
	v_pk_add_f16 v45, v45, v58
	v_pk_add_f16 v44, v44, v59
	v_rcp_f16_e32 v54, v45
	v_rcp_f16_sdwa v45, v45 dst_sel:DWORD dst_unused:UNUSED_PAD src0_sel:WORD_1
	v_pk_add_f16 v43, v43, v60
	v_rcp_f16_e32 v55, v44
	v_rcp_f16_sdwa v44, v44 dst_sel:DWORD dst_unused:UNUSED_PAD src0_sel:WORD_1
	v_pk_add_f16 v42, v42, v61
	v_pk_fma_f16 v30, v70, v58, v30
	v_rcp_f16_e32 v58, v43
	v_rcp_f16_sdwa v43, v43 dst_sel:DWORD dst_unused:UNUSED_PAD src0_sel:WORD_1
	v_pk_fma_f16 v31, v71, v59, v31
	v_rcp_f16_e32 v59, v42
	v_rcp_f16_sdwa v42, v42 dst_sel:DWORD dst_unused:UNUSED_PAD src0_sel:WORD_1
	v_pack_b32_f16 v45, v54, v45
	v_pk_mul_f16 v57, v30, v45
	v_pack_b32_f16 v30, v55, v44
	v_pk_fma_f16 v32, v72, v60, v32
	v_pk_mul_f16 v56, v31, v30
	v_pack_b32_f16 v30, v58, v43
	v_pk_fma_f16 v33, v73, v61, v33
	v_pk_mul_f16 v55, v32, v30
	v_pack_b32_f16 v30, v59, v42
	v_pk_mul_f16 v54, v33, v30
	s_waitcnt vmcnt(0)
	v_pk_mul_f16 v30, v204, v154 op_sel_hi:[0,1]
	v_pk_mul_f16 v31, v204, v155 op_sel_hi:[0,1]
	v_pk_mul_f16 v32, v204, v156 op_sel_hi:[0,1]
	v_pk_mul_f16 v33, v204, v157 op_sel_hi:[0,1]
	v_pk_mul_f16 v42, v202, v154 op_sel_hi:[0,1]
	v_pk_mul_f16 v43, v202, v155 op_sel_hi:[0,1]
	v_pk_mul_f16 v44, v202, v156 op_sel_hi:[0,1]
	v_pk_mul_f16 v45, v202, v157 op_sel_hi:[0,1]
	v_pk_mul_f16 v58, v203, v154 op_sel_hi:[0,1]
	v_pk_mul_f16 v59, v203, v155 op_sel_hi:[0,1]
	v_pk_mul_f16 v60, v203, v156 op_sel_hi:[0,1]
	v_pk_mul_f16 v61, v203, v157 op_sel_hi:[0,1]
	v_pk_fma_f16 v37, v37, v157, v33
	v_pk_fma_f16 v36, v36, v156, v32
	v_pk_fma_f16 v35, v35, v155, v31
	v_pk_fma_f16 v34, v34, v154, v30
	v_pk_fma_f16 v49, v49, v157, v45
	v_pk_fma_f16 v48, v48, v156, v44
	v_pk_fma_f16 v47, v47, v155, v43
	v_pk_fma_f16 v46, v46, v154, v42
	v_pk_fma_f16 v62, v69, v157, v61
	v_pk_fma_f16 v63, v68, v156, v60
	v_pk_fma_f16 v64, v67, v155, v59
	v_pk_fma_f16 v65, v66, v154, v58
	v_pk_fma_f16 v66, v89, v157, v33
	v_pk_fma_f16 v67, v88, v156, v32
	v_pk_fma_f16 v68, v87, v155, v31
	v_pk_fma_f16 v69, v86, v154, v30
	v_pk_fma_f16 v78, v117, v157, v45
	v_pk_fma_f16 v79, v116, v156, v44
	v_pk_fma_f16 v80, v115, v155, v43
	v_pk_fma_f16 v81, v114, v154, v42
	v_pk_fma_f16 v82, v133, v157, v61
	v_pk_fma_f16 v83, v132, v156, v60
	v_pk_fma_f16 v84, v131, v155, v59
	v_pk_fma_f16 v85, v130, v154, v58
	v_pk_fma_f16 v61, v17, v157, v61
	v_pk_fma_f16 v60, v16, v156, v60
	v_pk_fma_f16 v59, v15, v155, v59
	v_pk_fma_f16 v58, v14, v154, v58
	v_pk_maximum3_f16 v14, v34, v46, v65
	v_pk_maximum3_f16 v15, v35, v47, v64
	v_pk_maximum3_f16 v16, v36, v48, v63
	v_pk_maximum3_f16 v17, v37, v49, v62
	v_pk_maximum3_f16 v86, v69, v81, v85
	v_pk_maximum3_f16 v87, v68, v80, v84
	v_pk_maximum3_f16 v88, v67, v79, v83
	v_pk_maximum3_f16 v89, v66, v78, v82
	v_pk_fma_f16 v33, v145, v157, v33
	v_pk_fma_f16 v32, v144, v156, v32
	v_pk_fma_f16 v31, v143, v155, v31
	v_pk_fma_f16 v30, v142, v154, v30
	v_pk_fma_f16 v45, v153, v157, v45
	v_pk_fma_f16 v44, v152, v156, v44
	v_pk_fma_f16 v43, v151, v155, v43
	v_pk_fma_f16 v42, v150, v154, v42
	v_pk_maximum3_f16 v95, v31, v43, v59
	v_pk_maximum3_f16 v96, v32, v44, v60
	v_pk_maximum3_f16 v97, v33, v45, v61
	v_pk_maximum3_f16 v94, v30, v42, v58
	v_pk_maximum3_f16 v15, v15, v87, v95
	v_pk_maximum3_f16 v16, v16, v88, v96
	v_pk_maximum3_f16 v17, v17, v89, v97
	v_pk_maximum3_f16 v14, v14, v86, v94
	v_xor_b32_e32 v86, 0x80008000, v17
	v_xor_b32_e32 v87, 0x80008000, v16
	v_xor_b32_e32 v88, 0x80008000, v15
	v_xor_b32_e32 v89, 0x80008000, v14
	v_pk_add_f16 v14, v34, v89
	v_pk_add_f16 v15, v35, v88
	v_pk_add_f16 v16, v36, v87
	v_pk_add_f16 v17, v37, v86
	v_exp_f16_sdwa v34, v14 dst_sel:WORD_0 dst_unused:UNUSED_PAD src0_sel:WORD_0
	v_exp_f16_sdwa v35, v15 dst_sel:WORD_0 dst_unused:UNUSED_PAD src0_sel:WORD_0
	v_exp_f16_sdwa v36, v16 dst_sel:WORD_0 dst_unused:UNUSED_PAD src0_sel:WORD_0
	v_exp_f16_sdwa v37, v17 dst_sel:WORD_0 dst_unused:UNUSED_PAD src0_sel:WORD_0
	v_exp_f16_sdwa v34, v14 dst_sel:WORD_1 dst_unused:UNUSED_PRESERVE src0_sel:WORD_1
	v_exp_f16_sdwa v35, v15 dst_sel:WORD_1 dst_unused:UNUSED_PRESERVE src0_sel:WORD_1
	v_exp_f16_sdwa v36, v16 dst_sel:WORD_1 dst_unused:UNUSED_PRESERVE src0_sel:WORD_1
	v_exp_f16_sdwa v37, v17 dst_sel:WORD_1 dst_unused:UNUSED_PRESERVE src0_sel:WORD_1
	v_pk_add_f16 v14, v34, 0
	v_pk_add_f16 v15, v35, 0
	v_pk_add_f16 v16, v36, 0
	v_pk_add_f16 v17, v37, 0
	v_pk_fma_f16 v18, v18, v34, 0
	v_pk_fma_f16 v19, v19, v35, 0
	v_pk_fma_f16 v20, v20, v36, 0
	v_pk_fma_f16 v21, v21, v37, 0
	v_pk_add_f16 v34, v46, v89
	v_pk_add_f16 v35, v47, v88
	v_pk_add_f16 v36, v48, v87
	v_pk_add_f16 v37, v49, v86
	v_exp_f16_sdwa v46, v34 dst_sel:WORD_0 dst_unused:UNUSED_PAD src0_sel:WORD_0
	v_exp_f16_sdwa v47, v35 dst_sel:WORD_0 dst_unused:UNUSED_PAD src0_sel:WORD_0
	v_exp_f16_sdwa v48, v36 dst_sel:WORD_0 dst_unused:UNUSED_PAD src0_sel:WORD_0
	v_exp_f16_sdwa v49, v37 dst_sel:WORD_0 dst_unused:UNUSED_PAD src0_sel:WORD_0
	v_exp_f16_sdwa v46, v34 dst_sel:WORD_1 dst_unused:UNUSED_PRESERVE src0_sel:WORD_1
	v_exp_f16_sdwa v47, v35 dst_sel:WORD_1 dst_unused:UNUSED_PRESERVE src0_sel:WORD_1
	v_exp_f16_sdwa v48, v36 dst_sel:WORD_1 dst_unused:UNUSED_PRESERVE src0_sel:WORD_1
	v_exp_f16_sdwa v49, v37 dst_sel:WORD_1 dst_unused:UNUSED_PRESERVE src0_sel:WORD_1
	s_nop 0
	v_pk_add_f16 v17, v17, v49
	v_pk_add_f16 v16, v16, v48
	v_pk_add_f16 v15, v15, v47
	v_pk_add_f16 v14, v14, v46
	v_pk_fma_f16 v21, v25, v49, v21
	v_pk_fma_f16 v20, v24, v48, v20
	v_pk_fma_f16 v19, v23, v47, v19
	v_pk_fma_f16 v18, v22, v46, v18
	v_pk_add_f16 v22, v65, v89
	v_pk_add_f16 v23, v64, v88
	v_pk_add_f16 v24, v63, v87
	v_pk_add_f16 v25, v62, v86
	v_exp_f16_sdwa v34, v22 dst_sel:WORD_0 dst_unused:UNUSED_PAD src0_sel:WORD_0
	v_exp_f16_sdwa v35, v23 dst_sel:WORD_0 dst_unused:UNUSED_PAD src0_sel:WORD_0
	v_exp_f16_sdwa v36, v24 dst_sel:WORD_0 dst_unused:UNUSED_PAD src0_sel:WORD_0
	v_exp_f16_sdwa v37, v25 dst_sel:WORD_0 dst_unused:UNUSED_PAD src0_sel:WORD_0
	v_exp_f16_sdwa v34, v22 dst_sel:WORD_1 dst_unused:UNUSED_PRESERVE src0_sel:WORD_1
	v_exp_f16_sdwa v35, v23 dst_sel:WORD_1 dst_unused:UNUSED_PRESERVE src0_sel:WORD_1
	v_exp_f16_sdwa v36, v24 dst_sel:WORD_1 dst_unused:UNUSED_PRESERVE src0_sel:WORD_1
	v_exp_f16_sdwa v37, v25 dst_sel:WORD_1 dst_unused:UNUSED_PRESERVE src0_sel:WORD_1
	v_pk_add_f16 v22, v69, v89
	v_pk_add_f16 v14, v14, v34
	v_pk_add_f16 v15, v15, v35
	v_pk_add_f16 v16, v16, v36
	v_pk_add_f16 v17, v17, v37
	v_pk_fma_f16 v18, v26, v34, v18
	v_pk_fma_f16 v19, v27, v35, v19
	v_pk_fma_f16 v20, v28, v36, v20
	v_pk_fma_f16 v21, v29, v37, v21
	v_pk_add_f16 v23, v68, v88
	v_pk_add_f16 v24, v67, v87
	v_pk_add_f16 v25, v66, v86
	v_exp_f16_sdwa v26, v22 dst_sel:WORD_0 dst_unused:UNUSED_PAD src0_sel:WORD_0
	v_exp_f16_sdwa v27, v23 dst_sel:WORD_0 dst_unused:UNUSED_PAD src0_sel:WORD_0
	v_exp_f16_sdwa v28, v24 dst_sel:WORD_0 dst_unused:UNUSED_PAD src0_sel:WORD_0
	v_exp_f16_sdwa v29, v25 dst_sel:WORD_0 dst_unused:UNUSED_PAD src0_sel:WORD_0
	v_exp_f16_sdwa v26, v22 dst_sel:WORD_1 dst_unused:UNUSED_PRESERVE src0_sel:WORD_1
	v_exp_f16_sdwa v27, v23 dst_sel:WORD_1 dst_unused:UNUSED_PRESERVE src0_sel:WORD_1
	v_exp_f16_sdwa v28, v24 dst_sel:WORD_1 dst_unused:UNUSED_PRESERVE src0_sel:WORD_1
	v_exp_f16_sdwa v29, v25 dst_sel:WORD_1 dst_unused:UNUSED_PRESERVE src0_sel:WORD_1
	v_pk_add_f16 v22, v81, v89
	v_pk_add_f16 v17, v17, v29
	v_pk_add_f16 v16, v16, v28
	v_pk_add_f16 v15, v15, v27
	v_pk_add_f16 v14, v14, v26
	v_pk_fma_f16 v21, v41, v29, v21
	v_pk_fma_f16 v20, v40, v28, v20
	v_pk_fma_f16 v19, v39, v27, v19
	v_pk_fma_f16 v18, v38, v26, v18
	v_pk_add_f16 v23, v80, v88
	v_pk_add_f16 v24, v79, v87
	v_pk_add_f16 v25, v78, v86
	v_exp_f16_sdwa v26, v22 dst_sel:WORD_0 dst_unused:UNUSED_PAD src0_sel:WORD_0
	v_exp_f16_sdwa v27, v23 dst_sel:WORD_0 dst_unused:UNUSED_PAD src0_sel:WORD_0
	v_exp_f16_sdwa v28, v24 dst_sel:WORD_0 dst_unused:UNUSED_PAD src0_sel:WORD_0
	v_exp_f16_sdwa v29, v25 dst_sel:WORD_0 dst_unused:UNUSED_PAD src0_sel:WORD_0
	v_exp_f16_sdwa v26, v22 dst_sel:WORD_1 dst_unused:UNUSED_PRESERVE src0_sel:WORD_1
	v_exp_f16_sdwa v27, v23 dst_sel:WORD_1 dst_unused:UNUSED_PRESERVE src0_sel:WORD_1
	v_exp_f16_sdwa v28, v24 dst_sel:WORD_1 dst_unused:UNUSED_PRESERVE src0_sel:WORD_1
	v_exp_f16_sdwa v29, v25 dst_sel:WORD_1 dst_unused:UNUSED_PRESERVE src0_sel:WORD_1
	v_pk_add_f16 v22, v85, v89
	v_pk_add_f16 v14, v14, v26
	v_pk_add_f16 v15, v15, v27
	v_pk_add_f16 v16, v16, v28
	v_pk_add_f16 v17, v17, v29
	v_pk_fma_f16 v18, v50, v26, v18
	v_pk_fma_f16 v19, v51, v27, v19
	v_pk_fma_f16 v20, v52, v28, v20
	v_pk_fma_f16 v21, v53, v29, v21
	v_pk_add_f16 v23, v84, v88
	v_pk_add_f16 v24, v83, v87
	v_pk_add_f16 v25, v82, v86
	v_exp_f16_sdwa v26, v22 dst_sel:WORD_0 dst_unused:UNUSED_PAD src0_sel:WORD_0
	v_exp_f16_sdwa v27, v23 dst_sel:WORD_0 dst_unused:UNUSED_PAD src0_sel:WORD_0
	v_exp_f16_sdwa v28, v24 dst_sel:WORD_0 dst_unused:UNUSED_PAD src0_sel:WORD_0
	v_exp_f16_sdwa v29, v25 dst_sel:WORD_0 dst_unused:UNUSED_PAD src0_sel:WORD_0
	v_exp_f16_sdwa v26, v22 dst_sel:WORD_1 dst_unused:UNUSED_PRESERVE src0_sel:WORD_1
	v_exp_f16_sdwa v27, v23 dst_sel:WORD_1 dst_unused:UNUSED_PRESERVE src0_sel:WORD_1
	v_exp_f16_sdwa v28, v24 dst_sel:WORD_1 dst_unused:UNUSED_PRESERVE src0_sel:WORD_1
	v_exp_f16_sdwa v29, v25 dst_sel:WORD_1 dst_unused:UNUSED_PRESERVE src0_sel:WORD_1
	v_pk_add_f16 v22, v30, v89
	v_pk_add_f16 v17, v17, v29
	v_pk_add_f16 v16, v16, v28
	v_pk_add_f16 v15, v15, v27
	v_pk_add_f16 v14, v14, v26
	v_pk_fma_f16 v21, v73, v29, v21
	v_pk_fma_f16 v20, v72, v28, v20
	v_pk_fma_f16 v19, v71, v27, v19
	v_pk_fma_f16 v18, v70, v26, v18
	v_pk_add_f16 v23, v31, v88
	v_pk_add_f16 v24, v32, v87
	v_pk_add_f16 v25, v33, v86
	v_exp_f16_sdwa v26, v22 dst_sel:WORD_0 dst_unused:UNUSED_PAD src0_sel:WORD_0
	v_exp_f16_sdwa v27, v23 dst_sel:WORD_0 dst_unused:UNUSED_PAD src0_sel:WORD_0
	v_exp_f16_sdwa v28, v24 dst_sel:WORD_0 dst_unused:UNUSED_PAD src0_sel:WORD_0
	v_exp_f16_sdwa v29, v25 dst_sel:WORD_0 dst_unused:UNUSED_PAD src0_sel:WORD_0
	v_exp_f16_sdwa v26, v22 dst_sel:WORD_1 dst_unused:UNUSED_PRESERVE src0_sel:WORD_1
	v_exp_f16_sdwa v27, v23 dst_sel:WORD_1 dst_unused:UNUSED_PRESERVE src0_sel:WORD_1
	v_exp_f16_sdwa v28, v24 dst_sel:WORD_1 dst_unused:UNUSED_PRESERVE src0_sel:WORD_1
	v_exp_f16_sdwa v29, v25 dst_sel:WORD_1 dst_unused:UNUSED_PRESERVE src0_sel:WORD_1
	v_pk_add_f16 v22, v42, v89
	v_pk_add_f16 v14, v14, v26
	v_pk_add_f16 v15, v15, v27
	v_pk_add_f16 v16, v16, v28
	v_pk_add_f16 v17, v17, v29
	v_pk_fma_f16 v18, v90, v26, v18
	v_pk_fma_f16 v19, v91, v27, v19
	v_pk_fma_f16 v20, v92, v28, v20
	v_pk_fma_f16 v21, v93, v29, v21
	v_pk_add_f16 v23, v43, v88
	v_pk_add_f16 v24, v44, v87
	v_pk_add_f16 v25, v45, v86
	v_exp_f16_sdwa v26, v22 dst_sel:WORD_0 dst_unused:UNUSED_PAD src0_sel:WORD_0
	v_exp_f16_sdwa v27, v23 dst_sel:WORD_0 dst_unused:UNUSED_PAD src0_sel:WORD_0
	v_exp_f16_sdwa v28, v24 dst_sel:WORD_0 dst_unused:UNUSED_PAD src0_sel:WORD_0
	v_exp_f16_sdwa v29, v25 dst_sel:WORD_0 dst_unused:UNUSED_PAD src0_sel:WORD_0
	v_exp_f16_sdwa v26, v22 dst_sel:WORD_1 dst_unused:UNUSED_PRESERVE src0_sel:WORD_1
	v_exp_f16_sdwa v27, v23 dst_sel:WORD_1 dst_unused:UNUSED_PRESERVE src0_sel:WORD_1
	v_exp_f16_sdwa v28, v24 dst_sel:WORD_1 dst_unused:UNUSED_PRESERVE src0_sel:WORD_1
	v_exp_f16_sdwa v29, v25 dst_sel:WORD_1 dst_unused:UNUSED_PRESERVE src0_sel:WORD_1
	v_pk_add_f16 v22, v58, v89
	v_pk_add_f16 v17, v17, v29
	v_pk_add_f16 v16, v16, v28
	v_pk_add_f16 v15, v15, v27
	v_pk_add_f16 v14, v14, v26
	v_pk_fma_f16 v21, v113, v29, v21
	v_pk_fma_f16 v20, v112, v28, v20
	v_pk_fma_f16 v19, v111, v27, v19
	v_pk_fma_f16 v18, v110, v26, v18
	v_pk_add_f16 v23, v59, v88
	v_pk_add_f16 v24, v60, v87
	v_pk_add_f16 v25, v61, v86
	v_exp_f16_sdwa v30, v22 dst_sel:WORD_0 dst_unused:UNUSED_PAD src0_sel:WORD_0
	v_exp_f16_sdwa v31, v23 dst_sel:WORD_0 dst_unused:UNUSED_PAD src0_sel:WORD_0
	v_exp_f16_sdwa v32, v24 dst_sel:WORD_0 dst_unused:UNUSED_PAD src0_sel:WORD_0
	v_exp_f16_sdwa v33, v25 dst_sel:WORD_0 dst_unused:UNUSED_PAD src0_sel:WORD_0
	v_exp_f16_sdwa v30, v22 dst_sel:WORD_1 dst_unused:UNUSED_PRESERVE src0_sel:WORD_1
	v_exp_f16_sdwa v31, v23 dst_sel:WORD_1 dst_unused:UNUSED_PRESERVE src0_sel:WORD_1
	v_exp_f16_sdwa v32, v24 dst_sel:WORD_1 dst_unused:UNUSED_PRESERVE src0_sel:WORD_1
	v_exp_f16_sdwa v33, v25 dst_sel:WORD_1 dst_unused:UNUSED_PRESERVE src0_sel:WORD_1
	s_nop 0

.Lmyf_C2_7:
	s_mov_b64 exec, -1
	s_waitcnt vmcnt(21)
	v_cvt_f16_f32_e32 v158, v147
	v_cvt_f16_f32_e32 v160, v146
	v_cvt_f16_f32_e32 v159, v148
	v_add_u32_e32 v251, 0x48000, v200
	buffer_load_dwordx4 v[146:149], v251, s[36:39], 0 offen
	s_cmp_lt_u32 s94, 4
	s_cbranch_scc1 .Lmylp4_1
	s_setprio 1
.Lmylp4_1:
	s_waitcnt vmcnt(3)
	v_pk_mul_f16 v161, v160, v162 op_sel_hi:[0,1]
	v_pk_mul_f16 v204, v160, v165 op_sel_hi:[0,1]
	v_pk_mul_f16 v208, v158, v165 op_sel_hi:[0,1]
	v_pk_mul_f16 v212, v159, v165 op_sel_hi:[0,1]
	v_pk_mul_f16 v202, v160, v163 op_sel_hi:[0,1]
	v_pk_mul_f16 v203, v160, v164 op_sel_hi:[0,1]
	v_pk_mul_f16 v205, v158, v162 op_sel_hi:[0,1]
	s_mov_b64 exec, s[64:65]
	buffer_load_dwordx4 v[26:29], v245, s[36:39], 0 offen
	buffer_load_dwordx4 v[10:13], v245, s[36:39], 0 offen offset:512
	s_mov_b64 exec, -1
	v_pk_mul_f16 v206, v158, v163 op_sel_hi:[0,1]
	v_pk_mul_f16 v207, v158, v164 op_sel_hi:[0,1]
	v_pk_mul_f16 v209, v159, v162 op_sel_hi:[0,1]
	v_pk_mul_f16 v210, v159, v163 op_sel_hi:[0,1]
	v_pk_mul_f16 v211, v159, v164 op_sel_hi:[0,1]
	v_pk_fma_f16 v117, v117, v165, v204
	v_pk_fma_f16 v114, v114, v162, v161
	v_pk_fma_f16 v133, v133, v165, v204
	v_pk_fma_f16 v130, v130, v162, v161
	v_pk_fma_f16 v141, v141, v165, v204
	v_pk_fma_f16 v138, v138, v162, v161
	v_pk_fma_f16 v161, v89, v165, v208
	v_pk_fma_f16 v213, v113, v165, v208
	buffer_load_dwordx4 v[38:41], v246, s[36:39], 0 offen offset:512
	buffer_load_dwordx4 v[14:17], v246, s[36:39], 0 offen offset:1024
	v_pk_fma_f16 v208, v129, v165, v208
	v_pk_fma_f16 v217, v57, v165, v212
	v_pk_fma_f16 v221, v73, v165, v212
	v_pk_fma_f16 v165, v97, v165, v212
	v_pk_maximum3_f16 v212, v117, v133, v141
	v_pk_fma_f16 v116, v116, v164, v203
	v_pk_fma_f16 v115, v115, v163, v202
	v_pk_fma_f16 v132, v132, v164, v203
	v_pk_fma_f16 v131, v131, v163, v202
	v_pk_fma_f16 v140, v140, v164, v203
	v_pk_fma_f16 v139, v139, v163, v202
	v_pk_fma_f16 v202, v88, v164, v207
	v_pk_fma_f16 v203, v87, v163, v206
	v_pk_fma_f16 v204, v86, v162, v205
	v_pk_fma_f16 v214, v112, v164, v207
	v_pk_fma_f16 v215, v111, v163, v206
	s_mov_b64 exec, s[66:67]
	buffer_load_dwordx4 v[58:61], v246, s[36:39], 0 offen offset:2048
	buffer_load_dwordx4 v[18:21], v246, s[36:39], 0 offen offset:2560
	s_mov_b64 exec, -1
	v_pk_fma_f16 v216, v110, v162, v205
	v_pk_fma_f16 v207, v128, v164, v207
	v_pk_fma_f16 v206, v127, v163, v206
	v_pk_fma_f16 v205, v126, v162, v205
	v_pk_fma_f16 v218, v56, v164, v211
	v_pk_fma_f16 v219, v55, v163, v210
	v_pk_fma_f16 v220, v54, v162, v209
	v_pk_fma_f16 v222, v72, v164, v211
	v_pk_fma_f16 v223, v71, v163, v210
	v_pk_fma_f16 v224, v70, v162, v209
	v_pk_fma_f16 v164, v96, v164, v211
	v_pk_fma_f16 v163, v95, v163, v210
	v_pk_fma_f16 v162, v94, v162, v209
	v_pk_maximum3_f16 v209, v114, v130, v138
	v_pk_maximum3_f16 v210, v115, v131, v139
	v_pk_maximum3_f16 v211, v116, v132, v140
	v_pk_maximum3_f16 v228, v161, v213, v208
	v_pk_maximum3_f16 v232, v217, v221, v165
	v_pk_maximum3_f16 v225, v204, v216, v205
	v_pk_maximum3_f16 v226, v203, v215, v206
	v_pk_maximum3_f16 v227, v202, v214, v207
	v_pk_maximum3_f16 v229, v220, v224, v162
	v_pk_maximum3_f16 v230, v219, v223, v163
	v_pk_maximum3_f16 v212, v212, v228, v232
	v_pk_maximum3_f16 v231, v218, v222, v164
	v_pk_maximum3_f16 v209, v209, v225, v229
	v_pk_maximum3_f16 v210, v210, v226, v230
	v_pk_maximum3_f16 v211, v211, v227, v231
	v_pk_add_f16 v117, v117, v212 neg_lo:[0,1] neg_hi:[0,1]
	s_mov_b64 exec, s[64:65]
	buffer_load_dwordx4 v[78:81], v247, s[36:39], 0 offen
	buffer_load_dwordx4 v[30:33], v247, s[36:39], 0 offen offset:512
	s_mov_b64 exec, -1
	v_pk_add_f16 v114, v114, v209 neg_lo:[0,1] neg_hi:[0,1]
	v_pk_add_f16 v115, v115, v210 neg_lo:[0,1] neg_hi:[0,1]
	v_pk_add_f16 v116, v116, v211 neg_lo:[0,1] neg_hi:[0,1]
	v_pk_add_f16 v130, v130, v209 neg_lo:[0,1] neg_hi:[0,1]
	v_exp_f16_sdwa v225, v114 dst_sel:WORD_0 dst_unused:UNUSED_PAD src0_sel:WORD_0
	v_exp_f16_sdwa v226, v115 dst_sel:WORD_0 dst_unused:UNUSED_PAD src0_sel:WORD_0
	v_exp_f16_sdwa v227, v116 dst_sel:WORD_0 dst_unused:UNUSED_PAD src0_sel:WORD_0
	v_exp_f16_sdwa v228, v117 dst_sel:WORD_0 dst_unused:UNUSED_PAD src0_sel:WORD_0
	v_exp_f16_sdwa v225, v114 dst_sel:WORD_1 dst_unused:UNUSED_PRESERVE src0_sel:WORD_1
	v_exp_f16_sdwa v226, v115 dst_sel:WORD_1 dst_unused:UNUSED_PRESERVE src0_sel:WORD_1
	v_exp_f16_sdwa v227, v116 dst_sel:WORD_1 dst_unused:UNUSED_PRESERVE src0_sel:WORD_1
	v_exp_f16_sdwa v228, v117 dst_sel:WORD_1 dst_unused:UNUSED_PRESERVE src0_sel:WORD_1
	v_pk_add_f16 v131, v131, v210 neg_lo:[0,1] neg_hi:[0,1]
	v_pk_add_f16 v117, v225, 0
	v_pk_fma_f16 v77, v77, v228, 0
	v_pk_add_f16 v114, v228, 0
	v_pk_add_f16 v115, v227, 0
	v_pk_add_f16 v116, v226, 0
	v_pk_fma_f16 v76, v76, v227, 0
	v_pk_fma_f16 v75, v75, v226, 0
	v_pk_fma_f16 v74, v74, v225, 0
	v_pk_add_f16 v132, v132, v211 neg_lo:[0,1] neg_hi:[0,1]
	buffer_load_dwordx4 v[106:109], v248, s[36:39], 0 offen offset:512
	buffer_load_dwordx4 v[42:45], v248, s[36:39], 0 offen offset:1024
	v_pk_add_f16 v133, v133, v212 neg_lo:[0,1] neg_hi:[0,1]
	v_exp_f16_sdwa v225, v130 dst_sel:WORD_0 dst_unused:UNUSED_PAD src0_sel:WORD_0
	v_exp_f16_sdwa v226, v131 dst_sel:WORD_0 dst_unused:UNUSED_PAD src0_sel:WORD_0
	v_exp_f16_sdwa v227, v132 dst_sel:WORD_0 dst_unused:UNUSED_PAD src0_sel:WORD_0
	v_exp_f16_sdwa v228, v133 dst_sel:WORD_0 dst_unused:UNUSED_PAD src0_sel:WORD_0
	v_exp_f16_sdwa v225, v130 dst_sel:WORD_1 dst_unused:UNUSED_PRESERVE src0_sel:WORD_1
	v_exp_f16_sdwa v226, v131 dst_sel:WORD_1 dst_unused:UNUSED_PRESERVE src0_sel:WORD_1
	v_exp_f16_sdwa v227, v132 dst_sel:WORD_1 dst_unused:UNUSED_PRESERVE src0_sel:WORD_1
	v_exp_f16_sdwa v228, v133 dst_sel:WORD_1 dst_unused:UNUSED_PRESERVE src0_sel:WORD_1
	v_pk_add_f16 v117, v117, v225
	v_pk_fma_f16 v77, v101, v228, v77
	v_pk_add_f16 v101, v141, v212 neg_lo:[0,1] neg_hi:[0,1]
	v_pk_add_f16 v116, v116, v226
	v_pk_add_f16 v115, v115, v227
	v_pk_add_f16 v114, v114, v228
	v_pk_fma_f16 v74, v98, v225, v74
	v_pk_fma_f16 v75, v99, v226, v75
	v_pk_fma_f16 v76, v100, v227, v76
	v_pk_add_f16 v98, v138, v209 neg_lo:[0,1] neg_hi:[0,1]
	v_pk_add_f16 v99, v139, v210 neg_lo:[0,1] neg_hi:[0,1]
	v_pk_add_f16 v100, v140, v211 neg_lo:[0,1] neg_hi:[0,1]
	v_exp_f16_sdwa v130, v98 dst_sel:WORD_0 dst_unused:UNUSED_PAD src0_sel:WORD_0
	v_exp_f16_sdwa v131, v99 dst_sel:WORD_0 dst_unused:UNUSED_PAD src0_sel:WORD_0
	v_exp_f16_sdwa v132, v100 dst_sel:WORD_0 dst_unused:UNUSED_PAD src0_sel:WORD_0
	v_exp_f16_sdwa v133, v101 dst_sel:WORD_0 dst_unused:UNUSED_PAD src0_sel:WORD_0
	v_exp_f16_sdwa v130, v98 dst_sel:WORD_1 dst_unused:UNUSED_PRESERVE src0_sel:WORD_1
	v_exp_f16_sdwa v131, v99 dst_sel:WORD_1 dst_unused:UNUSED_PRESERVE src0_sel:WORD_1
	v_exp_f16_sdwa v132, v100 dst_sel:WORD_1 dst_unused:UNUSED_PRESERVE src0_sel:WORD_1
	v_exp_f16_sdwa v133, v101 dst_sel:WORD_1 dst_unused:UNUSED_PRESERVE src0_sel:WORD_1
	v_pk_add_f16 v101, v117, v130
	v_pk_add_f16 v98, v114, v133
	s_mov_b64 exec, s[66:67]
	buffer_load_dwordx4 v[122:125], v248, s[36:39], 0 offen offset:2048
	buffer_load_dwordx4 v[62:65], v248, s[36:39], 0 offen offset:2560
	s_mov_b64 exec, -1
	v_pk_add_f16 v99, v115, v132
	v_pk_add_f16 v100, v116, v131
	v_pk_fma_f16 v77, v121, v133, v77
	v_pk_fma_f16 v76, v120, v132, v76
	v_pk_fma_f16 v75, v119, v131, v75
	v_pk_fma_f16 v74, v118, v130, v74
	v_pk_add_f16 v114, v204, v209 neg_lo:[0,1] neg_hi:[0,1]
	v_pk_add_f16 v115, v203, v210 neg_lo:[0,1] neg_hi:[0,1]
	v_pk_add_f16 v116, v202, v211 neg_lo:[0,1] neg_hi:[0,1]
	v_pk_add_f16 v117, v161, v212 neg_lo:[0,1] neg_hi:[0,1]
	v_exp_f16_sdwa v118, v114 dst_sel:WORD_0 dst_unused:UNUSED_PAD src0_sel:WORD_0
	v_exp_f16_sdwa v119, v115 dst_sel:WORD_0 dst_unused:UNUSED_PAD src0_sel:WORD_0
	v_exp_f16_sdwa v120, v116 dst_sel:WORD_0 dst_unused:UNUSED_PAD src0_sel:WORD_0
	v_exp_f16_sdwa v121, v117 dst_sel:WORD_0 dst_unused:UNUSED_PAD src0_sel:WORD_0
	v_exp_f16_sdwa v118, v114 dst_sel:WORD_1 dst_unused:UNUSED_PRESERVE src0_sel:WORD_1
	v_exp_f16_sdwa v119, v115 dst_sel:WORD_1 dst_unused:UNUSED_PRESERVE src0_sel:WORD_1
	v_exp_f16_sdwa v120, v116 dst_sel:WORD_1 dst_unused:UNUSED_PRESERVE src0_sel:WORD_1
	v_exp_f16_sdwa v121, v117 dst_sel:WORD_1 dst_unused:UNUSED_PRESERVE src0_sel:WORD_1
	v_pk_add_f16 v114, v216, v209 neg_lo:[0,1] neg_hi:[0,1]
	v_pk_add_f16 v101, v101, v118
	v_pk_add_f16 v100, v100, v119
	v_pk_add_f16 v99, v99, v120
	s_mov_b64 exec, s[76:77]
	buffer_load_dwordx4 v[134:137], v249, s[36:39], 0 offen
	buffer_load_dwordx4 v[82:85], v249, s[36:39], 0 offen offset:512
	s_mov_b64 exec, -1
	v_pk_add_f16 v98, v98, v121
	v_pk_fma_f16 v74, v46, v118, v74
	v_pk_fma_f16 v75, v47, v119, v75
	v_pk_fma_f16 v76, v48, v120, v76
	v_pk_fma_f16 v77, v49, v121, v77
	v_pk_add_f16 v115, v215, v210 neg_lo:[0,1] neg_hi:[0,1]
	v_pk_add_f16 v116, v214, v211 neg_lo:[0,1] neg_hi:[0,1]
	v_pk_add_f16 v117, v213, v212 neg_lo:[0,1] neg_hi:[0,1]
	v_exp_f16_sdwa v118, v114 dst_sel:WORD_0 dst_unused:UNUSED_PAD src0_sel:WORD_0
	v_exp_f16_sdwa v119, v115 dst_sel:WORD_0 dst_unused:UNUSED_PAD src0_sel:WORD_0
	v_exp_f16_sdwa v120, v116 dst_sel:WORD_0 dst_unused:UNUSED_PAD src0_sel:WORD_0
	v_exp_f16_sdwa v121, v117 dst_sel:WORD_0 dst_unused:UNUSED_PAD src0_sel:WORD_0
	v_exp_f16_sdwa v118, v114 dst_sel:WORD_1 dst_unused:UNUSED_PRESERVE src0_sel:WORD_1
	v_exp_f16_sdwa v119, v115 dst_sel:WORD_1 dst_unused:UNUSED_PRESERVE src0_sel:WORD_1
	v_exp_f16_sdwa v120, v116 dst_sel:WORD_1 dst_unused:UNUSED_PRESERVE src0_sel:WORD_1
	v_exp_f16_sdwa v121, v117 dst_sel:WORD_1 dst_unused:UNUSED_PRESERVE src0_sel:WORD_1
	v_pk_add_f16 v114, v205, v209 neg_lo:[0,1] neg_hi:[0,1]
	v_pk_add_f16 v101, v101, v118
	v_pk_add_f16 v98, v98, v121
	v_pk_add_f16 v99, v99, v120
	v_pk_add_f16 v100, v100, v119
	v_pk_fma_f16 v77, v69, v121, v77
	v_pk_fma_f16 v76, v68, v120, v76
	s_mov_b64 exec, s[70:71]
	buffer_load_dwordx4 v[142:145], v250, s[36:39], 0 offen offset:512
	buffer_load_dwordx4 v[102:105], v250, s[36:39], 0 offen offset:1024
	s_mov_b64 exec, -1
	v_pk_fma_f16 v75, v67, v119, v75
	v_pk_fma_f16 v74, v66, v118, v74
	v_pk_add_f16 v115, v206, v210 neg_lo:[0,1] neg_hi:[0,1]
	v_pk_add_f16 v116, v207, v211 neg_lo:[0,1] neg_hi:[0,1]
	v_pk_add_f16 v117, v208, v212 neg_lo:[0,1] neg_hi:[0,1]
	v_exp_f16_sdwa v118, v114 dst_sel:WORD_0 dst_unused:UNUSED_PAD src0_sel:WORD_0
	v_exp_f16_sdwa v119, v115 dst_sel:WORD_0 dst_unused:UNUSED_PAD src0_sel:WORD_0
	v_exp_f16_sdwa v120, v116 dst_sel:WORD_0 dst_unused:UNUSED_PAD src0_sel:WORD_0
	v_exp_f16_sdwa v121, v117 dst_sel:WORD_0 dst_unused:UNUSED_PAD src0_sel:WORD_0
	v_exp_f16_sdwa v118, v114 dst_sel:WORD_1 dst_unused:UNUSED_PRESERVE src0_sel:WORD_1
	v_exp_f16_sdwa v119, v115 dst_sel:WORD_1 dst_unused:UNUSED_PRESERVE src0_sel:WORD_1
	v_exp_f16_sdwa v120, v116 dst_sel:WORD_1 dst_unused:UNUSED_PRESERVE src0_sel:WORD_1
	v_exp_f16_sdwa v121, v117 dst_sel:WORD_1 dst_unused:UNUSED_PRESERVE src0_sel:WORD_1
	v_pk_add_f16 v114, v220, v209 neg_lo:[0,1] neg_hi:[0,1]
	v_pk_add_f16 v101, v101, v118
	v_pk_add_f16 v100, v100, v119
	v_pk_add_f16 v99, v99, v120
	v_pk_add_f16 v98, v98, v121
	v_pk_fma_f16 v74, v90, v118, v74
	v_pk_fma_f16 v75, v91, v119, v75
	v_pk_fma_f16 v76, v92, v120, v76
	v_pk_fma_f16 v77, v93, v121, v77
	s_mov_b64 exec, s[78:79]
	buffer_load_dwordx4 v[6:9], v250, s[36:39], 0 offen offset:2048
	buffer_load_dwordx4 v[2:5], v250, s[36:39], 0 offen offset:2560
	s_mov_b64 exec, -1
	v_pk_add_f16 v115, v219, v210 neg_lo:[0,1] neg_hi:[0,1]
	v_pk_add_f16 v116, v218, v211 neg_lo:[0,1] neg_hi:[0,1]
	v_pk_add_f16 v117, v217, v212 neg_lo:[0,1] neg_hi:[0,1]
	v_exp_f16_sdwa v118, v114 dst_sel:WORD_0 dst_unused:UNUSED_PAD src0_sel:WORD_0
	v_exp_f16_sdwa v119, v115 dst_sel:WORD_0 dst_unused:UNUSED_PAD src0_sel:WORD_0
	v_exp_f16_sdwa v120, v116 dst_sel:WORD_0 dst_unused:UNUSED_PAD src0_sel:WORD_0
	v_exp_f16_sdwa v121, v117 dst_sel:WORD_0 dst_unused:UNUSED_PAD src0_sel:WORD_0
	v_exp_f16_sdwa v118, v114 dst_sel:WORD_1 dst_unused:UNUSED_PRESERVE src0_sel:WORD_1
	v_exp_f16_sdwa v119, v115 dst_sel:WORD_1 dst_unused:UNUSED_PRESERVE src0_sel:WORD_1
	v_exp_f16_sdwa v120, v116 dst_sel:WORD_1 dst_unused:UNUSED_PRESERVE src0_sel:WORD_1
	v_exp_f16_sdwa v121, v117 dst_sel:WORD_1 dst_unused:UNUSED_PRESERVE src0_sel:WORD_1
	v_pk_add_f16 v114, v224, v209 neg_lo:[0,1] neg_hi:[0,1]
	v_pk_add_f16 v101, v101, v118
	v_pk_add_f16 v98, v98, v121
	v_pk_add_f16 v99, v99, v120
	v_pk_add_f16 v100, v100, v119
	v_pk_fma_f16 v77, v25, v121, v77
	v_pk_fma_f16 v76, v24, v120, v76
	v_pk_fma_f16 v75, v23, v119, v75
	v_pk_fma_f16 v74, v22, v118, v74
	v_pk_add_f16 v115, v223, v210 neg_lo:[0,1] neg_hi:[0,1]
	v_pk_add_f16 v116, v222, v211 neg_lo:[0,1] neg_hi:[0,1]
	v_pk_add_f16 v117, v221, v212 neg_lo:[0,1] neg_hi:[0,1]
	v_exp_f16_sdwa v118, v114 dst_sel:WORD_0 dst_unused:UNUSED_PAD src0_sel:WORD_0
	v_exp_f16_sdwa v119, v115 dst_sel:WORD_0 dst_unused:UNUSED_PAD src0_sel:WORD_0
	v_exp_f16_sdwa v120, v116 dst_sel:WORD_0 dst_unused:UNUSED_PAD src0_sel:WORD_0
	v_exp_f16_sdwa v121, v117 dst_sel:WORD_0 dst_unused:UNUSED_PAD src0_sel:WORD_0
	v_exp_f16_sdwa v118, v114 dst_sel:WORD_1 dst_unused:UNUSED_PRESERVE src0_sel:WORD_1
	v_exp_f16_sdwa v119, v115 dst_sel:WORD_1 dst_unused:UNUSED_PRESERVE src0_sel:WORD_1
	v_exp_f16_sdwa v120, v116 dst_sel:WORD_1 dst_unused:UNUSED_PRESERVE src0_sel:WORD_1
	v_exp_f16_sdwa v121, v117 dst_sel:WORD_1 dst_unused:UNUSED_PRESERVE src0_sel:WORD_1
	v_pk_add_f16 v114, v162, v209 neg_lo:[0,1] neg_hi:[0,1]
	v_pk_add_f16 v101, v101, v118
	v_pk_add_f16 v100, v100, v119
	v_pk_add_f16 v99, v99, v120
	v_pk_add_f16 v98, v98, v121
	v_pk_fma_f16 v74, v34, v118, v74
	v_pk_fma_f16 v75, v35, v119, v75
	v_pk_fma_f16 v76, v36, v120, v76
	v_pk_fma_f16 v77, v37, v121, v77
	v_pk_add_f16 v115, v163, v210 neg_lo:[0,1] neg_hi:[0,1]
	v_pk_add_f16 v116, v164, v211 neg_lo:[0,1] neg_hi:[0,1]
	v_pk_add_f16 v117, v165, v212 neg_lo:[0,1] neg_hi:[0,1]
	v_exp_f16_sdwa v118, v114 dst_sel:WORD_0 dst_unused:UNUSED_PAD src0_sel:WORD_0
	v_exp_f16_sdwa v119, v115 dst_sel:WORD_0 dst_unused:UNUSED_PAD src0_sel:WORD_0
	v_exp_f16_sdwa v120, v116 dst_sel:WORD_0 dst_unused:UNUSED_PAD src0_sel:WORD_0
	v_exp_f16_sdwa v121, v117 dst_sel:WORD_0 dst_unused:UNUSED_PAD src0_sel:WORD_0
	v_exp_f16_sdwa v118, v114 dst_sel:WORD_1 dst_unused:UNUSED_PRESERVE src0_sel:WORD_1
	v_exp_f16_sdwa v119, v115 dst_sel:WORD_1 dst_unused:UNUSED_PRESERVE src0_sel:WORD_1
	v_exp_f16_sdwa v120, v116 dst_sel:WORD_1 dst_unused:UNUSED_PRESERVE src0_sel:WORD_1
	v_exp_f16_sdwa v121, v117 dst_sel:WORD_1 dst_unused:UNUSED_PRESERVE src0_sel:WORD_1
	v_pk_add_f16 v101, v101, v118
	v_pk_add_f16 v100, v100, v119
	v_rcp_f16_e32 v114, v101
	v_rcp_f16_sdwa v101, v101 dst_sel:DWORD dst_unused:UNUSED_PAD src0_sel:WORD_1
	v_pk_add_f16 v99, v99, v120
	v_rcp_f16_e32 v115, v100
	v_rcp_f16_sdwa v100, v100 dst_sel:DWORD dst_unused:UNUSED_PAD src0_sel:WORD_1
	v_pk_add_f16 v98, v98, v121
	v_rcp_f16_e32 v116, v99
	v_rcp_f16_sdwa v99, v99 dst_sel:DWORD dst_unused:UNUSED_PAD src0_sel:WORD_1
	v_rcp_f16_e32 v117, v98
	v_rcp_f16_sdwa v98, v98 dst_sel:DWORD dst_unused:UNUSED_PAD src0_sel:WORD_1
	v_pk_fma_f16 v74, v50, v118, v74
	v_pack_b32_f16 v101, v114, v101
	v_pk_fma_f16 v75, v51, v119, v75
	v_pk_mul_f16 v138, v74, v101
	v_pack_b32_f16 v74, v115, v100
	v_pk_fma_f16 v76, v52, v120, v76
	v_pk_mul_f16 v139, v75, v74
	v_pack_b32_f16 v74, v116, v99
	v_pk_fma_f16 v77, v53, v121, v77
	v_pk_mul_f16 v140, v76, v74
	v_pack_b32_f16 v74, v117, v98
	v_pk_mul_f16 v141, v77, v74
	s_waitcnt vmcnt(12)
	v_pk_mul_f16 v74, v160, v154 op_sel_hi:[0,1]
	v_pk_mul_f16 v77, v160, v157 op_sel_hi:[0,1]
	v_pk_mul_f16 v101, v158, v157 op_sel_hi:[0,1]
	v_pk_mul_f16 v117, v159, v157 op_sel_hi:[0,1]
	v_pk_mul_f16 v75, v160, v155 op_sel_hi:[0,1]
	v_pk_mul_f16 v76, v160, v156 op_sel_hi:[0,1]
	v_pk_mul_f16 v98, v158, v154 op_sel_hi:[0,1]
	v_pk_mul_f16 v99, v158, v155 op_sel_hi:[0,1]
	v_pk_mul_f16 v100, v158, v156 op_sel_hi:[0,1]
	v_pk_mul_f16 v114, v159, v154 op_sel_hi:[0,1]
	v_pk_mul_f16 v115, v159, v155 op_sel_hi:[0,1]
	v_pk_mul_f16 v116, v159, v156 op_sel_hi:[0,1]
	v_pk_fma_f16 v89, v89, v157, v77
	v_pk_fma_f16 v86, v86, v154, v74
	v_pk_fma_f16 v113, v113, v157, v77
	v_pk_fma_f16 v110, v110, v154, v74
	v_pk_fma_f16 v77, v129, v157, v77
	v_pk_fma_f16 v74, v126, v154, v74
	v_pk_fma_f16 v118, v57, v157, v101
	v_pk_fma_f16 v126, v73, v157, v101
	v_pk_fma_f16 v101, v97, v157, v101
	v_pk_fma_f16 v130, v29, v157, v117
	v_pk_fma_f16 v161, v41, v157, v117
	v_pk_fma_f16 v117, v61, v157, v117
	v_pk_maximum3_f16 v157, v89, v113, v77
	v_pk_fma_f16 v88, v88, v156, v76
	v_pk_fma_f16 v87, v87, v155, v75
	v_pk_fma_f16 v112, v112, v156, v76
	v_pk_fma_f16 v111, v111, v155, v75
	v_pk_fma_f16 v76, v128, v156, v76
	v_pk_fma_f16 v75, v127, v155, v75
	v_pk_fma_f16 v119, v56, v156, v100
	v_pk_fma_f16 v120, v55, v155, v99
	v_pk_fma_f16 v121, v54, v154, v98
	v_pk_fma_f16 v127, v72, v156, v100
	v_pk_fma_f16 v128, v71, v155, v99
	v_pk_fma_f16 v129, v70, v154, v98
	v_pk_fma_f16 v100, v96, v156, v100
	v_pk_fma_f16 v99, v95, v155, v99
	v_pk_fma_f16 v98, v94, v154, v98
	v_pk_fma_f16 v131, v28, v156, v116
	v_pk_fma_f16 v132, v27, v155, v115
	v_pk_fma_f16 v133, v26, v154, v114
	v_pk_fma_f16 v162, v40, v156, v116
	v_pk_fma_f16 v163, v39, v155, v115
	v_pk_fma_f16 v164, v38, v154, v114
	v_pk_fma_f16 v116, v60, v156, v116
	v_pk_fma_f16 v115, v59, v155, v115
	v_pk_fma_f16 v114, v58, v154, v114
	v_pk_maximum3_f16 v154, v86, v110, v74
	v_pk_maximum3_f16 v155, v87, v111, v75
	v_pk_maximum3_f16 v156, v88, v112, v76
	v_pk_maximum3_f16 v204, v118, v126, v101
	v_pk_maximum3_f16 v208, v130, v161, v117
	v_pk_maximum3_f16 v165, v121, v129, v98
	v_pk_maximum3_f16 v202, v120, v128, v99
	v_pk_maximum3_f16 v203, v119, v127, v100
	v_pk_maximum3_f16 v205, v133, v164, v114
	v_pk_maximum3_f16 v206, v132, v163, v115
	v_pk_maximum3_f16 v157, v157, v204, v208
	v_pk_maximum3_f16 v207, v131, v162, v116
	v_pk_maximum3_f16 v154, v154, v165, v205
	v_pk_maximum3_f16 v155, v155, v202, v206
	v_pk_maximum3_f16 v156, v156, v203, v207
	v_pk_add_f16 v89, v89, v157 neg_lo:[0,1] neg_hi:[0,1]
	v_pk_add_f16 v86, v86, v154 neg_lo:[0,1] neg_hi:[0,1]
	v_pk_add_f16 v87, v87, v155 neg_lo:[0,1] neg_hi:[0,1]
	v_pk_add_f16 v88, v88, v156 neg_lo:[0,1] neg_hi:[0,1]
	v_pk_add_f16 v110, v110, v154 neg_lo:[0,1] neg_hi:[0,1]
	v_exp_f16_sdwa v165, v86 dst_sel:WORD_0 dst_unused:UNUSED_PAD src0_sel:WORD_0
	v_exp_f16_sdwa v202, v87 dst_sel:WORD_0 dst_unused:UNUSED_PAD src0_sel:WORD_0
	v_exp_f16_sdwa v203, v88 dst_sel:WORD_0 dst_unused:UNUSED_PAD src0_sel:WORD_0
	v_exp_f16_sdwa v204, v89 dst_sel:WORD_0 dst_unused:UNUSED_PAD src0_sel:WORD_0
	v_exp_f16_sdwa v165, v86 dst_sel:WORD_1 dst_unused:UNUSED_PRESERVE src0_sel:WORD_1
	v_exp_f16_sdwa v202, v87 dst_sel:WORD_1 dst_unused:UNUSED_PRESERVE src0_sel:WORD_1
	v_exp_f16_sdwa v203, v88 dst_sel:WORD_1 dst_unused:UNUSED_PRESERVE src0_sel:WORD_1
	v_exp_f16_sdwa v204, v89 dst_sel:WORD_1 dst_unused:UNUSED_PRESERVE src0_sel:WORD_1
	v_pk_add_f16 v111, v111, v155 neg_lo:[0,1] neg_hi:[0,1]
	v_pk_add_f16 v89, v165, 0
	v_pk_fma_f16 v49, v49, v204, 0
	v_pk_add_f16 v86, v204, 0
	v_pk_add_f16 v87, v203, 0
	v_pk_add_f16 v88, v202, 0
	v_pk_fma_f16 v48, v48, v203, 0
	v_pk_fma_f16 v47, v47, v202, 0
	v_pk_fma_f16 v46, v46, v165, 0
	v_pk_add_f16 v112, v112, v156 neg_lo:[0,1] neg_hi:[0,1]
	v_pk_add_f16 v113, v113, v157 neg_lo:[0,1] neg_hi:[0,1]
	v_exp_f16_sdwa v165, v110 dst_sel:WORD_0 dst_unused:UNUSED_PAD src0_sel:WORD_0
	v_exp_f16_sdwa v202, v111 dst_sel:WORD_0 dst_unused:UNUSED_PAD src0_sel:WORD_0
	v_exp_f16_sdwa v203, v112 dst_sel:WORD_0 dst_unused:UNUSED_PAD src0_sel:WORD_0
	v_exp_f16_sdwa v204, v113 dst_sel:WORD_0 dst_unused:UNUSED_PAD src0_sel:WORD_0
	v_exp_f16_sdwa v165, v110 dst_sel:WORD_1 dst_unused:UNUSED_PRESERVE src0_sel:WORD_1
	v_exp_f16_sdwa v202, v111 dst_sel:WORD_1 dst_unused:UNUSED_PRESERVE src0_sel:WORD_1
	v_exp_f16_sdwa v203, v112 dst_sel:WORD_1 dst_unused:UNUSED_PRESERVE src0_sel:WORD_1
	v_exp_f16_sdwa v204, v113 dst_sel:WORD_1 dst_unused:UNUSED_PRESERVE src0_sel:WORD_1
	v_pk_add_f16 v89, v89, v165
	v_pk_fma_f16 v49, v69, v204, v49
	v_pk_add_f16 v69, v77, v157 neg_lo:[0,1] neg_hi:[0,1]
	v_pk_add_f16 v88, v88, v202
	v_pk_add_f16 v87, v87, v203
	v_pk_add_f16 v86, v86, v204
	v_pk_fma_f16 v46, v66, v165, v46
	v_pk_fma_f16 v47, v67, v202, v47
	v_pk_fma_f16 v48, v68, v203, v48
	v_pk_add_f16 v66, v74, v154 neg_lo:[0,1] neg_hi:[0,1]
	v_pk_add_f16 v67, v75, v155 neg_lo:[0,1] neg_hi:[0,1]
	v_pk_add_f16 v68, v76, v156 neg_lo:[0,1] neg_hi:[0,1]
	v_exp_f16_sdwa v74, v66 dst_sel:WORD_0 dst_unused:UNUSED_PAD src0_sel:WORD_0
	v_exp_f16_sdwa v75, v67 dst_sel:WORD_0 dst_unused:UNUSED_PAD src0_sel:WORD_0
	v_exp_f16_sdwa v76, v68 dst_sel:WORD_0 dst_unused:UNUSED_PAD src0_sel:WORD_0
	v_exp_f16_sdwa v77, v69 dst_sel:WORD_0 dst_unused:UNUSED_PAD src0_sel:WORD_0
	v_exp_f16_sdwa v74, v66 dst_sel:WORD_1 dst_unused:UNUSED_PRESERVE src0_sel:WORD_1
	v_exp_f16_sdwa v75, v67 dst_sel:WORD_1 dst_unused:UNUSED_PRESERVE src0_sel:WORD_1
	v_exp_f16_sdwa v76, v68 dst_sel:WORD_1 dst_unused:UNUSED_PRESERVE src0_sel:WORD_1
	v_exp_f16_sdwa v77, v69 dst_sel:WORD_1 dst_unused:UNUSED_PRESERVE src0_sel:WORD_1
	v_pk_add_f16 v69, v89, v74
	v_pk_add_f16 v66, v86, v77
	v_pk_add_f16 v67, v87, v76
	v_pk_add_f16 v68, v88, v75
	v_pk_fma_f16 v49, v93, v77, v49
	v_pk_fma_f16 v48, v92, v76, v48
	v_pk_fma_f16 v47, v91, v75, v47
	v_pk_fma_f16 v46, v90, v74, v46
	v_pk_add_f16 v74, v121, v154 neg_lo:[0,1] neg_hi:[0,1]
	v_pk_add_f16 v75, v120, v155 neg_lo:[0,1] neg_hi:[0,1]
	v_pk_add_f16 v76, v119, v156 neg_lo:[0,1] neg_hi:[0,1]
	v_pk_add_f16 v77, v118, v157 neg_lo:[0,1] neg_hi:[0,1]
	v_exp_f16_sdwa v86, v74 dst_sel:WORD_0 dst_unused:UNUSED_PAD src0_sel:WORD_0
	v_exp_f16_sdwa v87, v75 dst_sel:WORD_0 dst_unused:UNUSED_PAD src0_sel:WORD_0
	v_exp_f16_sdwa v88, v76 dst_sel:WORD_0 dst_unused:UNUSED_PAD src0_sel:WORD_0
	v_exp_f16_sdwa v89, v77 dst_sel:WORD_0 dst_unused:UNUSED_PAD src0_sel:WORD_0
	v_exp_f16_sdwa v86, v74 dst_sel:WORD_1 dst_unused:UNUSED_PRESERVE src0_sel:WORD_1
	v_exp_f16_sdwa v87, v75 dst_sel:WORD_1 dst_unused:UNUSED_PRESERVE src0_sel:WORD_1
	v_exp_f16_sdwa v88, v76 dst_sel:WORD_1 dst_unused:UNUSED_PRESERVE src0_sel:WORD_1
	v_exp_f16_sdwa v89, v77 dst_sel:WORD_1 dst_unused:UNUSED_PRESERVE src0_sel:WORD_1
	v_pk_add_f16 v74, v129, v154 neg_lo:[0,1] neg_hi:[0,1]
	v_pk_add_f16 v69, v69, v86
	v_pk_add_f16 v68, v68, v87
	v_pk_add_f16 v67, v67, v88
	v_pk_add_f16 v66, v66, v89
	v_pk_fma_f16 v46, v22, v86, v46
	v_pk_fma_f16 v47, v23, v87, v47
	v_pk_fma_f16 v48, v24, v88, v48
	v_pk_fma_f16 v49, v25, v89, v49
	v_pk_add_f16 v75, v128, v155 neg_lo:[0,1] neg_hi:[0,1]
	v_pk_add_f16 v76, v127, v156 neg_lo:[0,1] neg_hi:[0,1]
	v_pk_add_f16 v77, v126, v157 neg_lo:[0,1] neg_hi:[0,1]
	v_exp_f16_sdwa v86, v74 dst_sel:WORD_0 dst_unused:UNUSED_PAD src0_sel:WORD_0
	v_exp_f16_sdwa v87, v75 dst_sel:WORD_0 dst_unused:UNUSED_PAD src0_sel:WORD_0
	v_exp_f16_sdwa v88, v76 dst_sel:WORD_0 dst_unused:UNUSED_PAD src0_sel:WORD_0
	v_exp_f16_sdwa v89, v77 dst_sel:WORD_0 dst_unused:UNUSED_PAD src0_sel:WORD_0
	v_exp_f16_sdwa v86, v74 dst_sel:WORD_1 dst_unused:UNUSED_PRESERVE src0_sel:WORD_1
	v_exp_f16_sdwa v87, v75 dst_sel:WORD_1 dst_unused:UNUSED_PRESERVE src0_sel:WORD_1
	v_exp_f16_sdwa v88, v76 dst_sel:WORD_1 dst_unused:UNUSED_PRESERVE src0_sel:WORD_1
	v_exp_f16_sdwa v89, v77 dst_sel:WORD_1 dst_unused:UNUSED_PRESERVE src0_sel:WORD_1
	v_pk_add_f16 v74, v98, v154 neg_lo:[0,1] neg_hi:[0,1]
	v_pk_add_f16 v69, v69, v86
	v_pk_add_f16 v66, v66, v89
	v_pk_add_f16 v67, v67, v88
	v_pk_add_f16 v68, v68, v87
	v_pk_fma_f16 v49, v37, v89, v49
	v_pk_fma_f16 v48, v36, v88, v48
	v_pk_fma_f16 v47, v35, v87, v47
	v_pk_fma_f16 v46, v34, v86, v46
	v_pk_add_f16 v75, v99, v155 neg_lo:[0,1] neg_hi:[0,1]
	v_pk_add_f16 v76, v100, v156 neg_lo:[0,1] neg_hi:[0,1]
	v_pk_add_f16 v77, v101, v157 neg_lo:[0,1] neg_hi:[0,1]
	v_exp_f16_sdwa v86, v74 dst_sel:WORD_0 dst_unused:UNUSED_PAD src0_sel:WORD_0
	v_exp_f16_sdwa v87, v75 dst_sel:WORD_0 dst_unused:UNUSED_PAD src0_sel:WORD_0
	v_exp_f16_sdwa v88, v76 dst_sel:WORD_0 dst_unused:UNUSED_PAD src0_sel:WORD_0
	v_exp_f16_sdwa v89, v77 dst_sel:WORD_0 dst_unused:UNUSED_PAD src0_sel:WORD_0
	v_exp_f16_sdwa v86, v74 dst_sel:WORD_1 dst_unused:UNUSED_PRESERVE src0_sel:WORD_1
	v_exp_f16_sdwa v87, v75 dst_sel:WORD_1 dst_unused:UNUSED_PRESERVE src0_sel:WORD_1
	v_exp_f16_sdwa v88, v76 dst_sel:WORD_1 dst_unused:UNUSED_PRESERVE src0_sel:WORD_1
	v_exp_f16_sdwa v89, v77 dst_sel:WORD_1 dst_unused:UNUSED_PRESERVE src0_sel:WORD_1
	v_pk_add_f16 v74, v133, v154 neg_lo:[0,1] neg_hi:[0,1]
	v_pk_add_f16 v69, v69, v86
	v_pk_add_f16 v68, v68, v87
	v_pk_add_f16 v67, v67, v88
	v_pk_add_f16 v66, v66, v89
	v_pk_fma_f16 v46, v50, v86, v46
	v_pk_fma_f16 v47, v51, v87, v47
	v_pk_fma_f16 v48, v52, v88, v48
	v_pk_fma_f16 v49, v53, v89, v49
	v_pk_add_f16 v75, v132, v155 neg_lo:[0,1] neg_hi:[0,1]
	v_pk_add_f16 v76, v131, v156 neg_lo:[0,1] neg_hi:[0,1]
	v_pk_add_f16 v77, v130, v157 neg_lo:[0,1] neg_hi:[0,1]
	v_exp_f16_sdwa v86, v74 dst_sel:WORD_0 dst_unused:UNUSED_PAD src0_sel:WORD_0
	v_exp_f16_sdwa v87, v75 dst_sel:WORD_0 dst_unused:UNUSED_PAD src0_sel:WORD_0
	v_exp_f16_sdwa v88, v76 dst_sel:WORD_0 dst_unused:UNUSED_PAD src0_sel:WORD_0
	v_exp_f16_sdwa v89, v77 dst_sel:WORD_0 dst_unused:UNUSED_PAD src0_sel:WORD_0
	v_exp_f16_sdwa v86, v74 dst_sel:WORD_1 dst_unused:UNUSED_PRESERVE src0_sel:WORD_1
	v_exp_f16_sdwa v87, v75 dst_sel:WORD_1 dst_unused:UNUSED_PRESERVE src0_sel:WORD_1
	v_exp_f16_sdwa v88, v76 dst_sel:WORD_1 dst_unused:UNUSED_PRESERVE src0_sel:WORD_1
	v_exp_f16_sdwa v89, v77 dst_sel:WORD_1 dst_unused:UNUSED_PRESERVE src0_sel:WORD_1
	v_pk_add_f16 v74, v164, v154 neg_lo:[0,1] neg_hi:[0,1]
	v_pk_add_f16 v69, v69, v86
	v_pk_add_f16 v66, v66, v89
	v_pk_add_f16 v67, v67, v88
	v_pk_add_f16 v68, v68, v87
	v_pk_fma_f16 v49, v13, v89, v49
	v_pk_fma_f16 v48, v12, v88, v48
	v_pk_fma_f16 v47, v11, v87, v47
	v_pk_fma_f16 v46, v10, v86, v46
	v_pk_add_f16 v75, v163, v155 neg_lo:[0,1] neg_hi:[0,1]
	v_pk_add_f16 v76, v162, v156 neg_lo:[0,1] neg_hi:[0,1]
	v_pk_add_f16 v77, v161, v157 neg_lo:[0,1] neg_hi:[0,1]
	v_exp_f16_sdwa v86, v74 dst_sel:WORD_0 dst_unused:UNUSED_PAD src0_sel:WORD_0
	v_exp_f16_sdwa v87, v75 dst_sel:WORD_0 dst_unused:UNUSED_PAD src0_sel:WORD_0
	v_exp_f16_sdwa v88, v76 dst_sel:WORD_0 dst_unused:UNUSED_PAD src0_sel:WORD_0
	v_exp_f16_sdwa v89, v77 dst_sel:WORD_0 dst_unused:UNUSED_PAD src0_sel:WORD_0
	v_exp_f16_sdwa v86, v74 dst_sel:WORD_1 dst_unused:UNUSED_PRESERVE src0_sel:WORD_1
	v_exp_f16_sdwa v87, v75 dst_sel:WORD_1 dst_unused:UNUSED_PRESERVE src0_sel:WORD_1
	v_exp_f16_sdwa v88, v76 dst_sel:WORD_1 dst_unused:UNUSED_PRESERVE src0_sel:WORD_1
	v_exp_f16_sdwa v89, v77 dst_sel:WORD_1 dst_unused:UNUSED_PRESERVE src0_sel:WORD_1
	v_pk_add_f16 v74, v114, v154 neg_lo:[0,1] neg_hi:[0,1]
	v_pk_add_f16 v69, v69, v86
	v_pk_add_f16 v68, v68, v87
	v_pk_add_f16 v67, v67, v88
	v_pk_add_f16 v66, v66, v89
	v_pk_fma_f16 v46, v14, v86, v46
	v_pk_fma_f16 v47, v15, v87, v47
	v_pk_fma_f16 v48, v16, v88, v48
	v_pk_fma_f16 v49, v17, v89, v49
	v_pk_add_f16 v75, v115, v155 neg_lo:[0,1] neg_hi:[0,1]
	v_pk_add_f16 v76, v116, v156 neg_lo:[0,1] neg_hi:[0,1]
	v_pk_add_f16 v77, v117, v157 neg_lo:[0,1] neg_hi:[0,1]
	v_exp_f16_sdwa v86, v74 dst_sel:WORD_0 dst_unused:UNUSED_PAD src0_sel:WORD_0
	v_exp_f16_sdwa v87, v75 dst_sel:WORD_0 dst_unused:UNUSED_PAD src0_sel:WORD_0
	v_exp_f16_sdwa v88, v76 dst_sel:WORD_0 dst_unused:UNUSED_PAD src0_sel:WORD_0
	v_exp_f16_sdwa v89, v77 dst_sel:WORD_0 dst_unused:UNUSED_PAD src0_sel:WORD_0
	v_exp_f16_sdwa v86, v74 dst_sel:WORD_1 dst_unused:UNUSED_PRESERVE src0_sel:WORD_1
	v_exp_f16_sdwa v87, v75 dst_sel:WORD_1 dst_unused:UNUSED_PRESERVE src0_sel:WORD_1
	v_exp_f16_sdwa v88, v76 dst_sel:WORD_1 dst_unused:UNUSED_PRESERVE src0_sel:WORD_1
	v_exp_f16_sdwa v89, v77 dst_sel:WORD_1 dst_unused:UNUSED_PRESERVE src0_sel:WORD_1
	v_pk_add_f16 v69, v69, v86
	v_pk_add_f16 v68, v68, v87
	v_rcp_f16_e32 v74, v69
	v_rcp_f16_sdwa v69, v69 dst_sel:DWORD dst_unused:UNUSED_PAD src0_sel:WORD_1
	v_pk_add_f16 v67, v67, v88
	v_rcp_f16_e32 v75, v68
	v_rcp_f16_sdwa v68, v68 dst_sel:DWORD dst_unused:UNUSED_PAD src0_sel:WORD_1
	v_pk_add_f16 v66, v66, v89
	v_pk_fma_f16 v46, v18, v86, v46
	v_rcp_f16_e32 v86, v67
	v_rcp_f16_sdwa v67, v67 dst_sel:DWORD dst_unused:UNUSED_PAD src0_sel:WORD_1
	v_pk_fma_f16 v47, v19, v87, v47
	v_rcp_f16_e32 v87, v66
	v_rcp_f16_sdwa v66, v66 dst_sel:DWORD dst_unused:UNUSED_PAD src0_sel:WORD_1
	v_pack_b32_f16 v69, v74, v69
	v_pk_mul_f16 v77, v46, v69
	v_pack_b32_f16 v46, v75, v68
	v_pk_fma_f16 v48, v20, v88, v48
	v_pk_mul_f16 v76, v47, v46
	v_pack_b32_f16 v46, v86, v67
	v_pk_fma_f16 v49, v21, v89, v49
	v_pk_mul_f16 v75, v48, v46
	v_pack_b32_f16 v46, v87, v66
	v_pk_mul_f16 v74, v49, v46
	s_waitcnt vmcnt(6)
	v_pk_mul_f16 v49, v160, v153 op_sel_hi:[0,1]
	v_pk_mul_f16 v46, v160, v150 op_sel_hi:[0,1]
	v_pk_mul_f16 v47, v160, v151 op_sel_hi:[0,1]
	v_pk_mul_f16 v48, v160, v152 op_sel_hi:[0,1]
	v_pk_mul_f16 v69, v158, v153 op_sel_hi:[0,1]
	v_pk_mul_f16 v89, v159, v153 op_sel_hi:[0,1]
	v_pk_fma_f16 v57, v57, v153, v49
	v_pk_fma_f16 v73, v73, v153, v49
	v_pk_fma_f16 v49, v97, v153, v49
	v_pk_mul_f16 v66, v158, v150 op_sel_hi:[0,1]
	v_pk_maximum3_f16 v117, v57, v73, v49
	v_pk_mul_f16 v67, v158, v151 op_sel_hi:[0,1]
	v_pk_mul_f16 v68, v158, v152 op_sel_hi:[0,1]
	v_pk_mul_f16 v86, v159, v150 op_sel_hi:[0,1]
	v_pk_mul_f16 v87, v159, v151 op_sel_hi:[0,1]
	v_pk_mul_f16 v88, v159, v152 op_sel_hi:[0,1]
	v_pk_fma_f16 v56, v56, v152, v48
	v_pk_fma_f16 v55, v55, v151, v47
	v_pk_fma_f16 v54, v54, v150, v46
	v_pk_fma_f16 v72, v72, v152, v48
	v_pk_fma_f16 v71, v71, v151, v47
	v_pk_fma_f16 v70, v70, v150, v46
	v_pk_fma_f16 v48, v96, v152, v48
	v_pk_fma_f16 v47, v95, v151, v47
	v_pk_fma_f16 v46, v94, v150, v46
	v_pk_fma_f16 v90, v29, v153, v69
	v_pk_fma_f16 v94, v41, v153, v69
	v_pk_fma_f16 v69, v61, v153, v69
	v_pk_fma_f16 v98, v81, v153, v89
	v_pk_fma_f16 v110, v109, v153, v89
	v_pk_fma_f16 v89, v125, v153, v89
	v_pk_maximum3_f16 v114, v54, v70, v46
	v_pk_maximum3_f16 v115, v55, v71, v47
	v_pk_maximum3_f16 v116, v56, v72, v48
	v_pk_maximum3_f16 v121, v90, v94, v69
	v_pk_fma_f16 v91, v28, v152, v68
	v_pk_maximum3_f16 v129, v98, v110, v89
	v_pk_fma_f16 v92, v27, v151, v67
	v_pk_maximum3_f16 v117, v117, v121, v129
	v_pk_fma_f16 v93, v26, v150, v66
	v_pk_fma_f16 v95, v40, v152, v68
	v_pk_fma_f16 v96, v39, v151, v67
	v_pk_fma_f16 v97, v38, v150, v66
	v_pk_fma_f16 v68, v60, v152, v68
	v_pk_fma_f16 v67, v59, v151, v67
	v_pk_fma_f16 v66, v58, v150, v66
	v_pk_fma_f16 v99, v80, v152, v88
	v_pk_fma_f16 v100, v79, v151, v87
	v_pk_fma_f16 v101, v78, v150, v86
	v_pk_fma_f16 v111, v108, v152, v88
	v_pk_fma_f16 v112, v107, v151, v87
	v_pk_fma_f16 v113, v106, v150, v86
	v_pk_fma_f16 v88, v124, v152, v88
	v_pk_fma_f16 v87, v123, v151, v87
	v_pk_fma_f16 v86, v122, v150, v86
	v_pk_maximum3_f16 v118, v93, v97, v66
	v_pk_maximum3_f16 v119, v92, v96, v67
	v_pk_maximum3_f16 v120, v91, v95, v68
	v_pk_maximum3_f16 v127, v100, v112, v87
	v_pk_maximum3_f16 v128, v99, v111, v88
	v_pk_maximum3_f16 v126, v101, v113, v86
	v_pk_maximum3_f16 v114, v114, v118, v126
	v_pk_maximum3_f16 v115, v115, v119, v127
	v_pk_maximum3_f16 v116, v116, v120, v128
	v_pk_add_f16 v57, v57, v117 neg_lo:[0,1] neg_hi:[0,1]
	v_pk_add_f16 v54, v54, v114 neg_lo:[0,1] neg_hi:[0,1]
	v_pk_add_f16 v55, v55, v115 neg_lo:[0,1] neg_hi:[0,1]
	v_pk_add_f16 v56, v56, v116 neg_lo:[0,1] neg_hi:[0,1]
	v_pk_add_f16 v70, v70, v114 neg_lo:[0,1] neg_hi:[0,1]
	v_exp_f16_sdwa v118, v54 dst_sel:WORD_0 dst_unused:UNUSED_PAD src0_sel:WORD_0
	v_exp_f16_sdwa v119, v55 dst_sel:WORD_0 dst_unused:UNUSED_PAD src0_sel:WORD_0
	v_exp_f16_sdwa v120, v56 dst_sel:WORD_0 dst_unused:UNUSED_PAD src0_sel:WORD_0
	v_exp_f16_sdwa v121, v57 dst_sel:WORD_0 dst_unused:UNUSED_PAD src0_sel:WORD_0
	v_exp_f16_sdwa v118, v54 dst_sel:WORD_1 dst_unused:UNUSED_PRESERVE src0_sel:WORD_1
	v_exp_f16_sdwa v119, v55 dst_sel:WORD_1 dst_unused:UNUSED_PRESERVE src0_sel:WORD_1
	v_exp_f16_sdwa v120, v56 dst_sel:WORD_1 dst_unused:UNUSED_PRESERVE src0_sel:WORD_1
	v_exp_f16_sdwa v121, v57 dst_sel:WORD_1 dst_unused:UNUSED_PRESERVE src0_sel:WORD_1
	v_pk_add_f16 v71, v71, v115 neg_lo:[0,1] neg_hi:[0,1]
	v_pk_add_f16 v57, v118, 0
	v_pk_fma_f16 v25, v25, v121, 0
	v_pk_add_f16 v54, v121, 0
	v_pk_add_f16 v55, v120, 0
	v_pk_add_f16 v56, v119, 0
	v_pk_fma_f16 v24, v24, v120, 0
	v_pk_fma_f16 v23, v23, v119, 0
	v_pk_fma_f16 v22, v22, v118, 0
	v_pk_add_f16 v72, v72, v116 neg_lo:[0,1] neg_hi:[0,1]
	v_pk_add_f16 v73, v73, v117 neg_lo:[0,1] neg_hi:[0,1]
	v_exp_f16_sdwa v118, v70 dst_sel:WORD_0 dst_unused:UNUSED_PAD src0_sel:WORD_0
	v_exp_f16_sdwa v119, v71 dst_sel:WORD_0 dst_unused:UNUSED_PAD src0_sel:WORD_0
	v_exp_f16_sdwa v120, v72 dst_sel:WORD_0 dst_unused:UNUSED_PAD src0_sel:WORD_0
	v_exp_f16_sdwa v121, v73 dst_sel:WORD_0 dst_unused:UNUSED_PAD src0_sel:WORD_0
	v_exp_f16_sdwa v118, v70 dst_sel:WORD_1 dst_unused:UNUSED_PRESERVE src0_sel:WORD_1
	v_exp_f16_sdwa v119, v71 dst_sel:WORD_1 dst_unused:UNUSED_PRESERVE src0_sel:WORD_1
	v_exp_f16_sdwa v120, v72 dst_sel:WORD_1 dst_unused:UNUSED_PRESERVE src0_sel:WORD_1
	v_exp_f16_sdwa v121, v73 dst_sel:WORD_1 dst_unused:UNUSED_PRESERVE src0_sel:WORD_1
	v_pk_add_f16 v57, v57, v118
	v_pk_fma_f16 v25, v37, v121, v25
	v_pk_add_f16 v37, v49, v117 neg_lo:[0,1] neg_hi:[0,1]
	v_pk_add_f16 v56, v56, v119
	v_pk_add_f16 v55, v55, v120
	v_pk_add_f16 v54, v54, v121
	v_pk_fma_f16 v22, v34, v118, v22
	v_pk_fma_f16 v23, v35, v119, v23
	v_pk_fma_f16 v24, v36, v120, v24
	v_pk_add_f16 v34, v46, v114 neg_lo:[0,1] neg_hi:[0,1]
	v_pk_add_f16 v35, v47, v115 neg_lo:[0,1] neg_hi:[0,1]
	v_pk_add_f16 v36, v48, v116 neg_lo:[0,1] neg_hi:[0,1]
	v_exp_f16_sdwa v46, v34 dst_sel:WORD_0 dst_unused:UNUSED_PAD src0_sel:WORD_0
	v_exp_f16_sdwa v47, v35 dst_sel:WORD_0 dst_unused:UNUSED_PAD src0_sel:WORD_0
	v_exp_f16_sdwa v48, v36 dst_sel:WORD_0 dst_unused:UNUSED_PAD src0_sel:WORD_0
	v_exp_f16_sdwa v49, v37 dst_sel:WORD_0 dst_unused:UNUSED_PAD src0_sel:WORD_0
	v_exp_f16_sdwa v46, v34 dst_sel:WORD_1 dst_unused:UNUSED_PRESERVE src0_sel:WORD_1
	v_exp_f16_sdwa v47, v35 dst_sel:WORD_1 dst_unused:UNUSED_PRESERVE src0_sel:WORD_1
	v_exp_f16_sdwa v48, v36 dst_sel:WORD_1 dst_unused:UNUSED_PRESERVE src0_sel:WORD_1
	v_exp_f16_sdwa v49, v37 dst_sel:WORD_1 dst_unused:UNUSED_PRESERVE src0_sel:WORD_1
	v_pk_add_f16 v37, v57, v46
	v_pk_add_f16 v34, v54, v49
	v_pk_add_f16 v35, v55, v48
	v_pk_add_f16 v36, v56, v47
	v_pk_fma_f16 v25, v53, v49, v25
	v_pk_fma_f16 v24, v52, v48, v24
	v_pk_fma_f16 v23, v51, v47, v23
	v_pk_fma_f16 v22, v50, v46, v22
	v_pk_add_f16 v46, v93, v114 neg_lo:[0,1] neg_hi:[0,1]
	v_pk_add_f16 v47, v92, v115 neg_lo:[0,1] neg_hi:[0,1]
	v_pk_add_f16 v48, v91, v116 neg_lo:[0,1] neg_hi:[0,1]
	v_pk_add_f16 v49, v90, v117 neg_lo:[0,1] neg_hi:[0,1]
	v_exp_f16_sdwa v50, v46 dst_sel:WORD_0 dst_unused:UNUSED_PAD src0_sel:WORD_0
	v_exp_f16_sdwa v51, v47 dst_sel:WORD_0 dst_unused:UNUSED_PAD src0_sel:WORD_0
	v_exp_f16_sdwa v52, v48 dst_sel:WORD_0 dst_unused:UNUSED_PAD src0_sel:WORD_0
	v_exp_f16_sdwa v53, v49 dst_sel:WORD_0 dst_unused:UNUSED_PAD src0_sel:WORD_0
	v_exp_f16_sdwa v50, v46 dst_sel:WORD_1 dst_unused:UNUSED_PRESERVE src0_sel:WORD_1
	v_exp_f16_sdwa v51, v47 dst_sel:WORD_1 dst_unused:UNUSED_PRESERVE src0_sel:WORD_1
	v_exp_f16_sdwa v52, v48 dst_sel:WORD_1 dst_unused:UNUSED_PRESERVE src0_sel:WORD_1
	v_exp_f16_sdwa v53, v49 dst_sel:WORD_1 dst_unused:UNUSED_PRESERVE src0_sel:WORD_1
	v_pk_add_f16 v46, v97, v114 neg_lo:[0,1] neg_hi:[0,1]
	v_pk_add_f16 v37, v37, v50
	v_pk_add_f16 v36, v36, v51
	v_pk_add_f16 v35, v35, v52
	v_pk_add_f16 v34, v34, v53
	v_pk_fma_f16 v22, v10, v50, v22
	v_pk_fma_f16 v23, v11, v51, v23
	v_pk_fma_f16 v24, v12, v52, v24
	v_pk_fma_f16 v25, v13, v53, v25
	v_pk_add_f16 v47, v96, v115 neg_lo:[0,1] neg_hi:[0,1]
	v_pk_add_f16 v48, v95, v116 neg_lo:[0,1] neg_hi:[0,1]
	v_pk_add_f16 v49, v94, v117 neg_lo:[0,1] neg_hi:[0,1]
	v_exp_f16_sdwa v50, v46 dst_sel:WORD_0 dst_unused:UNUSED_PAD src0_sel:WORD_0
	v_exp_f16_sdwa v51, v47 dst_sel:WORD_0 dst_unused:UNUSED_PAD src0_sel:WORD_0
	v_exp_f16_sdwa v52, v48 dst_sel:WORD_0 dst_unused:UNUSED_PAD src0_sel:WORD_0
	v_exp_f16_sdwa v53, v49 dst_sel:WORD_0 dst_unused:UNUSED_PAD src0_sel:WORD_0
	v_exp_f16_sdwa v50, v46 dst_sel:WORD_1 dst_unused:UNUSED_PRESERVE src0_sel:WORD_1
	v_exp_f16_sdwa v51, v47 dst_sel:WORD_1 dst_unused:UNUSED_PRESERVE src0_sel:WORD_1
	v_exp_f16_sdwa v52, v48 dst_sel:WORD_1 dst_unused:UNUSED_PRESERVE src0_sel:WORD_1
	v_exp_f16_sdwa v53, v49 dst_sel:WORD_1 dst_unused:UNUSED_PRESERVE src0_sel:WORD_1
	v_pk_add_f16 v46, v66, v114 neg_lo:[0,1] neg_hi:[0,1]
	v_pk_add_f16 v37, v37, v50
	v_pk_add_f16 v34, v34, v53
	v_pk_add_f16 v35, v35, v52
	v_pk_add_f16 v36, v36, v51
	v_pk_fma_f16 v25, v17, v53, v25
	v_pk_fma_f16 v24, v16, v52, v24
	v_pk_fma_f16 v23, v15, v51, v23
	v_pk_fma_f16 v22, v14, v50, v22
	v_pk_add_f16 v47, v67, v115 neg_lo:[0,1] neg_hi:[0,1]
	v_pk_add_f16 v48, v68, v116 neg_lo:[0,1] neg_hi:[0,1]
	v_pk_add_f16 v49, v69, v117 neg_lo:[0,1] neg_hi:[0,1]
	v_exp_f16_sdwa v50, v46 dst_sel:WORD_0 dst_unused:UNUSED_PAD src0_sel:WORD_0
	v_exp_f16_sdwa v51, v47 dst_sel:WORD_0 dst_unused:UNUSED_PAD src0_sel:WORD_0
	v_exp_f16_sdwa v52, v48 dst_sel:WORD_0 dst_unused:UNUSED_PAD src0_sel:WORD_0
	v_exp_f16_sdwa v53, v49 dst_sel:WORD_0 dst_unused:UNUSED_PAD src0_sel:WORD_0
	v_exp_f16_sdwa v50, v46 dst_sel:WORD_1 dst_unused:UNUSED_PRESERVE src0_sel:WORD_1
	v_exp_f16_sdwa v51, v47 dst_sel:WORD_1 dst_unused:UNUSED_PRESERVE src0_sel:WORD_1
	v_exp_f16_sdwa v52, v48 dst_sel:WORD_1 dst_unused:UNUSED_PRESERVE src0_sel:WORD_1
	v_exp_f16_sdwa v53, v49 dst_sel:WORD_1 dst_unused:UNUSED_PRESERVE src0_sel:WORD_1
	v_pk_add_f16 v46, v101, v114 neg_lo:[0,1] neg_hi:[0,1]
	v_pk_add_f16 v37, v37, v50
	v_pk_add_f16 v36, v36, v51
	v_pk_add_f16 v35, v35, v52
	v_pk_add_f16 v34, v34, v53
	v_pk_fma_f16 v22, v18, v50, v22
	v_pk_fma_f16 v23, v19, v51, v23
	v_pk_fma_f16 v24, v20, v52, v24
	v_pk_fma_f16 v25, v21, v53, v25
	v_pk_add_f16 v47, v100, v115 neg_lo:[0,1] neg_hi:[0,1]
	v_pk_add_f16 v48, v99, v116 neg_lo:[0,1] neg_hi:[0,1]
	v_pk_add_f16 v49, v98, v117 neg_lo:[0,1] neg_hi:[0,1]
	v_exp_f16_sdwa v50, v46 dst_sel:WORD_0 dst_unused:UNUSED_PAD src0_sel:WORD_0
	v_exp_f16_sdwa v51, v47 dst_sel:WORD_0 dst_unused:UNUSED_PAD src0_sel:WORD_0
	v_exp_f16_sdwa v52, v48 dst_sel:WORD_0 dst_unused:UNUSED_PAD src0_sel:WORD_0
	v_exp_f16_sdwa v53, v49 dst_sel:WORD_0 dst_unused:UNUSED_PAD src0_sel:WORD_0
	v_exp_f16_sdwa v50, v46 dst_sel:WORD_1 dst_unused:UNUSED_PRESERVE src0_sel:WORD_1
	v_exp_f16_sdwa v51, v47 dst_sel:WORD_1 dst_unused:UNUSED_PRESERVE src0_sel:WORD_1
	v_exp_f16_sdwa v52, v48 dst_sel:WORD_1 dst_unused:UNUSED_PRESERVE src0_sel:WORD_1
	v_exp_f16_sdwa v53, v49 dst_sel:WORD_1 dst_unused:UNUSED_PRESERVE src0_sel:WORD_1
	v_pk_add_f16 v46, v113, v114 neg_lo:[0,1] neg_hi:[0,1]
	v_pk_add_f16 v37, v37, v50
	v_pk_add_f16 v34, v34, v53
	v_pk_add_f16 v35, v35, v52
	v_pk_add_f16 v36, v36, v51
	v_pk_fma_f16 v25, v33, v53, v25
	v_pk_fma_f16 v24, v32, v52, v24
	v_pk_fma_f16 v23, v31, v51, v23
	v_pk_fma_f16 v22, v30, v50, v22
	v_pk_add_f16 v47, v112, v115 neg_lo:[0,1] neg_hi:[0,1]
	v_pk_add_f16 v48, v111, v116 neg_lo:[0,1] neg_hi:[0,1]
	v_pk_add_f16 v49, v110, v117 neg_lo:[0,1] neg_hi:[0,1]
	v_exp_f16_sdwa v50, v46 dst_sel:WORD_0 dst_unused:UNUSED_PAD src0_sel:WORD_0
	v_exp_f16_sdwa v51, v47 dst_sel:WORD_0 dst_unused:UNUSED_PAD src0_sel:WORD_0
	v_exp_f16_sdwa v52, v48 dst_sel:WORD_0 dst_unused:UNUSED_PAD src0_sel:WORD_0
	v_exp_f16_sdwa v53, v49 dst_sel:WORD_0 dst_unused:UNUSED_PAD src0_sel:WORD_0
	v_exp_f16_sdwa v50, v46 dst_sel:WORD_1 dst_unused:UNUSED_PRESERVE src0_sel:WORD_1
	v_exp_f16_sdwa v51, v47 dst_sel:WORD_1 dst_unused:UNUSED_PRESERVE src0_sel:WORD_1
	v_exp_f16_sdwa v52, v48 dst_sel:WORD_1 dst_unused:UNUSED_PRESERVE src0_sel:WORD_1
	v_exp_f16_sdwa v53, v49 dst_sel:WORD_1 dst_unused:UNUSED_PRESERVE src0_sel:WORD_1
	v_pk_add_f16 v46, v86, v114 neg_lo:[0,1] neg_hi:[0,1]
	v_pk_add_f16 v37, v37, v50
	v_pk_add_f16 v36, v36, v51
	v_pk_add_f16 v35, v35, v52
	v_pk_add_f16 v34, v34, v53
	v_pk_fma_f16 v22, v42, v50, v22
	v_pk_fma_f16 v23, v43, v51, v23
	v_pk_fma_f16 v24, v44, v52, v24
	v_pk_fma_f16 v25, v45, v53, v25
	v_pk_add_f16 v47, v87, v115 neg_lo:[0,1] neg_hi:[0,1]
	v_pk_add_f16 v48, v88, v116 neg_lo:[0,1] neg_hi:[0,1]
	v_pk_add_f16 v49, v89, v117 neg_lo:[0,1] neg_hi:[0,1]
	v_exp_f16_sdwa v50, v46 dst_sel:WORD_0 dst_unused:UNUSED_PAD src0_sel:WORD_0
	v_exp_f16_sdwa v51, v47 dst_sel:WORD_0 dst_unused:UNUSED_PAD src0_sel:WORD_0
	v_exp_f16_sdwa v52, v48 dst_sel:WORD_0 dst_unused:UNUSED_PAD src0_sel:WORD_0
	v_exp_f16_sdwa v53, v49 dst_sel:WORD_0 dst_unused:UNUSED_PAD src0_sel:WORD_0
	v_exp_f16_sdwa v50, v46 dst_sel:WORD_1 dst_unused:UNUSED_PRESERVE src0_sel:WORD_1
	v_exp_f16_sdwa v51, v47 dst_sel:WORD_1 dst_unused:UNUSED_PRESERVE src0_sel:WORD_1
	v_exp_f16_sdwa v52, v48 dst_sel:WORD_1 dst_unused:UNUSED_PRESERVE src0_sel:WORD_1
	v_exp_f16_sdwa v53, v49 dst_sel:WORD_1 dst_unused:UNUSED_PRESERVE src0_sel:WORD_1
	v_pk_add_f16 v37, v37, v50
	v_pk_add_f16 v36, v36, v51
	v_rcp_f16_e32 v46, v37
	v_rcp_f16_sdwa v37, v37 dst_sel:DWORD dst_unused:UNUSED_PAD src0_sel:WORD_1
	v_pk_add_f16 v35, v35, v52
	v_rcp_f16_e32 v47, v36
	v_rcp_f16_sdwa v36, v36 dst_sel:DWORD dst_unused:UNUSED_PAD src0_sel:WORD_1
	v_pk_add_f16 v34, v34, v53
	v_rcp_f16_e32 v48, v35
	v_rcp_f16_sdwa v35, v35 dst_sel:DWORD dst_unused:UNUSED_PAD src0_sel:WORD_1
	v_rcp_f16_e32 v49, v34
	v_rcp_f16_sdwa v34, v34 dst_sel:DWORD dst_unused:UNUSED_PAD src0_sel:WORD_1
	v_pk_fma_f16 v22, v62, v50, v22
	v_pack_b32_f16 v37, v46, v37
	v_pk_fma_f16 v23, v63, v51, v23
	v_pk_mul_f16 v57, v22, v37
	v_pack_b32_f16 v22, v47, v36
	v_pk_fma_f16 v24, v64, v52, v24
	v_pk_mul_f16 v56, v23, v22
	v_pack_b32_f16 v22, v48, v35
	v_pk_fma_f16 v25, v65, v53, v25
	v_pk_mul_f16 v55, v24, v22
	v_pack_b32_f16 v22, v49, v34
	v_pk_mul_f16 v54, v25, v22
	s_waitcnt vmcnt(0)
	v_pk_mul_f16 v22, v160, v146 op_sel_hi:[0,1]
	v_pk_mul_f16 v23, v160, v147 op_sel_hi:[0,1]
	v_pk_mul_f16 v24, v160, v148 op_sel_hi:[0,1]
	v_pk_mul_f16 v25, v160, v149 op_sel_hi:[0,1]
	v_pk_mul_f16 v46, v159, v146 op_sel_hi:[0,1]
	v_pk_mul_f16 v47, v159, v147 op_sel_hi:[0,1]
	v_pk_mul_f16 v48, v159, v148 op_sel_hi:[0,1]
	v_pk_mul_f16 v49, v159, v149 op_sel_hi:[0,1]
	v_pk_mul_f16 v34, v158, v146 op_sel_hi:[0,1]
	v_pk_mul_f16 v35, v158, v147 op_sel_hi:[0,1]
	v_pk_mul_f16 v36, v158, v148 op_sel_hi:[0,1]
	v_pk_mul_f16 v37, v158, v149 op_sel_hi:[0,1]
	v_pk_fma_f16 v29, v29, v149, v25
	v_pk_fma_f16 v28, v28, v148, v24
	v_pk_fma_f16 v27, v27, v147, v23
	v_pk_fma_f16 v26, v26, v146, v22
	v_pk_fma_f16 v41, v41, v149, v25
	v_pk_fma_f16 v40, v40, v148, v24
	v_pk_fma_f16 v39, v39, v147, v23
	v_pk_fma_f16 v38, v38, v146, v22
	v_pk_fma_f16 v25, v61, v149, v25
	v_pk_fma_f16 v24, v60, v148, v24
	v_pk_fma_f16 v23, v59, v147, v23
	v_pk_fma_f16 v22, v58, v146, v22
	v_pk_fma_f16 v66, v137, v149, v49
	v_pk_fma_f16 v67, v136, v148, v48
	v_pk_fma_f16 v68, v135, v147, v47
	v_pk_fma_f16 v69, v134, v146, v46
	v_pk_fma_f16 v70, v145, v149, v49
	v_pk_fma_f16 v71, v144, v148, v48
	v_pk_fma_f16 v72, v143, v147, v47
	v_pk_fma_f16 v73, v142, v146, v46
	v_pk_fma_f16 v9, v9, v149, v49
	v_pk_fma_f16 v8, v8, v148, v48
	v_pk_fma_f16 v7, v7, v147, v47
	v_pk_fma_f16 v6, v6, v146, v46
	v_pk_maximum3_f16 v46, v26, v38, v22
	v_pk_maximum3_f16 v47, v27, v39, v23
	v_pk_maximum3_f16 v48, v28, v40, v24
	v_pk_maximum3_f16 v49, v29, v41, v25
	v_pk_fma_f16 v50, v81, v149, v37
	v_pk_fma_f16 v51, v80, v148, v36
	v_pk_fma_f16 v52, v79, v147, v35
	v_pk_fma_f16 v53, v78, v146, v34
	v_pk_fma_f16 v58, v109, v149, v37
	v_pk_fma_f16 v59, v108, v148, v36
	v_pk_fma_f16 v60, v107, v147, v35
	v_pk_fma_f16 v61, v106, v146, v34
	v_pk_fma_f16 v37, v125, v149, v37
	v_pk_fma_f16 v36, v124, v148, v36
	v_pk_fma_f16 v35, v123, v147, v35
	v_pk_fma_f16 v34, v122, v146, v34
	v_pk_maximum3_f16 v79, v52, v60, v35
	v_pk_maximum3_f16 v80, v51, v59, v36
	v_pk_maximum3_f16 v81, v50, v58, v37
	v_pk_maximum3_f16 v86, v69, v73, v6
	v_pk_maximum3_f16 v87, v68, v72, v7
	v_pk_maximum3_f16 v78, v53, v61, v34
	v_pk_maximum3_f16 v88, v67, v71, v8
	v_pk_maximum3_f16 v89, v66, v70, v9
	v_pk_maximum3_f16 v46, v46, v78, v86
	v_pk_maximum3_f16 v47, v47, v79, v87
	v_pk_maximum3_f16 v48, v48, v80, v88
	v_pk_maximum3_f16 v49, v49, v81, v89
	s_nop 0
	v_pk_add_f16 v26, v26, v46 neg_lo:[0,1] neg_hi:[0,1]
	v_pk_add_f16 v27, v27, v47 neg_lo:[0,1] neg_hi:[0,1]
	v_pk_add_f16 v28, v28, v48 neg_lo:[0,1] neg_hi:[0,1]
	v_pk_add_f16 v29, v29, v49 neg_lo:[0,1] neg_hi:[0,1]
	v_pk_add_f16 v38, v38, v46 neg_lo:[0,1] neg_hi:[0,1]
	v_exp_f16_sdwa v78, v26 dst_sel:WORD_0 dst_unused:UNUSED_PAD src0_sel:WORD_0
	v_exp_f16_sdwa v79, v27 dst_sel:WORD_0 dst_unused:UNUSED_PAD src0_sel:WORD_0
	v_exp_f16_sdwa v80, v28 dst_sel:WORD_0 dst_unused:UNUSED_PAD src0_sel:WORD_0
	v_exp_f16_sdwa v81, v29 dst_sel:WORD_0 dst_unused:UNUSED_PAD src0_sel:WORD_0
	v_exp_f16_sdwa v78, v26 dst_sel:WORD_1 dst_unused:UNUSED_PRESERVE src0_sel:WORD_1
	v_exp_f16_sdwa v79, v27 dst_sel:WORD_1 dst_unused:UNUSED_PRESERVE src0_sel:WORD_1
	v_exp_f16_sdwa v80, v28 dst_sel:WORD_1 dst_unused:UNUSED_PRESERVE src0_sel:WORD_1
	v_exp_f16_sdwa v81, v29 dst_sel:WORD_1 dst_unused:UNUSED_PRESERVE src0_sel:WORD_1
	v_pk_add_f16 v39, v39, v47 neg_lo:[0,1] neg_hi:[0,1]
	v_pk_add_f16 v26, v78, 0
	v_pk_add_f16 v27, v79, 0
	v_pk_add_f16 v28, v80, 0
	v_pk_add_f16 v29, v81, 0
	v_pk_fma_f16 v10, v10, v78, 0
	v_pk_fma_f16 v11, v11, v79, 0
	v_pk_fma_f16 v12, v12, v80, 0
	v_pk_fma_f16 v13, v13, v81, 0
	v_pk_add_f16 v40, v40, v48 neg_lo:[0,1] neg_hi:[0,1]
	v_pk_add_f16 v41, v41, v49 neg_lo:[0,1] neg_hi:[0,1]
	v_pk_add_f16 v6, v6, v46 neg_lo:[0,1] neg_hi:[0,1]
	v_exp_f16_sdwa v78, v38 dst_sel:WORD_0 dst_unused:UNUSED_PAD src0_sel:WORD_0
	v_exp_f16_sdwa v79, v39 dst_sel:WORD_0 dst_unused:UNUSED_PAD src0_sel:WORD_0
	v_exp_f16_sdwa v80, v40 dst_sel:WORD_0 dst_unused:UNUSED_PAD src0_sel:WORD_0
	v_exp_f16_sdwa v81, v41 dst_sel:WORD_0 dst_unused:UNUSED_PAD src0_sel:WORD_0
	v_exp_f16_sdwa v78, v38 dst_sel:WORD_1 dst_unused:UNUSED_PRESERVE src0_sel:WORD_1
	v_exp_f16_sdwa v79, v39 dst_sel:WORD_1 dst_unused:UNUSED_PRESERVE src0_sel:WORD_1
	v_exp_f16_sdwa v80, v40 dst_sel:WORD_1 dst_unused:UNUSED_PRESERVE src0_sel:WORD_1
	v_exp_f16_sdwa v81, v41 dst_sel:WORD_1 dst_unused:UNUSED_PRESERVE src0_sel:WORD_1
	v_pk_add_f16 v7, v7, v47 neg_lo:[0,1] neg_hi:[0,1]
	v_pk_add_f16 v29, v29, v81
	v_pk_add_f16 v28, v28, v80
	v_pk_add_f16 v27, v27, v79
	v_pk_add_f16 v26, v26, v78
	v_pk_fma_f16 v13, v17, v81, v13
	v_pk_fma_f16 v12, v16, v80, v12
	v_pk_fma_f16 v11, v15, v79, v11
	v_pk_fma_f16 v10, v14, v78, v10
	v_pk_add_f16 v14, v22, v46 neg_lo:[0,1] neg_hi:[0,1]
	v_pk_add_f16 v15, v23, v47 neg_lo:[0,1] neg_hi:[0,1]
	v_pk_add_f16 v16, v24, v48 neg_lo:[0,1] neg_hi:[0,1]
	v_pk_add_f16 v17, v25, v49 neg_lo:[0,1] neg_hi:[0,1]
	v_pk_add_f16 v8, v8, v48 neg_lo:[0,1] neg_hi:[0,1]
	v_exp_f16_sdwa v22, v14 dst_sel:WORD_0 dst_unused:UNUSED_PAD src0_sel:WORD_0
	v_exp_f16_sdwa v23, v15 dst_sel:WORD_0 dst_unused:UNUSED_PAD src0_sel:WORD_0
	v_exp_f16_sdwa v24, v16 dst_sel:WORD_0 dst_unused:UNUSED_PAD src0_sel:WORD_0
	v_exp_f16_sdwa v25, v17 dst_sel:WORD_0 dst_unused:UNUSED_PAD src0_sel:WORD_0
	v_exp_f16_sdwa v22, v14 dst_sel:WORD_1 dst_unused:UNUSED_PRESERVE src0_sel:WORD_1
	v_exp_f16_sdwa v23, v15 dst_sel:WORD_1 dst_unused:UNUSED_PRESERVE src0_sel:WORD_1
	v_exp_f16_sdwa v24, v16 dst_sel:WORD_1 dst_unused:UNUSED_PRESERVE src0_sel:WORD_1
	v_exp_f16_sdwa v25, v17 dst_sel:WORD_1 dst_unused:UNUSED_PRESERVE src0_sel:WORD_1
	v_pk_add_f16 v9, v9, v49 neg_lo:[0,1] neg_hi:[0,1]
	v_pk_add_f16 v14, v26, v22
	v_pk_add_f16 v15, v27, v23
	v_pk_add_f16 v16, v28, v24
	v_pk_add_f16 v17, v29, v25
	v_pk_fma_f16 v10, v18, v22, v10
	v_pk_fma_f16 v11, v19, v23, v11
	v_pk_fma_f16 v12, v20, v24, v12
	v_pk_fma_f16 v13, v21, v25, v13
	v_pk_add_f16 v18, v53, v46 neg_lo:[0,1] neg_hi:[0,1]
	v_pk_add_f16 v19, v52, v47 neg_lo:[0,1] neg_hi:[0,1]
	v_pk_add_f16 v20, v51, v48 neg_lo:[0,1] neg_hi:[0,1]
	v_pk_add_f16 v21, v50, v49 neg_lo:[0,1] neg_hi:[0,1]
	v_exp_f16_sdwa v22, v18 dst_sel:WORD_0 dst_unused:UNUSED_PAD src0_sel:WORD_0
	v_exp_f16_sdwa v23, v19 dst_sel:WORD_0 dst_unused:UNUSED_PAD src0_sel:WORD_0
	v_exp_f16_sdwa v24, v20 dst_sel:WORD_0 dst_unused:UNUSED_PAD src0_sel:WORD_0
	v_exp_f16_sdwa v25, v21 dst_sel:WORD_0 dst_unused:UNUSED_PAD src0_sel:WORD_0
	v_exp_f16_sdwa v22, v18 dst_sel:WORD_1 dst_unused:UNUSED_PRESERVE src0_sel:WORD_1
	v_exp_f16_sdwa v23, v19 dst_sel:WORD_1 dst_unused:UNUSED_PRESERVE src0_sel:WORD_1
	v_exp_f16_sdwa v24, v20 dst_sel:WORD_1 dst_unused:UNUSED_PRESERVE src0_sel:WORD_1
	v_exp_f16_sdwa v25, v21 dst_sel:WORD_1 dst_unused:UNUSED_PRESERVE src0_sel:WORD_1
	v_pk_add_f16 v18, v61, v46 neg_lo:[0,1] neg_hi:[0,1]
	v_pk_add_f16 v17, v17, v25
	v_pk_add_f16 v16, v16, v24
	v_pk_add_f16 v15, v15, v23
	v_pk_add_f16 v14, v14, v22
	v_pk_fma_f16 v13, v33, v25, v13
	v_pk_fma_f16 v12, v32, v24, v12
	v_pk_fma_f16 v11, v31, v23, v11
	v_pk_fma_f16 v10, v30, v22, v10
	v_pk_add_f16 v19, v60, v47 neg_lo:[0,1] neg_hi:[0,1]
	v_pk_add_f16 v20, v59, v48 neg_lo:[0,1] neg_hi:[0,1]
	v_pk_add_f16 v21, v58, v49 neg_lo:[0,1] neg_hi:[0,1]
	v_exp_f16_sdwa v30, v6 dst_sel:WORD_0 dst_unused:UNUSED_PAD src0_sel:WORD_0
	v_exp_f16_sdwa v31, v7 dst_sel:WORD_0 dst_unused:UNUSED_PAD src0_sel:WORD_0
	v_exp_f16_sdwa v32, v8 dst_sel:WORD_0 dst_unused:UNUSED_PAD src0_sel:WORD_0
	v_exp_f16_sdwa v33, v9 dst_sel:WORD_0 dst_unused:UNUSED_PAD src0_sel:WORD_0
	v_exp_f16_sdwa v30, v6 dst_sel:WORD_1 dst_unused:UNUSED_PRESERVE src0_sel:WORD_1
	v_exp_f16_sdwa v31, v7 dst_sel:WORD_1 dst_unused:UNUSED_PRESERVE src0_sel:WORD_1
	v_exp_f16_sdwa v32, v8 dst_sel:WORD_1 dst_unused:UNUSED_PRESERVE src0_sel:WORD_1
	v_exp_f16_sdwa v33, v9 dst_sel:WORD_1 dst_unused:UNUSED_PRESERVE src0_sel:WORD_1
	v_exp_f16_sdwa v22, v18 dst_sel:WORD_0 dst_unused:UNUSED_PAD src0_sel:WORD_0
	v_exp_f16_sdwa v23, v19 dst_sel:WORD_0 dst_unused:UNUSED_PAD src0_sel:WORD_0
	v_exp_f16_sdwa v24, v20 dst_sel:WORD_0 dst_unused:UNUSED_PAD src0_sel:WORD_0
	v_exp_f16_sdwa v25, v21 dst_sel:WORD_0 dst_unused:UNUSED_PAD src0_sel:WORD_0
	v_exp_f16_sdwa v22, v18 dst_sel:WORD_1 dst_unused:UNUSED_PRESERVE src0_sel:WORD_1
	v_exp_f16_sdwa v23, v19 dst_sel:WORD_1 dst_unused:UNUSED_PRESERVE src0_sel:WORD_1
	v_exp_f16_sdwa v24, v20 dst_sel:WORD_1 dst_unused:UNUSED_PRESERVE src0_sel:WORD_1
	v_exp_f16_sdwa v25, v21 dst_sel:WORD_1 dst_unused:UNUSED_PRESERVE src0_sel:WORD_1
	v_pk_add_f16 v18, v34, v46 neg_lo:[0,1] neg_hi:[0,1]
	v_pk_add_f16 v14, v14, v22
	v_pk_add_f16 v15, v15, v23
	v_pk_add_f16 v16, v16, v24
	v_pk_add_f16 v17, v17, v25
	v_pk_fma_f16 v10, v42, v22, v10
	v_pk_fma_f16 v11, v43, v23, v11
	v_pk_fma_f16 v12, v44, v24, v12
	v_pk_fma_f16 v13, v45, v25, v13
	v_pk_add_f16 v19, v35, v47 neg_lo:[0,1] neg_hi:[0,1]
	v_pk_add_f16 v20, v36, v48 neg_lo:[0,1] neg_hi:[0,1]
	v_pk_add_f16 v21, v37, v49 neg_lo:[0,1] neg_hi:[0,1]
	v_exp_f16_sdwa v22, v18 dst_sel:WORD_0 dst_unused:UNUSED_PAD src0_sel:WORD_0
	v_exp_f16_sdwa v23, v19 dst_sel:WORD_0 dst_unused:UNUSED_PAD src0_sel:WORD_0
	v_exp_f16_sdwa v24, v20 dst_sel:WORD_0 dst_unused:UNUSED_PAD src0_sel:WORD_0
	v_exp_f16_sdwa v25, v21 dst_sel:WORD_0 dst_unused:UNUSED_PAD src0_sel:WORD_0
	v_exp_f16_sdwa v22, v18 dst_sel:WORD_1 dst_unused:UNUSED_PRESERVE src0_sel:WORD_1
	v_exp_f16_sdwa v23, v19 dst_sel:WORD_1 dst_unused:UNUSED_PRESERVE src0_sel:WORD_1
	v_exp_f16_sdwa v24, v20 dst_sel:WORD_1 dst_unused:UNUSED_PRESERVE src0_sel:WORD_1
	v_exp_f16_sdwa v25, v21 dst_sel:WORD_1 dst_unused:UNUSED_PRESERVE src0_sel:WORD_1
	v_pk_add_f16 v18, v69, v46 neg_lo:[0,1] neg_hi:[0,1]
	v_pk_add_f16 v17, v17, v25
	v_pk_add_f16 v16, v16, v24
	v_pk_add_f16 v15, v15, v23
	v_pk_add_f16 v14, v14, v22
	v_pk_fma_f16 v13, v65, v25, v13
	v_pk_fma_f16 v12, v64, v24, v12
	v_pk_fma_f16 v11, v63, v23, v11
	v_pk_fma_f16 v10, v62, v22, v10
	v_pk_add_f16 v19, v68, v47 neg_lo:[0,1] neg_hi:[0,1]
	v_pk_add_f16 v20, v67, v48 neg_lo:[0,1] neg_hi:[0,1]
	v_pk_add_f16 v21, v66, v49 neg_lo:[0,1] neg_hi:[0,1]
	v_exp_f16_sdwa v22, v18 dst_sel:WORD_0 dst_unused:UNUSED_PAD src0_sel:WORD_0
	v_exp_f16_sdwa v23, v19 dst_sel:WORD_0 dst_unused:UNUSED_PAD src0_sel:WORD_0
	v_exp_f16_sdwa v24, v20 dst_sel:WORD_0 dst_unused:UNUSED_PAD src0_sel:WORD_0
	v_exp_f16_sdwa v25, v21 dst_sel:WORD_0 dst_unused:UNUSED_PAD src0_sel:WORD_0
	v_exp_f16_sdwa v22, v18 dst_sel:WORD_1 dst_unused:UNUSED_PRESERVE src0_sel:WORD_1
	v_exp_f16_sdwa v23, v19 dst_sel:WORD_1 dst_unused:UNUSED_PRESERVE src0_sel:WORD_1
	v_exp_f16_sdwa v24, v20 dst_sel:WORD_1 dst_unused:UNUSED_PRESERVE src0_sel:WORD_1
	v_exp_f16_sdwa v25, v21 dst_sel:WORD_1 dst_unused:UNUSED_PRESERVE src0_sel:WORD_1
	v_pk_add_f16 v18, v73, v46 neg_lo:[0,1] neg_hi:[0,1]
	v_pk_add_f16 v14, v14, v22
	v_pk_add_f16 v15, v15, v23
	v_pk_add_f16 v16, v16, v24
	v_pk_add_f16 v17, v17, v25
	v_pk_fma_f16 v10, v82, v22, v10
	v_pk_fma_f16 v11, v83, v23, v11
	v_pk_fma_f16 v12, v84, v24, v12
	v_pk_fma_f16 v13, v85, v25, v13
	v_pk_add_f16 v19, v72, v47 neg_lo:[0,1] neg_hi:[0,1]
	v_pk_add_f16 v20, v71, v48 neg_lo:[0,1] neg_hi:[0,1]
	v_pk_add_f16 v21, v70, v49 neg_lo:[0,1] neg_hi:[0,1]
	v_exp_f16_sdwa v22, v18 dst_sel:WORD_0 dst_unused:UNUSED_PAD src0_sel:WORD_0
	v_exp_f16_sdwa v23, v19 dst_sel:WORD_0 dst_unused:UNUSED_PAD src0_sel:WORD_0
	v_exp_f16_sdwa v24, v20 dst_sel:WORD_0 dst_unused:UNUSED_PAD src0_sel:WORD_0
	v_exp_f16_sdwa v25, v21 dst_sel:WORD_0 dst_unused:UNUSED_PAD src0_sel:WORD_0
	v_exp_f16_sdwa v22, v18 dst_sel:WORD_1 dst_unused:UNUSED_PRESERVE src0_sel:WORD_1
	v_exp_f16_sdwa v23, v19 dst_sel:WORD_1 dst_unused:UNUSED_PRESERVE src0_sel:WORD_1
	v_exp_f16_sdwa v24, v20 dst_sel:WORD_1 dst_unused:UNUSED_PRESERVE src0_sel:WORD_1
	v_exp_f16_sdwa v25, v21 dst_sel:WORD_1 dst_unused:UNUSED_PRESERVE src0_sel:WORD_1
	s_nop 0
	v_pk_add_f16 v17, v17, v25
	v_pk_add_f16 v16, v16, v24
	v_pk_add_f16 v15, v15, v23
	v_pk_add_f16 v14, v14, v22
	v_pk_fma_f16 v21, v105, v25, v13
	v_pk_fma_f16 v20, v104, v24, v12
	v_pk_fma_f16 v19, v103, v23, v11
	v_pk_fma_f16 v18, v102, v22, v10
	v_mov_b32_e32 v13, v5
	v_mov_b32_e32 v12, v4
	v_mov_b32_e32 v11, v3
	v_mov_b32_e32 v10, v2

.Lmyf_C3_7:
	s_mov_b64 exec, -1
	s_waitcnt vmcnt(21)
	v_cvt_f16_f32_e32 v206, v155
	v_cvt_f16_f32_e32 v208, v154
	v_cvt_f16_f32_e32 v207, v156
	v_add_u32_e32 v251, 0x48000, v200
	buffer_load_dwordx4 v[154:157], v251, s[12:15], 0 offen
	s_mov_b64 s[4:5], 0
	s_cmp_lt_u32 s94, 4
	s_cbranch_scc1 .Lmylp4_0
	s_setprio 1
.Lmylp4_0:
	s_waitcnt vmcnt(3)
	v_pk_mul_f16 v216, v208, v213 op_sel_hi:[0,1]
	v_pk_mul_f16 v220, v206, v213 op_sel_hi:[0,1]
	v_pk_mul_f16 v224, v207, v213 op_sel_hi:[0,1]
	v_pk_mul_f16 v209, v208, v210 op_sel_hi:[0,1]
	v_pk_mul_f16 v214, v208, v211 op_sel_hi:[0,1]
	v_pk_mul_f16 v215, v208, v212 op_sel_hi:[0,1]
	v_pk_mul_f16 v217, v206, v210 op_sel_hi:[0,1]
	s_mov_b64 exec, s[64:65]
	buffer_load_dwordx4 v[34:37], v245, s[12:15], 0 offen
	buffer_load_dwordx4 v[18:21], v245, s[12:15], 0 offen offset:512
	s_mov_b64 exec, -1
	v_pk_mul_f16 v218, v206, v211 op_sel_hi:[0,1]
	v_pk_mul_f16 v219, v206, v212 op_sel_hi:[0,1]
	v_pk_mul_f16 v221, v207, v210 op_sel_hi:[0,1]
	v_pk_mul_f16 v222, v207, v211 op_sel_hi:[0,1]
	v_pk_mul_f16 v223, v207, v212 op_sel_hi:[0,1]
	v_pk_fma_f16 v125, v125, v213, v216
	v_pk_fma_f16 v141, v141, v213, v220
	v_pk_fma_f16 v149, v149, v213, v224
	v_pk_fma_f16 v225, v97, v213, v216
	v_pk_fma_f16 v229, v121, v213, v220
	v_pk_fma_f16 v233, v137, v213, v224
	v_pk_fma_f16 v216, v65, v213, v216
	v_pk_fma_f16 v220, v81, v213, v220
	buffer_load_dwordx4 v[46:49], v246, s[12:15], 0 offen offset:512
	buffer_load_dwordx4 v[22:25], v246, s[12:15], 0 offen offset:1024
	v_pk_fma_f16 v213, v105, v213, v224
	v_pk_maximum3_f16 v224, v125, v141, v149
	v_pk_fma_f16 v124, v124, v212, v215
	v_pk_fma_f16 v123, v123, v211, v214
	v_pk_fma_f16 v122, v122, v210, v209
	v_pk_fma_f16 v140, v140, v212, v219
	v_pk_fma_f16 v139, v139, v211, v218
	v_pk_fma_f16 v138, v138, v210, v217
	v_pk_fma_f16 v148, v148, v212, v223
	v_pk_fma_f16 v147, v147, v211, v222
	v_pk_fma_f16 v146, v146, v210, v221
	v_pk_fma_f16 v226, v96, v212, v215
	v_pk_fma_f16 v227, v95, v211, v214
	v_pk_fma_f16 v228, v94, v210, v209
	v_pk_fma_f16 v230, v120, v212, v219
	v_pk_fma_f16 v231, v119, v211, v218
	s_mov_b64 exec, s[66:67]
	buffer_load_dwordx4 v[66:69], v246, s[12:15], 0 offen offset:2048
	buffer_load_dwordx4 v[26:29], v246, s[12:15], 0 offen offset:2560
	s_mov_b64 exec, -1
	v_pk_fma_f16 v232, v118, v210, v217
	v_pk_fma_f16 v234, v136, v212, v223
	v_pk_fma_f16 v235, v135, v211, v222
	v_pk_fma_f16 v236, v134, v210, v221
	v_pk_fma_f16 v215, v64, v212, v215
	v_pk_fma_f16 v214, v63, v211, v214
	v_pk_fma_f16 v209, v62, v210, v209
	v_pk_fma_f16 v219, v80, v212, v219
	v_pk_fma_f16 v218, v79, v211, v218
	v_pk_fma_f16 v217, v78, v210, v217
	v_pk_fma_f16 v212, v104, v212, v223
	v_pk_fma_f16 v211, v103, v211, v222
	v_pk_fma_f16 v210, v102, v210, v221
	v_pk_maximum3_f16 v221, v122, v138, v146
	v_pk_maximum3_f16 v222, v123, v139, v147
	v_pk_maximum3_f16 v223, v124, v140, v148
	v_pk_maximum3_f16 v240, v225, v229, v233
	v_pk_maximum3_f16 v244, v216, v220, v213
	v_pk_maximum3_f16 v237, v228, v232, v236
	v_pk_maximum3_f16 v238, v227, v231, v235
	v_pk_maximum3_f16 v239, v226, v230, v234
	v_pk_maximum3_f16 v241, v209, v217, v210
	v_pk_maximum3_f16 v242, v214, v218, v211
	v_pk_maximum3_f16 v224, v224, v240, v244
	v_pk_maximum3_f16 v243, v215, v219, v212
	v_pk_maximum3_f16 v221, v221, v237, v241
	v_pk_maximum3_f16 v222, v222, v238, v242
	v_pk_maximum3_f16 v223, v223, v239, v243
	v_pk_add_f16 v125, v125, v224 neg_lo:[0,1] neg_hi:[0,1]
	s_mov_b64 exec, s[64:65]
	buffer_load_dwordx4 v[86:89], v247, s[12:15], 0 offen
	buffer_load_dwordx4 v[38:41], v247, s[12:15], 0 offen offset:512
	s_mov_b64 exec, -1
	v_pk_add_f16 v122, v122, v221 neg_lo:[0,1] neg_hi:[0,1]
	v_pk_add_f16 v123, v123, v222 neg_lo:[0,1] neg_hi:[0,1]
	v_pk_add_f16 v124, v124, v223 neg_lo:[0,1] neg_hi:[0,1]
	v_pk_add_f16 v138, v138, v221 neg_lo:[0,1] neg_hi:[0,1]
	v_exp_f16_sdwa v237, v122 dst_sel:WORD_0 dst_unused:UNUSED_PAD src0_sel:WORD_0
	v_exp_f16_sdwa v238, v123 dst_sel:WORD_0 dst_unused:UNUSED_PAD src0_sel:WORD_0
	v_exp_f16_sdwa v239, v124 dst_sel:WORD_0 dst_unused:UNUSED_PAD src0_sel:WORD_0
	v_exp_f16_sdwa v240, v125 dst_sel:WORD_0 dst_unused:UNUSED_PAD src0_sel:WORD_0
	v_exp_f16_sdwa v237, v122 dst_sel:WORD_1 dst_unused:UNUSED_PRESERVE src0_sel:WORD_1
	v_exp_f16_sdwa v238, v123 dst_sel:WORD_1 dst_unused:UNUSED_PRESERVE src0_sel:WORD_1
	v_exp_f16_sdwa v239, v124 dst_sel:WORD_1 dst_unused:UNUSED_PRESERVE src0_sel:WORD_1
	v_exp_f16_sdwa v240, v125 dst_sel:WORD_1 dst_unused:UNUSED_PRESERVE src0_sel:WORD_1
	v_pk_add_f16 v139, v139, v222 neg_lo:[0,1] neg_hi:[0,1]
	v_pk_add_f16 v125, v237, 0
	v_pk_fma_f16 v85, v85, v240, 0
	v_pk_add_f16 v122, v240, 0
	v_pk_add_f16 v123, v239, 0
	v_pk_add_f16 v124, v238, 0
	v_pk_fma_f16 v84, v84, v239, 0
	v_pk_fma_f16 v83, v83, v238, 0
	v_pk_fma_f16 v82, v82, v237, 0
	v_pk_add_f16 v140, v140, v223 neg_lo:[0,1] neg_hi:[0,1]
	buffer_load_dwordx4 v[114:117], v248, s[12:15], 0 offen offset:512
	buffer_load_dwordx4 v[50:53], v248, s[12:15], 0 offen offset:1024
	v_pk_add_f16 v141, v141, v224 neg_lo:[0,1] neg_hi:[0,1]
	v_exp_f16_sdwa v237, v138 dst_sel:WORD_0 dst_unused:UNUSED_PAD src0_sel:WORD_0
	v_exp_f16_sdwa v238, v139 dst_sel:WORD_0 dst_unused:UNUSED_PAD src0_sel:WORD_0
	v_exp_f16_sdwa v239, v140 dst_sel:WORD_0 dst_unused:UNUSED_PAD src0_sel:WORD_0
	v_exp_f16_sdwa v240, v141 dst_sel:WORD_0 dst_unused:UNUSED_PAD src0_sel:WORD_0
	v_exp_f16_sdwa v237, v138 dst_sel:WORD_1 dst_unused:UNUSED_PRESERVE src0_sel:WORD_1
	v_exp_f16_sdwa v238, v139 dst_sel:WORD_1 dst_unused:UNUSED_PRESERVE src0_sel:WORD_1
	v_exp_f16_sdwa v239, v140 dst_sel:WORD_1 dst_unused:UNUSED_PRESERVE src0_sel:WORD_1
	v_exp_f16_sdwa v240, v141 dst_sel:WORD_1 dst_unused:UNUSED_PRESERVE src0_sel:WORD_1
	v_pk_add_f16 v125, v125, v237
	v_pk_fma_f16 v85, v109, v240, v85
	v_pk_add_f16 v109, v149, v224 neg_lo:[0,1] neg_hi:[0,1]
	v_pk_add_f16 v124, v124, v238
	v_pk_add_f16 v123, v123, v239
	v_pk_add_f16 v122, v122, v240
	v_pk_fma_f16 v82, v106, v237, v82
	v_pk_fma_f16 v83, v107, v238, v83
	v_pk_fma_f16 v84, v108, v239, v84
	v_pk_add_f16 v106, v146, v221 neg_lo:[0,1] neg_hi:[0,1]
	v_pk_add_f16 v107, v147, v222 neg_lo:[0,1] neg_hi:[0,1]
	v_pk_add_f16 v108, v148, v223 neg_lo:[0,1] neg_hi:[0,1]
	v_exp_f16_sdwa v138, v106 dst_sel:WORD_0 dst_unused:UNUSED_PAD src0_sel:WORD_0
	v_exp_f16_sdwa v139, v107 dst_sel:WORD_0 dst_unused:UNUSED_PAD src0_sel:WORD_0
	v_exp_f16_sdwa v140, v108 dst_sel:WORD_0 dst_unused:UNUSED_PAD src0_sel:WORD_0
	v_exp_f16_sdwa v141, v109 dst_sel:WORD_0 dst_unused:UNUSED_PAD src0_sel:WORD_0
	v_exp_f16_sdwa v138, v106 dst_sel:WORD_1 dst_unused:UNUSED_PRESERVE src0_sel:WORD_1
	v_exp_f16_sdwa v139, v107 dst_sel:WORD_1 dst_unused:UNUSED_PRESERVE src0_sel:WORD_1
	v_exp_f16_sdwa v140, v108 dst_sel:WORD_1 dst_unused:UNUSED_PRESERVE src0_sel:WORD_1
	v_exp_f16_sdwa v141, v109 dst_sel:WORD_1 dst_unused:UNUSED_PRESERVE src0_sel:WORD_1
	v_pk_add_f16 v109, v125, v138
	v_pk_add_f16 v106, v122, v141
	s_mov_b64 exec, s[66:67]
	buffer_load_dwordx4 v[130:133], v248, s[12:15], 0 offen offset:2048
	buffer_load_dwordx4 v[70:73], v248, s[12:15], 0 offen offset:2560
	s_mov_b64 exec, -1
	v_pk_add_f16 v107, v123, v140
	v_pk_add_f16 v108, v124, v139
	v_pk_fma_f16 v85, v129, v141, v85
	v_pk_fma_f16 v84, v128, v140, v84
	v_pk_fma_f16 v83, v127, v139, v83
	v_pk_fma_f16 v82, v126, v138, v82
	v_pk_add_f16 v122, v228, v221 neg_lo:[0,1] neg_hi:[0,1]
	v_pk_add_f16 v123, v227, v222 neg_lo:[0,1] neg_hi:[0,1]
	v_pk_add_f16 v124, v226, v223 neg_lo:[0,1] neg_hi:[0,1]
	v_pk_add_f16 v125, v225, v224 neg_lo:[0,1] neg_hi:[0,1]
	v_exp_f16_sdwa v126, v122 dst_sel:WORD_0 dst_unused:UNUSED_PAD src0_sel:WORD_0
	v_exp_f16_sdwa v127, v123 dst_sel:WORD_0 dst_unused:UNUSED_PAD src0_sel:WORD_0
	v_exp_f16_sdwa v128, v124 dst_sel:WORD_0 dst_unused:UNUSED_PAD src0_sel:WORD_0
	v_exp_f16_sdwa v129, v125 dst_sel:WORD_0 dst_unused:UNUSED_PAD src0_sel:WORD_0
	v_exp_f16_sdwa v126, v122 dst_sel:WORD_1 dst_unused:UNUSED_PRESERVE src0_sel:WORD_1
	v_exp_f16_sdwa v127, v123 dst_sel:WORD_1 dst_unused:UNUSED_PRESERVE src0_sel:WORD_1
	v_exp_f16_sdwa v128, v124 dst_sel:WORD_1 dst_unused:UNUSED_PRESERVE src0_sel:WORD_1
	v_exp_f16_sdwa v129, v125 dst_sel:WORD_1 dst_unused:UNUSED_PRESERVE src0_sel:WORD_1
	v_pk_add_f16 v122, v232, v221 neg_lo:[0,1] neg_hi:[0,1]
	v_pk_add_f16 v109, v109, v126
	v_pk_add_f16 v108, v108, v127
	v_pk_add_f16 v107, v107, v128
	s_mov_b64 exec, s[76:77]
	buffer_load_dwordx4 v[142:145], v249, s[12:15], 0 offen
	buffer_load_dwordx4 v[90:93], v249, s[12:15], 0 offen offset:512
	s_mov_b64 exec, -1
	v_pk_add_f16 v106, v106, v129
	v_pk_fma_f16 v82, v54, v126, v82
	v_pk_fma_f16 v83, v55, v127, v83
	v_pk_fma_f16 v84, v56, v128, v84
	v_pk_fma_f16 v85, v57, v129, v85
	v_pk_add_f16 v123, v231, v222 neg_lo:[0,1] neg_hi:[0,1]
	v_pk_add_f16 v124, v230, v223 neg_lo:[0,1] neg_hi:[0,1]
	v_pk_add_f16 v125, v229, v224 neg_lo:[0,1] neg_hi:[0,1]
	v_exp_f16_sdwa v126, v122 dst_sel:WORD_0 dst_unused:UNUSED_PAD src0_sel:WORD_0
	v_exp_f16_sdwa v127, v123 dst_sel:WORD_0 dst_unused:UNUSED_PAD src0_sel:WORD_0
	v_exp_f16_sdwa v128, v124 dst_sel:WORD_0 dst_unused:UNUSED_PAD src0_sel:WORD_0
	v_exp_f16_sdwa v129, v125 dst_sel:WORD_0 dst_unused:UNUSED_PAD src0_sel:WORD_0
	v_exp_f16_sdwa v126, v122 dst_sel:WORD_1 dst_unused:UNUSED_PRESERVE src0_sel:WORD_1
	v_exp_f16_sdwa v127, v123 dst_sel:WORD_1 dst_unused:UNUSED_PRESERVE src0_sel:WORD_1
	v_exp_f16_sdwa v128, v124 dst_sel:WORD_1 dst_unused:UNUSED_PRESERVE src0_sel:WORD_1
	v_exp_f16_sdwa v129, v125 dst_sel:WORD_1 dst_unused:UNUSED_PRESERVE src0_sel:WORD_1
	v_pk_add_f16 v122, v236, v221 neg_lo:[0,1] neg_hi:[0,1]
	v_pk_add_f16 v109, v109, v126
	v_pk_add_f16 v106, v106, v129
	v_pk_add_f16 v107, v107, v128
	v_pk_add_f16 v108, v108, v127
	v_pk_fma_f16 v85, v77, v129, v85
	v_pk_fma_f16 v84, v76, v128, v84
	s_mov_b64 exec, s[70:71]
	buffer_load_dwordx4 v[150:153], v250, s[12:15], 0 offen offset:512
	buffer_load_dwordx4 v[110:113], v250, s[12:15], 0 offen offset:1024
	s_mov_b64 exec, -1
	v_pk_fma_f16 v83, v75, v127, v83
	v_pk_fma_f16 v82, v74, v126, v82
	v_pk_add_f16 v123, v235, v222 neg_lo:[0,1] neg_hi:[0,1]
	v_pk_add_f16 v124, v234, v223 neg_lo:[0,1] neg_hi:[0,1]
	v_pk_add_f16 v125, v233, v224 neg_lo:[0,1] neg_hi:[0,1]
	v_exp_f16_sdwa v126, v122 dst_sel:WORD_0 dst_unused:UNUSED_PAD src0_sel:WORD_0
	v_exp_f16_sdwa v127, v123 dst_sel:WORD_0 dst_unused:UNUSED_PAD src0_sel:WORD_0
	v_exp_f16_sdwa v128, v124 dst_sel:WORD_0 dst_unused:UNUSED_PAD src0_sel:WORD_0
	v_exp_f16_sdwa v129, v125 dst_sel:WORD_0 dst_unused:UNUSED_PAD src0_sel:WORD_0
	v_exp_f16_sdwa v126, v122 dst_sel:WORD_1 dst_unused:UNUSED_PRESERVE src0_sel:WORD_1
	v_exp_f16_sdwa v127, v123 dst_sel:WORD_1 dst_unused:UNUSED_PRESERVE src0_sel:WORD_1
	v_exp_f16_sdwa v128, v124 dst_sel:WORD_1 dst_unused:UNUSED_PRESERVE src0_sel:WORD_1
	v_exp_f16_sdwa v129, v125 dst_sel:WORD_1 dst_unused:UNUSED_PRESERVE src0_sel:WORD_1
	v_pk_add_f16 v122, v209, v221 neg_lo:[0,1] neg_hi:[0,1]
	v_pk_add_f16 v109, v109, v126
	v_pk_add_f16 v108, v108, v127
	v_pk_add_f16 v107, v107, v128
	v_pk_add_f16 v106, v106, v129
	v_pk_fma_f16 v82, v98, v126, v82
	v_pk_fma_f16 v83, v99, v127, v83
	v_pk_fma_f16 v84, v100, v128, v84
	v_pk_fma_f16 v85, v101, v129, v85
	s_mov_b64 exec, s[78:79]
	buffer_load_dwordx4 v[14:17], v250, s[12:15], 0 offen offset:2048
	buffer_load_dwordx4 v[10:13], v250, s[12:15], 0 offen offset:2560
	s_mov_b64 exec, -1
	v_pk_add_f16 v123, v214, v222 neg_lo:[0,1] neg_hi:[0,1]
	v_pk_add_f16 v124, v215, v223 neg_lo:[0,1] neg_hi:[0,1]
	v_pk_add_f16 v125, v216, v224 neg_lo:[0,1] neg_hi:[0,1]
	v_exp_f16_sdwa v126, v122 dst_sel:WORD_0 dst_unused:UNUSED_PAD src0_sel:WORD_0
	v_exp_f16_sdwa v127, v123 dst_sel:WORD_0 dst_unused:UNUSED_PAD src0_sel:WORD_0
	v_exp_f16_sdwa v128, v124 dst_sel:WORD_0 dst_unused:UNUSED_PAD src0_sel:WORD_0
	v_exp_f16_sdwa v129, v125 dst_sel:WORD_0 dst_unused:UNUSED_PAD src0_sel:WORD_0
	v_exp_f16_sdwa v126, v122 dst_sel:WORD_1 dst_unused:UNUSED_PRESERVE src0_sel:WORD_1
	v_exp_f16_sdwa v127, v123 dst_sel:WORD_1 dst_unused:UNUSED_PRESERVE src0_sel:WORD_1
	v_exp_f16_sdwa v128, v124 dst_sel:WORD_1 dst_unused:UNUSED_PRESERVE src0_sel:WORD_1
	v_exp_f16_sdwa v129, v125 dst_sel:WORD_1 dst_unused:UNUSED_PRESERVE src0_sel:WORD_1
	v_pk_add_f16 v122, v217, v221 neg_lo:[0,1] neg_hi:[0,1]
	v_pk_add_f16 v109, v109, v126
	v_pk_add_f16 v106, v106, v129
	v_pk_add_f16 v107, v107, v128
	v_pk_add_f16 v108, v108, v127
	v_pk_fma_f16 v85, v33, v129, v85
	v_pk_fma_f16 v84, v32, v128, v84
	v_pk_fma_f16 v83, v31, v127, v83
	v_pk_fma_f16 v82, v30, v126, v82
	v_pk_add_f16 v123, v218, v222 neg_lo:[0,1] neg_hi:[0,1]
	v_pk_add_f16 v124, v219, v223 neg_lo:[0,1] neg_hi:[0,1]
	v_pk_add_f16 v125, v220, v224 neg_lo:[0,1] neg_hi:[0,1]
	v_exp_f16_sdwa v126, v122 dst_sel:WORD_0 dst_unused:UNUSED_PAD src0_sel:WORD_0
	v_exp_f16_sdwa v127, v123 dst_sel:WORD_0 dst_unused:UNUSED_PAD src0_sel:WORD_0
	v_exp_f16_sdwa v128, v124 dst_sel:WORD_0 dst_unused:UNUSED_PAD src0_sel:WORD_0
	v_exp_f16_sdwa v129, v125 dst_sel:WORD_0 dst_unused:UNUSED_PAD src0_sel:WORD_0
	v_exp_f16_sdwa v126, v122 dst_sel:WORD_1 dst_unused:UNUSED_PRESERVE src0_sel:WORD_1
	v_exp_f16_sdwa v127, v123 dst_sel:WORD_1 dst_unused:UNUSED_PRESERVE src0_sel:WORD_1
	v_exp_f16_sdwa v128, v124 dst_sel:WORD_1 dst_unused:UNUSED_PRESERVE src0_sel:WORD_1
	v_exp_f16_sdwa v129, v125 dst_sel:WORD_1 dst_unused:UNUSED_PRESERVE src0_sel:WORD_1
	v_pk_add_f16 v122, v210, v221 neg_lo:[0,1] neg_hi:[0,1]
	v_pk_add_f16 v109, v109, v126
	v_pk_add_f16 v108, v108, v127
	v_pk_add_f16 v107, v107, v128
	v_pk_add_f16 v106, v106, v129
	v_pk_fma_f16 v82, v42, v126, v82
	v_pk_fma_f16 v83, v43, v127, v83
	v_pk_fma_f16 v84, v44, v128, v84
	v_pk_fma_f16 v85, v45, v129, v85
	v_pk_add_f16 v123, v211, v222 neg_lo:[0,1] neg_hi:[0,1]
	v_pk_add_f16 v124, v212, v223 neg_lo:[0,1] neg_hi:[0,1]
	v_pk_add_f16 v125, v213, v224 neg_lo:[0,1] neg_hi:[0,1]
	v_exp_f16_sdwa v126, v122 dst_sel:WORD_0 dst_unused:UNUSED_PAD src0_sel:WORD_0
	v_exp_f16_sdwa v127, v123 dst_sel:WORD_0 dst_unused:UNUSED_PAD src0_sel:WORD_0
	v_exp_f16_sdwa v128, v124 dst_sel:WORD_0 dst_unused:UNUSED_PAD src0_sel:WORD_0
	v_exp_f16_sdwa v129, v125 dst_sel:WORD_0 dst_unused:UNUSED_PAD src0_sel:WORD_0
	v_exp_f16_sdwa v126, v122 dst_sel:WORD_1 dst_unused:UNUSED_PRESERVE src0_sel:WORD_1
	v_exp_f16_sdwa v127, v123 dst_sel:WORD_1 dst_unused:UNUSED_PRESERVE src0_sel:WORD_1
	v_exp_f16_sdwa v128, v124 dst_sel:WORD_1 dst_unused:UNUSED_PRESERVE src0_sel:WORD_1
	v_exp_f16_sdwa v129, v125 dst_sel:WORD_1 dst_unused:UNUSED_PRESERVE src0_sel:WORD_1
	v_pk_add_f16 v109, v109, v126
	v_pk_add_f16 v108, v108, v127
	v_rcp_f16_e32 v122, v109
	v_rcp_f16_sdwa v109, v109 dst_sel:DWORD dst_unused:UNUSED_PAD src0_sel:WORD_1
	v_pk_add_f16 v107, v107, v128
	v_rcp_f16_e32 v123, v108
	v_rcp_f16_sdwa v108, v108 dst_sel:DWORD dst_unused:UNUSED_PAD src0_sel:WORD_1
	v_pk_add_f16 v106, v106, v129
	v_rcp_f16_e32 v124, v107
	v_rcp_f16_sdwa v107, v107 dst_sel:DWORD dst_unused:UNUSED_PAD src0_sel:WORD_1
	v_rcp_f16_e32 v125, v106
	v_rcp_f16_sdwa v106, v106 dst_sel:DWORD dst_unused:UNUSED_PAD src0_sel:WORD_1
	v_pk_fma_f16 v82, v58, v126, v82
	v_pack_b32_f16 v109, v122, v109
	v_pk_fma_f16 v83, v59, v127, v83
	v_pk_mul_f16 v141, v82, v109
	v_pack_b32_f16 v82, v123, v108
	v_pk_fma_f16 v84, v60, v128, v84
	v_pk_mul_f16 v140, v83, v82
	v_pack_b32_f16 v82, v124, v107
	v_pk_fma_f16 v85, v61, v129, v85
	v_pk_mul_f16 v139, v84, v82
	v_pack_b32_f16 v82, v125, v106
	v_pk_mul_f16 v138, v85, v82
	s_waitcnt vmcnt(12)
	v_pk_mul_f16 v85, v208, v165 op_sel_hi:[0,1]
	v_pk_mul_f16 v109, v206, v165 op_sel_hi:[0,1]
	v_pk_mul_f16 v122, v207, v162 op_sel_hi:[0,1]
	v_pk_mul_f16 v125, v207, v165 op_sel_hi:[0,1]
	v_pk_mul_f16 v82, v208, v162 op_sel_hi:[0,1]
	v_pk_mul_f16 v83, v208, v163 op_sel_hi:[0,1]
	v_pk_mul_f16 v84, v208, v164 op_sel_hi:[0,1]
	v_pk_mul_f16 v106, v206, v162 op_sel_hi:[0,1]
	v_pk_mul_f16 v107, v206, v163 op_sel_hi:[0,1]
	v_pk_mul_f16 v108, v206, v164 op_sel_hi:[0,1]
	v_pk_mul_f16 v123, v207, v163 op_sel_hi:[0,1]
	v_pk_mul_f16 v124, v207, v164 op_sel_hi:[0,1]
	v_pk_fma_f16 v97, v97, v165, v85
	v_pk_fma_f16 v121, v121, v165, v109
	v_pk_fma_f16 v126, v137, v165, v125
	v_pk_fma_f16 v129, v134, v162, v122
	v_pk_fma_f16 v134, v65, v165, v85
	v_pk_fma_f16 v146, v81, v165, v109
	v_pk_fma_f16 v209, v105, v165, v125
	v_pk_fma_f16 v85, v37, v165, v85
	v_pk_fma_f16 v109, v49, v165, v109
	v_pk_fma_f16 v125, v69, v165, v125
	v_pk_maximum3_f16 v165, v97, v121, v126
	v_pk_fma_f16 v96, v96, v164, v84
	v_pk_fma_f16 v95, v95, v163, v83
	v_pk_fma_f16 v94, v94, v162, v82
	v_pk_fma_f16 v120, v120, v164, v108
	v_pk_fma_f16 v119, v119, v163, v107
	v_pk_fma_f16 v118, v118, v162, v106
	v_pk_fma_f16 v127, v136, v164, v124
	v_pk_fma_f16 v128, v135, v163, v123
	v_pk_fma_f16 v135, v64, v164, v84
	v_pk_fma_f16 v136, v63, v163, v83
	v_pk_fma_f16 v137, v62, v162, v82
	v_pk_fma_f16 v147, v80, v164, v108
	v_pk_fma_f16 v148, v79, v163, v107
	v_pk_fma_f16 v149, v78, v162, v106
	v_pk_fma_f16 v210, v104, v164, v124
	v_pk_fma_f16 v211, v103, v163, v123
	v_pk_fma_f16 v212, v102, v162, v122
	v_pk_fma_f16 v84, v36, v164, v84
	v_pk_fma_f16 v83, v35, v163, v83
	v_pk_fma_f16 v82, v34, v162, v82
	v_pk_fma_f16 v108, v48, v164, v108
	v_pk_fma_f16 v107, v47, v163, v107
	v_pk_fma_f16 v106, v46, v162, v106
	v_pk_fma_f16 v124, v68, v164, v124
	v_pk_fma_f16 v123, v67, v163, v123
	v_pk_fma_f16 v122, v66, v162, v122
	v_pk_maximum3_f16 v162, v94, v118, v129
	v_pk_maximum3_f16 v163, v95, v119, v128
	v_pk_maximum3_f16 v164, v96, v120, v127
	v_pk_maximum3_f16 v216, v134, v146, v209
	v_pk_maximum3_f16 v220, v85, v109, v125
	v_pk_maximum3_f16 v213, v137, v149, v212
	v_pk_maximum3_f16 v214, v136, v148, v211
	v_pk_maximum3_f16 v215, v135, v147, v210
	v_pk_maximum3_f16 v217, v82, v106, v122
	v_pk_maximum3_f16 v218, v83, v107, v123
	v_pk_maximum3_f16 v165, v165, v216, v220
	v_pk_maximum3_f16 v219, v84, v108, v124
	v_pk_maximum3_f16 v162, v162, v213, v217
	v_pk_maximum3_f16 v163, v163, v214, v218
	v_pk_maximum3_f16 v164, v164, v215, v219
	v_pk_add_f16 v97, v97, v165 neg_lo:[0,1] neg_hi:[0,1]
	v_pk_add_f16 v94, v94, v162 neg_lo:[0,1] neg_hi:[0,1]
	v_pk_add_f16 v95, v95, v163 neg_lo:[0,1] neg_hi:[0,1]
	v_pk_add_f16 v96, v96, v164 neg_lo:[0,1] neg_hi:[0,1]
	v_pk_add_f16 v118, v118, v162 neg_lo:[0,1] neg_hi:[0,1]
	v_exp_f16_sdwa v213, v94 dst_sel:WORD_0 dst_unused:UNUSED_PAD src0_sel:WORD_0
	v_exp_f16_sdwa v214, v95 dst_sel:WORD_0 dst_unused:UNUSED_PAD src0_sel:WORD_0
	v_exp_f16_sdwa v215, v96 dst_sel:WORD_0 dst_unused:UNUSED_PAD src0_sel:WORD_0
	v_exp_f16_sdwa v216, v97 dst_sel:WORD_0 dst_unused:UNUSED_PAD src0_sel:WORD_0
	v_exp_f16_sdwa v213, v94 dst_sel:WORD_1 dst_unused:UNUSED_PRESERVE src0_sel:WORD_1
	v_exp_f16_sdwa v214, v95 dst_sel:WORD_1 dst_unused:UNUSED_PRESERVE src0_sel:WORD_1
	v_exp_f16_sdwa v215, v96 dst_sel:WORD_1 dst_unused:UNUSED_PRESERVE src0_sel:WORD_1
	v_exp_f16_sdwa v216, v97 dst_sel:WORD_1 dst_unused:UNUSED_PRESERVE src0_sel:WORD_1
	v_pk_add_f16 v119, v119, v163 neg_lo:[0,1] neg_hi:[0,1]
	v_pk_add_f16 v97, v213, 0
	v_pk_fma_f16 v57, v57, v216, 0
	v_pk_add_f16 v94, v216, 0
	v_pk_add_f16 v95, v215, 0
	v_pk_add_f16 v96, v214, 0
	v_pk_fma_f16 v56, v56, v215, 0
	v_pk_fma_f16 v55, v55, v214, 0
	v_pk_fma_f16 v54, v54, v213, 0
	v_pk_add_f16 v120, v120, v164 neg_lo:[0,1] neg_hi:[0,1]
	v_pk_add_f16 v121, v121, v165 neg_lo:[0,1] neg_hi:[0,1]
	v_pk_add_f16 v82, v82, v162 neg_lo:[0,1] neg_hi:[0,1]
	v_exp_f16_sdwa v213, v118 dst_sel:WORD_0 dst_unused:UNUSED_PAD src0_sel:WORD_0
	v_exp_f16_sdwa v214, v119 dst_sel:WORD_0 dst_unused:UNUSED_PAD src0_sel:WORD_0
	v_exp_f16_sdwa v215, v120 dst_sel:WORD_0 dst_unused:UNUSED_PAD src0_sel:WORD_0
	v_exp_f16_sdwa v216, v121 dst_sel:WORD_0 dst_unused:UNUSED_PAD src0_sel:WORD_0
	v_exp_f16_sdwa v213, v118 dst_sel:WORD_1 dst_unused:UNUSED_PRESERVE src0_sel:WORD_1
	v_exp_f16_sdwa v214, v119 dst_sel:WORD_1 dst_unused:UNUSED_PRESERVE src0_sel:WORD_1
	v_exp_f16_sdwa v215, v120 dst_sel:WORD_1 dst_unused:UNUSED_PRESERVE src0_sel:WORD_1
	v_exp_f16_sdwa v216, v121 dst_sel:WORD_1 dst_unused:UNUSED_PRESERVE src0_sel:WORD_1
	v_pk_add_f16 v83, v83, v163 neg_lo:[0,1] neg_hi:[0,1]
	v_pk_add_f16 v97, v97, v213
	v_pk_fma_f16 v57, v77, v216, v57
	v_pk_add_f16 v77, v126, v165 neg_lo:[0,1] neg_hi:[0,1]
	v_pk_add_f16 v96, v96, v214
	v_pk_add_f16 v95, v95, v215
	v_pk_add_f16 v94, v94, v216
	v_pk_fma_f16 v54, v74, v213, v54
	v_pk_fma_f16 v55, v75, v214, v55
	v_pk_fma_f16 v56, v76, v215, v56
	v_pk_add_f16 v74, v129, v162 neg_lo:[0,1] neg_hi:[0,1]
	v_pk_add_f16 v75, v128, v163 neg_lo:[0,1] neg_hi:[0,1]
	v_pk_add_f16 v76, v127, v164 neg_lo:[0,1] neg_hi:[0,1]
	v_pk_add_f16 v84, v84, v164 neg_lo:[0,1] neg_hi:[0,1]
	v_exp_f16_sdwa v118, v74 dst_sel:WORD_0 dst_unused:UNUSED_PAD src0_sel:WORD_0
	v_exp_f16_sdwa v119, v75 dst_sel:WORD_0 dst_unused:UNUSED_PAD src0_sel:WORD_0
	v_exp_f16_sdwa v120, v76 dst_sel:WORD_0 dst_unused:UNUSED_PAD src0_sel:WORD_0
	v_exp_f16_sdwa v121, v77 dst_sel:WORD_0 dst_unused:UNUSED_PAD src0_sel:WORD_0
	v_exp_f16_sdwa v118, v74 dst_sel:WORD_1 dst_unused:UNUSED_PRESERVE src0_sel:WORD_1
	v_exp_f16_sdwa v119, v75 dst_sel:WORD_1 dst_unused:UNUSED_PRESERVE src0_sel:WORD_1
	v_exp_f16_sdwa v120, v76 dst_sel:WORD_1 dst_unused:UNUSED_PRESERVE src0_sel:WORD_1
	v_exp_f16_sdwa v121, v77 dst_sel:WORD_1 dst_unused:UNUSED_PRESERVE src0_sel:WORD_1
	v_pk_add_f16 v85, v85, v165 neg_lo:[0,1] neg_hi:[0,1]
	v_pk_add_f16 v77, v97, v118
	v_pk_add_f16 v74, v94, v121
	v_pk_add_f16 v75, v95, v120
	v_pk_add_f16 v76, v96, v119
	v_pk_fma_f16 v57, v101, v121, v57
	v_pk_fma_f16 v56, v100, v120, v56
	v_pk_fma_f16 v55, v99, v119, v55
	v_pk_fma_f16 v54, v98, v118, v54
	v_pk_add_f16 v94, v137, v162 neg_lo:[0,1] neg_hi:[0,1]
	v_pk_add_f16 v95, v136, v163 neg_lo:[0,1] neg_hi:[0,1]
	v_pk_add_f16 v96, v135, v164 neg_lo:[0,1] neg_hi:[0,1]
	v_pk_add_f16 v97, v134, v165 neg_lo:[0,1] neg_hi:[0,1]
	v_exp_f16_sdwa v98, v94 dst_sel:WORD_0 dst_unused:UNUSED_PAD src0_sel:WORD_0
	v_exp_f16_sdwa v99, v95 dst_sel:WORD_0 dst_unused:UNUSED_PAD src0_sel:WORD_0
	v_exp_f16_sdwa v100, v96 dst_sel:WORD_0 dst_unused:UNUSED_PAD src0_sel:WORD_0
	v_exp_f16_sdwa v101, v97 dst_sel:WORD_0 dst_unused:UNUSED_PAD src0_sel:WORD_0
	v_exp_f16_sdwa v98, v94 dst_sel:WORD_1 dst_unused:UNUSED_PRESERVE src0_sel:WORD_1
	v_exp_f16_sdwa v99, v95 dst_sel:WORD_1 dst_unused:UNUSED_PRESERVE src0_sel:WORD_1
	v_exp_f16_sdwa v100, v96 dst_sel:WORD_1 dst_unused:UNUSED_PRESERVE src0_sel:WORD_1
	v_exp_f16_sdwa v101, v97 dst_sel:WORD_1 dst_unused:UNUSED_PRESERVE src0_sel:WORD_1
	v_pk_add_f16 v94, v149, v162 neg_lo:[0,1] neg_hi:[0,1]
	v_pk_add_f16 v77, v77, v98
	v_pk_add_f16 v76, v76, v99
	v_pk_add_f16 v75, v75, v100
	v_pk_add_f16 v74, v74, v101
	v_pk_fma_f16 v54, v30, v98, v54
	v_pk_fma_f16 v55, v31, v99, v55
	v_pk_fma_f16 v56, v32, v100, v56
	v_pk_fma_f16 v57, v33, v101, v57
	v_pk_add_f16 v95, v148, v163 neg_lo:[0,1] neg_hi:[0,1]
	v_pk_add_f16 v96, v147, v164 neg_lo:[0,1] neg_hi:[0,1]
	v_pk_add_f16 v97, v146, v165 neg_lo:[0,1] neg_hi:[0,1]
	v_exp_f16_sdwa v98, v94 dst_sel:WORD_0 dst_unused:UNUSED_PAD src0_sel:WORD_0
	v_exp_f16_sdwa v99, v95 dst_sel:WORD_0 dst_unused:UNUSED_PAD src0_sel:WORD_0
	v_exp_f16_sdwa v100, v96 dst_sel:WORD_0 dst_unused:UNUSED_PAD src0_sel:WORD_0
	v_exp_f16_sdwa v101, v97 dst_sel:WORD_0 dst_unused:UNUSED_PAD src0_sel:WORD_0
	v_exp_f16_sdwa v98, v94 dst_sel:WORD_1 dst_unused:UNUSED_PRESERVE src0_sel:WORD_1
	v_exp_f16_sdwa v99, v95 dst_sel:WORD_1 dst_unused:UNUSED_PRESERVE src0_sel:WORD_1
	v_exp_f16_sdwa v100, v96 dst_sel:WORD_1 dst_unused:UNUSED_PRESERVE src0_sel:WORD_1
	v_exp_f16_sdwa v101, v97 dst_sel:WORD_1 dst_unused:UNUSED_PRESERVE src0_sel:WORD_1
	v_pk_add_f16 v94, v212, v162 neg_lo:[0,1] neg_hi:[0,1]
	v_pk_add_f16 v77, v77, v98
	v_pk_add_f16 v74, v74, v101
	v_pk_add_f16 v75, v75, v100
	v_pk_add_f16 v76, v76, v99
	v_pk_fma_f16 v57, v45, v101, v57
	v_pk_fma_f16 v56, v44, v100, v56
	v_pk_fma_f16 v55, v43, v99, v55
	v_pk_fma_f16 v54, v42, v98, v54
	v_pk_add_f16 v95, v211, v163 neg_lo:[0,1] neg_hi:[0,1]
	v_pk_add_f16 v96, v210, v164 neg_lo:[0,1] neg_hi:[0,1]
	v_pk_add_f16 v97, v209, v165 neg_lo:[0,1] neg_hi:[0,1]
	v_exp_f16_sdwa v98, v94 dst_sel:WORD_0 dst_unused:UNUSED_PAD src0_sel:WORD_0
	v_exp_f16_sdwa v99, v95 dst_sel:WORD_0 dst_unused:UNUSED_PAD src0_sel:WORD_0
	v_exp_f16_sdwa v100, v96 dst_sel:WORD_0 dst_unused:UNUSED_PAD src0_sel:WORD_0
	v_exp_f16_sdwa v101, v97 dst_sel:WORD_0 dst_unused:UNUSED_PAD src0_sel:WORD_0
	v_exp_f16_sdwa v98, v94 dst_sel:WORD_1 dst_unused:UNUSED_PRESERVE src0_sel:WORD_1
	v_exp_f16_sdwa v99, v95 dst_sel:WORD_1 dst_unused:UNUSED_PRESERVE src0_sel:WORD_1
	v_exp_f16_sdwa v100, v96 dst_sel:WORD_1 dst_unused:UNUSED_PRESERVE src0_sel:WORD_1
	v_exp_f16_sdwa v101, v97 dst_sel:WORD_1 dst_unused:UNUSED_PRESERVE src0_sel:WORD_1
	v_exp_f16_sdwa v94, v82 dst_sel:WORD_0 dst_unused:UNUSED_PAD src0_sel:WORD_0
	v_exp_f16_sdwa v95, v83 dst_sel:WORD_0 dst_unused:UNUSED_PAD src0_sel:WORD_0
	v_exp_f16_sdwa v96, v84 dst_sel:WORD_0 dst_unused:UNUSED_PAD src0_sel:WORD_0
	v_exp_f16_sdwa v97, v85 dst_sel:WORD_0 dst_unused:UNUSED_PAD src0_sel:WORD_0
	v_exp_f16_sdwa v94, v82 dst_sel:WORD_1 dst_unused:UNUSED_PRESERVE src0_sel:WORD_1
	v_exp_f16_sdwa v95, v83 dst_sel:WORD_1 dst_unused:UNUSED_PRESERVE src0_sel:WORD_1
	v_exp_f16_sdwa v96, v84 dst_sel:WORD_1 dst_unused:UNUSED_PRESERVE src0_sel:WORD_1
	v_exp_f16_sdwa v97, v85 dst_sel:WORD_1 dst_unused:UNUSED_PRESERVE src0_sel:WORD_1
	v_pk_add_f16 v82, v106, v162 neg_lo:[0,1] neg_hi:[0,1]
	v_pk_add_f16 v77, v77, v98
	v_pk_add_f16 v76, v76, v99
	v_pk_add_f16 v75, v75, v100
	v_pk_add_f16 v74, v74, v101
	v_pk_fma_f16 v54, v58, v98, v54
	v_pk_fma_f16 v55, v59, v99, v55
	v_pk_fma_f16 v56, v60, v100, v56
	v_pk_fma_f16 v57, v61, v101, v57
	v_pk_add_f16 v77, v77, v94
	v_pk_add_f16 v74, v74, v97
	v_pk_add_f16 v75, v75, v96
	v_pk_add_f16 v76, v76, v95
	v_pk_fma_f16 v57, v21, v97, v57
	v_pk_fma_f16 v56, v20, v96, v56
	v_pk_fma_f16 v55, v19, v95, v55
	v_pk_fma_f16 v54, v18, v94, v54
	v_pk_add_f16 v83, v107, v163 neg_lo:[0,1] neg_hi:[0,1]
	v_pk_add_f16 v84, v108, v164 neg_lo:[0,1] neg_hi:[0,1]
	v_pk_add_f16 v85, v109, v165 neg_lo:[0,1] neg_hi:[0,1]
	v_exp_f16_sdwa v94, v82 dst_sel:WORD_0 dst_unused:UNUSED_PAD src0_sel:WORD_0
	v_exp_f16_sdwa v95, v83 dst_sel:WORD_0 dst_unused:UNUSED_PAD src0_sel:WORD_0
	v_exp_f16_sdwa v96, v84 dst_sel:WORD_0 dst_unused:UNUSED_PAD src0_sel:WORD_0
	v_exp_f16_sdwa v97, v85 dst_sel:WORD_0 dst_unused:UNUSED_PAD src0_sel:WORD_0
	v_exp_f16_sdwa v94, v82 dst_sel:WORD_1 dst_unused:UNUSED_PRESERVE src0_sel:WORD_1
	v_exp_f16_sdwa v95, v83 dst_sel:WORD_1 dst_unused:UNUSED_PRESERVE src0_sel:WORD_1
	v_exp_f16_sdwa v96, v84 dst_sel:WORD_1 dst_unused:UNUSED_PRESERVE src0_sel:WORD_1
	v_exp_f16_sdwa v97, v85 dst_sel:WORD_1 dst_unused:UNUSED_PRESERVE src0_sel:WORD_1
	v_pk_add_f16 v82, v122, v162 neg_lo:[0,1] neg_hi:[0,1]
	v_pk_add_f16 v77, v77, v94
	v_pk_add_f16 v76, v76, v95
	v_pk_add_f16 v75, v75, v96
	v_pk_add_f16 v74, v74, v97
	v_pk_fma_f16 v54, v22, v94, v54
	v_pk_fma_f16 v55, v23, v95, v55
	v_pk_fma_f16 v56, v24, v96, v56
	v_pk_fma_f16 v57, v25, v97, v57
	v_pk_add_f16 v83, v123, v163 neg_lo:[0,1] neg_hi:[0,1]
	v_pk_add_f16 v84, v124, v164 neg_lo:[0,1] neg_hi:[0,1]
	v_pk_add_f16 v85, v125, v165 neg_lo:[0,1] neg_hi:[0,1]
	v_exp_f16_sdwa v94, v82 dst_sel:WORD_0 dst_unused:UNUSED_PAD src0_sel:WORD_0
	v_exp_f16_sdwa v95, v83 dst_sel:WORD_0 dst_unused:UNUSED_PAD src0_sel:WORD_0
	v_exp_f16_sdwa v96, v84 dst_sel:WORD_0 dst_unused:UNUSED_PAD src0_sel:WORD_0
	v_exp_f16_sdwa v97, v85 dst_sel:WORD_0 dst_unused:UNUSED_PAD src0_sel:WORD_0
	v_exp_f16_sdwa v94, v82 dst_sel:WORD_1 dst_unused:UNUSED_PRESERVE src0_sel:WORD_1
	v_exp_f16_sdwa v95, v83 dst_sel:WORD_1 dst_unused:UNUSED_PRESERVE src0_sel:WORD_1
	v_exp_f16_sdwa v96, v84 dst_sel:WORD_1 dst_unused:UNUSED_PRESERVE src0_sel:WORD_1
	v_exp_f16_sdwa v97, v85 dst_sel:WORD_1 dst_unused:UNUSED_PRESERVE src0_sel:WORD_1
	v_pk_add_f16 v77, v77, v94
	v_pk_add_f16 v76, v76, v95
	v_rcp_f16_e32 v82, v77
	v_rcp_f16_sdwa v77, v77 dst_sel:DWORD dst_unused:UNUSED_PAD src0_sel:WORD_1
	v_pk_add_f16 v75, v75, v96
	v_rcp_f16_e32 v83, v76
	v_rcp_f16_sdwa v76, v76 dst_sel:DWORD dst_unused:UNUSED_PAD src0_sel:WORD_1
	v_pk_add_f16 v74, v74, v97
	v_rcp_f16_e32 v84, v75
	v_rcp_f16_sdwa v75, v75 dst_sel:DWORD dst_unused:UNUSED_PAD src0_sel:WORD_1
	v_rcp_f16_e32 v85, v74
	v_rcp_f16_sdwa v74, v74 dst_sel:DWORD dst_unused:UNUSED_PAD src0_sel:WORD_1
	v_pk_fma_f16 v54, v26, v94, v54
	v_pack_b32_f16 v77, v82, v77
	v_pk_fma_f16 v57, v29, v97, v57
	v_pk_fma_f16 v55, v27, v95, v55
	v_pk_mul_f16 v97, v54, v77
	v_pack_b32_f16 v54, v83, v76
	v_pk_fma_f16 v56, v28, v96, v56
	v_pk_mul_f16 v96, v55, v54
	v_pack_b32_f16 v54, v84, v75
	v_pk_mul_f16 v95, v56, v54
	v_pack_b32_f16 v54, v85, v74
	v_pk_mul_f16 v94, v57, v54
	s_waitcnt vmcnt(6)
	v_pk_mul_f16 v57, v208, v161 op_sel_hi:[0,1]
	v_pk_mul_f16 v77, v206, v161 op_sel_hi:[0,1]
	v_pk_mul_f16 v85, v207, v161 op_sel_hi:[0,1]
	v_pk_mul_f16 v54, v208, v158 op_sel_hi:[0,1]
	v_pk_mul_f16 v55, v208, v159 op_sel_hi:[0,1]
	v_pk_mul_f16 v56, v208, v160 op_sel_hi:[0,1]
	v_pk_mul_f16 v74, v206, v158 op_sel_hi:[0,1]
	v_pk_mul_f16 v75, v206, v159 op_sel_hi:[0,1]
	v_pk_mul_f16 v76, v206, v160 op_sel_hi:[0,1]
	v_pk_mul_f16 v82, v207, v158 op_sel_hi:[0,1]
	v_pk_mul_f16 v83, v207, v159 op_sel_hi:[0,1]
	v_pk_mul_f16 v84, v207, v160 op_sel_hi:[0,1]
	v_pk_fma_f16 v65, v65, v161, v57
	v_pk_fma_f16 v81, v81, v161, v77
	v_pk_fma_f16 v98, v105, v161, v85
	v_pk_fma_f16 v64, v64, v160, v56
	v_pk_maximum3_f16 v125, v65, v81, v98
	v_pk_fma_f16 v63, v63, v159, v55
	v_pk_fma_f16 v62, v62, v158, v54
	v_pk_fma_f16 v80, v80, v160, v76
	v_pk_fma_f16 v79, v79, v159, v75
	v_pk_fma_f16 v78, v78, v158, v74
	v_pk_fma_f16 v99, v104, v160, v84
	v_pk_fma_f16 v100, v103, v159, v83
	v_pk_fma_f16 v101, v102, v158, v82
	v_pk_fma_f16 v102, v37, v161, v57
	v_pk_fma_f16 v106, v49, v161, v77
	v_pk_fma_f16 v118, v69, v161, v85
	v_pk_fma_f16 v57, v89, v161, v57
	v_pk_fma_f16 v77, v117, v161, v77
	v_pk_fma_f16 v85, v133, v161, v85
	v_pk_maximum3_f16 v122, v62, v78, v101
	v_pk_maximum3_f16 v123, v63, v79, v100
	v_pk_maximum3_f16 v124, v64, v80, v99
	v_pk_maximum3_f16 v129, v102, v106, v118
	v_pk_fma_f16 v103, v36, v160, v56
	v_pk_maximum3_f16 v137, v57, v77, v85
	v_pk_fma_f16 v104, v35, v159, v55
	v_pk_maximum3_f16 v125, v125, v129, v137
	v_pk_fma_f16 v105, v34, v158, v54
	v_pk_fma_f16 v107, v48, v160, v76
	v_pk_fma_f16 v108, v47, v159, v75
	v_pk_fma_f16 v109, v46, v158, v74
	v_pk_fma_f16 v119, v68, v160, v84
	v_pk_fma_f16 v120, v67, v159, v83
	v_pk_fma_f16 v121, v66, v158, v82
	v_pk_fma_f16 v56, v88, v160, v56
	v_pk_fma_f16 v55, v87, v159, v55
	v_pk_fma_f16 v54, v86, v158, v54
	v_pk_fma_f16 v76, v116, v160, v76
	v_pk_fma_f16 v75, v115, v159, v75
	v_pk_fma_f16 v74, v114, v158, v74
	v_pk_fma_f16 v84, v132, v160, v84
	v_pk_fma_f16 v83, v131, v159, v83
	v_pk_fma_f16 v82, v130, v158, v82
	v_pk_maximum3_f16 v126, v105, v109, v121
	v_pk_maximum3_f16 v127, v104, v108, v120
	v_pk_maximum3_f16 v128, v103, v107, v119
	v_pk_maximum3_f16 v135, v55, v75, v83
	v_pk_maximum3_f16 v136, v56, v76, v84
	v_pk_maximum3_f16 v134, v54, v74, v82
	v_pk_maximum3_f16 v122, v122, v126, v134
	v_pk_maximum3_f16 v123, v123, v127, v135
	v_pk_maximum3_f16 v124, v124, v128, v136
	v_pk_add_f16 v65, v65, v125 neg_lo:[0,1] neg_hi:[0,1]
	v_pk_add_f16 v62, v62, v122 neg_lo:[0,1] neg_hi:[0,1]
	v_pk_add_f16 v63, v63, v123 neg_lo:[0,1] neg_hi:[0,1]
	v_pk_add_f16 v64, v64, v124 neg_lo:[0,1] neg_hi:[0,1]
	v_pk_add_f16 v78, v78, v122 neg_lo:[0,1] neg_hi:[0,1]
	v_exp_f16_sdwa v126, v62 dst_sel:WORD_0 dst_unused:UNUSED_PAD src0_sel:WORD_0
	v_exp_f16_sdwa v127, v63 dst_sel:WORD_0 dst_unused:UNUSED_PAD src0_sel:WORD_0
	v_exp_f16_sdwa v128, v64 dst_sel:WORD_0 dst_unused:UNUSED_PAD src0_sel:WORD_0
	v_exp_f16_sdwa v129, v65 dst_sel:WORD_0 dst_unused:UNUSED_PAD src0_sel:WORD_0
	v_exp_f16_sdwa v126, v62 dst_sel:WORD_1 dst_unused:UNUSED_PRESERVE src0_sel:WORD_1
	v_exp_f16_sdwa v127, v63 dst_sel:WORD_1 dst_unused:UNUSED_PRESERVE src0_sel:WORD_1
	v_exp_f16_sdwa v128, v64 dst_sel:WORD_1 dst_unused:UNUSED_PRESERVE src0_sel:WORD_1
	v_exp_f16_sdwa v129, v65 dst_sel:WORD_1 dst_unused:UNUSED_PRESERVE src0_sel:WORD_1
	v_pk_add_f16 v79, v79, v123 neg_lo:[0,1] neg_hi:[0,1]
	v_pk_add_f16 v65, v126, 0
	v_pk_fma_f16 v33, v33, v129, 0
	v_pk_add_f16 v62, v129, 0
	v_pk_add_f16 v63, v128, 0
	v_pk_add_f16 v64, v127, 0
	v_pk_fma_f16 v32, v32, v128, 0
	v_pk_fma_f16 v31, v31, v127, 0
	v_pk_fma_f16 v30, v30, v126, 0
	v_pk_add_f16 v80, v80, v124 neg_lo:[0,1] neg_hi:[0,1]
	v_pk_add_f16 v81, v81, v125 neg_lo:[0,1] neg_hi:[0,1]
	v_pk_add_f16 v54, v54, v122 neg_lo:[0,1] neg_hi:[0,1]
	v_exp_f16_sdwa v126, v78 dst_sel:WORD_0 dst_unused:UNUSED_PAD src0_sel:WORD_0
	v_exp_f16_sdwa v127, v79 dst_sel:WORD_0 dst_unused:UNUSED_PAD src0_sel:WORD_0
	v_exp_f16_sdwa v128, v80 dst_sel:WORD_0 dst_unused:UNUSED_PAD src0_sel:WORD_0
	v_exp_f16_sdwa v129, v81 dst_sel:WORD_0 dst_unused:UNUSED_PAD src0_sel:WORD_0
	v_exp_f16_sdwa v126, v78 dst_sel:WORD_1 dst_unused:UNUSED_PRESERVE src0_sel:WORD_1
	v_exp_f16_sdwa v127, v79 dst_sel:WORD_1 dst_unused:UNUSED_PRESERVE src0_sel:WORD_1
	v_exp_f16_sdwa v128, v80 dst_sel:WORD_1 dst_unused:UNUSED_PRESERVE src0_sel:WORD_1
	v_exp_f16_sdwa v129, v81 dst_sel:WORD_1 dst_unused:UNUSED_PRESERVE src0_sel:WORD_1
	v_pk_add_f16 v55, v55, v123 neg_lo:[0,1] neg_hi:[0,1]
	v_pk_add_f16 v65, v65, v126
	v_pk_fma_f16 v33, v45, v129, v33
	v_pk_add_f16 v45, v98, v125 neg_lo:[0,1] neg_hi:[0,1]
	v_pk_add_f16 v64, v64, v127
	v_pk_add_f16 v63, v63, v128
	v_pk_add_f16 v62, v62, v129
	v_pk_fma_f16 v30, v42, v126, v30
	v_pk_fma_f16 v31, v43, v127, v31
	v_pk_fma_f16 v32, v44, v128, v32
	v_pk_add_f16 v42, v101, v122 neg_lo:[0,1] neg_hi:[0,1]
	v_pk_add_f16 v43, v100, v123 neg_lo:[0,1] neg_hi:[0,1]
	v_pk_add_f16 v44, v99, v124 neg_lo:[0,1] neg_hi:[0,1]
	v_pk_add_f16 v56, v56, v124 neg_lo:[0,1] neg_hi:[0,1]
	v_exp_f16_sdwa v78, v42 dst_sel:WORD_0 dst_unused:UNUSED_PAD src0_sel:WORD_0
	v_exp_f16_sdwa v79, v43 dst_sel:WORD_0 dst_unused:UNUSED_PAD src0_sel:WORD_0
	v_exp_f16_sdwa v80, v44 dst_sel:WORD_0 dst_unused:UNUSED_PAD src0_sel:WORD_0
	v_exp_f16_sdwa v81, v45 dst_sel:WORD_0 dst_unused:UNUSED_PAD src0_sel:WORD_0
	v_exp_f16_sdwa v78, v42 dst_sel:WORD_1 dst_unused:UNUSED_PRESERVE src0_sel:WORD_1
	v_exp_f16_sdwa v79, v43 dst_sel:WORD_1 dst_unused:UNUSED_PRESERVE src0_sel:WORD_1
	v_exp_f16_sdwa v80, v44 dst_sel:WORD_1 dst_unused:UNUSED_PRESERVE src0_sel:WORD_1
	v_exp_f16_sdwa v81, v45 dst_sel:WORD_1 dst_unused:UNUSED_PRESERVE src0_sel:WORD_1
	v_pk_add_f16 v57, v57, v125 neg_lo:[0,1] neg_hi:[0,1]
	v_pk_add_f16 v45, v65, v78
	v_pk_add_f16 v42, v62, v81
	v_pk_add_f16 v43, v63, v80
	v_pk_add_f16 v44, v64, v79
	v_pk_fma_f16 v33, v61, v81, v33
	v_pk_fma_f16 v32, v60, v80, v32
	v_pk_fma_f16 v31, v59, v79, v31
	v_pk_fma_f16 v30, v58, v78, v30
	v_pk_add_f16 v58, v105, v122 neg_lo:[0,1] neg_hi:[0,1]
	v_pk_add_f16 v59, v104, v123 neg_lo:[0,1] neg_hi:[0,1]
	v_pk_add_f16 v60, v103, v124 neg_lo:[0,1] neg_hi:[0,1]
	v_pk_add_f16 v61, v102, v125 neg_lo:[0,1] neg_hi:[0,1]
	v_exp_f16_sdwa v62, v58 dst_sel:WORD_0 dst_unused:UNUSED_PAD src0_sel:WORD_0
	v_exp_f16_sdwa v63, v59 dst_sel:WORD_0 dst_unused:UNUSED_PAD src0_sel:WORD_0
	v_exp_f16_sdwa v64, v60 dst_sel:WORD_0 dst_unused:UNUSED_PAD src0_sel:WORD_0
	v_exp_f16_sdwa v65, v61 dst_sel:WORD_0 dst_unused:UNUSED_PAD src0_sel:WORD_0
	v_exp_f16_sdwa v62, v58 dst_sel:WORD_1 dst_unused:UNUSED_PRESERVE src0_sel:WORD_1
	v_exp_f16_sdwa v63, v59 dst_sel:WORD_1 dst_unused:UNUSED_PRESERVE src0_sel:WORD_1
	v_exp_f16_sdwa v64, v60 dst_sel:WORD_1 dst_unused:UNUSED_PRESERVE src0_sel:WORD_1
	v_exp_f16_sdwa v65, v61 dst_sel:WORD_1 dst_unused:UNUSED_PRESERVE src0_sel:WORD_1
	v_pk_add_f16 v58, v109, v122 neg_lo:[0,1] neg_hi:[0,1]
	v_pk_add_f16 v45, v45, v62
	v_pk_add_f16 v44, v44, v63
	v_pk_add_f16 v43, v43, v64
	v_pk_add_f16 v42, v42, v65
	v_pk_fma_f16 v30, v18, v62, v30
	v_pk_fma_f16 v31, v19, v63, v31
	v_pk_fma_f16 v32, v20, v64, v32
	v_pk_fma_f16 v33, v21, v65, v33
	v_pk_add_f16 v59, v108, v123 neg_lo:[0,1] neg_hi:[0,1]
	v_pk_add_f16 v60, v107, v124 neg_lo:[0,1] neg_hi:[0,1]
	v_pk_add_f16 v61, v106, v125 neg_lo:[0,1] neg_hi:[0,1]
	v_exp_f16_sdwa v62, v58 dst_sel:WORD_0 dst_unused:UNUSED_PAD src0_sel:WORD_0
	v_exp_f16_sdwa v63, v59 dst_sel:WORD_0 dst_unused:UNUSED_PAD src0_sel:WORD_0
	v_exp_f16_sdwa v64, v60 dst_sel:WORD_0 dst_unused:UNUSED_PAD src0_sel:WORD_0
	v_exp_f16_sdwa v65, v61 dst_sel:WORD_0 dst_unused:UNUSED_PAD src0_sel:WORD_0
	v_exp_f16_sdwa v62, v58 dst_sel:WORD_1 dst_unused:UNUSED_PRESERVE src0_sel:WORD_1
	v_exp_f16_sdwa v63, v59 dst_sel:WORD_1 dst_unused:UNUSED_PRESERVE src0_sel:WORD_1
	v_exp_f16_sdwa v64, v60 dst_sel:WORD_1 dst_unused:UNUSED_PRESERVE src0_sel:WORD_1
	v_exp_f16_sdwa v65, v61 dst_sel:WORD_1 dst_unused:UNUSED_PRESERVE src0_sel:WORD_1
	v_pk_add_f16 v58, v121, v122 neg_lo:[0,1] neg_hi:[0,1]
	v_pk_add_f16 v45, v45, v62
	v_pk_add_f16 v42, v42, v65
	v_pk_add_f16 v43, v43, v64
	v_pk_add_f16 v44, v44, v63
	v_pk_fma_f16 v33, v25, v65, v33
	v_pk_fma_f16 v32, v24, v64, v32
	v_pk_fma_f16 v31, v23, v63, v31
	v_pk_fma_f16 v30, v22, v62, v30
	v_pk_add_f16 v59, v120, v123 neg_lo:[0,1] neg_hi:[0,1]
	v_pk_add_f16 v60, v119, v124 neg_lo:[0,1] neg_hi:[0,1]
	v_pk_add_f16 v61, v118, v125 neg_lo:[0,1] neg_hi:[0,1]
	v_exp_f16_sdwa v62, v58 dst_sel:WORD_0 dst_unused:UNUSED_PAD src0_sel:WORD_0
	v_exp_f16_sdwa v63, v59 dst_sel:WORD_0 dst_unused:UNUSED_PAD src0_sel:WORD_0
	v_exp_f16_sdwa v64, v60 dst_sel:WORD_0 dst_unused:UNUSED_PAD src0_sel:WORD_0
	v_exp_f16_sdwa v65, v61 dst_sel:WORD_0 dst_unused:UNUSED_PAD src0_sel:WORD_0
	v_exp_f16_sdwa v62, v58 dst_sel:WORD_1 dst_unused:UNUSED_PRESERVE src0_sel:WORD_1
	v_exp_f16_sdwa v63, v59 dst_sel:WORD_1 dst_unused:UNUSED_PRESERVE src0_sel:WORD_1
	v_exp_f16_sdwa v64, v60 dst_sel:WORD_1 dst_unused:UNUSED_PRESERVE src0_sel:WORD_1
	v_exp_f16_sdwa v65, v61 dst_sel:WORD_1 dst_unused:UNUSED_PRESERVE src0_sel:WORD_1
	v_exp_f16_sdwa v58, v54 dst_sel:WORD_0 dst_unused:UNUSED_PAD src0_sel:WORD_0
	v_exp_f16_sdwa v59, v55 dst_sel:WORD_0 dst_unused:UNUSED_PAD src0_sel:WORD_0
	v_exp_f16_sdwa v60, v56 dst_sel:WORD_0 dst_unused:UNUSED_PAD src0_sel:WORD_0
	v_exp_f16_sdwa v61, v57 dst_sel:WORD_0 dst_unused:UNUSED_PAD src0_sel:WORD_0
	v_exp_f16_sdwa v58, v54 dst_sel:WORD_1 dst_unused:UNUSED_PRESERVE src0_sel:WORD_1
	v_exp_f16_sdwa v59, v55 dst_sel:WORD_1 dst_unused:UNUSED_PRESERVE src0_sel:WORD_1
	v_exp_f16_sdwa v60, v56 dst_sel:WORD_1 dst_unused:UNUSED_PRESERVE src0_sel:WORD_1
	v_exp_f16_sdwa v61, v57 dst_sel:WORD_1 dst_unused:UNUSED_PRESERVE src0_sel:WORD_1
	v_pk_add_f16 v54, v74, v122 neg_lo:[0,1] neg_hi:[0,1]
	v_pk_add_f16 v45, v45, v62
	v_pk_add_f16 v44, v44, v63
	v_pk_add_f16 v43, v43, v64
	v_pk_add_f16 v42, v42, v65
	v_pk_fma_f16 v30, v26, v62, v30
	v_pk_fma_f16 v31, v27, v63, v31
	v_pk_fma_f16 v32, v28, v64, v32
	v_pk_fma_f16 v33, v29, v65, v33
	v_pk_add_f16 v45, v45, v58
	v_pk_add_f16 v42, v42, v61
	v_pk_add_f16 v43, v43, v60
	v_pk_add_f16 v44, v44, v59
	v_pk_fma_f16 v33, v41, v61, v33
	v_pk_fma_f16 v32, v40, v60, v32
	v_pk_fma_f16 v31, v39, v59, v31
	v_pk_fma_f16 v30, v38, v58, v30
	v_pk_add_f16 v55, v75, v123 neg_lo:[0,1] neg_hi:[0,1]
	v_pk_add_f16 v56, v76, v124 neg_lo:[0,1] neg_hi:[0,1]
	v_pk_add_f16 v57, v77, v125 neg_lo:[0,1] neg_hi:[0,1]
	v_exp_f16_sdwa v58, v54 dst_sel:WORD_0 dst_unused:UNUSED_PAD src0_sel:WORD_0
	v_exp_f16_sdwa v59, v55 dst_sel:WORD_0 dst_unused:UNUSED_PAD src0_sel:WORD_0
	v_exp_f16_sdwa v60, v56 dst_sel:WORD_0 dst_unused:UNUSED_PAD src0_sel:WORD_0
	v_exp_f16_sdwa v61, v57 dst_sel:WORD_0 dst_unused:UNUSED_PAD src0_sel:WORD_0
	v_exp_f16_sdwa v58, v54 dst_sel:WORD_1 dst_unused:UNUSED_PRESERVE src0_sel:WORD_1
	v_exp_f16_sdwa v59, v55 dst_sel:WORD_1 dst_unused:UNUSED_PRESERVE src0_sel:WORD_1
	v_exp_f16_sdwa v60, v56 dst_sel:WORD_1 dst_unused:UNUSED_PRESERVE src0_sel:WORD_1
	v_exp_f16_sdwa v61, v57 dst_sel:WORD_1 dst_unused:UNUSED_PRESERVE src0_sel:WORD_1
	v_pk_add_f16 v54, v82, v122 neg_lo:[0,1] neg_hi:[0,1]
	v_pk_add_f16 v45, v45, v58
	v_pk_add_f16 v44, v44, v59
	v_pk_add_f16 v43, v43, v60
	v_pk_add_f16 v42, v42, v61
	v_pk_fma_f16 v30, v50, v58, v30
	v_pk_fma_f16 v31, v51, v59, v31
	v_pk_fma_f16 v32, v52, v60, v32
	v_pk_fma_f16 v33, v53, v61, v33
	v_pk_add_f16 v55, v83, v123 neg_lo:[0,1] neg_hi:[0,1]
	v_pk_add_f16 v56, v84, v124 neg_lo:[0,1] neg_hi:[0,1]
	v_pk_add_f16 v57, v85, v125 neg_lo:[0,1] neg_hi:[0,1]
	v_exp_f16_sdwa v58, v54 dst_sel:WORD_0 dst_unused:UNUSED_PAD src0_sel:WORD_0
	v_exp_f16_sdwa v59, v55 dst_sel:WORD_0 dst_unused:UNUSED_PAD src0_sel:WORD_0
	v_exp_f16_sdwa v60, v56 dst_sel:WORD_0 dst_unused:UNUSED_PAD src0_sel:WORD_0
	v_exp_f16_sdwa v61, v57 dst_sel:WORD_0 dst_unused:UNUSED_PAD src0_sel:WORD_0
	v_exp_f16_sdwa v58, v54 dst_sel:WORD_1 dst_unused:UNUSED_PRESERVE src0_sel:WORD_1
	v_exp_f16_sdwa v59, v55 dst_sel:WORD_1 dst_unused:UNUSED_PRESERVE src0_sel:WORD_1
	v_exp_f16_sdwa v60, v56 dst_sel:WORD_1 dst_unused:UNUSED_PRESERVE src0_sel:WORD_1
	v_exp_f16_sdwa v61, v57 dst_sel:WORD_1 dst_unused:UNUSED_PRESERVE src0_sel:WORD_1
	v_pk_add_f16 v45, v45, v58
	v_pk_add_f16 v44, v44, v59
	v_rcp_f16_e32 v54, v45
	v_rcp_f16_sdwa v45, v45 dst_sel:DWORD dst_unused:UNUSED_PAD src0_sel:WORD_1
	v_pk_add_f16 v43, v43, v60
	v_rcp_f16_e32 v55, v44
	v_rcp_f16_sdwa v44, v44 dst_sel:DWORD dst_unused:UNUSED_PAD src0_sel:WORD_1
	v_pk_add_f16 v42, v42, v61
	v_rcp_f16_e32 v56, v43
	v_rcp_f16_sdwa v43, v43 dst_sel:DWORD dst_unused:UNUSED_PAD src0_sel:WORD_1
	v_rcp_f16_e32 v57, v42
	v_rcp_f16_sdwa v42, v42 dst_sel:DWORD dst_unused:UNUSED_PAD src0_sel:WORD_1
	v_pk_fma_f16 v30, v70, v58, v30
	v_pack_b32_f16 v45, v54, v45
	v_pk_fma_f16 v31, v71, v59, v31
	v_pk_mul_f16 v45, v30, v45
	v_pack_b32_f16 v30, v55, v44
	v_pk_fma_f16 v32, v72, v60, v32
	v_pk_mul_f16 v44, v31, v30
	v_pack_b32_f16 v30, v56, v43
	v_pk_fma_f16 v33, v73, v61, v33
	v_pk_mul_f16 v43, v32, v30
	v_pack_b32_f16 v30, v57, v42
	v_pk_mul_f16 v42, v33, v30
	s_waitcnt vmcnt(0)
	v_pk_mul_f16 v30, v208, v154 op_sel_hi:[0,1]
	v_pk_mul_f16 v31, v208, v155 op_sel_hi:[0,1]
	v_pk_mul_f16 v32, v208, v156 op_sel_hi:[0,1]
	v_pk_mul_f16 v33, v208, v157 op_sel_hi:[0,1]
	v_pk_mul_f16 v54, v206, v154 op_sel_hi:[0,1]
	v_pk_mul_f16 v55, v206, v155 op_sel_hi:[0,1]
	v_pk_mul_f16 v56, v206, v156 op_sel_hi:[0,1]
	v_pk_mul_f16 v57, v206, v157 op_sel_hi:[0,1]
	v_pk_mul_f16 v58, v207, v154 op_sel_hi:[0,1]
	v_pk_mul_f16 v59, v207, v155 op_sel_hi:[0,1]
	v_pk_mul_f16 v60, v207, v156 op_sel_hi:[0,1]
	v_pk_mul_f16 v61, v207, v157 op_sel_hi:[0,1]
	v_pk_fma_f16 v37, v37, v157, v33
	v_pk_fma_f16 v36, v36, v156, v32
	v_pk_fma_f16 v35, v35, v155, v31
	v_pk_fma_f16 v34, v34, v154, v30
	v_pk_fma_f16 v49, v49, v157, v57
	v_pk_fma_f16 v48, v48, v156, v56
	v_pk_fma_f16 v47, v47, v155, v55
	v_pk_fma_f16 v46, v46, v154, v54
	v_pk_fma_f16 v62, v69, v157, v61
	v_pk_fma_f16 v63, v68, v156, v60
	v_pk_fma_f16 v64, v67, v155, v59
	v_pk_fma_f16 v65, v66, v154, v58
	v_pk_fma_f16 v66, v89, v157, v33
	v_pk_fma_f16 v67, v88, v156, v32
	v_pk_fma_f16 v68, v87, v155, v31
	v_pk_fma_f16 v69, v86, v154, v30
	v_pk_fma_f16 v74, v117, v157, v57
	v_pk_fma_f16 v75, v116, v156, v56
	v_pk_fma_f16 v76, v115, v155, v55
	v_pk_fma_f16 v77, v114, v154, v54
	v_pk_fma_f16 v78, v133, v157, v61
	v_pk_fma_f16 v79, v132, v156, v60
	v_pk_fma_f16 v80, v131, v155, v59
	v_pk_fma_f16 v81, v130, v154, v58
	v_pk_fma_f16 v61, v17, v157, v61
	v_pk_fma_f16 v60, v16, v156, v60
	v_pk_fma_f16 v59, v15, v155, v59
	v_pk_fma_f16 v58, v14, v154, v58
	v_pk_maximum3_f16 v14, v34, v46, v65
	v_pk_maximum3_f16 v15, v35, v47, v64
	v_pk_maximum3_f16 v16, v36, v48, v63
	v_pk_maximum3_f16 v17, v37, v49, v62
	v_pk_maximum3_f16 v82, v69, v77, v81
	v_pk_maximum3_f16 v83, v68, v76, v80
	v_pk_maximum3_f16 v84, v67, v75, v79
	v_pk_maximum3_f16 v85, v66, v74, v78
	v_pk_fma_f16 v33, v145, v157, v33
	v_pk_fma_f16 v32, v144, v156, v32
	v_pk_fma_f16 v31, v143, v155, v31
	v_pk_fma_f16 v30, v142, v154, v30
	v_pk_fma_f16 v57, v153, v157, v57
	v_pk_fma_f16 v56, v152, v156, v56
	v_pk_fma_f16 v55, v151, v155, v55
	v_pk_fma_f16 v54, v150, v154, v54
	v_pk_maximum3_f16 v87, v31, v55, v59
	v_pk_maximum3_f16 v88, v32, v56, v60
	v_pk_maximum3_f16 v89, v33, v57, v61
	v_pk_maximum3_f16 v86, v30, v54, v58
	v_pk_maximum3_f16 v15, v15, v83, v87
	v_pk_maximum3_f16 v16, v16, v84, v88
	v_pk_maximum3_f16 v17, v17, v85, v89
	v_pk_maximum3_f16 v14, v14, v82, v86
	v_xor_b32_e32 v82, 0x80008000, v17
	v_xor_b32_e32 v83, 0x80008000, v16
	v_xor_b32_e32 v84, 0x80008000, v15
	v_xor_b32_e32 v85, 0x80008000, v14
	v_pk_add_f16 v14, v34, v85
	v_pk_add_f16 v15, v35, v84
	v_pk_add_f16 v16, v36, v83
	v_pk_add_f16 v17, v37, v82
	v_exp_f16_sdwa v34, v14 dst_sel:WORD_0 dst_unused:UNUSED_PAD src0_sel:WORD_0
	v_exp_f16_sdwa v35, v15 dst_sel:WORD_0 dst_unused:UNUSED_PAD src0_sel:WORD_0
	v_exp_f16_sdwa v36, v16 dst_sel:WORD_0 dst_unused:UNUSED_PAD src0_sel:WORD_0
	v_exp_f16_sdwa v37, v17 dst_sel:WORD_0 dst_unused:UNUSED_PAD src0_sel:WORD_0
	v_exp_f16_sdwa v34, v14 dst_sel:WORD_1 dst_unused:UNUSED_PRESERVE src0_sel:WORD_1
	v_exp_f16_sdwa v35, v15 dst_sel:WORD_1 dst_unused:UNUSED_PRESERVE src0_sel:WORD_1
	v_exp_f16_sdwa v36, v16 dst_sel:WORD_1 dst_unused:UNUSED_PRESERVE src0_sel:WORD_1
	v_exp_f16_sdwa v37, v17 dst_sel:WORD_1 dst_unused:UNUSED_PRESERVE src0_sel:WORD_1
	v_pk_add_f16 v14, v34, 0
	v_pk_add_f16 v15, v35, 0
	v_pk_add_f16 v16, v36, 0
	v_pk_add_f16 v17, v37, 0
	v_pk_fma_f16 v18, v18, v34, 0
	v_pk_fma_f16 v19, v19, v35, 0
	v_pk_fma_f16 v20, v20, v36, 0
	v_pk_fma_f16 v21, v21, v37, 0
	v_pk_add_f16 v34, v46, v85
	v_pk_add_f16 v35, v47, v84
	v_pk_add_f16 v36, v48, v83
	v_pk_add_f16 v37, v49, v82
	v_exp_f16_sdwa v46, v34 dst_sel:WORD_0 dst_unused:UNUSED_PAD src0_sel:WORD_0
	v_exp_f16_sdwa v47, v35 dst_sel:WORD_0 dst_unused:UNUSED_PAD src0_sel:WORD_0
	v_exp_f16_sdwa v48, v36 dst_sel:WORD_0 dst_unused:UNUSED_PAD src0_sel:WORD_0
	v_exp_f16_sdwa v49, v37 dst_sel:WORD_0 dst_unused:UNUSED_PAD src0_sel:WORD_0
	v_exp_f16_sdwa v46, v34 dst_sel:WORD_1 dst_unused:UNUSED_PRESERVE src0_sel:WORD_1
	v_exp_f16_sdwa v47, v35 dst_sel:WORD_1 dst_unused:UNUSED_PRESERVE src0_sel:WORD_1
	v_exp_f16_sdwa v48, v36 dst_sel:WORD_1 dst_unused:UNUSED_PRESERVE src0_sel:WORD_1
	v_exp_f16_sdwa v49, v37 dst_sel:WORD_1 dst_unused:UNUSED_PRESERVE src0_sel:WORD_1
	s_nop 0
	v_pk_add_f16 v17, v17, v49
	v_pk_add_f16 v16, v16, v48
	v_pk_add_f16 v15, v15, v47
	v_pk_add_f16 v14, v14, v46
	v_pk_fma_f16 v21, v25, v49, v21
	v_pk_fma_f16 v20, v24, v48, v20
	v_pk_fma_f16 v19, v23, v47, v19
	v_pk_fma_f16 v18, v22, v46, v18
	v_pk_add_f16 v22, v65, v85
	v_pk_add_f16 v23, v64, v84
	v_pk_add_f16 v24, v63, v83
	v_pk_add_f16 v25, v62, v82
	v_exp_f16_sdwa v34, v22 dst_sel:WORD_0 dst_unused:UNUSED_PAD src0_sel:WORD_0
	v_exp_f16_sdwa v35, v23 dst_sel:WORD_0 dst_unused:UNUSED_PAD src0_sel:WORD_0
	v_exp_f16_sdwa v36, v24 dst_sel:WORD_0 dst_unused:UNUSED_PAD src0_sel:WORD_0
	v_exp_f16_sdwa v37, v25 dst_sel:WORD_0 dst_unused:UNUSED_PAD src0_sel:WORD_0
	v_exp_f16_sdwa v34, v22 dst_sel:WORD_1 dst_unused:UNUSED_PRESERVE src0_sel:WORD_1
	v_exp_f16_sdwa v35, v23 dst_sel:WORD_1 dst_unused:UNUSED_PRESERVE src0_sel:WORD_1
	v_exp_f16_sdwa v36, v24 dst_sel:WORD_1 dst_unused:UNUSED_PRESERVE src0_sel:WORD_1
	v_exp_f16_sdwa v37, v25 dst_sel:WORD_1 dst_unused:UNUSED_PRESERVE src0_sel:WORD_1
	v_pk_add_f16 v22, v69, v85
	v_pk_add_f16 v14, v14, v34
	v_pk_add_f16 v15, v15, v35
	v_pk_add_f16 v16, v16, v36
	v_pk_add_f16 v17, v17, v37
	v_pk_fma_f16 v18, v26, v34, v18
	v_pk_fma_f16 v19, v27, v35, v19
	v_pk_fma_f16 v20, v28, v36, v20
	v_pk_fma_f16 v21, v29, v37, v21
	v_pk_add_f16 v23, v68, v84
	v_pk_add_f16 v24, v67, v83
	v_pk_add_f16 v25, v66, v82
	v_exp_f16_sdwa v26, v22 dst_sel:WORD_0 dst_unused:UNUSED_PAD src0_sel:WORD_0
	v_exp_f16_sdwa v27, v23 dst_sel:WORD_0 dst_unused:UNUSED_PAD src0_sel:WORD_0
	v_exp_f16_sdwa v28, v24 dst_sel:WORD_0 dst_unused:UNUSED_PAD src0_sel:WORD_0
	v_exp_f16_sdwa v29, v25 dst_sel:WORD_0 dst_unused:UNUSED_PAD src0_sel:WORD_0
	v_exp_f16_sdwa v26, v22 dst_sel:WORD_1 dst_unused:UNUSED_PRESERVE src0_sel:WORD_1
	v_exp_f16_sdwa v27, v23 dst_sel:WORD_1 dst_unused:UNUSED_PRESERVE src0_sel:WORD_1
	v_exp_f16_sdwa v28, v24 dst_sel:WORD_1 dst_unused:UNUSED_PRESERVE src0_sel:WORD_1
	v_exp_f16_sdwa v29, v25 dst_sel:WORD_1 dst_unused:UNUSED_PRESERVE src0_sel:WORD_1
	v_pk_add_f16 v22, v77, v85
	v_pk_add_f16 v17, v17, v29
	v_pk_add_f16 v16, v16, v28
	v_pk_add_f16 v15, v15, v27
	v_pk_add_f16 v14, v14, v26
	v_pk_fma_f16 v21, v41, v29, v21
	v_pk_fma_f16 v20, v40, v28, v20
	v_pk_fma_f16 v19, v39, v27, v19
	v_pk_fma_f16 v18, v38, v26, v18
	v_pk_add_f16 v23, v76, v84
	v_pk_add_f16 v24, v75, v83
	v_pk_add_f16 v25, v74, v82
	v_exp_f16_sdwa v26, v22 dst_sel:WORD_0 dst_unused:UNUSED_PAD src0_sel:WORD_0
	v_exp_f16_sdwa v27, v23 dst_sel:WORD_0 dst_unused:UNUSED_PAD src0_sel:WORD_0
	v_exp_f16_sdwa v28, v24 dst_sel:WORD_0 dst_unused:UNUSED_PAD src0_sel:WORD_0
	v_exp_f16_sdwa v29, v25 dst_sel:WORD_0 dst_unused:UNUSED_PAD src0_sel:WORD_0
	v_exp_f16_sdwa v26, v22 dst_sel:WORD_1 dst_unused:UNUSED_PRESERVE src0_sel:WORD_1
	v_exp_f16_sdwa v27, v23 dst_sel:WORD_1 dst_unused:UNUSED_PRESERVE src0_sel:WORD_1
	v_exp_f16_sdwa v28, v24 dst_sel:WORD_1 dst_unused:UNUSED_PRESERVE src0_sel:WORD_1
	v_exp_f16_sdwa v29, v25 dst_sel:WORD_1 dst_unused:UNUSED_PRESERVE src0_sel:WORD_1
	v_pk_add_f16 v22, v81, v85
	v_pk_add_f16 v14, v14, v26
	v_pk_add_f16 v15, v15, v27
	v_pk_add_f16 v16, v16, v28
	v_pk_add_f16 v17, v17, v29
	v_pk_fma_f16 v18, v50, v26, v18
	v_pk_fma_f16 v19, v51, v27, v19
	v_pk_fma_f16 v20, v52, v28, v20
	v_pk_fma_f16 v21, v53, v29, v21
	v_pk_add_f16 v23, v80, v84
	v_pk_add_f16 v24, v79, v83
	v_pk_add_f16 v25, v78, v82
	v_exp_f16_sdwa v26, v22 dst_sel:WORD_0 dst_unused:UNUSED_PAD src0_sel:WORD_0
	v_exp_f16_sdwa v27, v23 dst_sel:WORD_0 dst_unused:UNUSED_PAD src0_sel:WORD_0
	v_exp_f16_sdwa v28, v24 dst_sel:WORD_0 dst_unused:UNUSED_PAD src0_sel:WORD_0
	v_exp_f16_sdwa v29, v25 dst_sel:WORD_0 dst_unused:UNUSED_PAD src0_sel:WORD_0
	v_exp_f16_sdwa v26, v22 dst_sel:WORD_1 dst_unused:UNUSED_PRESERVE src0_sel:WORD_1
	v_exp_f16_sdwa v27, v23 dst_sel:WORD_1 dst_unused:UNUSED_PRESERVE src0_sel:WORD_1
	v_exp_f16_sdwa v28, v24 dst_sel:WORD_1 dst_unused:UNUSED_PRESERVE src0_sel:WORD_1
	v_exp_f16_sdwa v29, v25 dst_sel:WORD_1 dst_unused:UNUSED_PRESERVE src0_sel:WORD_1
	v_pk_add_f16 v22, v30, v85
	v_pk_add_f16 v17, v17, v29
	v_pk_add_f16 v16, v16, v28
	v_pk_add_f16 v15, v15, v27
	v_pk_add_f16 v14, v14, v26
	v_pk_fma_f16 v21, v73, v29, v21
	v_pk_fma_f16 v20, v72, v28, v20
	v_pk_fma_f16 v19, v71, v27, v19
	v_pk_fma_f16 v18, v70, v26, v18
	v_pk_add_f16 v23, v31, v84
	v_pk_add_f16 v24, v32, v83
	v_pk_add_f16 v25, v33, v82
	v_exp_f16_sdwa v26, v22 dst_sel:WORD_0 dst_unused:UNUSED_PAD src0_sel:WORD_0
	v_exp_f16_sdwa v27, v23 dst_sel:WORD_0 dst_unused:UNUSED_PAD src0_sel:WORD_0
	v_exp_f16_sdwa v28, v24 dst_sel:WORD_0 dst_unused:UNUSED_PAD src0_sel:WORD_0
	v_exp_f16_sdwa v29, v25 dst_sel:WORD_0 dst_unused:UNUSED_PAD src0_sel:WORD_0
	v_exp_f16_sdwa v26, v22 dst_sel:WORD_1 dst_unused:UNUSED_PRESERVE src0_sel:WORD_1
	v_exp_f16_sdwa v27, v23 dst_sel:WORD_1 dst_unused:UNUSED_PRESERVE src0_sel:WORD_1
	v_exp_f16_sdwa v28, v24 dst_sel:WORD_1 dst_unused:UNUSED_PRESERVE src0_sel:WORD_1
	v_exp_f16_sdwa v29, v25 dst_sel:WORD_1 dst_unused:UNUSED_PRESERVE src0_sel:WORD_1
	v_pk_add_f16 v22, v54, v85
	v_pk_add_f16 v14, v14, v26
	v_pk_add_f16 v15, v15, v27
	v_pk_add_f16 v16, v16, v28
	v_pk_add_f16 v17, v17, v29
	v_pk_fma_f16 v18, v90, v26, v18
	v_pk_fma_f16 v19, v91, v27, v19
	v_pk_fma_f16 v20, v92, v28, v20
	v_pk_fma_f16 v21, v93, v29, v21
	v_pk_add_f16 v23, v55, v84
	v_pk_add_f16 v24, v56, v83
	v_pk_add_f16 v25, v57, v82
	v_exp_f16_sdwa v26, v22 dst_sel:WORD_0 dst_unused:UNUSED_PAD src0_sel:WORD_0
	v_exp_f16_sdwa v27, v23 dst_sel:WORD_0 dst_unused:UNUSED_PAD src0_sel:WORD_0
	v_exp_f16_sdwa v28, v24 dst_sel:WORD_0 dst_unused:UNUSED_PAD src0_sel:WORD_0
	v_exp_f16_sdwa v29, v25 dst_sel:WORD_0 dst_unused:UNUSED_PAD src0_sel:WORD_0
	v_exp_f16_sdwa v26, v22 dst_sel:WORD_1 dst_unused:UNUSED_PRESERVE src0_sel:WORD_1
	v_exp_f16_sdwa v27, v23 dst_sel:WORD_1 dst_unused:UNUSED_PRESERVE src0_sel:WORD_1
	v_exp_f16_sdwa v28, v24 dst_sel:WORD_1 dst_unused:UNUSED_PRESERVE src0_sel:WORD_1
	v_exp_f16_sdwa v29, v25 dst_sel:WORD_1 dst_unused:UNUSED_PRESERVE src0_sel:WORD_1
	s_nop 0
	v_pk_add_f16 v17, v17, v29
	v_pk_add_f16 v16, v16, v28
	v_pk_add_f16 v15, v15, v27
	v_pk_add_f16 v14, v14, v26
	v_pk_fma_f16 v21, v113, v29, v21
	v_pk_fma_f16 v20, v112, v28, v20
	v_pk_fma_f16 v19, v111, v27, v19
	v_pk_fma_f16 v18, v110, v26, v18
	v_pk_add_f16 v26, v58, v85
	v_pk_add_f16 v27, v59, v84
	v_pk_add_f16 v28, v60, v83
	v_pk_add_f16 v29, v61, v82
	v_exp_f16_sdwa v22, v26 dst_sel:WORD_0 dst_unused:UNUSED_PAD src0_sel:WORD_0
	v_exp_f16_sdwa v23, v27 dst_sel:WORD_0 dst_unused:UNUSED_PAD src0_sel:WORD_0
	v_exp_f16_sdwa v24, v28 dst_sel:WORD_0 dst_unused:UNUSED_PAD src0_sel:WORD_0
	v_exp_f16_sdwa v25, v29 dst_sel:WORD_0 dst_unused:UNUSED_PAD src0_sel:WORD_0
	v_exp_f16_sdwa v22, v26 dst_sel:WORD_1 dst_unused:UNUSED_PRESERVE src0_sel:WORD_1
	v_exp_f16_sdwa v23, v27 dst_sel:WORD_1 dst_unused:UNUSED_PRESERVE src0_sel:WORD_1
	v_exp_f16_sdwa v24, v28 dst_sel:WORD_1 dst_unused:UNUSED_PRESERVE src0_sel:WORD_1
	v_exp_f16_sdwa v25, v29 dst_sel:WORD_1 dst_unused:UNUSED_PRESERVE src0_sel:WORD_1
	s_nop 0
